# baseline (speedup 1.0000x reference)
_Z7k_stageILi0ELi8EEv8AttnArgsPKDF16_PKfPDF16_iii:
	s_load_dwordx2 s[86:87], s[0:1], 0x70
	s_load_dwordx2 s[82:83], s[0:1], 0x88
	s_lshr_b32 s92, s2, 3
	s_mov_b32 s81, s3
	s_load_dwordx16 s[64:79], s[0:1], 0x0
	v_readfirstlane_b32 s94, v0
	s_nop 0
	s_lshr_b32 s94, s94, 6
	s_load_dwordx4 s[8:11], s[0:1], 0x88
	s_lshl_b32 s4, s2, 4
	s_and_b32 s4, s4, 0x70
	s_lshr_b32 s5, s2, 3
	s_add_i32 s4, s4, s5
	s_lshr_b32 s7, s4, 5
	s_lshl_b32 s6, s4, 1
	s_waitcnt lgkmcnt(0)
	s_lshl_b32 s11, s2, 1
	s_cmp_gt_i32 s10, 0
	v_readfirstlane_b32 s24, v0
	s_cbranch_scc1 .LBB3_2
	s_lshl_b32 s31, s7, 12
	s_ashr_i32 s2, s3, 31
	s_mov_b64 s[4:5], 0
	s_branch .LBB3_3

.LBB3_5:
	s_waitcnt lgkmcnt(0)
	v_cvt_f16_f32_e32 v180, s7
	v_cvt_f16_f32_e32 v182, s6
	v_cvt_f16_f32_e32 v181, s28
	s_waitcnt vmcnt(3)
	s_cmp_lg_u32 s10, 1
	s_cbranch_scc1 .Lmysw3_1
	s_mul_i32 s84, s81, s83
	s_add_i32 s84, s84, s82
	s_mul_i32 s84, s84, 0x60000
	s_lshl_b32 s85, s92, 3
	s_add_u32 s85, s85, s94
	s_mul_i32 s85, s85, 3072
	s_add_u32 s84, s84, s85
	s_add_u32 s88, s86, s84
	s_addc_u32 s89, s87, 0
	s_load_dword s90, s[88:89], 0x0
	s_load_dword s90, s[88:89], 0x80
	s_load_dword s90, s[88:89], 0x100
	s_load_dword s90, s[88:89], 0x180
	s_load_dword s90, s[88:89], 0x200
	s_load_dword s90, s[88:89], 0x280
	s_load_dword s90, s[88:89], 0x300
	s_load_dword s90, s[88:89], 0x380
	s_load_dword s90, s[88:89], 0x400
	s_load_dword s90, s[88:89], 0x480
	s_load_dword s90, s[88:89], 0x500
	s_load_dword s90, s[88:89], 0x580
	s_load_dword s90, s[88:89], 0x600
	s_load_dword s90, s[88:89], 0x680
	s_load_dword s90, s[88:89], 0x700
	s_load_dword s90, s[88:89], 0x780
	s_load_dword s90, s[88:89], 0x800
	s_load_dword s90, s[88:89], 0x880
	s_load_dword s90, s[88:89], 0x900
	s_load_dword s90, s[88:89], 0x980
	s_load_dword s90, s[88:89], 0xa00
	s_load_dword s90, s[88:89], 0xa80
	s_load_dword s90, s[88:89], 0xb00
	s_load_dword s90, s[88:89], 0xb80
.Lmysw3_1:
	v_pk_mul_f16 v183, v182, v184 op_sel_hi:[0,1]
	v_pk_mul_f16 v190, v182, v187 op_sel_hi:[0,1]
	v_pk_mul_f16 v194, v180, v187 op_sel_hi:[0,1]
	v_pk_mul_f16 v198, v181, v187 op_sel_hi:[0,1]
	v_pk_mul_f16 v188, v182, v185 op_sel_hi:[0,1]
	v_pk_mul_f16 v189, v182, v186 op_sel_hi:[0,1]
	v_pk_mul_f16 v191, v180, v184 op_sel_hi:[0,1]
	s_mov_b64 exec, s[64:65]
	buffer_load_dwordx4 v[18:21], v249, s[16:19], 0 offen
	buffer_load_dwordx4 v[6:9], v249, s[16:19], 0 offen offset:512
	s_mov_b64 exec, -1
	v_pk_mul_f16 v192, v180, v185 op_sel_hi:[0,1]
	v_pk_mul_f16 v193, v180, v186 op_sel_hi:[0,1]
	v_pk_mul_f16 v195, v181, v184 op_sel_hi:[0,1]
	v_pk_mul_f16 v196, v181, v185 op_sel_hi:[0,1]
	v_pk_mul_f16 v197, v181, v186 op_sel_hi:[0,1]
	v_pk_fma_f16 v113, v113, v187, v190
	v_pk_fma_f16 v110, v110, v184, v183
	v_pk_fma_f16 v129, v129, v187, v190
	v_pk_fma_f16 v126, v126, v184, v183
	v_pk_fma_f16 v141, v141, v187, v190
	v_pk_fma_f16 v138, v138, v184, v183
	v_pk_fma_f16 v183, v89, v187, v194
	v_pk_fma_f16 v199, v109, v187, v194
	buffer_load_dwordx4 v[30:33], v250, s[16:19], 0 offen offset:512
	buffer_load_dwordx4 v[10:13], v250, s[16:19], 0 offen offset:1024
	v_pk_fma_f16 v194, v125, v187, v194
	v_pk_fma_f16 v203, v53, v187, v198
	v_pk_fma_f16 v207, v69, v187, v198
	v_pk_fma_f16 v187, v97, v187, v198
	v_pk_maximum3_f16 v198, v113, v129, v141
	v_pk_fma_f16 v112, v112, v186, v189
	v_pk_fma_f16 v111, v111, v185, v188
	v_pk_fma_f16 v128, v128, v186, v189
	v_pk_fma_f16 v127, v127, v185, v188
	v_pk_fma_f16 v140, v140, v186, v189
	v_pk_fma_f16 v139, v139, v185, v188
	v_pk_fma_f16 v188, v88, v186, v193
	v_pk_fma_f16 v189, v87, v185, v192
	v_pk_fma_f16 v190, v86, v184, v191
	v_pk_fma_f16 v200, v108, v186, v193
	v_pk_fma_f16 v201, v107, v185, v192
	s_mov_b64 exec, s[66:67]
	buffer_load_dwordx4 v[54:57], v250, s[16:19], 0 offen offset:2048
	buffer_load_dwordx4 v[14:17], v250, s[16:19], 0 offen offset:2560
	s_mov_b64 exec, -1
	v_pk_fma_f16 v202, v106, v184, v191
	v_pk_fma_f16 v193, v124, v186, v193
	v_pk_fma_f16 v192, v123, v185, v192
	v_pk_fma_f16 v191, v122, v184, v191
	v_pk_fma_f16 v204, v52, v186, v197
	v_pk_fma_f16 v205, v51, v185, v196
	v_pk_fma_f16 v206, v50, v184, v195
	v_pk_fma_f16 v208, v68, v186, v197
	v_pk_fma_f16 v209, v67, v185, v196
	v_pk_fma_f16 v210, v66, v184, v195
	v_pk_fma_f16 v186, v96, v186, v197
	v_pk_fma_f16 v185, v95, v185, v196
	v_pk_fma_f16 v184, v94, v184, v195
	v_pk_maximum3_f16 v195, v110, v126, v138
	v_pk_maximum3_f16 v196, v111, v127, v139
	v_pk_maximum3_f16 v197, v112, v128, v140
	v_pk_maximum3_f16 v214, v183, v199, v194
	v_pk_maximum3_f16 v218, v203, v207, v187
	v_pk_maximum3_f16 v211, v190, v202, v191
	v_pk_maximum3_f16 v212, v189, v201, v192
	v_pk_maximum3_f16 v213, v188, v200, v193
	v_pk_maximum3_f16 v215, v206, v210, v184
	v_pk_maximum3_f16 v216, v205, v209, v185
	v_pk_maximum3_f16 v198, v198, v214, v218
	v_pk_maximum3_f16 v217, v204, v208, v186
	v_pk_maximum3_f16 v195, v195, v211, v215
	v_pk_maximum3_f16 v196, v196, v212, v216
	v_pk_maximum3_f16 v197, v197, v213, v217
	v_pk_add_f16 v113, v113, v198 neg_lo:[0,1] neg_hi:[0,1]
	s_mov_b64 exec, s[64:65]
	buffer_load_dwordx4 v[74:77], v251, s[16:19], 0 offen
	buffer_load_dwordx4 v[26:29], v251, s[16:19], 0 offen offset:512
	s_mov_b64 exec, -1
	v_pk_add_f16 v110, v110, v195 neg_lo:[0,1] neg_hi:[0,1]
	v_pk_add_f16 v111, v111, v196 neg_lo:[0,1] neg_hi:[0,1]
	v_pk_add_f16 v112, v112, v197 neg_lo:[0,1] neg_hi:[0,1]
	v_pk_add_f16 v126, v126, v195 neg_lo:[0,1] neg_hi:[0,1]
	v_exp_f16_sdwa v211, v110 dst_sel:WORD_0 dst_unused:UNUSED_PAD src0_sel:WORD_0
	v_exp_f16_sdwa v212, v111 dst_sel:WORD_0 dst_unused:UNUSED_PAD src0_sel:WORD_0
	v_exp_f16_sdwa v213, v112 dst_sel:WORD_0 dst_unused:UNUSED_PAD src0_sel:WORD_0
	v_exp_f16_sdwa v214, v113 dst_sel:WORD_0 dst_unused:UNUSED_PAD src0_sel:WORD_0
	v_exp_f16_sdwa v211, v110 dst_sel:WORD_1 dst_unused:UNUSED_PRESERVE src0_sel:WORD_1
	v_exp_f16_sdwa v212, v111 dst_sel:WORD_1 dst_unused:UNUSED_PRESERVE src0_sel:WORD_1
	v_exp_f16_sdwa v213, v112 dst_sel:WORD_1 dst_unused:UNUSED_PRESERVE src0_sel:WORD_1
	v_exp_f16_sdwa v214, v113 dst_sel:WORD_1 dst_unused:UNUSED_PRESERVE src0_sel:WORD_1
	v_pk_add_f16 v127, v127, v196 neg_lo:[0,1] neg_hi:[0,1]
	v_pk_add_f16 v113, v211, 0
	v_pk_fma_f16 v81, v81, v214, 0
	v_pk_add_f16 v110, v214, 0
	v_pk_add_f16 v111, v213, 0
	v_pk_add_f16 v112, v212, 0
	v_pk_fma_f16 v80, v80, v213, 0
	v_pk_fma_f16 v79, v79, v212, 0
	v_pk_fma_f16 v78, v78, v211, 0
	v_pk_add_f16 v128, v128, v197 neg_lo:[0,1] neg_hi:[0,1]
	buffer_load_dwordx4 v[98:101], v252, s[16:19], 0 offen offset:512
	buffer_load_dwordx4 v[38:41], v252, s[16:19], 0 offen offset:1024
	v_pk_add_f16 v129, v129, v198 neg_lo:[0,1] neg_hi:[0,1]
	v_exp_f16_sdwa v211, v126 dst_sel:WORD_0 dst_unused:UNUSED_PAD src0_sel:WORD_0
	v_exp_f16_sdwa v212, v127 dst_sel:WORD_0 dst_unused:UNUSED_PAD src0_sel:WORD_0
	v_exp_f16_sdwa v213, v128 dst_sel:WORD_0 dst_unused:UNUSED_PAD src0_sel:WORD_0
	v_exp_f16_sdwa v214, v129 dst_sel:WORD_0 dst_unused:UNUSED_PAD src0_sel:WORD_0
	v_exp_f16_sdwa v211, v126 dst_sel:WORD_1 dst_unused:UNUSED_PRESERVE src0_sel:WORD_1
	v_exp_f16_sdwa v212, v127 dst_sel:WORD_1 dst_unused:UNUSED_PRESERVE src0_sel:WORD_1
	v_exp_f16_sdwa v213, v128 dst_sel:WORD_1 dst_unused:UNUSED_PRESERVE src0_sel:WORD_1
	v_exp_f16_sdwa v214, v129 dst_sel:WORD_1 dst_unused:UNUSED_PRESERVE src0_sel:WORD_1
	v_pk_add_f16 v113, v113, v211
	v_pk_fma_f16 v81, v105, v214, v81
	v_pk_add_f16 v105, v141, v198 neg_lo:[0,1] neg_hi:[0,1]
	v_pk_add_f16 v112, v112, v212
	v_pk_add_f16 v111, v111, v213
	v_pk_add_f16 v110, v110, v214
	v_pk_fma_f16 v78, v102, v211, v78
	v_pk_fma_f16 v79, v103, v212, v79
	v_pk_fma_f16 v80, v104, v213, v80
	v_pk_add_f16 v102, v138, v195 neg_lo:[0,1] neg_hi:[0,1]
	v_pk_add_f16 v103, v139, v196 neg_lo:[0,1] neg_hi:[0,1]
	v_pk_add_f16 v104, v140, v197 neg_lo:[0,1] neg_hi:[0,1]
	v_exp_f16_sdwa v126, v102 dst_sel:WORD_0 dst_unused:UNUSED_PAD src0_sel:WORD_0
	v_exp_f16_sdwa v127, v103 dst_sel:WORD_0 dst_unused:UNUSED_PAD src0_sel:WORD_0
	v_exp_f16_sdwa v128, v104 dst_sel:WORD_0 dst_unused:UNUSED_PAD src0_sel:WORD_0
	v_exp_f16_sdwa v129, v105 dst_sel:WORD_0 dst_unused:UNUSED_PAD src0_sel:WORD_0
	v_exp_f16_sdwa v126, v102 dst_sel:WORD_1 dst_unused:UNUSED_PRESERVE src0_sel:WORD_1
	v_exp_f16_sdwa v127, v103 dst_sel:WORD_1 dst_unused:UNUSED_PRESERVE src0_sel:WORD_1
	v_exp_f16_sdwa v128, v104 dst_sel:WORD_1 dst_unused:UNUSED_PRESERVE src0_sel:WORD_1
	v_exp_f16_sdwa v129, v105 dst_sel:WORD_1 dst_unused:UNUSED_PRESERVE src0_sel:WORD_1
	v_pk_add_f16 v105, v113, v126
	v_pk_add_f16 v102, v110, v129
	s_mov_b64 exec, s[66:67]
	buffer_load_dwordx4 v[114:117], v252, s[16:19], 0 offen offset:2048
	buffer_load_dwordx4 v[58:61], v252, s[16:19], 0 offen offset:2560
	s_mov_b64 exec, -1
	v_pk_add_f16 v103, v111, v128
	v_pk_add_f16 v104, v112, v127
	v_pk_fma_f16 v81, v121, v129, v81
	v_pk_fma_f16 v80, v120, v128, v80
	v_pk_fma_f16 v79, v119, v127, v79
	v_pk_fma_f16 v78, v118, v126, v78
	v_pk_add_f16 v110, v190, v195 neg_lo:[0,1] neg_hi:[0,1]
	v_pk_add_f16 v111, v189, v196 neg_lo:[0,1] neg_hi:[0,1]
	v_pk_add_f16 v112, v188, v197 neg_lo:[0,1] neg_hi:[0,1]
	v_pk_add_f16 v113, v183, v198 neg_lo:[0,1] neg_hi:[0,1]
	v_exp_f16_sdwa v118, v110 dst_sel:WORD_0 dst_unused:UNUSED_PAD src0_sel:WORD_0
	v_exp_f16_sdwa v119, v111 dst_sel:WORD_0 dst_unused:UNUSED_PAD src0_sel:WORD_0
	v_exp_f16_sdwa v120, v112 dst_sel:WORD_0 dst_unused:UNUSED_PAD src0_sel:WORD_0
	v_exp_f16_sdwa v121, v113 dst_sel:WORD_0 dst_unused:UNUSED_PAD src0_sel:WORD_0
	v_exp_f16_sdwa v118, v110 dst_sel:WORD_1 dst_unused:UNUSED_PRESERVE src0_sel:WORD_1
	v_exp_f16_sdwa v119, v111 dst_sel:WORD_1 dst_unused:UNUSED_PRESERVE src0_sel:WORD_1
	v_exp_f16_sdwa v120, v112 dst_sel:WORD_1 dst_unused:UNUSED_PRESERVE src0_sel:WORD_1
	v_exp_f16_sdwa v121, v113 dst_sel:WORD_1 dst_unused:UNUSED_PRESERVE src0_sel:WORD_1
	v_pk_add_f16 v110, v202, v195 neg_lo:[0,1] neg_hi:[0,1]
	v_pk_add_f16 v105, v105, v118
	v_pk_add_f16 v104, v104, v119
	v_pk_add_f16 v103, v103, v120
	s_mov_b64 exec, s[76:77]
	buffer_load_dwordx4 v[130:133], v253, s[16:19], 0 offen
	buffer_load_dwordx4 v[70:73], v253, s[16:19], 0 offen offset:512
	s_mov_b64 exec, -1
	v_pk_add_f16 v102, v102, v121
	v_pk_fma_f16 v78, v46, v118, v78
	v_pk_fma_f16 v79, v47, v119, v79
	v_pk_fma_f16 v80, v48, v120, v80
	v_pk_fma_f16 v81, v49, v121, v81
	v_pk_add_f16 v111, v201, v196 neg_lo:[0,1] neg_hi:[0,1]
	v_pk_add_f16 v112, v200, v197 neg_lo:[0,1] neg_hi:[0,1]
	v_pk_add_f16 v113, v199, v198 neg_lo:[0,1] neg_hi:[0,1]
	v_exp_f16_sdwa v118, v110 dst_sel:WORD_0 dst_unused:UNUSED_PAD src0_sel:WORD_0
	v_exp_f16_sdwa v119, v111 dst_sel:WORD_0 dst_unused:UNUSED_PAD src0_sel:WORD_0
	v_exp_f16_sdwa v120, v112 dst_sel:WORD_0 dst_unused:UNUSED_PAD src0_sel:WORD_0
	v_exp_f16_sdwa v121, v113 dst_sel:WORD_0 dst_unused:UNUSED_PAD src0_sel:WORD_0
	v_exp_f16_sdwa v118, v110 dst_sel:WORD_1 dst_unused:UNUSED_PRESERVE src0_sel:WORD_1
	v_exp_f16_sdwa v119, v111 dst_sel:WORD_1 dst_unused:UNUSED_PRESERVE src0_sel:WORD_1
	v_exp_f16_sdwa v120, v112 dst_sel:WORD_1 dst_unused:UNUSED_PRESERVE src0_sel:WORD_1
	v_exp_f16_sdwa v121, v113 dst_sel:WORD_1 dst_unused:UNUSED_PRESERVE src0_sel:WORD_1
	v_pk_add_f16 v110, v191, v195 neg_lo:[0,1] neg_hi:[0,1]
	v_pk_add_f16 v105, v105, v118
	v_pk_add_f16 v102, v102, v121
	v_pk_add_f16 v103, v103, v120
	v_pk_add_f16 v104, v104, v119
	v_pk_fma_f16 v81, v65, v121, v81
	v_pk_fma_f16 v80, v64, v120, v80
	s_mov_b64 exec, s[70:71]
	buffer_load_dwordx4 v[134:137], v254, s[16:19], 0 offen offset:512
	buffer_load_dwordx4 v[90:93], v254, s[16:19], 0 offen offset:1024
	s_mov_b64 exec, -1
	v_pk_fma_f16 v79, v63, v119, v79
	v_pk_fma_f16 v78, v62, v118, v78
	v_pk_add_f16 v111, v192, v196 neg_lo:[0,1] neg_hi:[0,1]
	v_pk_add_f16 v112, v193, v197 neg_lo:[0,1] neg_hi:[0,1]
	v_pk_add_f16 v113, v194, v198 neg_lo:[0,1] neg_hi:[0,1]
	v_exp_f16_sdwa v118, v110 dst_sel:WORD_0 dst_unused:UNUSED_PAD src0_sel:WORD_0
	v_exp_f16_sdwa v119, v111 dst_sel:WORD_0 dst_unused:UNUSED_PAD src0_sel:WORD_0
	v_exp_f16_sdwa v120, v112 dst_sel:WORD_0 dst_unused:UNUSED_PAD src0_sel:WORD_0
	v_exp_f16_sdwa v121, v113 dst_sel:WORD_0 dst_unused:UNUSED_PAD src0_sel:WORD_0
	v_exp_f16_sdwa v118, v110 dst_sel:WORD_1 dst_unused:UNUSED_PRESERVE src0_sel:WORD_1
	v_exp_f16_sdwa v119, v111 dst_sel:WORD_1 dst_unused:UNUSED_PRESERVE src0_sel:WORD_1
	v_exp_f16_sdwa v120, v112 dst_sel:WORD_1 dst_unused:UNUSED_PRESERVE src0_sel:WORD_1
	v_exp_f16_sdwa v121, v113 dst_sel:WORD_1 dst_unused:UNUSED_PRESERVE src0_sel:WORD_1
	v_pk_add_f16 v110, v206, v195 neg_lo:[0,1] neg_hi:[0,1]
	v_pk_add_f16 v105, v105, v118
	v_pk_add_f16 v104, v104, v119
	v_pk_add_f16 v103, v103, v120
	v_pk_add_f16 v102, v102, v121
	v_pk_fma_f16 v78, v82, v118, v78
	v_pk_fma_f16 v79, v83, v119, v79
	v_pk_fma_f16 v80, v84, v120, v80
	v_pk_fma_f16 v81, v85, v121, v81
	s_mov_b64 exec, s[78:79]
	buffer_load_dwordx4 v[142:145], v254, s[16:19], 0 offen offset:2048
	buffer_load_dwordx4 v[2:5], v254, s[16:19], 0 offen offset:2560
	s_mov_b64 exec, -1
	v_pk_add_f16 v111, v205, v196 neg_lo:[0,1] neg_hi:[0,1]
	v_pk_add_f16 v112, v204, v197 neg_lo:[0,1] neg_hi:[0,1]
	v_pk_add_f16 v113, v203, v198 neg_lo:[0,1] neg_hi:[0,1]
	v_exp_f16_sdwa v118, v110 dst_sel:WORD_0 dst_unused:UNUSED_PAD src0_sel:WORD_0
	v_exp_f16_sdwa v119, v111 dst_sel:WORD_0 dst_unused:UNUSED_PAD src0_sel:WORD_0
	v_exp_f16_sdwa v120, v112 dst_sel:WORD_0 dst_unused:UNUSED_PAD src0_sel:WORD_0
	v_exp_f16_sdwa v121, v113 dst_sel:WORD_0 dst_unused:UNUSED_PAD src0_sel:WORD_0
	v_exp_f16_sdwa v118, v110 dst_sel:WORD_1 dst_unused:UNUSED_PRESERVE src0_sel:WORD_1
	v_exp_f16_sdwa v119, v111 dst_sel:WORD_1 dst_unused:UNUSED_PRESERVE src0_sel:WORD_1
	v_exp_f16_sdwa v120, v112 dst_sel:WORD_1 dst_unused:UNUSED_PRESERVE src0_sel:WORD_1
	v_exp_f16_sdwa v121, v113 dst_sel:WORD_1 dst_unused:UNUSED_PRESERVE src0_sel:WORD_1
	v_pk_add_f16 v110, v210, v195 neg_lo:[0,1] neg_hi:[0,1]
	v_pk_add_f16 v105, v105, v118
	v_pk_add_f16 v102, v102, v121
	v_pk_add_f16 v103, v103, v120
	v_pk_add_f16 v104, v104, v119
	v_pk_fma_f16 v81, v25, v121, v81
	v_pk_fma_f16 v80, v24, v120, v80
	v_pk_fma_f16 v79, v23, v119, v79
	v_pk_fma_f16 v78, v22, v118, v78
	v_pk_add_f16 v111, v209, v196 neg_lo:[0,1] neg_hi:[0,1]
	v_pk_add_f16 v112, v208, v197 neg_lo:[0,1] neg_hi:[0,1]
	v_pk_add_f16 v113, v207, v198 neg_lo:[0,1] neg_hi:[0,1]
	v_exp_f16_sdwa v118, v110 dst_sel:WORD_0 dst_unused:UNUSED_PAD src0_sel:WORD_0
	v_exp_f16_sdwa v119, v111 dst_sel:WORD_0 dst_unused:UNUSED_PAD src0_sel:WORD_0
	v_exp_f16_sdwa v120, v112 dst_sel:WORD_0 dst_unused:UNUSED_PAD src0_sel:WORD_0
	v_exp_f16_sdwa v121, v113 dst_sel:WORD_0 dst_unused:UNUSED_PAD src0_sel:WORD_0
	v_exp_f16_sdwa v118, v110 dst_sel:WORD_1 dst_unused:UNUSED_PRESERVE src0_sel:WORD_1
	v_exp_f16_sdwa v119, v111 dst_sel:WORD_1 dst_unused:UNUSED_PRESERVE src0_sel:WORD_1
	v_exp_f16_sdwa v120, v112 dst_sel:WORD_1 dst_unused:UNUSED_PRESERVE src0_sel:WORD_1
	v_exp_f16_sdwa v121, v113 dst_sel:WORD_1 dst_unused:UNUSED_PRESERVE src0_sel:WORD_1
	v_pk_add_f16 v110, v184, v195 neg_lo:[0,1] neg_hi:[0,1]
	v_pk_add_f16 v105, v105, v118
	v_pk_add_f16 v104, v104, v119
	v_pk_add_f16 v103, v103, v120
	v_pk_add_f16 v102, v102, v121
	v_pk_fma_f16 v78, v34, v118, v78
	v_pk_fma_f16 v79, v35, v119, v79
	v_pk_fma_f16 v80, v36, v120, v80
	v_pk_fma_f16 v81, v37, v121, v81
	v_pk_add_f16 v111, v185, v196 neg_lo:[0,1] neg_hi:[0,1]
	v_pk_add_f16 v112, v186, v197 neg_lo:[0,1] neg_hi:[0,1]
	v_pk_add_f16 v113, v187, v198 neg_lo:[0,1] neg_hi:[0,1]
	v_exp_f16_sdwa v118, v110 dst_sel:WORD_0 dst_unused:UNUSED_PAD src0_sel:WORD_0
	v_exp_f16_sdwa v119, v111 dst_sel:WORD_0 dst_unused:UNUSED_PAD src0_sel:WORD_0
	v_exp_f16_sdwa v120, v112 dst_sel:WORD_0 dst_unused:UNUSED_PAD src0_sel:WORD_0
	v_exp_f16_sdwa v121, v113 dst_sel:WORD_0 dst_unused:UNUSED_PAD src0_sel:WORD_0
	v_exp_f16_sdwa v118, v110 dst_sel:WORD_1 dst_unused:UNUSED_PRESERVE src0_sel:WORD_1
	v_exp_f16_sdwa v119, v111 dst_sel:WORD_1 dst_unused:UNUSED_PRESERVE src0_sel:WORD_1
	v_exp_f16_sdwa v120, v112 dst_sel:WORD_1 dst_unused:UNUSED_PRESERVE src0_sel:WORD_1
	v_exp_f16_sdwa v121, v113 dst_sel:WORD_1 dst_unused:UNUSED_PRESERVE src0_sel:WORD_1
	v_pk_add_f16 v105, v105, v118
	v_pk_add_f16 v104, v104, v119
	v_rcp_f16_e32 v110, v105
	v_rcp_f16_sdwa v105, v105 dst_sel:DWORD dst_unused:UNUSED_PAD src0_sel:WORD_1
	v_pk_add_f16 v103, v103, v120
	v_rcp_f16_e32 v111, v104
	v_rcp_f16_sdwa v104, v104 dst_sel:DWORD dst_unused:UNUSED_PAD src0_sel:WORD_1
	v_pk_add_f16 v102, v102, v121
	v_rcp_f16_e32 v112, v103
	v_rcp_f16_sdwa v103, v103 dst_sel:DWORD dst_unused:UNUSED_PAD src0_sel:WORD_1
	v_rcp_f16_e32 v113, v102
	v_rcp_f16_sdwa v102, v102 dst_sel:DWORD dst_unused:UNUSED_PAD src0_sel:WORD_1
	v_pk_fma_f16 v78, v42, v118, v78
	v_pack_b32_f16 v105, v110, v105
	v_pk_fma_f16 v79, v43, v119, v79
	v_pk_mul_f16 v110, v78, v105
	v_pack_b32_f16 v78, v111, v104
	v_pk_fma_f16 v80, v44, v120, v80
	v_pk_mul_f16 v111, v79, v78
	v_pack_b32_f16 v78, v112, v103
	v_pk_fma_f16 v81, v45, v121, v81
	v_pk_mul_f16 v112, v80, v78
	v_pack_b32_f16 v78, v113, v102
	v_pk_mul_f16 v113, v81, v78
	s_waitcnt vmcnt(12)
	v_pk_mul_f16 v78, v182, v154 op_sel_hi:[0,1]
	v_pk_mul_f16 v81, v182, v157 op_sel_hi:[0,1]
	v_pk_mul_f16 v105, v180, v157 op_sel_hi:[0,1]
	v_pk_mul_f16 v121, v181, v157 op_sel_hi:[0,1]
	v_pk_mul_f16 v79, v182, v155 op_sel_hi:[0,1]
	v_pk_mul_f16 v80, v182, v156 op_sel_hi:[0,1]
	v_pk_mul_f16 v102, v180, v154 op_sel_hi:[0,1]
	v_pk_mul_f16 v103, v180, v155 op_sel_hi:[0,1]
	v_pk_mul_f16 v104, v180, v156 op_sel_hi:[0,1]
	v_pk_mul_f16 v118, v181, v154 op_sel_hi:[0,1]
	v_pk_mul_f16 v119, v181, v155 op_sel_hi:[0,1]
	v_pk_mul_f16 v120, v181, v156 op_sel_hi:[0,1]
	v_pk_fma_f16 v89, v89, v157, v81
	v_pk_fma_f16 v86, v86, v154, v78
	v_pk_fma_f16 v109, v109, v157, v81
	v_pk_fma_f16 v106, v106, v154, v78
	v_pk_fma_f16 v81, v125, v157, v81
	v_pk_fma_f16 v78, v122, v154, v78
	v_pk_fma_f16 v122, v53, v157, v105
	v_pk_fma_f16 v126, v69, v157, v105
	v_pk_fma_f16 v105, v97, v157, v105
	v_pk_fma_f16 v138, v21, v157, v121
	v_pk_fma_f16 v183, v33, v157, v121
	v_pk_fma_f16 v121, v57, v157, v121
	v_pk_maximum3_f16 v157, v89, v109, v81
	v_pk_fma_f16 v88, v88, v156, v80
	v_pk_fma_f16 v87, v87, v155, v79
	v_pk_fma_f16 v108, v108, v156, v80
	v_pk_fma_f16 v107, v107, v155, v79
	v_pk_fma_f16 v80, v124, v156, v80
	v_pk_fma_f16 v79, v123, v155, v79
	v_pk_fma_f16 v123, v52, v156, v104
	v_pk_fma_f16 v124, v51, v155, v103
	v_pk_fma_f16 v125, v50, v154, v102
	v_pk_fma_f16 v127, v68, v156, v104
	v_pk_fma_f16 v128, v67, v155, v103
	v_pk_fma_f16 v129, v66, v154, v102
	v_pk_fma_f16 v104, v96, v156, v104
	v_pk_fma_f16 v103, v95, v155, v103
	v_pk_fma_f16 v102, v94, v154, v102
	v_pk_fma_f16 v139, v20, v156, v120
	v_pk_fma_f16 v140, v19, v155, v119
	v_pk_fma_f16 v141, v18, v154, v118
	v_pk_fma_f16 v184, v32, v156, v120
	v_pk_fma_f16 v185, v31, v155, v119
	v_pk_fma_f16 v186, v30, v154, v118
	v_pk_fma_f16 v120, v56, v156, v120
	v_pk_fma_f16 v119, v55, v155, v119
	v_pk_fma_f16 v118, v54, v154, v118
	v_pk_maximum3_f16 v154, v86, v106, v78
	v_pk_maximum3_f16 v155, v87, v107, v79
	v_pk_maximum3_f16 v156, v88, v108, v80
	v_pk_maximum3_f16 v190, v122, v126, v105
	v_pk_maximum3_f16 v194, v138, v183, v121
	v_pk_maximum3_f16 v187, v125, v129, v102
	v_pk_maximum3_f16 v188, v124, v128, v103
	v_pk_maximum3_f16 v189, v123, v127, v104
	v_pk_maximum3_f16 v191, v141, v186, v118
	v_pk_maximum3_f16 v192, v140, v185, v119
	v_pk_maximum3_f16 v157, v157, v190, v194
	v_pk_maximum3_f16 v193, v139, v184, v120
	v_pk_maximum3_f16 v154, v154, v187, v191
	v_pk_maximum3_f16 v155, v155, v188, v192
	v_pk_maximum3_f16 v156, v156, v189, v193
	v_pk_add_f16 v89, v89, v157 neg_lo:[0,1] neg_hi:[0,1]
	v_pk_add_f16 v86, v86, v154 neg_lo:[0,1] neg_hi:[0,1]
	v_pk_add_f16 v87, v87, v155 neg_lo:[0,1] neg_hi:[0,1]
	v_pk_add_f16 v88, v88, v156 neg_lo:[0,1] neg_hi:[0,1]
	v_pk_add_f16 v106, v106, v154 neg_lo:[0,1] neg_hi:[0,1]
	v_exp_f16_sdwa v187, v86 dst_sel:WORD_0 dst_unused:UNUSED_PAD src0_sel:WORD_0
	v_exp_f16_sdwa v188, v87 dst_sel:WORD_0 dst_unused:UNUSED_PAD src0_sel:WORD_0
	v_exp_f16_sdwa v189, v88 dst_sel:WORD_0 dst_unused:UNUSED_PAD src0_sel:WORD_0
	v_exp_f16_sdwa v190, v89 dst_sel:WORD_0 dst_unused:UNUSED_PAD src0_sel:WORD_0
	v_exp_f16_sdwa v187, v86 dst_sel:WORD_1 dst_unused:UNUSED_PRESERVE src0_sel:WORD_1
	v_exp_f16_sdwa v188, v87 dst_sel:WORD_1 dst_unused:UNUSED_PRESERVE src0_sel:WORD_1
	v_exp_f16_sdwa v189, v88 dst_sel:WORD_1 dst_unused:UNUSED_PRESERVE src0_sel:WORD_1
	v_exp_f16_sdwa v190, v89 dst_sel:WORD_1 dst_unused:UNUSED_PRESERVE src0_sel:WORD_1
	v_pk_add_f16 v107, v107, v155 neg_lo:[0,1] neg_hi:[0,1]
	v_pk_add_f16 v89, v187, 0
	v_pk_fma_f16 v49, v49, v190, 0
	v_pk_add_f16 v86, v190, 0
	v_pk_add_f16 v87, v189, 0
	v_pk_add_f16 v88, v188, 0
	v_pk_fma_f16 v48, v48, v189, 0
	v_pk_fma_f16 v47, v47, v188, 0
	v_pk_fma_f16 v46, v46, v187, 0
	v_pk_add_f16 v108, v108, v156 neg_lo:[0,1] neg_hi:[0,1]
	v_pk_add_f16 v109, v109, v157 neg_lo:[0,1] neg_hi:[0,1]
	v_exp_f16_sdwa v187, v106 dst_sel:WORD_0 dst_unused:UNUSED_PAD src0_sel:WORD_0
	v_exp_f16_sdwa v188, v107 dst_sel:WORD_0 dst_unused:UNUSED_PAD src0_sel:WORD_0
	v_exp_f16_sdwa v189, v108 dst_sel:WORD_0 dst_unused:UNUSED_PAD src0_sel:WORD_0
	v_exp_f16_sdwa v190, v109 dst_sel:WORD_0 dst_unused:UNUSED_PAD src0_sel:WORD_0
	v_exp_f16_sdwa v187, v106 dst_sel:WORD_1 dst_unused:UNUSED_PRESERVE src0_sel:WORD_1
	v_exp_f16_sdwa v188, v107 dst_sel:WORD_1 dst_unused:UNUSED_PRESERVE src0_sel:WORD_1
	v_exp_f16_sdwa v189, v108 dst_sel:WORD_1 dst_unused:UNUSED_PRESERVE src0_sel:WORD_1
	v_exp_f16_sdwa v190, v109 dst_sel:WORD_1 dst_unused:UNUSED_PRESERVE src0_sel:WORD_1
	v_pk_add_f16 v89, v89, v187
	v_pk_fma_f16 v49, v65, v190, v49
	v_pk_add_f16 v65, v81, v157 neg_lo:[0,1] neg_hi:[0,1]
	v_pk_add_f16 v88, v88, v188
	v_pk_add_f16 v87, v87, v189
	v_pk_add_f16 v86, v86, v190
	v_pk_fma_f16 v46, v62, v187, v46
	v_pk_fma_f16 v47, v63, v188, v47
	v_pk_fma_f16 v48, v64, v189, v48
	v_pk_add_f16 v62, v78, v154 neg_lo:[0,1] neg_hi:[0,1]
	v_pk_add_f16 v63, v79, v155 neg_lo:[0,1] neg_hi:[0,1]
	v_pk_add_f16 v64, v80, v156 neg_lo:[0,1] neg_hi:[0,1]
	v_exp_f16_sdwa v78, v62 dst_sel:WORD_0 dst_unused:UNUSED_PAD src0_sel:WORD_0
	v_exp_f16_sdwa v79, v63 dst_sel:WORD_0 dst_unused:UNUSED_PAD src0_sel:WORD_0
	v_exp_f16_sdwa v80, v64 dst_sel:WORD_0 dst_unused:UNUSED_PAD src0_sel:WORD_0
	v_exp_f16_sdwa v81, v65 dst_sel:WORD_0 dst_unused:UNUSED_PAD src0_sel:WORD_0
	v_exp_f16_sdwa v78, v62 dst_sel:WORD_1 dst_unused:UNUSED_PRESERVE src0_sel:WORD_1
	v_exp_f16_sdwa v79, v63 dst_sel:WORD_1 dst_unused:UNUSED_PRESERVE src0_sel:WORD_1
	v_exp_f16_sdwa v80, v64 dst_sel:WORD_1 dst_unused:UNUSED_PRESERVE src0_sel:WORD_1
	v_exp_f16_sdwa v81, v65 dst_sel:WORD_1 dst_unused:UNUSED_PRESERVE src0_sel:WORD_1
	v_pk_add_f16 v65, v89, v78
	v_pk_add_f16 v62, v86, v81
	v_pk_add_f16 v63, v87, v80
	v_pk_add_f16 v64, v88, v79
	v_pk_fma_f16 v49, v85, v81, v49
	v_pk_fma_f16 v48, v84, v80, v48
	v_pk_fma_f16 v47, v83, v79, v47
	v_pk_fma_f16 v46, v82, v78, v46
	v_pk_add_f16 v78, v125, v154 neg_lo:[0,1] neg_hi:[0,1]
	v_pk_add_f16 v79, v124, v155 neg_lo:[0,1] neg_hi:[0,1]
	v_pk_add_f16 v80, v123, v156 neg_lo:[0,1] neg_hi:[0,1]
	v_pk_add_f16 v81, v122, v157 neg_lo:[0,1] neg_hi:[0,1]
	v_exp_f16_sdwa v82, v78 dst_sel:WORD_0 dst_unused:UNUSED_PAD src0_sel:WORD_0
	v_exp_f16_sdwa v83, v79 dst_sel:WORD_0 dst_unused:UNUSED_PAD src0_sel:WORD_0
	v_exp_f16_sdwa v84, v80 dst_sel:WORD_0 dst_unused:UNUSED_PAD src0_sel:WORD_0
	v_exp_f16_sdwa v85, v81 dst_sel:WORD_0 dst_unused:UNUSED_PAD src0_sel:WORD_0
	v_exp_f16_sdwa v82, v78 dst_sel:WORD_1 dst_unused:UNUSED_PRESERVE src0_sel:WORD_1
	v_exp_f16_sdwa v83, v79 dst_sel:WORD_1 dst_unused:UNUSED_PRESERVE src0_sel:WORD_1
	v_exp_f16_sdwa v84, v80 dst_sel:WORD_1 dst_unused:UNUSED_PRESERVE src0_sel:WORD_1
	v_exp_f16_sdwa v85, v81 dst_sel:WORD_1 dst_unused:UNUSED_PRESERVE src0_sel:WORD_1
	v_pk_add_f16 v78, v129, v154 neg_lo:[0,1] neg_hi:[0,1]
	v_pk_add_f16 v65, v65, v82
	v_pk_add_f16 v64, v64, v83
	v_pk_add_f16 v63, v63, v84
	v_pk_add_f16 v62, v62, v85
	v_pk_fma_f16 v46, v22, v82, v46
	v_pk_fma_f16 v47, v23, v83, v47
	v_pk_fma_f16 v48, v24, v84, v48
	v_pk_fma_f16 v49, v25, v85, v49
	v_pk_add_f16 v79, v128, v155 neg_lo:[0,1] neg_hi:[0,1]
	v_pk_add_f16 v80, v127, v156 neg_lo:[0,1] neg_hi:[0,1]
	v_pk_add_f16 v81, v126, v157 neg_lo:[0,1] neg_hi:[0,1]
	v_exp_f16_sdwa v82, v78 dst_sel:WORD_0 dst_unused:UNUSED_PAD src0_sel:WORD_0
	v_exp_f16_sdwa v83, v79 dst_sel:WORD_0 dst_unused:UNUSED_PAD src0_sel:WORD_0
	v_exp_f16_sdwa v84, v80 dst_sel:WORD_0 dst_unused:UNUSED_PAD src0_sel:WORD_0
	v_exp_f16_sdwa v85, v81 dst_sel:WORD_0 dst_unused:UNUSED_PAD src0_sel:WORD_0
	v_exp_f16_sdwa v82, v78 dst_sel:WORD_1 dst_unused:UNUSED_PRESERVE src0_sel:WORD_1
	v_exp_f16_sdwa v83, v79 dst_sel:WORD_1 dst_unused:UNUSED_PRESERVE src0_sel:WORD_1
	v_exp_f16_sdwa v84, v80 dst_sel:WORD_1 dst_unused:UNUSED_PRESERVE src0_sel:WORD_1
	v_exp_f16_sdwa v85, v81 dst_sel:WORD_1 dst_unused:UNUSED_PRESERVE src0_sel:WORD_1
	v_pk_add_f16 v78, v102, v154 neg_lo:[0,1] neg_hi:[0,1]
	v_pk_add_f16 v65, v65, v82
	v_pk_add_f16 v62, v62, v85
	v_pk_add_f16 v63, v63, v84
	v_pk_add_f16 v64, v64, v83
	v_pk_fma_f16 v49, v37, v85, v49
	v_pk_fma_f16 v48, v36, v84, v48
	v_pk_fma_f16 v47, v35, v83, v47
	v_pk_fma_f16 v46, v34, v82, v46
	v_pk_add_f16 v79, v103, v155 neg_lo:[0,1] neg_hi:[0,1]
	v_pk_add_f16 v80, v104, v156 neg_lo:[0,1] neg_hi:[0,1]
	v_pk_add_f16 v81, v105, v157 neg_lo:[0,1] neg_hi:[0,1]
	v_exp_f16_sdwa v82, v78 dst_sel:WORD_0 dst_unused:UNUSED_PAD src0_sel:WORD_0
	v_exp_f16_sdwa v83, v79 dst_sel:WORD_0 dst_unused:UNUSED_PAD src0_sel:WORD_0
	v_exp_f16_sdwa v84, v80 dst_sel:WORD_0 dst_unused:UNUSED_PAD src0_sel:WORD_0
	v_exp_f16_sdwa v85, v81 dst_sel:WORD_0 dst_unused:UNUSED_PAD src0_sel:WORD_0
	v_exp_f16_sdwa v82, v78 dst_sel:WORD_1 dst_unused:UNUSED_PRESERVE src0_sel:WORD_1
	v_exp_f16_sdwa v83, v79 dst_sel:WORD_1 dst_unused:UNUSED_PRESERVE src0_sel:WORD_1
	v_exp_f16_sdwa v84, v80 dst_sel:WORD_1 dst_unused:UNUSED_PRESERVE src0_sel:WORD_1
	v_exp_f16_sdwa v85, v81 dst_sel:WORD_1 dst_unused:UNUSED_PRESERVE src0_sel:WORD_1
	v_pk_add_f16 v78, v141, v154 neg_lo:[0,1] neg_hi:[0,1]
	v_pk_add_f16 v65, v65, v82
	v_pk_add_f16 v64, v64, v83
	v_pk_add_f16 v63, v63, v84
	v_pk_add_f16 v62, v62, v85
	v_pk_fma_f16 v46, v42, v82, v46
	v_pk_fma_f16 v47, v43, v83, v47
	v_pk_fma_f16 v48, v44, v84, v48
	v_pk_fma_f16 v49, v45, v85, v49
	v_pk_add_f16 v79, v140, v155 neg_lo:[0,1] neg_hi:[0,1]
	v_pk_add_f16 v80, v139, v156 neg_lo:[0,1] neg_hi:[0,1]
	v_pk_add_f16 v81, v138, v157 neg_lo:[0,1] neg_hi:[0,1]
	v_exp_f16_sdwa v82, v78 dst_sel:WORD_0 dst_unused:UNUSED_PAD src0_sel:WORD_0
	v_exp_f16_sdwa v83, v79 dst_sel:WORD_0 dst_unused:UNUSED_PAD src0_sel:WORD_0
	v_exp_f16_sdwa v84, v80 dst_sel:WORD_0 dst_unused:UNUSED_PAD src0_sel:WORD_0
	v_exp_f16_sdwa v85, v81 dst_sel:WORD_0 dst_unused:UNUSED_PAD src0_sel:WORD_0
	v_exp_f16_sdwa v82, v78 dst_sel:WORD_1 dst_unused:UNUSED_PRESERVE src0_sel:WORD_1
	v_exp_f16_sdwa v83, v79 dst_sel:WORD_1 dst_unused:UNUSED_PRESERVE src0_sel:WORD_1
	v_exp_f16_sdwa v84, v80 dst_sel:WORD_1 dst_unused:UNUSED_PRESERVE src0_sel:WORD_1
	v_exp_f16_sdwa v85, v81 dst_sel:WORD_1 dst_unused:UNUSED_PRESERVE src0_sel:WORD_1
	v_pk_add_f16 v78, v186, v154 neg_lo:[0,1] neg_hi:[0,1]
	v_pk_add_f16 v65, v65, v82
	v_pk_add_f16 v62, v62, v85
	v_pk_add_f16 v63, v63, v84
	v_pk_add_f16 v64, v64, v83
	v_pk_fma_f16 v49, v9, v85, v49
	v_pk_fma_f16 v48, v8, v84, v48
	v_pk_fma_f16 v47, v7, v83, v47
	v_pk_fma_f16 v46, v6, v82, v46
	v_pk_add_f16 v79, v185, v155 neg_lo:[0,1] neg_hi:[0,1]
	v_pk_add_f16 v80, v184, v156 neg_lo:[0,1] neg_hi:[0,1]
	v_pk_add_f16 v81, v183, v157 neg_lo:[0,1] neg_hi:[0,1]
	v_exp_f16_sdwa v82, v78 dst_sel:WORD_0 dst_unused:UNUSED_PAD src0_sel:WORD_0
	v_exp_f16_sdwa v83, v79 dst_sel:WORD_0 dst_unused:UNUSED_PAD src0_sel:WORD_0
	v_exp_f16_sdwa v84, v80 dst_sel:WORD_0 dst_unused:UNUSED_PAD src0_sel:WORD_0
	v_exp_f16_sdwa v85, v81 dst_sel:WORD_0 dst_unused:UNUSED_PAD src0_sel:WORD_0
	v_exp_f16_sdwa v82, v78 dst_sel:WORD_1 dst_unused:UNUSED_PRESERVE src0_sel:WORD_1
	v_exp_f16_sdwa v83, v79 dst_sel:WORD_1 dst_unused:UNUSED_PRESERVE src0_sel:WORD_1
	v_exp_f16_sdwa v84, v80 dst_sel:WORD_1 dst_unused:UNUSED_PRESERVE src0_sel:WORD_1
	v_exp_f16_sdwa v85, v81 dst_sel:WORD_1 dst_unused:UNUSED_PRESERVE src0_sel:WORD_1
	v_pk_add_f16 v78, v118, v154 neg_lo:[0,1] neg_hi:[0,1]
	v_pk_add_f16 v65, v65, v82
	v_pk_add_f16 v64, v64, v83
	v_pk_add_f16 v63, v63, v84
	v_pk_add_f16 v62, v62, v85
	v_pk_fma_f16 v46, v10, v82, v46
	v_pk_fma_f16 v47, v11, v83, v47
	v_pk_fma_f16 v48, v12, v84, v48
	v_pk_fma_f16 v49, v13, v85, v49
	v_pk_add_f16 v79, v119, v155 neg_lo:[0,1] neg_hi:[0,1]
	v_pk_add_f16 v80, v120, v156 neg_lo:[0,1] neg_hi:[0,1]
	v_pk_add_f16 v81, v121, v157 neg_lo:[0,1] neg_hi:[0,1]
	v_exp_f16_sdwa v82, v78 dst_sel:WORD_0 dst_unused:UNUSED_PAD src0_sel:WORD_0
	v_exp_f16_sdwa v83, v79 dst_sel:WORD_0 dst_unused:UNUSED_PAD src0_sel:WORD_0
	v_exp_f16_sdwa v84, v80 dst_sel:WORD_0 dst_unused:UNUSED_PAD src0_sel:WORD_0
	v_exp_f16_sdwa v85, v81 dst_sel:WORD_0 dst_unused:UNUSED_PAD src0_sel:WORD_0
	v_exp_f16_sdwa v82, v78 dst_sel:WORD_1 dst_unused:UNUSED_PRESERVE src0_sel:WORD_1
	v_exp_f16_sdwa v83, v79 dst_sel:WORD_1 dst_unused:UNUSED_PRESERVE src0_sel:WORD_1
	v_exp_f16_sdwa v84, v80 dst_sel:WORD_1 dst_unused:UNUSED_PRESERVE src0_sel:WORD_1
	v_exp_f16_sdwa v85, v81 dst_sel:WORD_1 dst_unused:UNUSED_PRESERVE src0_sel:WORD_1
	v_pk_add_f16 v65, v65, v82
	v_pk_add_f16 v64, v64, v83
	v_rcp_f16_e32 v78, v65
	v_rcp_f16_sdwa v65, v65 dst_sel:DWORD dst_unused:UNUSED_PAD src0_sel:WORD_1
	v_pk_add_f16 v63, v63, v84
	v_rcp_f16_e32 v79, v64
	v_rcp_f16_sdwa v64, v64 dst_sel:DWORD dst_unused:UNUSED_PAD src0_sel:WORD_1
	v_pk_add_f16 v62, v62, v85
	v_rcp_f16_e32 v80, v63
	v_rcp_f16_sdwa v81, v63 dst_sel:DWORD dst_unused:UNUSED_PAD src0_sel:WORD_1
	v_pk_fma_f16 v47, v15, v83, v47
	v_pk_fma_f16 v46, v14, v82, v46
	v_rcp_f16_e32 v82, v62
	v_rcp_f16_sdwa v83, v62 dst_sel:DWORD dst_unused:UNUSED_PAD src0_sel:WORD_1
	v_pack_b32_f16 v62, v78, v65
	v_pk_mul_f16 v62, v46, v62
	v_pack_b32_f16 v46, v79, v64
	v_pk_fma_f16 v48, v16, v84, v48
	v_pk_mul_f16 v63, v47, v46
	v_pack_b32_f16 v46, v80, v81
	v_pk_fma_f16 v49, v17, v85, v49
	v_pk_mul_f16 v64, v48, v46
	v_pack_b32_f16 v46, v82, v83
	v_pk_mul_f16 v65, v49, v46
	s_waitcnt vmcnt(6)
	v_pk_mul_f16 v46, v182, v150 op_sel_hi:[0,1]
	v_pk_mul_f16 v47, v182, v151 op_sel_hi:[0,1]
	v_pk_mul_f16 v48, v182, v152 op_sel_hi:[0,1]
	v_pk_mul_f16 v49, v182, v153 op_sel_hi:[0,1]
	v_pk_mul_f16 v78, v180, v150 op_sel_hi:[0,1]
	v_pk_mul_f16 v82, v181, v150 op_sel_hi:[0,1]
	v_pk_fma_f16 v50, v50, v150, v46
	v_pk_fma_f16 v66, v66, v150, v46
	v_pk_fma_f16 v46, v94, v150, v46
	v_pk_mul_f16 v79, v180, v151 op_sel_hi:[0,1]
	v_pk_maximum3_f16 v118, v50, v66, v46
	v_pk_mul_f16 v80, v180, v152 op_sel_hi:[0,1]
	v_pk_mul_f16 v81, v180, v153 op_sel_hi:[0,1]
	v_pk_mul_f16 v83, v181, v151 op_sel_hi:[0,1]
	v_pk_mul_f16 v84, v181, v152 op_sel_hi:[0,1]
	v_pk_mul_f16 v85, v181, v153 op_sel_hi:[0,1]
	v_pk_fma_f16 v53, v53, v153, v49
	v_pk_fma_f16 v52, v52, v152, v48
	v_pk_fma_f16 v51, v51, v151, v47
	v_pk_fma_f16 v69, v69, v153, v49
	v_pk_fma_f16 v68, v68, v152, v48
	v_pk_fma_f16 v67, v67, v151, v47
	v_pk_fma_f16 v49, v97, v153, v49
	v_pk_fma_f16 v48, v96, v152, v48
	v_pk_fma_f16 v47, v95, v151, v47
	v_pk_fma_f16 v89, v18, v150, v78
	v_pk_fma_f16 v97, v30, v150, v78
	v_pk_fma_f16 v78, v54, v150, v78
	v_pk_fma_f16 v105, v74, v150, v82
	v_pk_fma_f16 v109, v98, v150, v82
	v_pk_fma_f16 v82, v114, v150, v82
	v_pk_maximum3_f16 v119, v51, v67, v47
	v_pk_maximum3_f16 v120, v52, v68, v48
	v_pk_maximum3_f16 v121, v53, v69, v49
	v_pk_maximum3_f16 v122, v89, v97, v78
	v_pk_fma_f16 v86, v21, v153, v81
	v_pk_maximum3_f16 v126, v105, v109, v82
	v_pk_fma_f16 v87, v20, v152, v80
	v_pk_maximum3_f16 v118, v118, v122, v126
	v_pk_fma_f16 v88, v19, v151, v79
	v_pk_fma_f16 v94, v33, v153, v81
	v_pk_fma_f16 v95, v32, v152, v80
	v_pk_fma_f16 v96, v31, v151, v79
	v_pk_fma_f16 v81, v57, v153, v81
	v_pk_fma_f16 v80, v56, v152, v80
	v_pk_fma_f16 v79, v55, v151, v79
	v_pk_fma_f16 v102, v77, v153, v85
	v_pk_fma_f16 v103, v76, v152, v84
	v_pk_fma_f16 v104, v75, v151, v83
	v_pk_fma_f16 v106, v101, v153, v85
	v_pk_fma_f16 v107, v100, v152, v84
	v_pk_fma_f16 v108, v99, v151, v83
	v_pk_fma_f16 v85, v117, v153, v85
	v_pk_fma_f16 v84, v116, v152, v84
	v_pk_fma_f16 v83, v115, v151, v83
	v_pk_maximum3_f16 v123, v88, v96, v79
	v_pk_maximum3_f16 v124, v87, v95, v80
	v_pk_maximum3_f16 v125, v86, v94, v81
	v_pk_maximum3_f16 v128, v103, v107, v84
	v_pk_maximum3_f16 v129, v102, v106, v85
	v_pk_maximum3_f16 v127, v104, v108, v83
	v_pk_maximum3_f16 v119, v119, v123, v127
	v_pk_maximum3_f16 v120, v120, v124, v128
	v_pk_maximum3_f16 v121, v121, v125, v129
	v_pk_add_f16 v50, v50, v118 neg_lo:[0,1] neg_hi:[0,1]
	v_pk_add_f16 v51, v51, v119 neg_lo:[0,1] neg_hi:[0,1]
	v_pk_add_f16 v52, v52, v120 neg_lo:[0,1] neg_hi:[0,1]
	v_pk_add_f16 v53, v53, v121 neg_lo:[0,1] neg_hi:[0,1]
	v_pk_add_f16 v66, v66, v118 neg_lo:[0,1] neg_hi:[0,1]
	v_exp_f16_sdwa v122, v50 dst_sel:WORD_0 dst_unused:UNUSED_PAD src0_sel:WORD_0
	v_exp_f16_sdwa v123, v51 dst_sel:WORD_0 dst_unused:UNUSED_PAD src0_sel:WORD_0
	v_exp_f16_sdwa v124, v52 dst_sel:WORD_0 dst_unused:UNUSED_PAD src0_sel:WORD_0
	v_exp_f16_sdwa v125, v53 dst_sel:WORD_0 dst_unused:UNUSED_PAD src0_sel:WORD_0
	v_exp_f16_sdwa v122, v50 dst_sel:WORD_1 dst_unused:UNUSED_PRESERVE src0_sel:WORD_1
	v_exp_f16_sdwa v123, v51 dst_sel:WORD_1 dst_unused:UNUSED_PRESERVE src0_sel:WORD_1
	v_exp_f16_sdwa v124, v52 dst_sel:WORD_1 dst_unused:UNUSED_PRESERVE src0_sel:WORD_1
	v_exp_f16_sdwa v125, v53 dst_sel:WORD_1 dst_unused:UNUSED_PRESERVE src0_sel:WORD_1
	v_pk_add_f16 v67, v67, v119 neg_lo:[0,1] neg_hi:[0,1]
	v_pk_add_f16 v50, v125, 0
	v_pk_fma_f16 v22, v22, v122, 0
	v_pk_add_f16 v51, v124, 0
	v_pk_add_f16 v52, v123, 0
	v_pk_add_f16 v53, v122, 0
	v_pk_fma_f16 v23, v23, v123, 0
	v_pk_fma_f16 v24, v24, v124, 0
	v_pk_fma_f16 v25, v25, v125, 0
	v_pk_add_f16 v68, v68, v120 neg_lo:[0,1] neg_hi:[0,1]
	v_pk_add_f16 v69, v69, v121 neg_lo:[0,1] neg_hi:[0,1]
	v_exp_f16_sdwa v122, v66 dst_sel:WORD_0 dst_unused:UNUSED_PAD src0_sel:WORD_0
	v_exp_f16_sdwa v123, v67 dst_sel:WORD_0 dst_unused:UNUSED_PAD src0_sel:WORD_0
	v_exp_f16_sdwa v124, v68 dst_sel:WORD_0 dst_unused:UNUSED_PAD src0_sel:WORD_0
	v_exp_f16_sdwa v125, v69 dst_sel:WORD_0 dst_unused:UNUSED_PAD src0_sel:WORD_0
	v_exp_f16_sdwa v122, v66 dst_sel:WORD_1 dst_unused:UNUSED_PRESERVE src0_sel:WORD_1
	v_exp_f16_sdwa v123, v67 dst_sel:WORD_1 dst_unused:UNUSED_PRESERVE src0_sel:WORD_1
	v_exp_f16_sdwa v124, v68 dst_sel:WORD_1 dst_unused:UNUSED_PRESERVE src0_sel:WORD_1
	v_exp_f16_sdwa v125, v69 dst_sel:WORD_1 dst_unused:UNUSED_PRESERVE src0_sel:WORD_1
	s_nop 0
	v_pk_add_f16 v50, v50, v125
	v_pk_fma_f16 v22, v34, v122, v22
	v_pk_add_f16 v34, v46, v118 neg_lo:[0,1] neg_hi:[0,1]
	v_pk_add_f16 v53, v53, v122
	v_pk_add_f16 v52, v52, v123
	v_pk_add_f16 v51, v51, v124
	v_pk_fma_f16 v25, v37, v125, v25
	v_pk_fma_f16 v24, v36, v124, v24
	v_pk_fma_f16 v23, v35, v123, v23
	v_pk_add_f16 v35, v47, v119 neg_lo:[0,1] neg_hi:[0,1]
	v_pk_add_f16 v36, v48, v120 neg_lo:[0,1] neg_hi:[0,1]
	v_pk_add_f16 v37, v49, v121 neg_lo:[0,1] neg_hi:[0,1]
	v_exp_f16_sdwa v46, v34 dst_sel:WORD_0 dst_unused:UNUSED_PAD src0_sel:WORD_0
	v_exp_f16_sdwa v47, v35 dst_sel:WORD_0 dst_unused:UNUSED_PAD src0_sel:WORD_0
	v_exp_f16_sdwa v48, v36 dst_sel:WORD_0 dst_unused:UNUSED_PAD src0_sel:WORD_0
	v_exp_f16_sdwa v49, v37 dst_sel:WORD_0 dst_unused:UNUSED_PAD src0_sel:WORD_0
	v_exp_f16_sdwa v46, v34 dst_sel:WORD_1 dst_unused:UNUSED_PRESERVE src0_sel:WORD_1
	v_exp_f16_sdwa v47, v35 dst_sel:WORD_1 dst_unused:UNUSED_PRESERVE src0_sel:WORD_1
	v_exp_f16_sdwa v48, v36 dst_sel:WORD_1 dst_unused:UNUSED_PRESERVE src0_sel:WORD_1
	v_exp_f16_sdwa v49, v37 dst_sel:WORD_1 dst_unused:UNUSED_PRESERVE src0_sel:WORD_1
	s_nop 0
	v_pk_add_f16 v34, v50, v49
	v_pk_add_f16 v35, v51, v48
	v_pk_add_f16 v36, v52, v47
	v_pk_add_f16 v37, v53, v46
	v_pk_fma_f16 v22, v42, v46, v22
	v_pk_fma_f16 v23, v43, v47, v23
	v_pk_fma_f16 v24, v44, v48, v24
	v_pk_fma_f16 v25, v45, v49, v25
	v_pk_add_f16 v42, v89, v118 neg_lo:[0,1] neg_hi:[0,1]
	v_pk_add_f16 v43, v88, v119 neg_lo:[0,1] neg_hi:[0,1]
	v_pk_add_f16 v44, v87, v120 neg_lo:[0,1] neg_hi:[0,1]
	v_pk_add_f16 v45, v86, v121 neg_lo:[0,1] neg_hi:[0,1]
	v_exp_f16_sdwa v46, v42 dst_sel:WORD_0 dst_unused:UNUSED_PAD src0_sel:WORD_0
	v_exp_f16_sdwa v47, v43 dst_sel:WORD_0 dst_unused:UNUSED_PAD src0_sel:WORD_0
	v_exp_f16_sdwa v48, v44 dst_sel:WORD_0 dst_unused:UNUSED_PAD src0_sel:WORD_0
	v_exp_f16_sdwa v49, v45 dst_sel:WORD_0 dst_unused:UNUSED_PAD src0_sel:WORD_0
	v_exp_f16_sdwa v46, v42 dst_sel:WORD_1 dst_unused:UNUSED_PRESERVE src0_sel:WORD_1
	v_exp_f16_sdwa v47, v43 dst_sel:WORD_1 dst_unused:UNUSED_PRESERVE src0_sel:WORD_1
	v_exp_f16_sdwa v48, v44 dst_sel:WORD_1 dst_unused:UNUSED_PRESERVE src0_sel:WORD_1
	v_exp_f16_sdwa v49, v45 dst_sel:WORD_1 dst_unused:UNUSED_PRESERVE src0_sel:WORD_1
	v_pk_add_f16 v42, v97, v118 neg_lo:[0,1] neg_hi:[0,1]
	v_pk_add_f16 v34, v34, v49
	v_pk_add_f16 v37, v37, v46
	v_pk_add_f16 v36, v36, v47
	v_pk_add_f16 v35, v35, v48
	v_pk_fma_f16 v25, v9, v49, v25
	v_pk_fma_f16 v24, v8, v48, v24
	v_pk_fma_f16 v23, v7, v47, v23
	v_pk_fma_f16 v22, v6, v46, v22
	v_pk_add_f16 v43, v96, v119 neg_lo:[0,1] neg_hi:[0,1]
	v_pk_add_f16 v44, v95, v120 neg_lo:[0,1] neg_hi:[0,1]
	v_pk_add_f16 v45, v94, v121 neg_lo:[0,1] neg_hi:[0,1]
	v_exp_f16_sdwa v46, v42 dst_sel:WORD_0 dst_unused:UNUSED_PAD src0_sel:WORD_0
	v_exp_f16_sdwa v47, v43 dst_sel:WORD_0 dst_unused:UNUSED_PAD src0_sel:WORD_0
	v_exp_f16_sdwa v48, v44 dst_sel:WORD_0 dst_unused:UNUSED_PAD src0_sel:WORD_0
	v_exp_f16_sdwa v49, v45 dst_sel:WORD_0 dst_unused:UNUSED_PAD src0_sel:WORD_0
	v_exp_f16_sdwa v46, v42 dst_sel:WORD_1 dst_unused:UNUSED_PRESERVE src0_sel:WORD_1
	v_exp_f16_sdwa v47, v43 dst_sel:WORD_1 dst_unused:UNUSED_PRESERVE src0_sel:WORD_1
	v_exp_f16_sdwa v48, v44 dst_sel:WORD_1 dst_unused:UNUSED_PRESERVE src0_sel:WORD_1
	v_exp_f16_sdwa v49, v45 dst_sel:WORD_1 dst_unused:UNUSED_PRESERVE src0_sel:WORD_1
	v_pk_add_f16 v42, v78, v118 neg_lo:[0,1] neg_hi:[0,1]
	v_pk_add_f16 v34, v34, v49
	v_pk_add_f16 v35, v35, v48
	v_pk_add_f16 v36, v36, v47
	v_pk_add_f16 v37, v37, v46
	v_pk_fma_f16 v22, v10, v46, v22
	v_pk_fma_f16 v23, v11, v47, v23
	v_pk_fma_f16 v24, v12, v48, v24
	v_pk_fma_f16 v25, v13, v49, v25
	v_pk_add_f16 v43, v79, v119 neg_lo:[0,1] neg_hi:[0,1]
	v_pk_add_f16 v44, v80, v120 neg_lo:[0,1] neg_hi:[0,1]
	v_pk_add_f16 v45, v81, v121 neg_lo:[0,1] neg_hi:[0,1]
	v_exp_f16_sdwa v46, v42 dst_sel:WORD_0 dst_unused:UNUSED_PAD src0_sel:WORD_0
	v_exp_f16_sdwa v47, v43 dst_sel:WORD_0 dst_unused:UNUSED_PAD src0_sel:WORD_0
	v_exp_f16_sdwa v48, v44 dst_sel:WORD_0 dst_unused:UNUSED_PAD src0_sel:WORD_0
	v_exp_f16_sdwa v49, v45 dst_sel:WORD_0 dst_unused:UNUSED_PAD src0_sel:WORD_0
	v_exp_f16_sdwa v46, v42 dst_sel:WORD_1 dst_unused:UNUSED_PRESERVE src0_sel:WORD_1
	v_exp_f16_sdwa v47, v43 dst_sel:WORD_1 dst_unused:UNUSED_PRESERVE src0_sel:WORD_1
	v_exp_f16_sdwa v48, v44 dst_sel:WORD_1 dst_unused:UNUSED_PRESERVE src0_sel:WORD_1
	v_exp_f16_sdwa v49, v45 dst_sel:WORD_1 dst_unused:UNUSED_PRESERVE src0_sel:WORD_1
	v_pk_add_f16 v42, v105, v118 neg_lo:[0,1] neg_hi:[0,1]
	v_pk_add_f16 v34, v34, v49
	v_pk_add_f16 v37, v37, v46
	v_pk_add_f16 v36, v36, v47
	v_pk_add_f16 v35, v35, v48
	v_pk_fma_f16 v25, v17, v49, v25
	v_pk_fma_f16 v24, v16, v48, v24
	v_pk_fma_f16 v23, v15, v47, v23
	v_pk_fma_f16 v22, v14, v46, v22
	v_pk_add_f16 v43, v104, v119 neg_lo:[0,1] neg_hi:[0,1]
	v_pk_add_f16 v44, v103, v120 neg_lo:[0,1] neg_hi:[0,1]
	v_pk_add_f16 v45, v102, v121 neg_lo:[0,1] neg_hi:[0,1]
	v_exp_f16_sdwa v46, v42 dst_sel:WORD_0 dst_unused:UNUSED_PAD src0_sel:WORD_0
	v_exp_f16_sdwa v47, v43 dst_sel:WORD_0 dst_unused:UNUSED_PAD src0_sel:WORD_0
	v_exp_f16_sdwa v48, v44 dst_sel:WORD_0 dst_unused:UNUSED_PAD src0_sel:WORD_0
	v_exp_f16_sdwa v49, v45 dst_sel:WORD_0 dst_unused:UNUSED_PAD src0_sel:WORD_0
	v_exp_f16_sdwa v46, v42 dst_sel:WORD_1 dst_unused:UNUSED_PRESERVE src0_sel:WORD_1
	v_exp_f16_sdwa v47, v43 dst_sel:WORD_1 dst_unused:UNUSED_PRESERVE src0_sel:WORD_1
	v_exp_f16_sdwa v48, v44 dst_sel:WORD_1 dst_unused:UNUSED_PRESERVE src0_sel:WORD_1
	v_exp_f16_sdwa v49, v45 dst_sel:WORD_1 dst_unused:UNUSED_PRESERVE src0_sel:WORD_1
	v_pk_add_f16 v42, v109, v118 neg_lo:[0,1] neg_hi:[0,1]
	v_pk_add_f16 v34, v34, v49
	v_pk_add_f16 v35, v35, v48
	v_pk_add_f16 v36, v36, v47
	v_pk_add_f16 v37, v37, v46
	v_pk_fma_f16 v22, v26, v46, v22
	v_pk_fma_f16 v23, v27, v47, v23
	v_pk_fma_f16 v24, v28, v48, v24
	v_pk_fma_f16 v25, v29, v49, v25
	v_pk_add_f16 v43, v108, v119 neg_lo:[0,1] neg_hi:[0,1]
	v_pk_add_f16 v44, v107, v120 neg_lo:[0,1] neg_hi:[0,1]
	v_pk_add_f16 v45, v106, v121 neg_lo:[0,1] neg_hi:[0,1]
	v_exp_f16_sdwa v46, v42 dst_sel:WORD_0 dst_unused:UNUSED_PAD src0_sel:WORD_0
	v_exp_f16_sdwa v47, v43 dst_sel:WORD_0 dst_unused:UNUSED_PAD src0_sel:WORD_0
	v_exp_f16_sdwa v48, v44 dst_sel:WORD_0 dst_unused:UNUSED_PAD src0_sel:WORD_0
	v_exp_f16_sdwa v49, v45 dst_sel:WORD_0 dst_unused:UNUSED_PAD src0_sel:WORD_0
	v_exp_f16_sdwa v46, v42 dst_sel:WORD_1 dst_unused:UNUSED_PRESERVE src0_sel:WORD_1
	v_exp_f16_sdwa v47, v43 dst_sel:WORD_1 dst_unused:UNUSED_PRESERVE src0_sel:WORD_1
	v_exp_f16_sdwa v48, v44 dst_sel:WORD_1 dst_unused:UNUSED_PRESERVE src0_sel:WORD_1
	v_exp_f16_sdwa v49, v45 dst_sel:WORD_1 dst_unused:UNUSED_PRESERVE src0_sel:WORD_1
	v_pk_add_f16 v42, v82, v118 neg_lo:[0,1] neg_hi:[0,1]
	v_pk_add_f16 v34, v34, v49
	v_pk_add_f16 v37, v37, v46
	v_pk_add_f16 v36, v36, v47
	v_pk_add_f16 v35, v35, v48
	v_pk_fma_f16 v25, v41, v49, v25
	v_pk_fma_f16 v24, v40, v48, v24
	v_pk_fma_f16 v23, v39, v47, v23
	v_pk_fma_f16 v22, v38, v46, v22
	v_pk_add_f16 v43, v83, v119 neg_lo:[0,1] neg_hi:[0,1]
	v_pk_add_f16 v44, v84, v120 neg_lo:[0,1] neg_hi:[0,1]
	v_pk_add_f16 v45, v85, v121 neg_lo:[0,1] neg_hi:[0,1]
	v_exp_f16_sdwa v46, v42 dst_sel:WORD_0 dst_unused:UNUSED_PAD src0_sel:WORD_0
	v_exp_f16_sdwa v47, v43 dst_sel:WORD_0 dst_unused:UNUSED_PAD src0_sel:WORD_0
	v_exp_f16_sdwa v48, v44 dst_sel:WORD_0 dst_unused:UNUSED_PAD src0_sel:WORD_0
	v_exp_f16_sdwa v49, v45 dst_sel:WORD_0 dst_unused:UNUSED_PAD src0_sel:WORD_0
	v_exp_f16_sdwa v46, v42 dst_sel:WORD_1 dst_unused:UNUSED_PRESERVE src0_sel:WORD_1
	v_exp_f16_sdwa v47, v43 dst_sel:WORD_1 dst_unused:UNUSED_PRESERVE src0_sel:WORD_1
	v_exp_f16_sdwa v48, v44 dst_sel:WORD_1 dst_unused:UNUSED_PRESERVE src0_sel:WORD_1
	v_exp_f16_sdwa v49, v45 dst_sel:WORD_1 dst_unused:UNUSED_PRESERVE src0_sel:WORD_1
	s_nop 0
	v_pk_add_f16 v34, v34, v49
	v_pk_add_f16 v35, v35, v48
	v_rcp_f16_e32 v44, v34
	v_rcp_f16_sdwa v34, v34 dst_sel:DWORD dst_unused:UNUSED_PAD src0_sel:WORD_1
	v_pk_add_f16 v36, v36, v47
	v_rcp_f16_e32 v45, v35
	v_rcp_f16_sdwa v35, v35 dst_sel:DWORD dst_unused:UNUSED_PAD src0_sel:WORD_1
	v_pk_add_f16 v37, v37, v46
	v_rcp_f16_e32 v43, v36
	v_rcp_f16_sdwa v36, v36 dst_sel:DWORD dst_unused:UNUSED_PAD src0_sel:WORD_1
	v_rcp_f16_e32 v42, v37
	v_rcp_f16_sdwa v37, v37 dst_sel:DWORD dst_unused:UNUSED_PAD src0_sel:WORD_1
	v_pk_fma_f16 v25, v61, v49, v25
	v_pack_b32_f16 v34, v44, v34
	v_pk_fma_f16 v24, v60, v48, v24
	v_pk_mul_f16 v25, v25, v34
	v_pack_b32_f16 v34, v45, v35
	v_pk_fma_f16 v23, v59, v47, v23
	v_pk_mul_f16 v24, v24, v34
	v_pack_b32_f16 v34, v43, v36
	v_pk_fma_f16 v22, v58, v46, v22
	v_pk_mul_f16 v23, v23, v34
	v_pack_b32_f16 v34, v42, v37
	v_pk_mul_f16 v22, v22, v34
	s_waitcnt vmcnt(0)
	v_pk_mul_f16 v34, v182, v146 op_sel_hi:[0,1]
	v_pk_mul_f16 v35, v182, v147 op_sel_hi:[0,1]
	v_pk_mul_f16 v36, v182, v148 op_sel_hi:[0,1]
	v_pk_mul_f16 v37, v182, v149 op_sel_hi:[0,1]
	v_pk_mul_f16 v42, v180, v146 op_sel_hi:[0,1]
	v_pk_mul_f16 v43, v180, v147 op_sel_hi:[0,1]
	v_pk_mul_f16 v44, v180, v148 op_sel_hi:[0,1]
	v_pk_mul_f16 v45, v180, v149 op_sel_hi:[0,1]
	v_pk_mul_f16 v46, v181, v146 op_sel_hi:[0,1]
	v_pk_mul_f16 v47, v181, v147 op_sel_hi:[0,1]
	v_pk_mul_f16 v48, v181, v148 op_sel_hi:[0,1]
	v_pk_mul_f16 v49, v181, v149 op_sel_hi:[0,1]
	v_pk_fma_f16 v21, v21, v149, v37
	v_pk_fma_f16 v20, v20, v148, v36
	v_pk_fma_f16 v19, v19, v147, v35
	v_pk_fma_f16 v18, v18, v146, v34
	v_pk_fma_f16 v33, v33, v149, v37
	v_pk_fma_f16 v32, v32, v148, v36
	v_pk_fma_f16 v31, v31, v147, v35
	v_pk_fma_f16 v30, v30, v146, v34
	v_pk_fma_f16 v37, v57, v149, v37
	v_pk_fma_f16 v36, v56, v148, v36
	v_pk_fma_f16 v35, v55, v147, v35
	v_pk_fma_f16 v34, v54, v146, v34
	v_pk_maximum3_f16 v79, v19, v31, v35
	v_pk_maximum3_f16 v80, v20, v32, v36
	v_pk_maximum3_f16 v81, v21, v33, v37
	v_pk_fma_f16 v50, v77, v149, v45
	v_pk_maximum3_f16 v78, v18, v30, v34
	v_pk_fma_f16 v51, v76, v148, v44
	v_pk_fma_f16 v52, v75, v147, v43
	v_pk_fma_f16 v53, v74, v146, v42
	v_pk_fma_f16 v54, v101, v149, v45
	v_pk_fma_f16 v55, v100, v148, v44
	v_pk_fma_f16 v56, v99, v147, v43
	v_pk_fma_f16 v57, v98, v146, v42
	v_pk_fma_f16 v45, v117, v149, v45
	v_pk_fma_f16 v44, v116, v148, v44
	v_pk_fma_f16 v43, v115, v147, v43
	v_pk_fma_f16 v42, v114, v146, v42
	v_pk_fma_f16 v66, v133, v149, v49
	v_pk_fma_f16 v67, v132, v148, v48
	v_pk_fma_f16 v68, v131, v147, v47
	v_pk_fma_f16 v69, v130, v146, v46
	v_pk_fma_f16 v74, v137, v149, v49
	v_pk_fma_f16 v75, v136, v148, v48
	v_pk_fma_f16 v76, v135, v147, v47
	v_pk_fma_f16 v77, v134, v146, v46
	v_pk_fma_f16 v49, v145, v149, v49
	v_pk_fma_f16 v48, v144, v148, v48
	v_pk_fma_f16 v47, v143, v147, v47
	v_pk_fma_f16 v46, v142, v146, v46
	v_pk_maximum3_f16 v82, v53, v57, v42
	v_pk_maximum3_f16 v83, v52, v56, v43
	v_pk_maximum3_f16 v84, v51, v55, v44
	v_pk_maximum3_f16 v85, v50, v54, v45
	v_pk_maximum3_f16 v87, v68, v76, v47
	v_pk_maximum3_f16 v86, v69, v77, v46
	v_pk_maximum3_f16 v88, v67, v75, v48
	v_pk_maximum3_f16 v89, v66, v74, v49
	v_pk_maximum3_f16 v78, v78, v82, v86
	v_pk_maximum3_f16 v79, v79, v83, v87
	v_pk_maximum3_f16 v80, v80, v84, v88
	v_pk_maximum3_f16 v81, v81, v85, v89
	s_nop 0
	v_pk_add_f16 v18, v18, v78 neg_lo:[0,1] neg_hi:[0,1]
	v_pk_add_f16 v19, v19, v79 neg_lo:[0,1] neg_hi:[0,1]
	v_pk_add_f16 v20, v20, v80 neg_lo:[0,1] neg_hi:[0,1]
	v_pk_add_f16 v21, v21, v81 neg_lo:[0,1] neg_hi:[0,1]
	v_pk_add_f16 v30, v30, v78 neg_lo:[0,1] neg_hi:[0,1]
	v_exp_f16_sdwa v82, v18 dst_sel:WORD_0 dst_unused:UNUSED_PAD src0_sel:WORD_0
	v_exp_f16_sdwa v83, v19 dst_sel:WORD_0 dst_unused:UNUSED_PAD src0_sel:WORD_0
	v_exp_f16_sdwa v84, v20 dst_sel:WORD_0 dst_unused:UNUSED_PAD src0_sel:WORD_0
	v_exp_f16_sdwa v85, v21 dst_sel:WORD_0 dst_unused:UNUSED_PAD src0_sel:WORD_0
	v_exp_f16_sdwa v82, v18 dst_sel:WORD_1 dst_unused:UNUSED_PRESERVE src0_sel:WORD_1
	v_exp_f16_sdwa v83, v19 dst_sel:WORD_1 dst_unused:UNUSED_PRESERVE src0_sel:WORD_1
	v_exp_f16_sdwa v84, v20 dst_sel:WORD_1 dst_unused:UNUSED_PRESERVE src0_sel:WORD_1
	v_exp_f16_sdwa v85, v21 dst_sel:WORD_1 dst_unused:UNUSED_PRESERVE src0_sel:WORD_1
	v_pk_add_f16 v31, v31, v79 neg_lo:[0,1] neg_hi:[0,1]
	v_pk_add_f16 v18, v82, 0
	v_pk_add_f16 v19, v83, 0
	v_pk_add_f16 v20, v84, 0
	v_pk_add_f16 v21, v85, 0
	v_pk_fma_f16 v6, v6, v82, 0
	v_pk_fma_f16 v7, v7, v83, 0
	v_pk_fma_f16 v8, v8, v84, 0
	v_pk_fma_f16 v9, v9, v85, 0
	v_pk_add_f16 v32, v32, v80 neg_lo:[0,1] neg_hi:[0,1]
	v_pk_add_f16 v33, v33, v81 neg_lo:[0,1] neg_hi:[0,1]
	v_exp_f16_sdwa v82, v30 dst_sel:WORD_0 dst_unused:UNUSED_PAD src0_sel:WORD_0
	v_exp_f16_sdwa v83, v31 dst_sel:WORD_0 dst_unused:UNUSED_PAD src0_sel:WORD_0
	v_exp_f16_sdwa v84, v32 dst_sel:WORD_0 dst_unused:UNUSED_PAD src0_sel:WORD_0
	v_exp_f16_sdwa v85, v33 dst_sel:WORD_0 dst_unused:UNUSED_PAD src0_sel:WORD_0
	v_exp_f16_sdwa v82, v30 dst_sel:WORD_1 dst_unused:UNUSED_PRESERVE src0_sel:WORD_1
	v_exp_f16_sdwa v83, v31 dst_sel:WORD_1 dst_unused:UNUSED_PRESERVE src0_sel:WORD_1
	v_exp_f16_sdwa v84, v32 dst_sel:WORD_1 dst_unused:UNUSED_PRESERVE src0_sel:WORD_1
	v_exp_f16_sdwa v85, v33 dst_sel:WORD_1 dst_unused:UNUSED_PRESERVE src0_sel:WORD_1
	s_nop 0
	v_pk_add_f16 v21, v21, v85
	v_pk_add_f16 v20, v20, v84
	v_pk_add_f16 v19, v19, v83
	v_pk_add_f16 v18, v18, v82
	v_pk_fma_f16 v9, v13, v85, v9
	v_pk_fma_f16 v8, v12, v84, v8
	v_pk_fma_f16 v7, v11, v83, v7
	v_pk_fma_f16 v6, v10, v82, v6
	v_pk_add_f16 v10, v34, v78 neg_lo:[0,1] neg_hi:[0,1]
	v_pk_add_f16 v11, v35, v79 neg_lo:[0,1] neg_hi:[0,1]
	v_pk_add_f16 v12, v36, v80 neg_lo:[0,1] neg_hi:[0,1]
	v_pk_add_f16 v13, v37, v81 neg_lo:[0,1] neg_hi:[0,1]
	v_exp_f16_sdwa v30, v10 dst_sel:WORD_0 dst_unused:UNUSED_PAD src0_sel:WORD_0
	v_exp_f16_sdwa v31, v11 dst_sel:WORD_0 dst_unused:UNUSED_PAD src0_sel:WORD_0
	v_exp_f16_sdwa v32, v12 dst_sel:WORD_0 dst_unused:UNUSED_PAD src0_sel:WORD_0
	v_exp_f16_sdwa v33, v13 dst_sel:WORD_0 dst_unused:UNUSED_PAD src0_sel:WORD_0
	v_exp_f16_sdwa v30, v10 dst_sel:WORD_1 dst_unused:UNUSED_PRESERVE src0_sel:WORD_1
	v_exp_f16_sdwa v31, v11 dst_sel:WORD_1 dst_unused:UNUSED_PRESERVE src0_sel:WORD_1
	v_exp_f16_sdwa v32, v12 dst_sel:WORD_1 dst_unused:UNUSED_PRESERVE src0_sel:WORD_1
	v_exp_f16_sdwa v33, v13 dst_sel:WORD_1 dst_unused:UNUSED_PRESERVE src0_sel:WORD_1
	v_pk_add_f16 v10, v18, v30
	v_pk_add_f16 v11, v19, v31
	v_pk_add_f16 v12, v20, v32
	v_pk_add_f16 v13, v21, v33
	v_pk_fma_f16 v6, v14, v30, v6
	v_pk_fma_f16 v7, v15, v31, v7
	v_pk_fma_f16 v8, v16, v32, v8
	v_pk_fma_f16 v9, v17, v33, v9
	v_pk_add_f16 v14, v53, v78 neg_lo:[0,1] neg_hi:[0,1]
	v_pk_add_f16 v15, v52, v79 neg_lo:[0,1] neg_hi:[0,1]
	v_pk_add_f16 v16, v51, v80 neg_lo:[0,1] neg_hi:[0,1]
	v_pk_add_f16 v17, v50, v81 neg_lo:[0,1] neg_hi:[0,1]
	v_exp_f16_sdwa v18, v14 dst_sel:WORD_0 dst_unused:UNUSED_PAD src0_sel:WORD_0
	v_exp_f16_sdwa v19, v15 dst_sel:WORD_0 dst_unused:UNUSED_PAD src0_sel:WORD_0
	v_exp_f16_sdwa v20, v16 dst_sel:WORD_0 dst_unused:UNUSED_PAD src0_sel:WORD_0
	v_exp_f16_sdwa v21, v17 dst_sel:WORD_0 dst_unused:UNUSED_PAD src0_sel:WORD_0
	v_exp_f16_sdwa v18, v14 dst_sel:WORD_1 dst_unused:UNUSED_PRESERVE src0_sel:WORD_1
	v_exp_f16_sdwa v19, v15 dst_sel:WORD_1 dst_unused:UNUSED_PRESERVE src0_sel:WORD_1
	v_exp_f16_sdwa v20, v16 dst_sel:WORD_1 dst_unused:UNUSED_PRESERVE src0_sel:WORD_1
	v_exp_f16_sdwa v21, v17 dst_sel:WORD_1 dst_unused:UNUSED_PRESERVE src0_sel:WORD_1
	v_pk_add_f16 v14, v57, v78 neg_lo:[0,1] neg_hi:[0,1]
	v_pk_add_f16 v13, v13, v21
	v_pk_add_f16 v12, v12, v20
	v_pk_add_f16 v11, v11, v19
	v_pk_add_f16 v10, v10, v18
	v_pk_fma_f16 v9, v29, v21, v9
	v_pk_fma_f16 v8, v28, v20, v8
	v_pk_fma_f16 v7, v27, v19, v7
	v_pk_fma_f16 v6, v26, v18, v6
	v_pk_add_f16 v15, v56, v79 neg_lo:[0,1] neg_hi:[0,1]
	v_pk_add_f16 v16, v55, v80 neg_lo:[0,1] neg_hi:[0,1]
	v_pk_add_f16 v17, v54, v81 neg_lo:[0,1] neg_hi:[0,1]
	v_exp_f16_sdwa v18, v14 dst_sel:WORD_0 dst_unused:UNUSED_PAD src0_sel:WORD_0
	v_exp_f16_sdwa v19, v15 dst_sel:WORD_0 dst_unused:UNUSED_PAD src0_sel:WORD_0
	v_exp_f16_sdwa v20, v16 dst_sel:WORD_0 dst_unused:UNUSED_PAD src0_sel:WORD_0
	v_exp_f16_sdwa v21, v17 dst_sel:WORD_0 dst_unused:UNUSED_PAD src0_sel:WORD_0
	v_exp_f16_sdwa v18, v14 dst_sel:WORD_1 dst_unused:UNUSED_PRESERVE src0_sel:WORD_1
	v_exp_f16_sdwa v19, v15 dst_sel:WORD_1 dst_unused:UNUSED_PRESERVE src0_sel:WORD_1
	v_exp_f16_sdwa v20, v16 dst_sel:WORD_1 dst_unused:UNUSED_PRESERVE src0_sel:WORD_1
	v_exp_f16_sdwa v21, v17 dst_sel:WORD_1 dst_unused:UNUSED_PRESERVE src0_sel:WORD_1
	v_pk_add_f16 v14, v42, v78 neg_lo:[0,1] neg_hi:[0,1]
	v_pk_add_f16 v10, v10, v18
	v_pk_add_f16 v11, v11, v19
	v_pk_add_f16 v12, v12, v20
	v_pk_add_f16 v13, v13, v21
	v_pk_fma_f16 v6, v38, v18, v6
	v_pk_fma_f16 v7, v39, v19, v7
	v_pk_fma_f16 v8, v40, v20, v8
	v_pk_fma_f16 v9, v41, v21, v9
	v_pk_add_f16 v15, v43, v79 neg_lo:[0,1] neg_hi:[0,1]
	v_pk_add_f16 v16, v44, v80 neg_lo:[0,1] neg_hi:[0,1]
	v_pk_add_f16 v17, v45, v81 neg_lo:[0,1] neg_hi:[0,1]
	v_exp_f16_sdwa v18, v14 dst_sel:WORD_0 dst_unused:UNUSED_PAD src0_sel:WORD_0
	v_exp_f16_sdwa v19, v15 dst_sel:WORD_0 dst_unused:UNUSED_PAD src0_sel:WORD_0
	v_exp_f16_sdwa v20, v16 dst_sel:WORD_0 dst_unused:UNUSED_PAD src0_sel:WORD_0
	v_exp_f16_sdwa v21, v17 dst_sel:WORD_0 dst_unused:UNUSED_PAD src0_sel:WORD_0
	v_exp_f16_sdwa v18, v14 dst_sel:WORD_1 dst_unused:UNUSED_PRESERVE src0_sel:WORD_1
	v_exp_f16_sdwa v19, v15 dst_sel:WORD_1 dst_unused:UNUSED_PRESERVE src0_sel:WORD_1
	v_exp_f16_sdwa v20, v16 dst_sel:WORD_1 dst_unused:UNUSED_PRESERVE src0_sel:WORD_1
	v_exp_f16_sdwa v21, v17 dst_sel:WORD_1 dst_unused:UNUSED_PRESERVE src0_sel:WORD_1
	v_pk_add_f16 v14, v69, v78 neg_lo:[0,1] neg_hi:[0,1]
	v_pk_add_f16 v13, v13, v21
	v_pk_add_f16 v12, v12, v20
	v_pk_add_f16 v11, v11, v19
	v_pk_add_f16 v10, v10, v18
	v_pk_fma_f16 v9, v61, v21, v9
	v_pk_fma_f16 v8, v60, v20, v8
	v_pk_fma_f16 v7, v59, v19, v7
	v_pk_fma_f16 v6, v58, v18, v6
	v_pk_add_f16 v15, v68, v79 neg_lo:[0,1] neg_hi:[0,1]
	v_pk_add_f16 v16, v67, v80 neg_lo:[0,1] neg_hi:[0,1]
	v_pk_add_f16 v17, v66, v81 neg_lo:[0,1] neg_hi:[0,1]
	v_exp_f16_sdwa v18, v14 dst_sel:WORD_0 dst_unused:UNUSED_PAD src0_sel:WORD_0
	v_exp_f16_sdwa v19, v15 dst_sel:WORD_0 dst_unused:UNUSED_PAD src0_sel:WORD_0
	v_exp_f16_sdwa v20, v16 dst_sel:WORD_0 dst_unused:UNUSED_PAD src0_sel:WORD_0
	v_exp_f16_sdwa v21, v17 dst_sel:WORD_0 dst_unused:UNUSED_PAD src0_sel:WORD_0
	v_exp_f16_sdwa v18, v14 dst_sel:WORD_1 dst_unused:UNUSED_PRESERVE src0_sel:WORD_1
	v_exp_f16_sdwa v19, v15 dst_sel:WORD_1 dst_unused:UNUSED_PRESERVE src0_sel:WORD_1
	v_exp_f16_sdwa v20, v16 dst_sel:WORD_1 dst_unused:UNUSED_PRESERVE src0_sel:WORD_1
	v_exp_f16_sdwa v21, v17 dst_sel:WORD_1 dst_unused:UNUSED_PRESERVE src0_sel:WORD_1
	v_pk_add_f16 v10, v10, v18
	v_pk_add_f16 v11, v11, v19
	v_pk_add_f16 v12, v12, v20
	v_pk_add_f16 v13, v13, v21
	v_pk_fma_f16 v14, v70, v18, v6
	v_pk_fma_f16 v15, v71, v19, v7
	v_pk_fma_f16 v16, v72, v20, v8
	v_pk_fma_f16 v17, v73, v21, v9
	v_pk_add_f16 v6, v77, v78 neg_lo:[0,1] neg_hi:[0,1]
	v_pk_add_f16 v7, v76, v79 neg_lo:[0,1] neg_hi:[0,1]
	v_pk_add_f16 v8, v75, v80 neg_lo:[0,1] neg_hi:[0,1]
	v_pk_add_f16 v9, v74, v81 neg_lo:[0,1] neg_hi:[0,1]
	v_exp_f16_sdwa v18, v6 dst_sel:WORD_0 dst_unused:UNUSED_PAD src0_sel:WORD_0
	v_exp_f16_sdwa v19, v7 dst_sel:WORD_0 dst_unused:UNUSED_PAD src0_sel:WORD_0
	v_exp_f16_sdwa v20, v8 dst_sel:WORD_0 dst_unused:UNUSED_PAD src0_sel:WORD_0
	v_exp_f16_sdwa v21, v9 dst_sel:WORD_0 dst_unused:UNUSED_PAD src0_sel:WORD_0
	v_exp_f16_sdwa v18, v6 dst_sel:WORD_1 dst_unused:UNUSED_PRESERVE src0_sel:WORD_1
	v_exp_f16_sdwa v19, v7 dst_sel:WORD_1 dst_unused:UNUSED_PRESERVE src0_sel:WORD_1
	v_exp_f16_sdwa v20, v8 dst_sel:WORD_1 dst_unused:UNUSED_PRESERVE src0_sel:WORD_1
	v_exp_f16_sdwa v21, v9 dst_sel:WORD_1 dst_unused:UNUSED_PRESERVE src0_sel:WORD_1
	s_nop 0
	v_pk_add_f16 v9, v13, v21
	v_pk_add_f16 v8, v12, v20
	v_pk_add_f16 v7, v11, v19
	v_pk_add_f16 v6, v10, v18
	v_pk_fma_f16 v13, v93, v21, v17
	v_pk_fma_f16 v12, v92, v20, v16
	v_pk_fma_f16 v11, v91, v19, v15
	v_pk_fma_f16 v10, v90, v18, v14
	v_pk_add_f16 v18, v46, v78 neg_lo:[0,1] neg_hi:[0,1]
	v_pk_add_f16 v19, v47, v79 neg_lo:[0,1] neg_hi:[0,1]
	v_pk_add_f16 v20, v48, v80 neg_lo:[0,1] neg_hi:[0,1]
	v_pk_add_f16 v21, v49, v81 neg_lo:[0,1] neg_hi:[0,1]
	v_exp_f16_sdwa v14, v18 dst_sel:WORD_0 dst_unused:UNUSED_PAD src0_sel:WORD_0
	v_exp_f16_sdwa v17, v19 dst_sel:WORD_0 dst_unused:UNUSED_PAD src0_sel:WORD_0
	v_exp_f16_sdwa v15, v20 dst_sel:WORD_0 dst_unused:UNUSED_PAD src0_sel:WORD_0
	v_exp_f16_sdwa v16, v21 dst_sel:WORD_0 dst_unused:UNUSED_PAD src0_sel:WORD_0
	v_exp_f16_sdwa v14, v18 dst_sel:WORD_1 dst_unused:UNUSED_PRESERVE src0_sel:WORD_1
	v_exp_f16_sdwa v17, v19 dst_sel:WORD_1 dst_unused:UNUSED_PRESERVE src0_sel:WORD_1
	v_exp_f16_sdwa v15, v20 dst_sel:WORD_1 dst_unused:UNUSED_PRESERVE src0_sel:WORD_1
	v_exp_f16_sdwa v16, v21 dst_sel:WORD_1 dst_unused:UNUSED_PRESERVE src0_sel:WORD_1
	s_nop 0

.Lmyf_B1_7:
	s_mov_b64 exec, -1
	s_waitcnt lgkmcnt(0)
	v_cvt_f16_f32_e32 v183, s27
	v_cvt_f16_f32_e32 v185, s26
	v_cvt_f16_f32_e32 v184, s34
	s_mov_b64 s[4:5], 0
	s_waitcnt vmcnt(3)
	s_cmp_lg_u32 s10, 1
	s_cbranch_scc1 .Lmysw3_0
	s_mul_i32 s84, s81, s83
	s_add_i32 s84, s84, s82
	s_mul_i32 s84, s84, 0x60000
	s_lshl_b32 s85, s92, 3
	s_add_u32 s85, s85, s94
	s_mul_i32 s85, s85, 3072
	s_add_u32 s84, s84, s85
	s_add_u32 s88, s86, s84
	s_addc_u32 s89, s87, 0
	s_load_dword s90, s[88:89], 0x0
	s_load_dword s90, s[88:89], 0x80
	s_load_dword s90, s[88:89], 0x100
	s_load_dword s90, s[88:89], 0x180
	s_load_dword s90, s[88:89], 0x200
	s_load_dword s90, s[88:89], 0x280
	s_load_dword s90, s[88:89], 0x300
	s_load_dword s90, s[88:89], 0x380
	s_load_dword s90, s[88:89], 0x400
	s_load_dword s90, s[88:89], 0x480
	s_load_dword s90, s[88:89], 0x500
	s_load_dword s90, s[88:89], 0x580
	s_load_dword s90, s[88:89], 0x600
	s_load_dword s90, s[88:89], 0x680
	s_load_dword s90, s[88:89], 0x700
	s_load_dword s90, s[88:89], 0x780
	s_load_dword s90, s[88:89], 0x800
	s_load_dword s90, s[88:89], 0x880
	s_load_dword s90, s[88:89], 0x900
	s_load_dword s90, s[88:89], 0x980
	s_load_dword s90, s[88:89], 0xa00
	s_load_dword s90, s[88:89], 0xa80
	s_load_dword s90, s[88:89], 0xb00
	s_load_dword s90, s[88:89], 0xb80
.Lmysw3_0:
	v_pk_mul_f16 v193, v185, v189 op_sel_hi:[0,1]
	v_pk_mul_f16 v197, v183, v189 op_sel_hi:[0,1]
	v_pk_mul_f16 v201, v184, v189 op_sel_hi:[0,1]
	v_pk_mul_f16 v190, v185, v186 op_sel_hi:[0,1]
	v_pk_mul_f16 v191, v185, v187 op_sel_hi:[0,1]
	v_pk_mul_f16 v192, v185, v188 op_sel_hi:[0,1]
	v_pk_mul_f16 v194, v183, v186 op_sel_hi:[0,1]
	s_mov_b64 exec, s[64:65]
	buffer_load_dwordx4 v[18:21], v249, s[16:19], 0 offen
	buffer_load_dwordx4 v[6:9], v249, s[16:19], 0 offen offset:512
	s_mov_b64 exec, -1
	v_pk_mul_f16 v195, v183, v187 op_sel_hi:[0,1]
	v_pk_mul_f16 v196, v183, v188 op_sel_hi:[0,1]
	v_pk_mul_f16 v198, v184, v186 op_sel_hi:[0,1]
	v_pk_mul_f16 v199, v184, v187 op_sel_hi:[0,1]
	v_pk_mul_f16 v200, v184, v188 op_sel_hi:[0,1]
	v_pk_fma_f16 v113, v113, v189, v193
	v_pk_fma_f16 v129, v129, v189, v197
	v_pk_fma_f16 v137, v137, v189, v201
	v_pk_fma_f16 v202, v85, v189, v193
	v_pk_fma_f16 v206, v109, v189, v197
	v_pk_fma_f16 v210, v125, v189, v201
	v_pk_fma_f16 v193, v53, v189, v193
	v_pk_fma_f16 v197, v69, v189, v197
	buffer_load_dwordx4 v[34:37], v250, s[16:19], 0 offen offset:512
	buffer_load_dwordx4 v[10:13], v250, s[16:19], 0 offen offset:1024
	v_pk_fma_f16 v189, v97, v189, v201
	v_pk_maximum3_f16 v201, v113, v129, v137
	v_pk_fma_f16 v112, v112, v188, v192
	v_pk_fma_f16 v111, v111, v187, v191
	v_pk_fma_f16 v110, v110, v186, v190
	v_pk_fma_f16 v128, v128, v188, v196
	v_pk_fma_f16 v127, v127, v187, v195
	v_pk_fma_f16 v126, v126, v186, v194
	v_pk_fma_f16 v136, v136, v188, v200
	v_pk_fma_f16 v135, v135, v187, v199
	v_pk_fma_f16 v134, v134, v186, v198
	v_pk_fma_f16 v203, v84, v188, v192
	v_pk_fma_f16 v204, v83, v187, v191
	v_pk_fma_f16 v205, v82, v186, v190
	v_pk_fma_f16 v207, v108, v188, v196
	v_pk_fma_f16 v208, v107, v187, v195
	s_mov_b64 exec, s[66:67]
	buffer_load_dwordx4 v[54:57], v250, s[16:19], 0 offen offset:2048
	buffer_load_dwordx4 v[14:17], v250, s[16:19], 0 offen offset:2560
	s_mov_b64 exec, -1
	v_pk_fma_f16 v209, v106, v186, v194
	v_pk_fma_f16 v211, v124, v188, v200
	v_pk_fma_f16 v212, v123, v187, v199
	v_pk_fma_f16 v213, v122, v186, v198
	v_pk_fma_f16 v192, v52, v188, v192
	v_pk_fma_f16 v191, v51, v187, v191
	v_pk_fma_f16 v190, v50, v186, v190
	v_pk_fma_f16 v196, v68, v188, v196
	v_pk_fma_f16 v195, v67, v187, v195
	v_pk_fma_f16 v194, v66, v186, v194
	v_pk_fma_f16 v188, v96, v188, v200
	v_pk_fma_f16 v187, v95, v187, v199
	v_pk_fma_f16 v186, v94, v186, v198
	v_pk_maximum3_f16 v198, v110, v126, v134
	v_pk_maximum3_f16 v199, v111, v127, v135
	v_pk_maximum3_f16 v200, v112, v128, v136
	v_pk_maximum3_f16 v217, v202, v206, v210
	v_pk_maximum3_f16 v221, v193, v197, v189
	v_pk_maximum3_f16 v214, v205, v209, v213
	v_pk_maximum3_f16 v215, v204, v208, v212
	v_pk_maximum3_f16 v216, v203, v207, v211
	v_pk_maximum3_f16 v218, v190, v194, v186
	v_pk_maximum3_f16 v219, v191, v195, v187
	v_pk_maximum3_f16 v201, v201, v217, v221
	v_pk_maximum3_f16 v220, v192, v196, v188
	v_pk_maximum3_f16 v198, v198, v214, v218
	v_pk_maximum3_f16 v199, v199, v215, v219
	v_pk_maximum3_f16 v200, v200, v216, v220
	v_pk_add_f16 v113, v113, v201 neg_lo:[0,1] neg_hi:[0,1]
	s_mov_b64 exec, s[64:65]
	buffer_load_dwordx4 v[74:77], v251, s[16:19], 0 offen
	buffer_load_dwordx4 v[26:29], v251, s[16:19], 0 offen offset:512
	s_mov_b64 exec, -1
	v_pk_add_f16 v110, v110, v198 neg_lo:[0,1] neg_hi:[0,1]
	v_pk_add_f16 v111, v111, v199 neg_lo:[0,1] neg_hi:[0,1]
	v_pk_add_f16 v112, v112, v200 neg_lo:[0,1] neg_hi:[0,1]
	v_pk_add_f16 v126, v126, v198 neg_lo:[0,1] neg_hi:[0,1]
	v_exp_f16_sdwa v214, v110 dst_sel:WORD_0 dst_unused:UNUSED_PAD src0_sel:WORD_0
	v_exp_f16_sdwa v215, v111 dst_sel:WORD_0 dst_unused:UNUSED_PAD src0_sel:WORD_0
	v_exp_f16_sdwa v216, v112 dst_sel:WORD_0 dst_unused:UNUSED_PAD src0_sel:WORD_0
	v_exp_f16_sdwa v217, v113 dst_sel:WORD_0 dst_unused:UNUSED_PAD src0_sel:WORD_0
	v_exp_f16_sdwa v214, v110 dst_sel:WORD_1 dst_unused:UNUSED_PRESERVE src0_sel:WORD_1
	v_exp_f16_sdwa v215, v111 dst_sel:WORD_1 dst_unused:UNUSED_PRESERVE src0_sel:WORD_1
	v_exp_f16_sdwa v216, v112 dst_sel:WORD_1 dst_unused:UNUSED_PRESERVE src0_sel:WORD_1
	v_exp_f16_sdwa v217, v113 dst_sel:WORD_1 dst_unused:UNUSED_PRESERVE src0_sel:WORD_1
	v_pk_add_f16 v127, v127, v199 neg_lo:[0,1] neg_hi:[0,1]
	v_pk_add_f16 v113, v214, 0
	v_pk_fma_f16 v73, v73, v217, 0
	v_pk_add_f16 v110, v217, 0
	v_pk_add_f16 v111, v216, 0
	v_pk_add_f16 v112, v215, 0
	v_pk_fma_f16 v72, v72, v216, 0
	v_pk_fma_f16 v71, v71, v215, 0
	v_pk_fma_f16 v70, v70, v214, 0
	v_pk_add_f16 v128, v128, v200 neg_lo:[0,1] neg_hi:[0,1]
	buffer_load_dwordx4 v[102:105], v252, s[16:19], 0 offen offset:512
	buffer_load_dwordx4 v[38:41], v252, s[16:19], 0 offen offset:1024
	v_pk_add_f16 v129, v129, v201 neg_lo:[0,1] neg_hi:[0,1]
	v_exp_f16_sdwa v214, v126 dst_sel:WORD_0 dst_unused:UNUSED_PAD src0_sel:WORD_0
	v_exp_f16_sdwa v215, v127 dst_sel:WORD_0 dst_unused:UNUSED_PAD src0_sel:WORD_0
	v_exp_f16_sdwa v216, v128 dst_sel:WORD_0 dst_unused:UNUSED_PAD src0_sel:WORD_0
	v_exp_f16_sdwa v217, v129 dst_sel:WORD_0 dst_unused:UNUSED_PAD src0_sel:WORD_0
	v_exp_f16_sdwa v214, v126 dst_sel:WORD_1 dst_unused:UNUSED_PRESERVE src0_sel:WORD_1
	v_exp_f16_sdwa v215, v127 dst_sel:WORD_1 dst_unused:UNUSED_PRESERVE src0_sel:WORD_1
	v_exp_f16_sdwa v216, v128 dst_sel:WORD_1 dst_unused:UNUSED_PRESERVE src0_sel:WORD_1
	v_exp_f16_sdwa v217, v129 dst_sel:WORD_1 dst_unused:UNUSED_PRESERVE src0_sel:WORD_1
	v_pk_add_f16 v113, v113, v214
	v_pk_fma_f16 v73, v101, v217, v73
	v_pk_add_f16 v101, v137, v201 neg_lo:[0,1] neg_hi:[0,1]
	v_pk_add_f16 v112, v112, v215
	v_pk_add_f16 v111, v111, v216
	v_pk_add_f16 v110, v110, v217
	v_pk_fma_f16 v70, v98, v214, v70
	v_pk_fma_f16 v71, v99, v215, v71
	v_pk_fma_f16 v72, v100, v216, v72
	v_pk_add_f16 v98, v134, v198 neg_lo:[0,1] neg_hi:[0,1]
	v_pk_add_f16 v99, v135, v199 neg_lo:[0,1] neg_hi:[0,1]
	v_pk_add_f16 v100, v136, v200 neg_lo:[0,1] neg_hi:[0,1]
	v_exp_f16_sdwa v126, v98 dst_sel:WORD_0 dst_unused:UNUSED_PAD src0_sel:WORD_0
	v_exp_f16_sdwa v127, v99 dst_sel:WORD_0 dst_unused:UNUSED_PAD src0_sel:WORD_0
	v_exp_f16_sdwa v128, v100 dst_sel:WORD_0 dst_unused:UNUSED_PAD src0_sel:WORD_0
	v_exp_f16_sdwa v129, v101 dst_sel:WORD_0 dst_unused:UNUSED_PAD src0_sel:WORD_0
	v_exp_f16_sdwa v126, v98 dst_sel:WORD_1 dst_unused:UNUSED_PRESERVE src0_sel:WORD_1
	v_exp_f16_sdwa v127, v99 dst_sel:WORD_1 dst_unused:UNUSED_PRESERVE src0_sel:WORD_1
	v_exp_f16_sdwa v128, v100 dst_sel:WORD_1 dst_unused:UNUSED_PRESERVE src0_sel:WORD_1
	v_exp_f16_sdwa v129, v101 dst_sel:WORD_1 dst_unused:UNUSED_PRESERVE src0_sel:WORD_1
	v_pk_add_f16 v101, v113, v126
	v_pk_add_f16 v98, v110, v129
	s_mov_b64 exec, s[66:67]
	buffer_load_dwordx4 v[118:121], v252, s[16:19], 0 offen offset:2048
	buffer_load_dwordx4 v[58:61], v252, s[16:19], 0 offen offset:2560
	s_mov_b64 exec, -1
	v_pk_add_f16 v99, v111, v128
	v_pk_add_f16 v100, v112, v127
	v_pk_fma_f16 v73, v117, v129, v73
	v_pk_fma_f16 v72, v116, v128, v72
	v_pk_fma_f16 v71, v115, v127, v71
	v_pk_fma_f16 v70, v114, v126, v70
	v_pk_add_f16 v110, v205, v198 neg_lo:[0,1] neg_hi:[0,1]
	v_pk_add_f16 v111, v204, v199 neg_lo:[0,1] neg_hi:[0,1]
	v_pk_add_f16 v112, v203, v200 neg_lo:[0,1] neg_hi:[0,1]
	v_pk_add_f16 v113, v202, v201 neg_lo:[0,1] neg_hi:[0,1]
	v_exp_f16_sdwa v114, v110 dst_sel:WORD_0 dst_unused:UNUSED_PAD src0_sel:WORD_0
	v_exp_f16_sdwa v115, v111 dst_sel:WORD_0 dst_unused:UNUSED_PAD src0_sel:WORD_0
	v_exp_f16_sdwa v116, v112 dst_sel:WORD_0 dst_unused:UNUSED_PAD src0_sel:WORD_0
	v_exp_f16_sdwa v117, v113 dst_sel:WORD_0 dst_unused:UNUSED_PAD src0_sel:WORD_0
	v_exp_f16_sdwa v114, v110 dst_sel:WORD_1 dst_unused:UNUSED_PRESERVE src0_sel:WORD_1
	v_exp_f16_sdwa v115, v111 dst_sel:WORD_1 dst_unused:UNUSED_PRESERVE src0_sel:WORD_1
	v_exp_f16_sdwa v116, v112 dst_sel:WORD_1 dst_unused:UNUSED_PRESERVE src0_sel:WORD_1
	v_exp_f16_sdwa v117, v113 dst_sel:WORD_1 dst_unused:UNUSED_PRESERVE src0_sel:WORD_1
	v_pk_add_f16 v110, v209, v198 neg_lo:[0,1] neg_hi:[0,1]
	v_pk_add_f16 v101, v101, v114
	v_pk_add_f16 v100, v100, v115
	v_pk_add_f16 v99, v99, v116
	s_mov_b64 exec, s[76:77]
	buffer_load_dwordx4 v[130:133], v253, s[16:19], 0 offen
	buffer_load_dwordx4 v[78:81], v253, s[16:19], 0 offen offset:512
	s_mov_b64 exec, -1
	v_pk_add_f16 v98, v98, v117
	v_pk_fma_f16 v70, v42, v114, v70
	v_pk_fma_f16 v71, v43, v115, v71
	v_pk_fma_f16 v72, v44, v116, v72
	v_pk_fma_f16 v73, v45, v117, v73
	v_pk_add_f16 v111, v208, v199 neg_lo:[0,1] neg_hi:[0,1]
	v_pk_add_f16 v112, v207, v200 neg_lo:[0,1] neg_hi:[0,1]
	v_pk_add_f16 v113, v206, v201 neg_lo:[0,1] neg_hi:[0,1]
	v_exp_f16_sdwa v114, v110 dst_sel:WORD_0 dst_unused:UNUSED_PAD src0_sel:WORD_0
	v_exp_f16_sdwa v115, v111 dst_sel:WORD_0 dst_unused:UNUSED_PAD src0_sel:WORD_0
	v_exp_f16_sdwa v116, v112 dst_sel:WORD_0 dst_unused:UNUSED_PAD src0_sel:WORD_0
	v_exp_f16_sdwa v117, v113 dst_sel:WORD_0 dst_unused:UNUSED_PAD src0_sel:WORD_0
	v_exp_f16_sdwa v114, v110 dst_sel:WORD_1 dst_unused:UNUSED_PRESERVE src0_sel:WORD_1
	v_exp_f16_sdwa v115, v111 dst_sel:WORD_1 dst_unused:UNUSED_PRESERVE src0_sel:WORD_1
	v_exp_f16_sdwa v116, v112 dst_sel:WORD_1 dst_unused:UNUSED_PRESERVE src0_sel:WORD_1
	v_exp_f16_sdwa v117, v113 dst_sel:WORD_1 dst_unused:UNUSED_PRESERVE src0_sel:WORD_1
	v_pk_add_f16 v110, v213, v198 neg_lo:[0,1] neg_hi:[0,1]
	v_pk_add_f16 v101, v101, v114
	v_pk_add_f16 v98, v98, v117
	v_pk_add_f16 v99, v99, v116
	v_pk_add_f16 v100, v100, v115
	v_pk_fma_f16 v73, v65, v117, v73
	v_pk_fma_f16 v72, v64, v116, v72
	s_mov_b64 exec, s[70:71]
	buffer_load_dwordx4 v[138:141], v254, s[16:19], 0 offen offset:512
	buffer_load_dwordx4 v[90:93], v254, s[16:19], 0 offen offset:1024
	s_mov_b64 exec, -1
	v_pk_fma_f16 v71, v63, v115, v71
	v_pk_fma_f16 v70, v62, v114, v70
	v_pk_add_f16 v111, v212, v199 neg_lo:[0,1] neg_hi:[0,1]
	v_pk_add_f16 v112, v211, v200 neg_lo:[0,1] neg_hi:[0,1]
	v_pk_add_f16 v113, v210, v201 neg_lo:[0,1] neg_hi:[0,1]
	v_exp_f16_sdwa v114, v110 dst_sel:WORD_0 dst_unused:UNUSED_PAD src0_sel:WORD_0
	v_exp_f16_sdwa v115, v111 dst_sel:WORD_0 dst_unused:UNUSED_PAD src0_sel:WORD_0
	v_exp_f16_sdwa v116, v112 dst_sel:WORD_0 dst_unused:UNUSED_PAD src0_sel:WORD_0
	v_exp_f16_sdwa v117, v113 dst_sel:WORD_0 dst_unused:UNUSED_PAD src0_sel:WORD_0
	v_exp_f16_sdwa v114, v110 dst_sel:WORD_1 dst_unused:UNUSED_PRESERVE src0_sel:WORD_1
	v_exp_f16_sdwa v115, v111 dst_sel:WORD_1 dst_unused:UNUSED_PRESERVE src0_sel:WORD_1
	v_exp_f16_sdwa v116, v112 dst_sel:WORD_1 dst_unused:UNUSED_PRESERVE src0_sel:WORD_1
	v_exp_f16_sdwa v117, v113 dst_sel:WORD_1 dst_unused:UNUSED_PRESERVE src0_sel:WORD_1
	v_pk_add_f16 v110, v190, v198 neg_lo:[0,1] neg_hi:[0,1]
	v_pk_add_f16 v101, v101, v114
	v_pk_add_f16 v100, v100, v115
	v_pk_add_f16 v99, v99, v116
	v_pk_add_f16 v98, v98, v117
	v_pk_fma_f16 v70, v86, v114, v70
	v_pk_fma_f16 v71, v87, v115, v71
	v_pk_fma_f16 v72, v88, v116, v72
	v_pk_fma_f16 v73, v89, v117, v73
	s_mov_b64 exec, s[78:79]
	buffer_load_dwordx4 v[142:145], v254, s[16:19], 0 offen offset:2048
	buffer_load_dwordx4 v[2:5], v254, s[16:19], 0 offen offset:2560
	s_mov_b64 exec, -1
	v_pk_add_f16 v111, v191, v199 neg_lo:[0,1] neg_hi:[0,1]
	v_pk_add_f16 v112, v192, v200 neg_lo:[0,1] neg_hi:[0,1]
	v_pk_add_f16 v113, v193, v201 neg_lo:[0,1] neg_hi:[0,1]
	v_exp_f16_sdwa v114, v110 dst_sel:WORD_0 dst_unused:UNUSED_PAD src0_sel:WORD_0
	v_exp_f16_sdwa v115, v111 dst_sel:WORD_0 dst_unused:UNUSED_PAD src0_sel:WORD_0
	v_exp_f16_sdwa v116, v112 dst_sel:WORD_0 dst_unused:UNUSED_PAD src0_sel:WORD_0
	v_exp_f16_sdwa v117, v113 dst_sel:WORD_0 dst_unused:UNUSED_PAD src0_sel:WORD_0
	v_exp_f16_sdwa v114, v110 dst_sel:WORD_1 dst_unused:UNUSED_PRESERVE src0_sel:WORD_1
	v_exp_f16_sdwa v115, v111 dst_sel:WORD_1 dst_unused:UNUSED_PRESERVE src0_sel:WORD_1
	v_exp_f16_sdwa v116, v112 dst_sel:WORD_1 dst_unused:UNUSED_PRESERVE src0_sel:WORD_1
	v_exp_f16_sdwa v117, v113 dst_sel:WORD_1 dst_unused:UNUSED_PRESERVE src0_sel:WORD_1
	v_pk_add_f16 v110, v194, v198 neg_lo:[0,1] neg_hi:[0,1]
	v_pk_add_f16 v101, v101, v114
	v_pk_add_f16 v98, v98, v117
	v_pk_add_f16 v99, v99, v116
	v_pk_add_f16 v100, v100, v115
	v_pk_fma_f16 v73, v25, v117, v73
	v_pk_fma_f16 v72, v24, v116, v72
	v_pk_fma_f16 v71, v23, v115, v71
	v_pk_fma_f16 v70, v22, v114, v70
	v_pk_add_f16 v111, v195, v199 neg_lo:[0,1] neg_hi:[0,1]
	v_pk_add_f16 v112, v196, v200 neg_lo:[0,1] neg_hi:[0,1]
	v_pk_add_f16 v113, v197, v201 neg_lo:[0,1] neg_hi:[0,1]
	v_exp_f16_sdwa v114, v110 dst_sel:WORD_0 dst_unused:UNUSED_PAD src0_sel:WORD_0
	v_exp_f16_sdwa v115, v111 dst_sel:WORD_0 dst_unused:UNUSED_PAD src0_sel:WORD_0
	v_exp_f16_sdwa v116, v112 dst_sel:WORD_0 dst_unused:UNUSED_PAD src0_sel:WORD_0
	v_exp_f16_sdwa v117, v113 dst_sel:WORD_0 dst_unused:UNUSED_PAD src0_sel:WORD_0
	v_exp_f16_sdwa v114, v110 dst_sel:WORD_1 dst_unused:UNUSED_PRESERVE src0_sel:WORD_1
	v_exp_f16_sdwa v115, v111 dst_sel:WORD_1 dst_unused:UNUSED_PRESERVE src0_sel:WORD_1
	v_exp_f16_sdwa v116, v112 dst_sel:WORD_1 dst_unused:UNUSED_PRESERVE src0_sel:WORD_1
	v_exp_f16_sdwa v117, v113 dst_sel:WORD_1 dst_unused:UNUSED_PRESERVE src0_sel:WORD_1
	v_pk_add_f16 v110, v186, v198 neg_lo:[0,1] neg_hi:[0,1]
	v_pk_add_f16 v101, v101, v114
	v_pk_add_f16 v100, v100, v115
	v_pk_add_f16 v99, v99, v116
	v_pk_add_f16 v98, v98, v117
	v_pk_fma_f16 v70, v30, v114, v70
	v_pk_fma_f16 v71, v31, v115, v71
	v_pk_fma_f16 v72, v32, v116, v72
	v_pk_fma_f16 v73, v33, v117, v73
	v_pk_add_f16 v111, v187, v199 neg_lo:[0,1] neg_hi:[0,1]
	v_pk_add_f16 v112, v188, v200 neg_lo:[0,1] neg_hi:[0,1]
	v_pk_add_f16 v113, v189, v201 neg_lo:[0,1] neg_hi:[0,1]
	v_exp_f16_sdwa v114, v110 dst_sel:WORD_0 dst_unused:UNUSED_PAD src0_sel:WORD_0
	v_exp_f16_sdwa v115, v111 dst_sel:WORD_0 dst_unused:UNUSED_PAD src0_sel:WORD_0
	v_exp_f16_sdwa v116, v112 dst_sel:WORD_0 dst_unused:UNUSED_PAD src0_sel:WORD_0
	v_exp_f16_sdwa v117, v113 dst_sel:WORD_0 dst_unused:UNUSED_PAD src0_sel:WORD_0
	v_exp_f16_sdwa v114, v110 dst_sel:WORD_1 dst_unused:UNUSED_PRESERVE src0_sel:WORD_1
	v_exp_f16_sdwa v115, v111 dst_sel:WORD_1 dst_unused:UNUSED_PRESERVE src0_sel:WORD_1
	v_exp_f16_sdwa v116, v112 dst_sel:WORD_1 dst_unused:UNUSED_PRESERVE src0_sel:WORD_1
	v_exp_f16_sdwa v117, v113 dst_sel:WORD_1 dst_unused:UNUSED_PRESERVE src0_sel:WORD_1
	v_pk_add_f16 v101, v101, v114
	v_pk_add_f16 v100, v100, v115
	v_rcp_f16_e32 v110, v101
	v_rcp_f16_sdwa v101, v101 dst_sel:DWORD dst_unused:UNUSED_PAD src0_sel:WORD_1
	v_pk_add_f16 v99, v99, v116
	v_rcp_f16_e32 v111, v100
	v_rcp_f16_sdwa v100, v100 dst_sel:DWORD dst_unused:UNUSED_PAD src0_sel:WORD_1
	v_pk_add_f16 v98, v98, v117
	v_rcp_f16_e32 v112, v99
	v_rcp_f16_sdwa v99, v99 dst_sel:DWORD dst_unused:UNUSED_PAD src0_sel:WORD_1
	v_rcp_f16_e32 v113, v98
	v_rcp_f16_sdwa v98, v98 dst_sel:DWORD dst_unused:UNUSED_PAD src0_sel:WORD_1
	v_pk_fma_f16 v70, v46, v114, v70
	v_pack_b32_f16 v101, v110, v101
	v_pk_fma_f16 v71, v47, v115, v71
	v_pk_mul_f16 v110, v70, v101
	v_pack_b32_f16 v70, v111, v100
	v_pk_fma_f16 v72, v48, v116, v72
	v_pk_mul_f16 v111, v71, v70
	v_pack_b32_f16 v70, v112, v99
	v_pk_fma_f16 v73, v49, v117, v73
	v_pk_mul_f16 v112, v72, v70
	v_pack_b32_f16 v70, v113, v98
	v_pk_mul_f16 v113, v73, v70
	s_waitcnt vmcnt(12)
	v_pk_mul_f16 v73, v185, v157 op_sel_hi:[0,1]
	v_pk_mul_f16 v101, v183, v157 op_sel_hi:[0,1]
	v_pk_mul_f16 v117, v184, v157 op_sel_hi:[0,1]
	v_pk_mul_f16 v70, v185, v154 op_sel_hi:[0,1]
	v_pk_mul_f16 v71, v185, v155 op_sel_hi:[0,1]
	v_pk_mul_f16 v72, v185, v156 op_sel_hi:[0,1]
	v_pk_mul_f16 v98, v183, v154 op_sel_hi:[0,1]
	v_pk_mul_f16 v99, v183, v155 op_sel_hi:[0,1]
	v_pk_mul_f16 v100, v183, v156 op_sel_hi:[0,1]
	v_pk_mul_f16 v114, v184, v154 op_sel_hi:[0,1]
	v_pk_mul_f16 v115, v184, v155 op_sel_hi:[0,1]
	v_pk_mul_f16 v116, v184, v156 op_sel_hi:[0,1]
	v_pk_fma_f16 v85, v85, v157, v73
	v_pk_fma_f16 v109, v109, v157, v101
	v_pk_fma_f16 v125, v125, v157, v117
	v_pk_fma_f16 v126, v53, v157, v73
	v_pk_fma_f16 v134, v69, v157, v101
	v_pk_fma_f16 v186, v97, v157, v117
	v_pk_fma_f16 v73, v21, v157, v73
	v_pk_fma_f16 v101, v37, v157, v101
	v_pk_fma_f16 v117, v57, v157, v117
	v_pk_maximum3_f16 v157, v85, v109, v125
	v_pk_fma_f16 v84, v84, v156, v72
	v_pk_fma_f16 v83, v83, v155, v71
	v_pk_fma_f16 v82, v82, v154, v70
	v_pk_fma_f16 v108, v108, v156, v100
	v_pk_fma_f16 v107, v107, v155, v99
	v_pk_fma_f16 v106, v106, v154, v98
	v_pk_fma_f16 v124, v124, v156, v116
	v_pk_fma_f16 v123, v123, v155, v115
	v_pk_fma_f16 v122, v122, v154, v114
	v_pk_fma_f16 v127, v52, v156, v72
	v_pk_fma_f16 v128, v51, v155, v71
	v_pk_fma_f16 v129, v50, v154, v70
	v_pk_fma_f16 v135, v68, v156, v100
	v_pk_fma_f16 v136, v67, v155, v99
	v_pk_fma_f16 v137, v66, v154, v98
	v_pk_fma_f16 v187, v96, v156, v116
	v_pk_fma_f16 v188, v95, v155, v115
	v_pk_fma_f16 v189, v94, v154, v114
	v_pk_fma_f16 v72, v20, v156, v72
	v_pk_fma_f16 v71, v19, v155, v71
	v_pk_fma_f16 v70, v18, v154, v70
	v_pk_fma_f16 v100, v36, v156, v100
	v_pk_fma_f16 v99, v35, v155, v99
	v_pk_fma_f16 v98, v34, v154, v98
	v_pk_fma_f16 v116, v56, v156, v116
	v_pk_fma_f16 v115, v55, v155, v115
	v_pk_fma_f16 v114, v54, v154, v114
	v_pk_maximum3_f16 v154, v82, v106, v122
	v_pk_maximum3_f16 v155, v83, v107, v123
	v_pk_maximum3_f16 v156, v84, v108, v124
	v_pk_maximum3_f16 v193, v126, v134, v186
	v_pk_maximum3_f16 v197, v73, v101, v117
	v_pk_maximum3_f16 v190, v129, v137, v189
	v_pk_maximum3_f16 v191, v128, v136, v188
	v_pk_maximum3_f16 v192, v127, v135, v187
	v_pk_maximum3_f16 v194, v70, v98, v114
	v_pk_maximum3_f16 v195, v71, v99, v115
	v_pk_maximum3_f16 v157, v157, v193, v197
	v_pk_maximum3_f16 v196, v72, v100, v116
	v_pk_maximum3_f16 v154, v154, v190, v194
	v_pk_maximum3_f16 v155, v155, v191, v195
	v_pk_maximum3_f16 v156, v156, v192, v196
	v_pk_add_f16 v85, v85, v157 neg_lo:[0,1] neg_hi:[0,1]
	v_pk_add_f16 v82, v82, v154 neg_lo:[0,1] neg_hi:[0,1]
	v_pk_add_f16 v83, v83, v155 neg_lo:[0,1] neg_hi:[0,1]
	v_pk_add_f16 v84, v84, v156 neg_lo:[0,1] neg_hi:[0,1]
	v_pk_add_f16 v106, v106, v154 neg_lo:[0,1] neg_hi:[0,1]
	v_exp_f16_sdwa v190, v82 dst_sel:WORD_0 dst_unused:UNUSED_PAD src0_sel:WORD_0
	v_exp_f16_sdwa v191, v83 dst_sel:WORD_0 dst_unused:UNUSED_PAD src0_sel:WORD_0
	v_exp_f16_sdwa v192, v84 dst_sel:WORD_0 dst_unused:UNUSED_PAD src0_sel:WORD_0
	v_exp_f16_sdwa v193, v85 dst_sel:WORD_0 dst_unused:UNUSED_PAD src0_sel:WORD_0
	v_exp_f16_sdwa v190, v82 dst_sel:WORD_1 dst_unused:UNUSED_PRESERVE src0_sel:WORD_1
	v_exp_f16_sdwa v191, v83 dst_sel:WORD_1 dst_unused:UNUSED_PRESERVE src0_sel:WORD_1
	v_exp_f16_sdwa v192, v84 dst_sel:WORD_1 dst_unused:UNUSED_PRESERVE src0_sel:WORD_1
	v_exp_f16_sdwa v193, v85 dst_sel:WORD_1 dst_unused:UNUSED_PRESERVE src0_sel:WORD_1
	v_pk_add_f16 v107, v107, v155 neg_lo:[0,1] neg_hi:[0,1]
	v_pk_add_f16 v85, v190, 0
	v_pk_fma_f16 v45, v45, v193, 0
	v_pk_add_f16 v82, v193, 0
	v_pk_add_f16 v83, v192, 0
	v_pk_add_f16 v84, v191, 0
	v_pk_fma_f16 v44, v44, v192, 0
	v_pk_fma_f16 v43, v43, v191, 0
	v_pk_fma_f16 v42, v42, v190, 0
	v_pk_add_f16 v108, v108, v156 neg_lo:[0,1] neg_hi:[0,1]
	v_pk_add_f16 v109, v109, v157 neg_lo:[0,1] neg_hi:[0,1]
	v_pk_add_f16 v70, v70, v154 neg_lo:[0,1] neg_hi:[0,1]
	v_exp_f16_sdwa v190, v106 dst_sel:WORD_0 dst_unused:UNUSED_PAD src0_sel:WORD_0
	v_exp_f16_sdwa v191, v107 dst_sel:WORD_0 dst_unused:UNUSED_PAD src0_sel:WORD_0
	v_exp_f16_sdwa v192, v108 dst_sel:WORD_0 dst_unused:UNUSED_PAD src0_sel:WORD_0
	v_exp_f16_sdwa v193, v109 dst_sel:WORD_0 dst_unused:UNUSED_PAD src0_sel:WORD_0
	v_exp_f16_sdwa v190, v106 dst_sel:WORD_1 dst_unused:UNUSED_PRESERVE src0_sel:WORD_1
	v_exp_f16_sdwa v191, v107 dst_sel:WORD_1 dst_unused:UNUSED_PRESERVE src0_sel:WORD_1
	v_exp_f16_sdwa v192, v108 dst_sel:WORD_1 dst_unused:UNUSED_PRESERVE src0_sel:WORD_1
	v_exp_f16_sdwa v193, v109 dst_sel:WORD_1 dst_unused:UNUSED_PRESERVE src0_sel:WORD_1
	v_pk_add_f16 v71, v71, v155 neg_lo:[0,1] neg_hi:[0,1]
	v_pk_add_f16 v85, v85, v190
	v_pk_fma_f16 v45, v65, v193, v45
	v_pk_add_f16 v65, v125, v157 neg_lo:[0,1] neg_hi:[0,1]
	v_pk_add_f16 v84, v84, v191
	v_pk_add_f16 v83, v83, v192
	v_pk_add_f16 v82, v82, v193
	v_pk_fma_f16 v42, v62, v190, v42
	v_pk_fma_f16 v43, v63, v191, v43
	v_pk_fma_f16 v44, v64, v192, v44
	v_pk_add_f16 v62, v122, v154 neg_lo:[0,1] neg_hi:[0,1]
	v_pk_add_f16 v63, v123, v155 neg_lo:[0,1] neg_hi:[0,1]
	v_pk_add_f16 v64, v124, v156 neg_lo:[0,1] neg_hi:[0,1]
	v_pk_add_f16 v72, v72, v156 neg_lo:[0,1] neg_hi:[0,1]
	v_exp_f16_sdwa v106, v62 dst_sel:WORD_0 dst_unused:UNUSED_PAD src0_sel:WORD_0
	v_exp_f16_sdwa v107, v63 dst_sel:WORD_0 dst_unused:UNUSED_PAD src0_sel:WORD_0
	v_exp_f16_sdwa v108, v64 dst_sel:WORD_0 dst_unused:UNUSED_PAD src0_sel:WORD_0
	v_exp_f16_sdwa v109, v65 dst_sel:WORD_0 dst_unused:UNUSED_PAD src0_sel:WORD_0
	v_exp_f16_sdwa v106, v62 dst_sel:WORD_1 dst_unused:UNUSED_PRESERVE src0_sel:WORD_1
	v_exp_f16_sdwa v107, v63 dst_sel:WORD_1 dst_unused:UNUSED_PRESERVE src0_sel:WORD_1
	v_exp_f16_sdwa v108, v64 dst_sel:WORD_1 dst_unused:UNUSED_PRESERVE src0_sel:WORD_1
	v_exp_f16_sdwa v109, v65 dst_sel:WORD_1 dst_unused:UNUSED_PRESERVE src0_sel:WORD_1
	v_pk_add_f16 v73, v73, v157 neg_lo:[0,1] neg_hi:[0,1]
	v_pk_add_f16 v65, v85, v106
	v_pk_add_f16 v62, v82, v109
	v_pk_add_f16 v63, v83, v108
	v_pk_add_f16 v64, v84, v107
	v_pk_fma_f16 v45, v89, v109, v45
	v_pk_fma_f16 v44, v88, v108, v44
	v_pk_fma_f16 v43, v87, v107, v43
	v_pk_fma_f16 v42, v86, v106, v42
	v_pk_add_f16 v82, v129, v154 neg_lo:[0,1] neg_hi:[0,1]
	v_pk_add_f16 v83, v128, v155 neg_lo:[0,1] neg_hi:[0,1]
	v_pk_add_f16 v84, v127, v156 neg_lo:[0,1] neg_hi:[0,1]
	v_pk_add_f16 v85, v126, v157 neg_lo:[0,1] neg_hi:[0,1]
	v_exp_f16_sdwa v86, v82 dst_sel:WORD_0 dst_unused:UNUSED_PAD src0_sel:WORD_0
	v_exp_f16_sdwa v87, v83 dst_sel:WORD_0 dst_unused:UNUSED_PAD src0_sel:WORD_0
	v_exp_f16_sdwa v88, v84 dst_sel:WORD_0 dst_unused:UNUSED_PAD src0_sel:WORD_0
	v_exp_f16_sdwa v89, v85 dst_sel:WORD_0 dst_unused:UNUSED_PAD src0_sel:WORD_0
	v_exp_f16_sdwa v86, v82 dst_sel:WORD_1 dst_unused:UNUSED_PRESERVE src0_sel:WORD_1
	v_exp_f16_sdwa v87, v83 dst_sel:WORD_1 dst_unused:UNUSED_PRESERVE src0_sel:WORD_1
	v_exp_f16_sdwa v88, v84 dst_sel:WORD_1 dst_unused:UNUSED_PRESERVE src0_sel:WORD_1
	v_exp_f16_sdwa v89, v85 dst_sel:WORD_1 dst_unused:UNUSED_PRESERVE src0_sel:WORD_1
	v_pk_add_f16 v82, v137, v154 neg_lo:[0,1] neg_hi:[0,1]
	v_pk_add_f16 v65, v65, v86
	v_pk_add_f16 v64, v64, v87
	v_pk_add_f16 v63, v63, v88
	v_pk_add_f16 v62, v62, v89
	v_pk_fma_f16 v42, v22, v86, v42
	v_pk_fma_f16 v43, v23, v87, v43
	v_pk_fma_f16 v44, v24, v88, v44
	v_pk_fma_f16 v45, v25, v89, v45
	v_pk_add_f16 v83, v136, v155 neg_lo:[0,1] neg_hi:[0,1]
	v_pk_add_f16 v84, v135, v156 neg_lo:[0,1] neg_hi:[0,1]
	v_pk_add_f16 v85, v134, v157 neg_lo:[0,1] neg_hi:[0,1]
	v_exp_f16_sdwa v86, v82 dst_sel:WORD_0 dst_unused:UNUSED_PAD src0_sel:WORD_0
	v_exp_f16_sdwa v87, v83 dst_sel:WORD_0 dst_unused:UNUSED_PAD src0_sel:WORD_0
	v_exp_f16_sdwa v88, v84 dst_sel:WORD_0 dst_unused:UNUSED_PAD src0_sel:WORD_0
	v_exp_f16_sdwa v89, v85 dst_sel:WORD_0 dst_unused:UNUSED_PAD src0_sel:WORD_0
	v_exp_f16_sdwa v86, v82 dst_sel:WORD_1 dst_unused:UNUSED_PRESERVE src0_sel:WORD_1
	v_exp_f16_sdwa v87, v83 dst_sel:WORD_1 dst_unused:UNUSED_PRESERVE src0_sel:WORD_1
	v_exp_f16_sdwa v88, v84 dst_sel:WORD_1 dst_unused:UNUSED_PRESERVE src0_sel:WORD_1
	v_exp_f16_sdwa v89, v85 dst_sel:WORD_1 dst_unused:UNUSED_PRESERVE src0_sel:WORD_1
	v_pk_add_f16 v82, v189, v154 neg_lo:[0,1] neg_hi:[0,1]
	v_pk_add_f16 v65, v65, v86
	v_pk_add_f16 v62, v62, v89
	v_pk_add_f16 v63, v63, v88
	v_pk_add_f16 v64, v64, v87
	v_pk_fma_f16 v45, v33, v89, v45
	v_pk_fma_f16 v44, v32, v88, v44
	v_pk_fma_f16 v43, v31, v87, v43
	v_pk_fma_f16 v42, v30, v86, v42
	v_pk_add_f16 v83, v188, v155 neg_lo:[0,1] neg_hi:[0,1]
	v_pk_add_f16 v84, v187, v156 neg_lo:[0,1] neg_hi:[0,1]
	v_pk_add_f16 v85, v186, v157 neg_lo:[0,1] neg_hi:[0,1]
	v_exp_f16_sdwa v86, v82 dst_sel:WORD_0 dst_unused:UNUSED_PAD src0_sel:WORD_0
	v_exp_f16_sdwa v87, v83 dst_sel:WORD_0 dst_unused:UNUSED_PAD src0_sel:WORD_0
	v_exp_f16_sdwa v88, v84 dst_sel:WORD_0 dst_unused:UNUSED_PAD src0_sel:WORD_0
	v_exp_f16_sdwa v89, v85 dst_sel:WORD_0 dst_unused:UNUSED_PAD src0_sel:WORD_0
	v_exp_f16_sdwa v86, v82 dst_sel:WORD_1 dst_unused:UNUSED_PRESERVE src0_sel:WORD_1
	v_exp_f16_sdwa v87, v83 dst_sel:WORD_1 dst_unused:UNUSED_PRESERVE src0_sel:WORD_1
	v_exp_f16_sdwa v88, v84 dst_sel:WORD_1 dst_unused:UNUSED_PRESERVE src0_sel:WORD_1
	v_exp_f16_sdwa v89, v85 dst_sel:WORD_1 dst_unused:UNUSED_PRESERVE src0_sel:WORD_1
	v_exp_f16_sdwa v82, v70 dst_sel:WORD_0 dst_unused:UNUSED_PAD src0_sel:WORD_0
	v_exp_f16_sdwa v83, v71 dst_sel:WORD_0 dst_unused:UNUSED_PAD src0_sel:WORD_0
	v_exp_f16_sdwa v84, v72 dst_sel:WORD_0 dst_unused:UNUSED_PAD src0_sel:WORD_0
	v_exp_f16_sdwa v85, v73 dst_sel:WORD_0 dst_unused:UNUSED_PAD src0_sel:WORD_0
	v_exp_f16_sdwa v82, v70 dst_sel:WORD_1 dst_unused:UNUSED_PRESERVE src0_sel:WORD_1
	v_exp_f16_sdwa v83, v71 dst_sel:WORD_1 dst_unused:UNUSED_PRESERVE src0_sel:WORD_1
	v_exp_f16_sdwa v84, v72 dst_sel:WORD_1 dst_unused:UNUSED_PRESERVE src0_sel:WORD_1
	v_exp_f16_sdwa v85, v73 dst_sel:WORD_1 dst_unused:UNUSED_PRESERVE src0_sel:WORD_1
	v_pk_add_f16 v70, v98, v154 neg_lo:[0,1] neg_hi:[0,1]
	v_pk_add_f16 v65, v65, v86
	v_pk_add_f16 v64, v64, v87
	v_pk_add_f16 v63, v63, v88
	v_pk_add_f16 v62, v62, v89
	v_pk_fma_f16 v42, v46, v86, v42
	v_pk_fma_f16 v43, v47, v87, v43
	v_pk_fma_f16 v44, v48, v88, v44
	v_pk_fma_f16 v45, v49, v89, v45
	v_pk_add_f16 v65, v65, v82
	v_pk_add_f16 v62, v62, v85
	v_pk_add_f16 v63, v63, v84
	v_pk_add_f16 v64, v64, v83
	v_pk_fma_f16 v45, v9, v85, v45
	v_pk_fma_f16 v44, v8, v84, v44
	v_pk_fma_f16 v43, v7, v83, v43
	v_pk_fma_f16 v42, v6, v82, v42
	v_pk_add_f16 v71, v99, v155 neg_lo:[0,1] neg_hi:[0,1]
	v_pk_add_f16 v72, v100, v156 neg_lo:[0,1] neg_hi:[0,1]
	v_pk_add_f16 v73, v101, v157 neg_lo:[0,1] neg_hi:[0,1]
	v_exp_f16_sdwa v82, v70 dst_sel:WORD_0 dst_unused:UNUSED_PAD src0_sel:WORD_0
	v_exp_f16_sdwa v83, v71 dst_sel:WORD_0 dst_unused:UNUSED_PAD src0_sel:WORD_0
	v_exp_f16_sdwa v84, v72 dst_sel:WORD_0 dst_unused:UNUSED_PAD src0_sel:WORD_0
	v_exp_f16_sdwa v85, v73 dst_sel:WORD_0 dst_unused:UNUSED_PAD src0_sel:WORD_0
	v_exp_f16_sdwa v82, v70 dst_sel:WORD_1 dst_unused:UNUSED_PRESERVE src0_sel:WORD_1
	v_exp_f16_sdwa v83, v71 dst_sel:WORD_1 dst_unused:UNUSED_PRESERVE src0_sel:WORD_1
	v_exp_f16_sdwa v84, v72 dst_sel:WORD_1 dst_unused:UNUSED_PRESERVE src0_sel:WORD_1
	v_exp_f16_sdwa v85, v73 dst_sel:WORD_1 dst_unused:UNUSED_PRESERVE src0_sel:WORD_1
	v_pk_add_f16 v70, v114, v154 neg_lo:[0,1] neg_hi:[0,1]
	v_pk_add_f16 v65, v65, v82
	v_pk_add_f16 v64, v64, v83
	v_pk_add_f16 v63, v63, v84
	v_pk_add_f16 v62, v62, v85
	v_pk_fma_f16 v42, v10, v82, v42
	v_pk_fma_f16 v43, v11, v83, v43
	v_pk_fma_f16 v44, v12, v84, v44
	v_pk_fma_f16 v45, v13, v85, v45
	v_pk_add_f16 v71, v115, v155 neg_lo:[0,1] neg_hi:[0,1]
	v_pk_add_f16 v72, v116, v156 neg_lo:[0,1] neg_hi:[0,1]
	v_pk_add_f16 v73, v117, v157 neg_lo:[0,1] neg_hi:[0,1]
	v_exp_f16_sdwa v82, v70 dst_sel:WORD_0 dst_unused:UNUSED_PAD src0_sel:WORD_0
	v_exp_f16_sdwa v83, v71 dst_sel:WORD_0 dst_unused:UNUSED_PAD src0_sel:WORD_0
	v_exp_f16_sdwa v84, v72 dst_sel:WORD_0 dst_unused:UNUSED_PAD src0_sel:WORD_0
	v_exp_f16_sdwa v85, v73 dst_sel:WORD_0 dst_unused:UNUSED_PAD src0_sel:WORD_0
	v_exp_f16_sdwa v82, v70 dst_sel:WORD_1 dst_unused:UNUSED_PRESERVE src0_sel:WORD_1
	v_exp_f16_sdwa v83, v71 dst_sel:WORD_1 dst_unused:UNUSED_PRESERVE src0_sel:WORD_1
	v_exp_f16_sdwa v84, v72 dst_sel:WORD_1 dst_unused:UNUSED_PRESERVE src0_sel:WORD_1
	v_exp_f16_sdwa v85, v73 dst_sel:WORD_1 dst_unused:UNUSED_PRESERVE src0_sel:WORD_1
	v_pk_add_f16 v65, v65, v82
	v_pk_add_f16 v64, v64, v83
	v_rcp_f16_e32 v70, v65
	v_rcp_f16_sdwa v65, v65 dst_sel:DWORD dst_unused:UNUSED_PAD src0_sel:WORD_1
	v_pk_add_f16 v63, v63, v84
	v_rcp_f16_e32 v71, v64
	v_rcp_f16_sdwa v64, v64 dst_sel:DWORD dst_unused:UNUSED_PAD src0_sel:WORD_1
	v_pk_add_f16 v62, v62, v85
	v_rcp_f16_e32 v72, v63
	v_rcp_f16_sdwa v73, v63 dst_sel:DWORD dst_unused:UNUSED_PAD src0_sel:WORD_1
	v_pk_fma_f16 v43, v15, v83, v43
	v_pk_fma_f16 v42, v14, v82, v42
	v_rcp_f16_e32 v82, v62
	v_rcp_f16_sdwa v83, v62 dst_sel:DWORD dst_unused:UNUSED_PAD src0_sel:WORD_1
	v_pack_b32_f16 v62, v70, v65
	v_pk_mul_f16 v62, v42, v62
	v_pack_b32_f16 v42, v71, v64
	v_pk_fma_f16 v44, v16, v84, v44
	v_pk_mul_f16 v63, v43, v42
	v_pack_b32_f16 v42, v72, v73
	v_pk_fma_f16 v45, v17, v85, v45
	v_pk_mul_f16 v64, v44, v42
	v_pack_b32_f16 v42, v82, v83
	v_pk_mul_f16 v65, v45, v42
	s_waitcnt vmcnt(6)
	v_pk_mul_f16 v42, v185, v150 op_sel_hi:[0,1]
	v_pk_mul_f16 v70, v183, v150 op_sel_hi:[0,1]
	v_pk_mul_f16 v82, v184, v150 op_sel_hi:[0,1]
	v_pk_mul_f16 v43, v185, v151 op_sel_hi:[0,1]
	v_pk_mul_f16 v44, v185, v152 op_sel_hi:[0,1]
	v_pk_mul_f16 v45, v185, v153 op_sel_hi:[0,1]
	v_pk_mul_f16 v71, v183, v151 op_sel_hi:[0,1]
	v_pk_mul_f16 v72, v183, v152 op_sel_hi:[0,1]
	v_pk_mul_f16 v73, v183, v153 op_sel_hi:[0,1]
	v_pk_mul_f16 v83, v184, v151 op_sel_hi:[0,1]
	v_pk_mul_f16 v84, v184, v152 op_sel_hi:[0,1]
	v_pk_mul_f16 v85, v184, v153 op_sel_hi:[0,1]
	v_pk_fma_f16 v50, v50, v150, v42
	v_pk_fma_f16 v66, v66, v150, v70
	v_pk_fma_f16 v89, v94, v150, v82
	v_pk_fma_f16 v53, v53, v153, v45
	v_pk_maximum3_f16 v114, v50, v66, v89
	v_pk_fma_f16 v52, v52, v152, v44
	v_pk_fma_f16 v51, v51, v151, v43
	v_pk_fma_f16 v69, v69, v153, v73
	v_pk_fma_f16 v68, v68, v152, v72
	v_pk_fma_f16 v67, v67, v151, v71
	v_pk_fma_f16 v86, v97, v153, v85
	v_pk_fma_f16 v87, v96, v152, v84
	v_pk_fma_f16 v88, v95, v151, v83
	v_pk_fma_f16 v97, v18, v150, v42
	v_pk_fma_f16 v101, v34, v150, v70
	v_pk_fma_f16 v109, v54, v150, v82
	v_pk_fma_f16 v42, v74, v150, v42
	v_pk_fma_f16 v70, v102, v150, v70
	v_pk_fma_f16 v82, v118, v150, v82
	v_pk_maximum3_f16 v115, v51, v67, v88
	v_pk_maximum3_f16 v116, v52, v68, v87
	v_pk_maximum3_f16 v117, v53, v69, v86
	v_pk_maximum3_f16 v122, v97, v101, v109
	v_pk_fma_f16 v94, v21, v153, v45
	v_pk_maximum3_f16 v126, v42, v70, v82
	v_pk_fma_f16 v95, v20, v152, v44
	v_pk_maximum3_f16 v114, v114, v122, v126
	v_pk_fma_f16 v96, v19, v151, v43
	v_pk_fma_f16 v98, v37, v153, v73
	v_pk_fma_f16 v99, v36, v152, v72
	v_pk_fma_f16 v100, v35, v151, v71
	v_pk_fma_f16 v106, v57, v153, v85
	v_pk_fma_f16 v107, v56, v152, v84
	v_pk_fma_f16 v108, v55, v151, v83
	v_pk_fma_f16 v45, v77, v153, v45
	v_pk_fma_f16 v44, v76, v152, v44
	v_pk_fma_f16 v43, v75, v151, v43
	v_pk_fma_f16 v73, v105, v153, v73
	v_pk_fma_f16 v72, v104, v152, v72
	v_pk_fma_f16 v71, v103, v151, v71
	v_pk_fma_f16 v85, v121, v153, v85
	v_pk_fma_f16 v84, v120, v152, v84
	v_pk_fma_f16 v83, v119, v151, v83
	v_pk_maximum3_f16 v123, v96, v100, v108
	v_pk_maximum3_f16 v124, v95, v99, v107
	v_pk_maximum3_f16 v125, v94, v98, v106
	v_pk_maximum3_f16 v128, v44, v72, v84
	v_pk_maximum3_f16 v129, v45, v73, v85
	v_pk_maximum3_f16 v127, v43, v71, v83
	v_pk_maximum3_f16 v115, v115, v123, v127
	v_pk_maximum3_f16 v116, v116, v124, v128
	v_pk_maximum3_f16 v117, v117, v125, v129
	v_pk_add_f16 v50, v50, v114 neg_lo:[0,1] neg_hi:[0,1]
	v_pk_add_f16 v51, v51, v115 neg_lo:[0,1] neg_hi:[0,1]
	v_pk_add_f16 v52, v52, v116 neg_lo:[0,1] neg_hi:[0,1]
	v_pk_add_f16 v53, v53, v117 neg_lo:[0,1] neg_hi:[0,1]
	v_pk_add_f16 v66, v66, v114 neg_lo:[0,1] neg_hi:[0,1]
	v_exp_f16_sdwa v122, v50 dst_sel:WORD_0 dst_unused:UNUSED_PAD src0_sel:WORD_0
	v_exp_f16_sdwa v123, v51 dst_sel:WORD_0 dst_unused:UNUSED_PAD src0_sel:WORD_0
	v_exp_f16_sdwa v124, v52 dst_sel:WORD_0 dst_unused:UNUSED_PAD src0_sel:WORD_0
	v_exp_f16_sdwa v125, v53 dst_sel:WORD_0 dst_unused:UNUSED_PAD src0_sel:WORD_0
	v_exp_f16_sdwa v122, v50 dst_sel:WORD_1 dst_unused:UNUSED_PRESERVE src0_sel:WORD_1
	v_exp_f16_sdwa v123, v51 dst_sel:WORD_1 dst_unused:UNUSED_PRESERVE src0_sel:WORD_1
	v_exp_f16_sdwa v124, v52 dst_sel:WORD_1 dst_unused:UNUSED_PRESERVE src0_sel:WORD_1
	v_exp_f16_sdwa v125, v53 dst_sel:WORD_1 dst_unused:UNUSED_PRESERVE src0_sel:WORD_1
	v_pk_add_f16 v67, v67, v115 neg_lo:[0,1] neg_hi:[0,1]
	v_pk_add_f16 v50, v125, 0
	v_pk_fma_f16 v22, v22, v122, 0
	v_pk_add_f16 v51, v124, 0
	v_pk_add_f16 v52, v123, 0
	v_pk_add_f16 v53, v122, 0
	v_pk_fma_f16 v23, v23, v123, 0
	v_pk_fma_f16 v24, v24, v124, 0
	v_pk_fma_f16 v25, v25, v125, 0
	v_pk_add_f16 v68, v68, v116 neg_lo:[0,1] neg_hi:[0,1]
	v_pk_add_f16 v69, v69, v117 neg_lo:[0,1] neg_hi:[0,1]
	v_pk_add_f16 v42, v42, v114 neg_lo:[0,1] neg_hi:[0,1]
	v_exp_f16_sdwa v122, v66 dst_sel:WORD_0 dst_unused:UNUSED_PAD src0_sel:WORD_0
	v_exp_f16_sdwa v123, v67 dst_sel:WORD_0 dst_unused:UNUSED_PAD src0_sel:WORD_0
	v_exp_f16_sdwa v124, v68 dst_sel:WORD_0 dst_unused:UNUSED_PAD src0_sel:WORD_0
	v_exp_f16_sdwa v125, v69 dst_sel:WORD_0 dst_unused:UNUSED_PAD src0_sel:WORD_0
	v_exp_f16_sdwa v122, v66 dst_sel:WORD_1 dst_unused:UNUSED_PRESERVE src0_sel:WORD_1
	v_exp_f16_sdwa v123, v67 dst_sel:WORD_1 dst_unused:UNUSED_PRESERVE src0_sel:WORD_1
	v_exp_f16_sdwa v124, v68 dst_sel:WORD_1 dst_unused:UNUSED_PRESERVE src0_sel:WORD_1
	v_exp_f16_sdwa v125, v69 dst_sel:WORD_1 dst_unused:UNUSED_PRESERVE src0_sel:WORD_1
	v_pk_add_f16 v43, v43, v115 neg_lo:[0,1] neg_hi:[0,1]
	v_pk_add_f16 v50, v50, v125
	v_pk_fma_f16 v22, v30, v122, v22
	v_pk_add_f16 v30, v89, v114 neg_lo:[0,1] neg_hi:[0,1]
	v_pk_add_f16 v53, v53, v122
	v_pk_add_f16 v52, v52, v123
	v_pk_add_f16 v51, v51, v124
	v_pk_fma_f16 v25, v33, v125, v25
	v_pk_fma_f16 v24, v32, v124, v24
	v_pk_fma_f16 v23, v31, v123, v23
	v_pk_add_f16 v31, v88, v115 neg_lo:[0,1] neg_hi:[0,1]
	v_pk_add_f16 v32, v87, v116 neg_lo:[0,1] neg_hi:[0,1]
	v_pk_add_f16 v33, v86, v117 neg_lo:[0,1] neg_hi:[0,1]
	v_pk_add_f16 v44, v44, v116 neg_lo:[0,1] neg_hi:[0,1]
	v_exp_f16_sdwa v66, v30 dst_sel:WORD_0 dst_unused:UNUSED_PAD src0_sel:WORD_0
	v_exp_f16_sdwa v67, v31 dst_sel:WORD_0 dst_unused:UNUSED_PAD src0_sel:WORD_0
	v_exp_f16_sdwa v68, v32 dst_sel:WORD_0 dst_unused:UNUSED_PAD src0_sel:WORD_0
	v_exp_f16_sdwa v69, v33 dst_sel:WORD_0 dst_unused:UNUSED_PAD src0_sel:WORD_0
	v_exp_f16_sdwa v66, v30 dst_sel:WORD_1 dst_unused:UNUSED_PRESERVE src0_sel:WORD_1
	v_exp_f16_sdwa v67, v31 dst_sel:WORD_1 dst_unused:UNUSED_PRESERVE src0_sel:WORD_1
	v_exp_f16_sdwa v68, v32 dst_sel:WORD_1 dst_unused:UNUSED_PRESERVE src0_sel:WORD_1
	v_exp_f16_sdwa v69, v33 dst_sel:WORD_1 dst_unused:UNUSED_PRESERVE src0_sel:WORD_1
	v_pk_add_f16 v45, v45, v117 neg_lo:[0,1] neg_hi:[0,1]
	v_pk_add_f16 v30, v50, v69
	v_pk_add_f16 v31, v51, v68
	v_pk_add_f16 v32, v52, v67
	v_pk_add_f16 v33, v53, v66
	v_pk_fma_f16 v22, v46, v66, v22
	v_pk_fma_f16 v23, v47, v67, v23
	v_pk_fma_f16 v24, v48, v68, v24
	v_pk_fma_f16 v25, v49, v69, v25
	v_pk_add_f16 v46, v97, v114 neg_lo:[0,1] neg_hi:[0,1]
	v_pk_add_f16 v47, v96, v115 neg_lo:[0,1] neg_hi:[0,1]
	v_pk_add_f16 v48, v95, v116 neg_lo:[0,1] neg_hi:[0,1]
	v_pk_add_f16 v49, v94, v117 neg_lo:[0,1] neg_hi:[0,1]
	v_exp_f16_sdwa v50, v46 dst_sel:WORD_0 dst_unused:UNUSED_PAD src0_sel:WORD_0
	v_exp_f16_sdwa v51, v47 dst_sel:WORD_0 dst_unused:UNUSED_PAD src0_sel:WORD_0
	v_exp_f16_sdwa v52, v48 dst_sel:WORD_0 dst_unused:UNUSED_PAD src0_sel:WORD_0
	v_exp_f16_sdwa v53, v49 dst_sel:WORD_0 dst_unused:UNUSED_PAD src0_sel:WORD_0
	v_exp_f16_sdwa v50, v46 dst_sel:WORD_1 dst_unused:UNUSED_PRESERVE src0_sel:WORD_1
	v_exp_f16_sdwa v51, v47 dst_sel:WORD_1 dst_unused:UNUSED_PRESERVE src0_sel:WORD_1
	v_exp_f16_sdwa v52, v48 dst_sel:WORD_1 dst_unused:UNUSED_PRESERVE src0_sel:WORD_1
	v_exp_f16_sdwa v53, v49 dst_sel:WORD_1 dst_unused:UNUSED_PRESERVE src0_sel:WORD_1
	v_pk_add_f16 v46, v101, v114 neg_lo:[0,1] neg_hi:[0,1]
	v_pk_add_f16 v30, v30, v53
	v_pk_add_f16 v33, v33, v50
	v_pk_add_f16 v32, v32, v51
	v_pk_add_f16 v31, v31, v52
	v_pk_fma_f16 v25, v9, v53, v25
	v_pk_fma_f16 v24, v8, v52, v24
	v_pk_fma_f16 v23, v7, v51, v23
	v_pk_fma_f16 v22, v6, v50, v22
	v_pk_add_f16 v47, v100, v115 neg_lo:[0,1] neg_hi:[0,1]
	v_pk_add_f16 v48, v99, v116 neg_lo:[0,1] neg_hi:[0,1]
	v_pk_add_f16 v49, v98, v117 neg_lo:[0,1] neg_hi:[0,1]
	v_exp_f16_sdwa v50, v46 dst_sel:WORD_0 dst_unused:UNUSED_PAD src0_sel:WORD_0
	v_exp_f16_sdwa v51, v47 dst_sel:WORD_0 dst_unused:UNUSED_PAD src0_sel:WORD_0
	v_exp_f16_sdwa v52, v48 dst_sel:WORD_0 dst_unused:UNUSED_PAD src0_sel:WORD_0
	v_exp_f16_sdwa v53, v49 dst_sel:WORD_0 dst_unused:UNUSED_PAD src0_sel:WORD_0
	v_exp_f16_sdwa v50, v46 dst_sel:WORD_1 dst_unused:UNUSED_PRESERVE src0_sel:WORD_1
	v_exp_f16_sdwa v51, v47 dst_sel:WORD_1 dst_unused:UNUSED_PRESERVE src0_sel:WORD_1
	v_exp_f16_sdwa v52, v48 dst_sel:WORD_1 dst_unused:UNUSED_PRESERVE src0_sel:WORD_1
	v_exp_f16_sdwa v53, v49 dst_sel:WORD_1 dst_unused:UNUSED_PRESERVE src0_sel:WORD_1
	v_pk_add_f16 v46, v109, v114 neg_lo:[0,1] neg_hi:[0,1]
	v_pk_add_f16 v30, v30, v53
	v_pk_add_f16 v31, v31, v52
	v_pk_add_f16 v32, v32, v51
	v_pk_add_f16 v33, v33, v50
	v_pk_fma_f16 v22, v10, v50, v22
	v_pk_fma_f16 v23, v11, v51, v23
	v_pk_fma_f16 v24, v12, v52, v24
	v_pk_fma_f16 v25, v13, v53, v25
	v_pk_add_f16 v47, v108, v115 neg_lo:[0,1] neg_hi:[0,1]
	v_pk_add_f16 v48, v107, v116 neg_lo:[0,1] neg_hi:[0,1]
	v_pk_add_f16 v49, v106, v117 neg_lo:[0,1] neg_hi:[0,1]
	v_exp_f16_sdwa v50, v46 dst_sel:WORD_0 dst_unused:UNUSED_PAD src0_sel:WORD_0
	v_exp_f16_sdwa v51, v47 dst_sel:WORD_0 dst_unused:UNUSED_PAD src0_sel:WORD_0
	v_exp_f16_sdwa v52, v48 dst_sel:WORD_0 dst_unused:UNUSED_PAD src0_sel:WORD_0
	v_exp_f16_sdwa v53, v49 dst_sel:WORD_0 dst_unused:UNUSED_PAD src0_sel:WORD_0
	v_exp_f16_sdwa v50, v46 dst_sel:WORD_1 dst_unused:UNUSED_PRESERVE src0_sel:WORD_1
	v_exp_f16_sdwa v51, v47 dst_sel:WORD_1 dst_unused:UNUSED_PRESERVE src0_sel:WORD_1
	v_exp_f16_sdwa v52, v48 dst_sel:WORD_1 dst_unused:UNUSED_PRESERVE src0_sel:WORD_1
	v_exp_f16_sdwa v53, v49 dst_sel:WORD_1 dst_unused:UNUSED_PRESERVE src0_sel:WORD_1
	v_exp_f16_sdwa v46, v42 dst_sel:WORD_0 dst_unused:UNUSED_PAD src0_sel:WORD_0
	v_exp_f16_sdwa v47, v43 dst_sel:WORD_0 dst_unused:UNUSED_PAD src0_sel:WORD_0
	v_exp_f16_sdwa v48, v44 dst_sel:WORD_0 dst_unused:UNUSED_PAD src0_sel:WORD_0
	v_exp_f16_sdwa v49, v45 dst_sel:WORD_0 dst_unused:UNUSED_PAD src0_sel:WORD_0
	v_exp_f16_sdwa v46, v42 dst_sel:WORD_1 dst_unused:UNUSED_PRESERVE src0_sel:WORD_1
	v_exp_f16_sdwa v47, v43 dst_sel:WORD_1 dst_unused:UNUSED_PRESERVE src0_sel:WORD_1
	v_exp_f16_sdwa v48, v44 dst_sel:WORD_1 dst_unused:UNUSED_PRESERVE src0_sel:WORD_1
	v_exp_f16_sdwa v49, v45 dst_sel:WORD_1 dst_unused:UNUSED_PRESERVE src0_sel:WORD_1
	v_pk_add_f16 v42, v70, v114 neg_lo:[0,1] neg_hi:[0,1]
	v_pk_add_f16 v30, v30, v53
	v_pk_add_f16 v33, v33, v50
	v_pk_add_f16 v32, v32, v51
	v_pk_add_f16 v31, v31, v52
	v_pk_fma_f16 v25, v17, v53, v25
	v_pk_fma_f16 v24, v16, v52, v24
	v_pk_fma_f16 v23, v15, v51, v23
	v_pk_fma_f16 v22, v14, v50, v22
	v_pk_add_f16 v30, v30, v49
	v_pk_add_f16 v31, v31, v48
	v_pk_add_f16 v32, v32, v47
	v_pk_add_f16 v33, v33, v46
	v_pk_fma_f16 v22, v26, v46, v22
	v_pk_fma_f16 v23, v27, v47, v23
	v_pk_fma_f16 v24, v28, v48, v24
	v_pk_fma_f16 v25, v29, v49, v25
	v_pk_add_f16 v43, v71, v115 neg_lo:[0,1] neg_hi:[0,1]
	v_pk_add_f16 v44, v72, v116 neg_lo:[0,1] neg_hi:[0,1]
	v_pk_add_f16 v45, v73, v117 neg_lo:[0,1] neg_hi:[0,1]
	v_exp_f16_sdwa v46, v42 dst_sel:WORD_0 dst_unused:UNUSED_PAD src0_sel:WORD_0
	v_exp_f16_sdwa v47, v43 dst_sel:WORD_0 dst_unused:UNUSED_PAD src0_sel:WORD_0
	v_exp_f16_sdwa v48, v44 dst_sel:WORD_0 dst_unused:UNUSED_PAD src0_sel:WORD_0
	v_exp_f16_sdwa v49, v45 dst_sel:WORD_0 dst_unused:UNUSED_PAD src0_sel:WORD_0
	v_exp_f16_sdwa v46, v42 dst_sel:WORD_1 dst_unused:UNUSED_PRESERVE src0_sel:WORD_1
	v_exp_f16_sdwa v47, v43 dst_sel:WORD_1 dst_unused:UNUSED_PRESERVE src0_sel:WORD_1
	v_exp_f16_sdwa v48, v44 dst_sel:WORD_1 dst_unused:UNUSED_PRESERVE src0_sel:WORD_1
	v_exp_f16_sdwa v49, v45 dst_sel:WORD_1 dst_unused:UNUSED_PRESERVE src0_sel:WORD_1
	v_pk_add_f16 v42, v82, v114 neg_lo:[0,1] neg_hi:[0,1]
	v_pk_add_f16 v30, v30, v49
	v_pk_add_f16 v33, v33, v46
	v_pk_add_f16 v32, v32, v47
	v_pk_add_f16 v31, v31, v48
	v_pk_fma_f16 v25, v41, v49, v25
	v_pk_fma_f16 v24, v40, v48, v24
	v_pk_fma_f16 v23, v39, v47, v23
	v_pk_fma_f16 v22, v38, v46, v22
	v_pk_add_f16 v43, v83, v115 neg_lo:[0,1] neg_hi:[0,1]
	v_pk_add_f16 v44, v84, v116 neg_lo:[0,1] neg_hi:[0,1]
	v_pk_add_f16 v45, v85, v117 neg_lo:[0,1] neg_hi:[0,1]
	v_exp_f16_sdwa v46, v42 dst_sel:WORD_0 dst_unused:UNUSED_PAD src0_sel:WORD_0
	v_exp_f16_sdwa v47, v43 dst_sel:WORD_0 dst_unused:UNUSED_PAD src0_sel:WORD_0
	v_exp_f16_sdwa v48, v44 dst_sel:WORD_0 dst_unused:UNUSED_PAD src0_sel:WORD_0
	v_exp_f16_sdwa v49, v45 dst_sel:WORD_0 dst_unused:UNUSED_PAD src0_sel:WORD_0
	v_exp_f16_sdwa v46, v42 dst_sel:WORD_1 dst_unused:UNUSED_PRESERVE src0_sel:WORD_1
	v_exp_f16_sdwa v47, v43 dst_sel:WORD_1 dst_unused:UNUSED_PRESERVE src0_sel:WORD_1
	v_exp_f16_sdwa v48, v44 dst_sel:WORD_1 dst_unused:UNUSED_PRESERVE src0_sel:WORD_1
	v_exp_f16_sdwa v49, v45 dst_sel:WORD_1 dst_unused:UNUSED_PRESERVE src0_sel:WORD_1
	s_nop 0
	v_pk_add_f16 v30, v30, v49
	v_pk_add_f16 v31, v31, v48
	v_rcp_f16_e32 v44, v30
	v_rcp_f16_sdwa v30, v30 dst_sel:DWORD dst_unused:UNUSED_PAD src0_sel:WORD_1
	v_pk_add_f16 v32, v32, v47
	v_rcp_f16_e32 v45, v31
	v_rcp_f16_sdwa v31, v31 dst_sel:DWORD dst_unused:UNUSED_PAD src0_sel:WORD_1
	v_pk_add_f16 v33, v33, v46
	v_rcp_f16_e32 v43, v32
	v_rcp_f16_sdwa v32, v32 dst_sel:DWORD dst_unused:UNUSED_PAD src0_sel:WORD_1
	v_rcp_f16_e32 v42, v33
	v_rcp_f16_sdwa v33, v33 dst_sel:DWORD dst_unused:UNUSED_PAD src0_sel:WORD_1
	v_pk_fma_f16 v25, v61, v49, v25
	v_pack_b32_f16 v30, v44, v30
	v_pk_fma_f16 v24, v60, v48, v24
	v_pk_mul_f16 v25, v25, v30
	v_pack_b32_f16 v30, v45, v31
	v_pk_fma_f16 v23, v59, v47, v23
	v_pk_mul_f16 v24, v24, v30
	v_pack_b32_f16 v30, v43, v32
	v_pk_fma_f16 v22, v58, v46, v22
	v_pk_mul_f16 v23, v23, v30
	v_pack_b32_f16 v30, v42, v33
	v_pk_mul_f16 v22, v22, v30
	s_waitcnt vmcnt(0)
	v_pk_mul_f16 v30, v185, v146 op_sel_hi:[0,1]
	v_pk_mul_f16 v31, v185, v147 op_sel_hi:[0,1]
	v_pk_mul_f16 v32, v185, v148 op_sel_hi:[0,1]
	v_pk_mul_f16 v33, v185, v149 op_sel_hi:[0,1]
	v_pk_mul_f16 v42, v183, v146 op_sel_hi:[0,1]
	v_pk_mul_f16 v43, v183, v147 op_sel_hi:[0,1]
	v_pk_mul_f16 v44, v183, v148 op_sel_hi:[0,1]
	v_pk_mul_f16 v45, v183, v149 op_sel_hi:[0,1]
	v_pk_mul_f16 v46, v184, v146 op_sel_hi:[0,1]
	v_pk_mul_f16 v47, v184, v147 op_sel_hi:[0,1]
	v_pk_mul_f16 v48, v184, v148 op_sel_hi:[0,1]
	v_pk_mul_f16 v49, v184, v149 op_sel_hi:[0,1]
	v_pk_fma_f16 v21, v21, v149, v33
	v_pk_fma_f16 v20, v20, v148, v32
	v_pk_fma_f16 v19, v19, v147, v31
	v_pk_fma_f16 v18, v18, v146, v30
	v_pk_fma_f16 v37, v37, v149, v45
	v_pk_fma_f16 v36, v36, v148, v44
	v_pk_fma_f16 v35, v35, v147, v43
	v_pk_fma_f16 v34, v34, v146, v42
	v_pk_fma_f16 v50, v57, v149, v49
	v_pk_fma_f16 v51, v56, v148, v48
	v_pk_fma_f16 v52, v55, v147, v47
	v_pk_fma_f16 v53, v54, v146, v46
	v_pk_fma_f16 v54, v77, v149, v33
	v_pk_fma_f16 v55, v76, v148, v32
	v_pk_fma_f16 v56, v75, v147, v31
	v_pk_fma_f16 v57, v74, v146, v30
	v_pk_maximum3_f16 v74, v18, v34, v53
	v_pk_maximum3_f16 v75, v19, v35, v52
	v_pk_maximum3_f16 v76, v20, v36, v51
	v_pk_maximum3_f16 v77, v21, v37, v50
	v_pk_fma_f16 v66, v105, v149, v45
	v_pk_fma_f16 v67, v104, v148, v44
	v_pk_fma_f16 v68, v103, v147, v43
	v_pk_fma_f16 v69, v102, v146, v42
	v_pk_fma_f16 v70, v121, v149, v49
	v_pk_fma_f16 v71, v120, v148, v48
	v_pk_fma_f16 v72, v119, v147, v47
	v_pk_fma_f16 v73, v118, v146, v46
	v_pk_fma_f16 v33, v133, v149, v33
	v_pk_fma_f16 v32, v132, v148, v32
	v_pk_fma_f16 v31, v131, v147, v31
	v_pk_fma_f16 v30, v130, v146, v30
	v_pk_fma_f16 v45, v141, v149, v45
	v_pk_fma_f16 v44, v140, v148, v44
	v_pk_fma_f16 v43, v139, v147, v43
	v_pk_fma_f16 v42, v138, v146, v42
	v_pk_fma_f16 v49, v145, v149, v49
	v_pk_fma_f16 v48, v144, v148, v48
	v_pk_fma_f16 v47, v143, v147, v47
	v_pk_fma_f16 v46, v142, v146, v46
	v_pk_maximum3_f16 v82, v57, v69, v73
	v_pk_maximum3_f16 v83, v56, v68, v72
	v_pk_maximum3_f16 v84, v55, v67, v71
	v_pk_maximum3_f16 v85, v54, v66, v70
	v_pk_maximum3_f16 v87, v31, v43, v47
	v_pk_maximum3_f16 v86, v30, v42, v46
	v_pk_maximum3_f16 v88, v32, v44, v48
	v_pk_maximum3_f16 v89, v33, v45, v49
	v_pk_maximum3_f16 v74, v74, v82, v86
	v_pk_maximum3_f16 v75, v75, v83, v87
	v_pk_maximum3_f16 v76, v76, v84, v88
	v_pk_maximum3_f16 v77, v77, v85, v89
	s_nop 0
	v_pk_add_f16 v18, v18, v74 neg_lo:[0,1] neg_hi:[0,1]
	v_pk_add_f16 v19, v19, v75 neg_lo:[0,1] neg_hi:[0,1]
	v_pk_add_f16 v20, v20, v76 neg_lo:[0,1] neg_hi:[0,1]
	v_pk_add_f16 v21, v21, v77 neg_lo:[0,1] neg_hi:[0,1]
	v_pk_add_f16 v34, v34, v74 neg_lo:[0,1] neg_hi:[0,1]
	v_exp_f16_sdwa v82, v18 dst_sel:WORD_0 dst_unused:UNUSED_PAD src0_sel:WORD_0
	v_exp_f16_sdwa v83, v19 dst_sel:WORD_0 dst_unused:UNUSED_PAD src0_sel:WORD_0
	v_exp_f16_sdwa v84, v20 dst_sel:WORD_0 dst_unused:UNUSED_PAD src0_sel:WORD_0
	v_exp_f16_sdwa v85, v21 dst_sel:WORD_0 dst_unused:UNUSED_PAD src0_sel:WORD_0
	v_exp_f16_sdwa v82, v18 dst_sel:WORD_1 dst_unused:UNUSED_PRESERVE src0_sel:WORD_1
	v_exp_f16_sdwa v83, v19 dst_sel:WORD_1 dst_unused:UNUSED_PRESERVE src0_sel:WORD_1
	v_exp_f16_sdwa v84, v20 dst_sel:WORD_1 dst_unused:UNUSED_PRESERVE src0_sel:WORD_1
	v_exp_f16_sdwa v85, v21 dst_sel:WORD_1 dst_unused:UNUSED_PRESERVE src0_sel:WORD_1
	v_pk_add_f16 v35, v35, v75 neg_lo:[0,1] neg_hi:[0,1]
	v_pk_add_f16 v18, v82, 0
	v_pk_add_f16 v19, v83, 0
	v_pk_add_f16 v20, v84, 0
	v_pk_add_f16 v21, v85, 0
	v_pk_fma_f16 v6, v6, v82, 0
	v_pk_fma_f16 v7, v7, v83, 0
	v_pk_fma_f16 v8, v8, v84, 0
	v_pk_fma_f16 v9, v9, v85, 0
	v_pk_add_f16 v36, v36, v76 neg_lo:[0,1] neg_hi:[0,1]
	v_pk_add_f16 v37, v37, v77 neg_lo:[0,1] neg_hi:[0,1]
	v_exp_f16_sdwa v82, v34 dst_sel:WORD_0 dst_unused:UNUSED_PAD src0_sel:WORD_0
	v_exp_f16_sdwa v83, v35 dst_sel:WORD_0 dst_unused:UNUSED_PAD src0_sel:WORD_0
	v_exp_f16_sdwa v84, v36 dst_sel:WORD_0 dst_unused:UNUSED_PAD src0_sel:WORD_0
	v_exp_f16_sdwa v85, v37 dst_sel:WORD_0 dst_unused:UNUSED_PAD src0_sel:WORD_0
	v_exp_f16_sdwa v82, v34 dst_sel:WORD_1 dst_unused:UNUSED_PRESERVE src0_sel:WORD_1
	v_exp_f16_sdwa v83, v35 dst_sel:WORD_1 dst_unused:UNUSED_PRESERVE src0_sel:WORD_1
	v_exp_f16_sdwa v84, v36 dst_sel:WORD_1 dst_unused:UNUSED_PRESERVE src0_sel:WORD_1
	v_exp_f16_sdwa v85, v37 dst_sel:WORD_1 dst_unused:UNUSED_PRESERVE src0_sel:WORD_1
	s_nop 0
	v_pk_add_f16 v21, v21, v85
	v_pk_add_f16 v20, v20, v84
	v_pk_add_f16 v19, v19, v83
	v_pk_add_f16 v18, v18, v82
	v_pk_fma_f16 v9, v13, v85, v9
	v_pk_fma_f16 v8, v12, v84, v8
	v_pk_fma_f16 v7, v11, v83, v7
	v_pk_fma_f16 v6, v10, v82, v6
	v_pk_add_f16 v10, v53, v74 neg_lo:[0,1] neg_hi:[0,1]
	v_pk_add_f16 v11, v52, v75 neg_lo:[0,1] neg_hi:[0,1]
	v_pk_add_f16 v12, v51, v76 neg_lo:[0,1] neg_hi:[0,1]
	v_pk_add_f16 v13, v50, v77 neg_lo:[0,1] neg_hi:[0,1]
	v_exp_f16_sdwa v34, v10 dst_sel:WORD_0 dst_unused:UNUSED_PAD src0_sel:WORD_0
	v_exp_f16_sdwa v35, v11 dst_sel:WORD_0 dst_unused:UNUSED_PAD src0_sel:WORD_0
	v_exp_f16_sdwa v36, v12 dst_sel:WORD_0 dst_unused:UNUSED_PAD src0_sel:WORD_0
	v_exp_f16_sdwa v37, v13 dst_sel:WORD_0 dst_unused:UNUSED_PAD src0_sel:WORD_0
	v_exp_f16_sdwa v34, v10 dst_sel:WORD_1 dst_unused:UNUSED_PRESERVE src0_sel:WORD_1
	v_exp_f16_sdwa v35, v11 dst_sel:WORD_1 dst_unused:UNUSED_PRESERVE src0_sel:WORD_1
	v_exp_f16_sdwa v36, v12 dst_sel:WORD_1 dst_unused:UNUSED_PRESERVE src0_sel:WORD_1
	v_exp_f16_sdwa v37, v13 dst_sel:WORD_1 dst_unused:UNUSED_PRESERVE src0_sel:WORD_1
	v_pk_add_f16 v10, v18, v34
	v_pk_add_f16 v11, v19, v35
	v_pk_add_f16 v12, v20, v36
	v_pk_add_f16 v13, v21, v37
	v_pk_fma_f16 v6, v14, v34, v6
	v_pk_fma_f16 v7, v15, v35, v7
	v_pk_fma_f16 v8, v16, v36, v8
	v_pk_fma_f16 v9, v17, v37, v9
	v_pk_add_f16 v14, v57, v74 neg_lo:[0,1] neg_hi:[0,1]
	v_pk_add_f16 v15, v56, v75 neg_lo:[0,1] neg_hi:[0,1]
	v_pk_add_f16 v16, v55, v76 neg_lo:[0,1] neg_hi:[0,1]
	v_pk_add_f16 v17, v54, v77 neg_lo:[0,1] neg_hi:[0,1]
	v_exp_f16_sdwa v18, v14 dst_sel:WORD_0 dst_unused:UNUSED_PAD src0_sel:WORD_0
	v_exp_f16_sdwa v19, v15 dst_sel:WORD_0 dst_unused:UNUSED_PAD src0_sel:WORD_0
	v_exp_f16_sdwa v20, v16 dst_sel:WORD_0 dst_unused:UNUSED_PAD src0_sel:WORD_0
	v_exp_f16_sdwa v21, v17 dst_sel:WORD_0 dst_unused:UNUSED_PAD src0_sel:WORD_0
	v_exp_f16_sdwa v18, v14 dst_sel:WORD_1 dst_unused:UNUSED_PRESERVE src0_sel:WORD_1
	v_exp_f16_sdwa v19, v15 dst_sel:WORD_1 dst_unused:UNUSED_PRESERVE src0_sel:WORD_1
	v_exp_f16_sdwa v20, v16 dst_sel:WORD_1 dst_unused:UNUSED_PRESERVE src0_sel:WORD_1
	v_exp_f16_sdwa v21, v17 dst_sel:WORD_1 dst_unused:UNUSED_PRESERVE src0_sel:WORD_1
	v_pk_add_f16 v14, v69, v74 neg_lo:[0,1] neg_hi:[0,1]
	v_pk_add_f16 v13, v13, v21
	v_pk_add_f16 v12, v12, v20
	v_pk_add_f16 v11, v11, v19
	v_pk_add_f16 v10, v10, v18
	v_pk_fma_f16 v9, v29, v21, v9
	v_pk_fma_f16 v8, v28, v20, v8
	v_pk_fma_f16 v7, v27, v19, v7
	v_pk_fma_f16 v6, v26, v18, v6
	v_pk_add_f16 v15, v68, v75 neg_lo:[0,1] neg_hi:[0,1]
	v_pk_add_f16 v16, v67, v76 neg_lo:[0,1] neg_hi:[0,1]
	v_pk_add_f16 v17, v66, v77 neg_lo:[0,1] neg_hi:[0,1]
	v_exp_f16_sdwa v18, v14 dst_sel:WORD_0 dst_unused:UNUSED_PAD src0_sel:WORD_0
	v_exp_f16_sdwa v19, v15 dst_sel:WORD_0 dst_unused:UNUSED_PAD src0_sel:WORD_0
	v_exp_f16_sdwa v20, v16 dst_sel:WORD_0 dst_unused:UNUSED_PAD src0_sel:WORD_0
	v_exp_f16_sdwa v21, v17 dst_sel:WORD_0 dst_unused:UNUSED_PAD src0_sel:WORD_0
	v_exp_f16_sdwa v18, v14 dst_sel:WORD_1 dst_unused:UNUSED_PRESERVE src0_sel:WORD_1
	v_exp_f16_sdwa v19, v15 dst_sel:WORD_1 dst_unused:UNUSED_PRESERVE src0_sel:WORD_1
	v_exp_f16_sdwa v20, v16 dst_sel:WORD_1 dst_unused:UNUSED_PRESERVE src0_sel:WORD_1
	v_exp_f16_sdwa v21, v17 dst_sel:WORD_1 dst_unused:UNUSED_PRESERVE src0_sel:WORD_1
	v_pk_add_f16 v14, v73, v74 neg_lo:[0,1] neg_hi:[0,1]
	v_pk_add_f16 v10, v10, v18
	v_pk_add_f16 v11, v11, v19
	v_pk_add_f16 v12, v12, v20
	v_pk_add_f16 v13, v13, v21
	v_pk_fma_f16 v6, v38, v18, v6
	v_pk_fma_f16 v7, v39, v19, v7
	v_pk_fma_f16 v8, v40, v20, v8
	v_pk_fma_f16 v9, v41, v21, v9
	v_pk_add_f16 v15, v72, v75 neg_lo:[0,1] neg_hi:[0,1]
	v_pk_add_f16 v16, v71, v76 neg_lo:[0,1] neg_hi:[0,1]
	v_pk_add_f16 v17, v70, v77 neg_lo:[0,1] neg_hi:[0,1]
	v_exp_f16_sdwa v18, v14 dst_sel:WORD_0 dst_unused:UNUSED_PAD src0_sel:WORD_0
	v_exp_f16_sdwa v19, v15 dst_sel:WORD_0 dst_unused:UNUSED_PAD src0_sel:WORD_0
	v_exp_f16_sdwa v20, v16 dst_sel:WORD_0 dst_unused:UNUSED_PAD src0_sel:WORD_0
	v_exp_f16_sdwa v21, v17 dst_sel:WORD_0 dst_unused:UNUSED_PAD src0_sel:WORD_0
	v_exp_f16_sdwa v18, v14 dst_sel:WORD_1 dst_unused:UNUSED_PRESERVE src0_sel:WORD_1
	v_exp_f16_sdwa v19, v15 dst_sel:WORD_1 dst_unused:UNUSED_PRESERVE src0_sel:WORD_1
	v_exp_f16_sdwa v20, v16 dst_sel:WORD_1 dst_unused:UNUSED_PRESERVE src0_sel:WORD_1
	v_exp_f16_sdwa v21, v17 dst_sel:WORD_1 dst_unused:UNUSED_PRESERVE src0_sel:WORD_1
	v_pk_add_f16 v14, v30, v74 neg_lo:[0,1] neg_hi:[0,1]
	v_pk_add_f16 v13, v13, v21
	v_pk_add_f16 v12, v12, v20
	v_pk_add_f16 v11, v11, v19
	v_pk_add_f16 v10, v10, v18
	v_pk_fma_f16 v9, v61, v21, v9
	v_pk_fma_f16 v8, v60, v20, v8
	v_pk_fma_f16 v7, v59, v19, v7
	v_pk_fma_f16 v6, v58, v18, v6
	v_pk_add_f16 v15, v31, v75 neg_lo:[0,1] neg_hi:[0,1]
	v_pk_add_f16 v16, v32, v76 neg_lo:[0,1] neg_hi:[0,1]
	v_pk_add_f16 v17, v33, v77 neg_lo:[0,1] neg_hi:[0,1]
	v_exp_f16_sdwa v18, v14 dst_sel:WORD_0 dst_unused:UNUSED_PAD src0_sel:WORD_0
	v_exp_f16_sdwa v19, v15 dst_sel:WORD_0 dst_unused:UNUSED_PAD src0_sel:WORD_0
	v_exp_f16_sdwa v20, v16 dst_sel:WORD_0 dst_unused:UNUSED_PAD src0_sel:WORD_0
	v_exp_f16_sdwa v21, v17 dst_sel:WORD_0 dst_unused:UNUSED_PAD src0_sel:WORD_0
	v_exp_f16_sdwa v18, v14 dst_sel:WORD_1 dst_unused:UNUSED_PRESERVE src0_sel:WORD_1
	v_exp_f16_sdwa v19, v15 dst_sel:WORD_1 dst_unused:UNUSED_PRESERVE src0_sel:WORD_1
	v_exp_f16_sdwa v20, v16 dst_sel:WORD_1 dst_unused:UNUSED_PRESERVE src0_sel:WORD_1
	v_exp_f16_sdwa v21, v17 dst_sel:WORD_1 dst_unused:UNUSED_PRESERVE src0_sel:WORD_1
	v_pk_add_f16 v10, v10, v18
	v_pk_add_f16 v11, v11, v19
	v_pk_add_f16 v12, v12, v20
	v_pk_add_f16 v13, v13, v21
	v_pk_fma_f16 v14, v78, v18, v6
	v_pk_fma_f16 v15, v79, v19, v7
	v_pk_fma_f16 v16, v80, v20, v8
	v_pk_fma_f16 v17, v81, v21, v9
	v_pk_add_f16 v6, v42, v74 neg_lo:[0,1] neg_hi:[0,1]
	v_pk_add_f16 v7, v43, v75 neg_lo:[0,1] neg_hi:[0,1]
	v_pk_add_f16 v8, v44, v76 neg_lo:[0,1] neg_hi:[0,1]
	v_pk_add_f16 v9, v45, v77 neg_lo:[0,1] neg_hi:[0,1]
	v_exp_f16_sdwa v18, v6 dst_sel:WORD_0 dst_unused:UNUSED_PAD src0_sel:WORD_0
	v_exp_f16_sdwa v19, v7 dst_sel:WORD_0 dst_unused:UNUSED_PAD src0_sel:WORD_0
	v_exp_f16_sdwa v20, v8 dst_sel:WORD_0 dst_unused:UNUSED_PAD src0_sel:WORD_0
	v_exp_f16_sdwa v21, v9 dst_sel:WORD_0 dst_unused:UNUSED_PAD src0_sel:WORD_0
	v_exp_f16_sdwa v18, v6 dst_sel:WORD_1 dst_unused:UNUSED_PRESERVE src0_sel:WORD_1
	v_exp_f16_sdwa v19, v7 dst_sel:WORD_1 dst_unused:UNUSED_PRESERVE src0_sel:WORD_1
	v_exp_f16_sdwa v20, v8 dst_sel:WORD_1 dst_unused:UNUSED_PRESERVE src0_sel:WORD_1
	v_exp_f16_sdwa v21, v9 dst_sel:WORD_1 dst_unused:UNUSED_PRESERVE src0_sel:WORD_1
	s_nop 0
	v_pk_add_f16 v9, v13, v21
	v_pk_add_f16 v8, v12, v20
	v_pk_add_f16 v7, v11, v19
	v_pk_add_f16 v6, v10, v18
	v_pk_fma_f16 v13, v93, v21, v17
	v_pk_fma_f16 v12, v92, v20, v16
	v_pk_fma_f16 v11, v91, v19, v15
	v_pk_fma_f16 v10, v90, v18, v14
	v_pk_add_f16 v18, v46, v74 neg_lo:[0,1] neg_hi:[0,1]
	v_pk_add_f16 v19, v47, v75 neg_lo:[0,1] neg_hi:[0,1]
	v_pk_add_f16 v20, v48, v76 neg_lo:[0,1] neg_hi:[0,1]
	v_pk_add_f16 v21, v49, v77 neg_lo:[0,1] neg_hi:[0,1]
	v_exp_f16_sdwa v14, v18 dst_sel:WORD_0 dst_unused:UNUSED_PAD src0_sel:WORD_0
	v_exp_f16_sdwa v17, v19 dst_sel:WORD_0 dst_unused:UNUSED_PAD src0_sel:WORD_0
	v_exp_f16_sdwa v15, v20 dst_sel:WORD_0 dst_unused:UNUSED_PAD src0_sel:WORD_0
	v_exp_f16_sdwa v16, v21 dst_sel:WORD_0 dst_unused:UNUSED_PAD src0_sel:WORD_0
	v_exp_f16_sdwa v14, v18 dst_sel:WORD_1 dst_unused:UNUSED_PRESERVE src0_sel:WORD_1
	v_exp_f16_sdwa v17, v19 dst_sel:WORD_1 dst_unused:UNUSED_PRESERVE src0_sel:WORD_1
	v_exp_f16_sdwa v15, v20 dst_sel:WORD_1 dst_unused:UNUSED_PRESERVE src0_sel:WORD_1
	v_exp_f16_sdwa v16, v21 dst_sel:WORD_1 dst_unused:UNUSED_PRESERVE src0_sel:WORD_1
	s_nop 0

_Z7k_stageILi1ELi4EEv8AttnArgsPKDF16_PKfPDF16_iii:
	s_load_dwordx2 s[86:87], s[0:1], 0x70
	s_load_dwordx2 s[82:83], s[0:1], 0x88
	s_lshr_b32 s92, s2, 3
	s_mov_b32 s81, s3
	s_load_dwordx16 s[64:79], s[0:1], 0x0
	v_readfirstlane_b32 s94, v0
	s_nop 0
	s_lshr_b32 s94, s94, 6
	s_load_dwordx4 s[28:31], s[0:1], 0x70
	s_load_dwordx2 s[24:25], s[0:1], 0x80
	s_load_dword s33, s[0:1], 0x90
	s_lshl_b32 s4, s2, 5
	s_and_b32 s45, s4, 0xe0
	s_lshr_b32 s4, s2, 3
	s_add_i32 s45, s45, s4
	s_and_b32 s44, s2, 56
	v_readfirstlane_b32 s3, v0
	v_and_b32_e32 v1, 15, v0
	s_waitcnt lgkmcnt(0)
	s_cmp_lt_i32 s33, 1
	v_bfe_u32 v167, v0, 4, 2
	s_cbranch_scc1 .LBB4_155
	s_lshr_b32 s2, s3, 2
	v_lshrrev_b32_e32 v7, 7, v0
	v_lshrrev_b32_e32 v2, 5, v0
	v_lshrrev_b32_e32 v3, 4, v0
	s_and_b32 s2, s2, 16
	v_lshrrev_b32_e32 v4, 6, v0
	v_and_b32_e32 v7, 1, v7
	v_and_b32_e32 v2, 4, v2
	v_or_b32_e32 v179, s2, v1
	v_and_b32_e32 v5, 4, v4
	s_load_dwordx2 s[40:41], s[0:1], 0x60
	s_bitcmp1_b32 s3, 6
	v_lshlrev_b16_e32 v7, 2, v7
	v_and_b32_e32 v8, 3, v3
	s_load_dwordx4 s[36:39], s[0:1], 0x0
	s_load_dwordx2 s[4:5], s[0:1], 0x10
	s_load_dwordx8 s[8:15], s[0:1], 0x18
	s_load_dwordx2 s[6:7], s[0:1], 0x38
	s_load_dwordx8 s[16:23], s[0:1], 0x40
	v_or_b32_e32 v178, v2, v167
	v_and_or_b32 v180, s45, 56, v5
	s_cselect_b64 s[26:27], -1, 0
	s_and_b32 s3, s45, 0x3ffffc0
	v_bitop3_b16 v3, v7, v3, 3 bitop3:0xf8
	v_bitop3_b16 v7, v7, 8, v8 bitop3:0xfe
	v_lshlrev_b32_e32 v8, 12, v5
	v_bitop3_b32 v2, v2, v179, v167 bitop3:0x36
	v_or_b32_e32 v6, s3, v180
	s_and_b32 s3, s45, 0x1ffc0
	v_and_b32_e32 v3, 0xffff, v3
	v_lshl_or_b32 v184, v2, 4, v8
	v_lshlrev_b32_e32 v2, 3, v5
	v_mov_b32_e32 v169, 0
	v_lshlrev_b32_e32 v168, 5, v179
	v_lshlrev_b32_e32 v181, 6, v6
	v_or_b32_e32 v6, s3, v180
	v_and_b32_e32 v7, 0xffff, v7
	v_or_b32_e32 v186, 8, v2
	v_or_b32_e32 v188, 16, v2
	v_bitop3_b32 v2, s2, v3, v1 bitop3:0x36
	v_lshlrev_b32_e32 v166, 3, v179
	s_waitcnt lgkmcnt(0)
	v_lshl_add_u64 v[170:171], s[38:39], 0, v[168:169]
	s_mov_b32 s39, 0x20000
	v_lshlrev_b32_e32 v189, 4, v2
	v_bitop3_b32 v2, s2, v7, v1 bitop3:0x36
	v_lshlrev_b32_e32 v193, 15, v6
	v_lshl_add_u64 v[172:173], s[4:5], 0, v[168:169]
	s_and_b32 s37, s37, 0xffff
	s_mov_b32 s38, 0x1800000
	v_add_u32_e32 v182, -1, v180
	v_add_u32_e32 v183, 4, v180
	v_lshl_add_u64 v[174:175], s[14:15], 0, v[168:169]
	v_lshl_add_u64 v[176:177], s[6:7], 0, v[168:169]
	s_and_b32 s13, s13, 0xffff
	s_mov_b32 s42, 0x800000
	s_mov_b32 s43, s39
	s_and_b32 s41, s41, 0xffff
	v_or_b32_e32 v185, 64, v181
	v_or_b32_e32 v187, 0x80, v181
	v_or_b32_e32 v190, 0xc0, v181
	v_lshl_or_b32 v191, v4, 3, 24
	v_lshlrev_b32_e32 v192, 4, v2
	v_lshlrev_b32_e32 v194, 4, v179
	v_or_b32_e32 v195, 0x8000, v193
	v_or_b32_e32 v196, 0x10000, v193
	v_or_b32_e32 v197, 0x18000, v193
	s_mov_b32 s46, 0
	s_movk_i32 s47, 0x300
	v_lshlrev_b32_e32 v198, 1, v166
	s_branch .LBB4_4
.LBB4_2:
	s_waitcnt vmcnt(3)
	s_mul_i32 s84, s81, s83
	s_add_i32 s84, s84, s82
	s_mul_i32 s84, s84, 0x60000
	s_lshl_b32 s85, s92, 3
	s_add_u32 s85, s85, s94
	s_mul_i32 s85, s85, 1536
	s_add_u32 s84, s84, s85
	s_add_u32 s88, s86, s84
	s_addc_u32 s89, s87, 0
	s_load_dword s90, s[88:89], 0x0
	s_load_dword s90, s[88:89], 0x80
	s_load_dword s90, s[88:89], 0x100
	s_load_dword s90, s[88:89], 0x180
	s_load_dword s90, s[88:89], 0x200
	s_load_dword s90, s[88:89], 0x280
	s_load_dword s90, s[88:89], 0x300
	s_load_dword s90, s[88:89], 0x380
	s_load_dword s90, s[88:89], 0x400
	s_load_dword s90, s[88:89], 0x480
	s_load_dword s90, s[88:89], 0x500
	s_load_dword s90, s[88:89], 0x580
	v_pk_mul_f16 v161, v160, v162 op_sel_hi:[0,1]
	v_pk_mul_f16 v206, v160, v165 op_sel_hi:[0,1]
	v_pk_mul_f16 v210, v158, v165 op_sel_hi:[0,1]
	v_pk_mul_f16 v214, v159, v165 op_sel_hi:[0,1]
	v_pk_mul_f16 v200, v160, v163 op_sel_hi:[0,1]
	v_pk_mul_f16 v201, v160, v164 op_sel_hi:[0,1]
	v_pk_mul_f16 v207, v158, v162 op_sel_hi:[0,1]
	s_mov_b64 exec, s[64:65]
	buffer_load_dwordx4 v[26:29], v245, s[12:15], 0 offen
	buffer_load_dwordx4 v[10:13], v245, s[12:15], 0 offen offset:512
	s_mov_b64 exec, -1
	v_pk_mul_f16 v208, v158, v163 op_sel_hi:[0,1]
	v_pk_mul_f16 v209, v158, v164 op_sel_hi:[0,1]
	v_pk_mul_f16 v211, v159, v162 op_sel_hi:[0,1]
	v_pk_mul_f16 v212, v159, v163 op_sel_hi:[0,1]
	v_pk_mul_f16 v213, v159, v164 op_sel_hi:[0,1]
	v_pk_fma_f16 v117, v117, v165, v206
	v_pk_fma_f16 v114, v114, v162, v161
	v_pk_fma_f16 v133, v133, v165, v206
	v_pk_fma_f16 v130, v130, v162, v161
	v_pk_fma_f16 v141, v141, v165, v206
	v_pk_fma_f16 v138, v138, v162, v161
	v_pk_fma_f16 v161, v89, v165, v210
	v_pk_fma_f16 v215, v113, v165, v210
	buffer_load_dwordx4 v[38:41], v246, s[12:15], 0 offen offset:512
	buffer_load_dwordx4 v[14:17], v246, s[12:15], 0 offen offset:1024
	v_pk_fma_f16 v210, v129, v165, v210
	v_pk_fma_f16 v219, v57, v165, v214
	v_pk_fma_f16 v223, v77, v165, v214
	v_pk_fma_f16 v165, v101, v165, v214
	v_pk_maximum3_f16 v214, v117, v133, v141
	v_pk_fma_f16 v116, v116, v164, v201
	v_pk_fma_f16 v115, v115, v163, v200
	v_pk_fma_f16 v132, v132, v164, v201
	v_pk_fma_f16 v131, v131, v163, v200
	v_pk_fma_f16 v140, v140, v164, v201
	v_pk_fma_f16 v139, v139, v163, v200
	v_pk_fma_f16 v200, v88, v164, v209
	v_pk_fma_f16 v201, v87, v163, v208
	v_pk_fma_f16 v206, v86, v162, v207
	v_pk_fma_f16 v216, v112, v164, v209
	v_pk_fma_f16 v217, v111, v163, v208
	s_mov_b64 exec, s[66:67]
	buffer_load_dwordx4 v[58:61], v246, s[12:15], 0 offen offset:2048
	buffer_load_dwordx4 v[18:21], v246, s[12:15], 0 offen offset:2560
	s_mov_b64 exec, -1
	v_pk_fma_f16 v218, v110, v162, v207
	v_pk_fma_f16 v209, v128, v164, v209
	v_pk_fma_f16 v208, v127, v163, v208
	v_pk_fma_f16 v207, v126, v162, v207
	v_pk_fma_f16 v220, v56, v164, v213
	v_pk_fma_f16 v221, v55, v163, v212
	v_pk_fma_f16 v222, v54, v162, v211
	v_pk_fma_f16 v224, v76, v164, v213
	v_pk_fma_f16 v225, v75, v163, v212
	v_pk_fma_f16 v226, v74, v162, v211
	v_pk_fma_f16 v164, v100, v164, v213
	v_pk_fma_f16 v163, v99, v163, v212
	v_pk_fma_f16 v162, v98, v162, v211
	v_pk_maximum3_f16 v211, v114, v130, v138
	v_pk_maximum3_f16 v212, v115, v131, v139
	v_pk_maximum3_f16 v213, v116, v132, v140
	v_pk_maximum3_f16 v230, v161, v215, v210
	v_pk_maximum3_f16 v234, v219, v223, v165
	v_pk_maximum3_f16 v227, v206, v218, v207
	v_pk_maximum3_f16 v228, v201, v217, v208
	v_pk_maximum3_f16 v229, v200, v216, v209
	v_pk_maximum3_f16 v231, v222, v226, v162
	v_pk_maximum3_f16 v232, v221, v225, v163
	v_pk_maximum3_f16 v214, v214, v230, v234
	v_pk_maximum3_f16 v233, v220, v224, v164
	v_pk_maximum3_f16 v211, v211, v227, v231
	v_pk_maximum3_f16 v212, v212, v228, v232
	v_pk_maximum3_f16 v213, v213, v229, v233
	v_pk_add_f16 v117, v117, v214 neg_lo:[0,1] neg_hi:[0,1]
	s_mov_b64 exec, s[64:65]
	buffer_load_dwordx4 v[78:81], v247, s[12:15], 0 offen
	buffer_load_dwordx4 v[30:33], v247, s[12:15], 0 offen offset:512
	s_mov_b64 exec, -1
	v_pk_add_f16 v114, v114, v211 neg_lo:[0,1] neg_hi:[0,1]
	v_pk_add_f16 v115, v115, v212 neg_lo:[0,1] neg_hi:[0,1]
	v_pk_add_f16 v116, v116, v213 neg_lo:[0,1] neg_hi:[0,1]
	v_pk_add_f16 v130, v130, v211 neg_lo:[0,1] neg_hi:[0,1]
	v_exp_f16_sdwa v227, v114 dst_sel:WORD_0 dst_unused:UNUSED_PAD src0_sel:WORD_0
	v_exp_f16_sdwa v228, v115 dst_sel:WORD_0 dst_unused:UNUSED_PAD src0_sel:WORD_0
	v_exp_f16_sdwa v229, v116 dst_sel:WORD_0 dst_unused:UNUSED_PAD src0_sel:WORD_0
	v_exp_f16_sdwa v230, v117 dst_sel:WORD_0 dst_unused:UNUSED_PAD src0_sel:WORD_0
	v_exp_f16_sdwa v227, v114 dst_sel:WORD_1 dst_unused:UNUSED_PRESERVE src0_sel:WORD_1
	v_exp_f16_sdwa v228, v115 dst_sel:WORD_1 dst_unused:UNUSED_PRESERVE src0_sel:WORD_1
	v_exp_f16_sdwa v229, v116 dst_sel:WORD_1 dst_unused:UNUSED_PRESERVE src0_sel:WORD_1
	v_exp_f16_sdwa v230, v117 dst_sel:WORD_1 dst_unused:UNUSED_PRESERVE src0_sel:WORD_1
	v_pk_add_f16 v131, v131, v212 neg_lo:[0,1] neg_hi:[0,1]
	v_pk_add_f16 v117, v227, 0
	v_pk_fma_f16 v73, v73, v230, 0
	v_pk_add_f16 v114, v230, 0
	v_pk_add_f16 v115, v229, 0
	v_pk_add_f16 v116, v228, 0
	v_pk_fma_f16 v72, v72, v229, 0
	v_pk_fma_f16 v71, v71, v228, 0
	v_pk_fma_f16 v70, v70, v227, 0
	v_pk_add_f16 v132, v132, v213 neg_lo:[0,1] neg_hi:[0,1]
	buffer_load_dwordx4 v[106:109], v248, s[12:15], 0 offen offset:512
	buffer_load_dwordx4 v[46:49], v248, s[12:15], 0 offen offset:1024
	v_pk_add_f16 v133, v133, v214 neg_lo:[0,1] neg_hi:[0,1]
	v_exp_f16_sdwa v227, v130 dst_sel:WORD_0 dst_unused:UNUSED_PAD src0_sel:WORD_0
	v_exp_f16_sdwa v228, v131 dst_sel:WORD_0 dst_unused:UNUSED_PAD src0_sel:WORD_0
	v_exp_f16_sdwa v229, v132 dst_sel:WORD_0 dst_unused:UNUSED_PAD src0_sel:WORD_0
	v_exp_f16_sdwa v230, v133 dst_sel:WORD_0 dst_unused:UNUSED_PAD src0_sel:WORD_0
	v_exp_f16_sdwa v227, v130 dst_sel:WORD_1 dst_unused:UNUSED_PRESERVE src0_sel:WORD_1
	v_exp_f16_sdwa v228, v131 dst_sel:WORD_1 dst_unused:UNUSED_PRESERVE src0_sel:WORD_1
	v_exp_f16_sdwa v229, v132 dst_sel:WORD_1 dst_unused:UNUSED_PRESERVE src0_sel:WORD_1
	v_exp_f16_sdwa v230, v133 dst_sel:WORD_1 dst_unused:UNUSED_PRESERVE src0_sel:WORD_1
	v_pk_add_f16 v117, v117, v227
	v_pk_fma_f16 v73, v97, v230, v73
	v_pk_add_f16 v97, v141, v214 neg_lo:[0,1] neg_hi:[0,1]
	v_pk_add_f16 v116, v116, v228
	v_pk_add_f16 v115, v115, v229
	v_pk_add_f16 v114, v114, v230
	v_pk_fma_f16 v70, v94, v227, v70
	v_pk_fma_f16 v71, v95, v228, v71
	v_pk_fma_f16 v72, v96, v229, v72
	v_pk_add_f16 v94, v138, v211 neg_lo:[0,1] neg_hi:[0,1]
	v_pk_add_f16 v95, v139, v212 neg_lo:[0,1] neg_hi:[0,1]
	v_pk_add_f16 v96, v140, v213 neg_lo:[0,1] neg_hi:[0,1]
	v_exp_f16_sdwa v130, v94 dst_sel:WORD_0 dst_unused:UNUSED_PAD src0_sel:WORD_0
	v_exp_f16_sdwa v131, v95 dst_sel:WORD_0 dst_unused:UNUSED_PAD src0_sel:WORD_0
	v_exp_f16_sdwa v132, v96 dst_sel:WORD_0 dst_unused:UNUSED_PAD src0_sel:WORD_0
	v_exp_f16_sdwa v133, v97 dst_sel:WORD_0 dst_unused:UNUSED_PAD src0_sel:WORD_0
	v_exp_f16_sdwa v130, v94 dst_sel:WORD_1 dst_unused:UNUSED_PRESERVE src0_sel:WORD_1
	v_exp_f16_sdwa v131, v95 dst_sel:WORD_1 dst_unused:UNUSED_PRESERVE src0_sel:WORD_1
	v_exp_f16_sdwa v132, v96 dst_sel:WORD_1 dst_unused:UNUSED_PRESERVE src0_sel:WORD_1
	v_exp_f16_sdwa v133, v97 dst_sel:WORD_1 dst_unused:UNUSED_PRESERVE src0_sel:WORD_1
	v_pk_add_f16 v97, v117, v130
	v_pk_add_f16 v94, v114, v133
	s_mov_b64 exec, s[66:67]
	buffer_load_dwordx4 v[122:125], v248, s[12:15], 0 offen offset:2048
	buffer_load_dwordx4 v[62:65], v248, s[12:15], 0 offen offset:2560
	s_mov_b64 exec, -1
	v_pk_add_f16 v95, v115, v132
	v_pk_add_f16 v96, v116, v131
	v_pk_fma_f16 v73, v121, v133, v73
	v_pk_fma_f16 v72, v120, v132, v72
	v_pk_fma_f16 v71, v119, v131, v71
	v_pk_fma_f16 v70, v118, v130, v70
	v_pk_add_f16 v114, v206, v211 neg_lo:[0,1] neg_hi:[0,1]
	v_pk_add_f16 v115, v201, v212 neg_lo:[0,1] neg_hi:[0,1]
	v_pk_add_f16 v116, v200, v213 neg_lo:[0,1] neg_hi:[0,1]
	v_pk_add_f16 v117, v161, v214 neg_lo:[0,1] neg_hi:[0,1]
	v_exp_f16_sdwa v118, v114 dst_sel:WORD_0 dst_unused:UNUSED_PAD src0_sel:WORD_0
	v_exp_f16_sdwa v119, v115 dst_sel:WORD_0 dst_unused:UNUSED_PAD src0_sel:WORD_0
	v_exp_f16_sdwa v120, v116 dst_sel:WORD_0 dst_unused:UNUSED_PAD src0_sel:WORD_0
	v_exp_f16_sdwa v121, v117 dst_sel:WORD_0 dst_unused:UNUSED_PAD src0_sel:WORD_0
	v_exp_f16_sdwa v118, v114 dst_sel:WORD_1 dst_unused:UNUSED_PRESERVE src0_sel:WORD_1
	v_exp_f16_sdwa v119, v115 dst_sel:WORD_1 dst_unused:UNUSED_PRESERVE src0_sel:WORD_1
	v_exp_f16_sdwa v120, v116 dst_sel:WORD_1 dst_unused:UNUSED_PRESERVE src0_sel:WORD_1
	v_exp_f16_sdwa v121, v117 dst_sel:WORD_1 dst_unused:UNUSED_PRESERVE src0_sel:WORD_1
	v_pk_add_f16 v114, v218, v211 neg_lo:[0,1] neg_hi:[0,1]
	v_pk_add_f16 v97, v97, v118
	v_pk_add_f16 v96, v96, v119
	v_pk_add_f16 v95, v95, v120
	s_mov_b64 exec, s[76:77]
	buffer_load_dwordx4 v[134:137], v249, s[12:15], 0 offen
	buffer_load_dwordx4 v[82:85], v249, s[12:15], 0 offen offset:512
	s_mov_b64 exec, -1
	v_pk_add_f16 v94, v94, v121
	v_pk_fma_f16 v70, v42, v118, v70
	v_pk_fma_f16 v71, v43, v119, v71
	v_pk_fma_f16 v72, v44, v120, v72
	v_pk_fma_f16 v73, v45, v121, v73
	v_pk_add_f16 v115, v217, v212 neg_lo:[0,1] neg_hi:[0,1]
	v_pk_add_f16 v116, v216, v213 neg_lo:[0,1] neg_hi:[0,1]
	v_pk_add_f16 v117, v215, v214 neg_lo:[0,1] neg_hi:[0,1]
	v_exp_f16_sdwa v118, v114 dst_sel:WORD_0 dst_unused:UNUSED_PAD src0_sel:WORD_0
	v_exp_f16_sdwa v119, v115 dst_sel:WORD_0 dst_unused:UNUSED_PAD src0_sel:WORD_0
	v_exp_f16_sdwa v120, v116 dst_sel:WORD_0 dst_unused:UNUSED_PAD src0_sel:WORD_0
	v_exp_f16_sdwa v121, v117 dst_sel:WORD_0 dst_unused:UNUSED_PAD src0_sel:WORD_0
	v_exp_f16_sdwa v118, v114 dst_sel:WORD_1 dst_unused:UNUSED_PRESERVE src0_sel:WORD_1
	v_exp_f16_sdwa v119, v115 dst_sel:WORD_1 dst_unused:UNUSED_PRESERVE src0_sel:WORD_1
	v_exp_f16_sdwa v120, v116 dst_sel:WORD_1 dst_unused:UNUSED_PRESERVE src0_sel:WORD_1
	v_exp_f16_sdwa v121, v117 dst_sel:WORD_1 dst_unused:UNUSED_PRESERVE src0_sel:WORD_1
	v_pk_add_f16 v114, v207, v211 neg_lo:[0,1] neg_hi:[0,1]
	v_pk_add_f16 v97, v97, v118
	v_pk_add_f16 v94, v94, v121
	v_pk_add_f16 v95, v95, v120
	v_pk_add_f16 v96, v96, v119
	v_pk_fma_f16 v73, v69, v121, v73
	v_pk_fma_f16 v72, v68, v120, v72
	s_mov_b64 exec, s[70:71]
	buffer_load_dwordx4 v[142:145], v250, s[12:15], 0 offen offset:512
	buffer_load_dwordx4 v[102:105], v250, s[12:15], 0 offen offset:1024
	s_mov_b64 exec, -1
	v_pk_fma_f16 v71, v67, v119, v71
	v_pk_fma_f16 v70, v66, v118, v70
	v_pk_add_f16 v115, v208, v212 neg_lo:[0,1] neg_hi:[0,1]
	v_pk_add_f16 v116, v209, v213 neg_lo:[0,1] neg_hi:[0,1]
	v_pk_add_f16 v117, v210, v214 neg_lo:[0,1] neg_hi:[0,1]
	v_exp_f16_sdwa v118, v114 dst_sel:WORD_0 dst_unused:UNUSED_PAD src0_sel:WORD_0
	v_exp_f16_sdwa v119, v115 dst_sel:WORD_0 dst_unused:UNUSED_PAD src0_sel:WORD_0
	v_exp_f16_sdwa v120, v116 dst_sel:WORD_0 dst_unused:UNUSED_PAD src0_sel:WORD_0
	v_exp_f16_sdwa v121, v117 dst_sel:WORD_0 dst_unused:UNUSED_PAD src0_sel:WORD_0
	v_exp_f16_sdwa v118, v114 dst_sel:WORD_1 dst_unused:UNUSED_PRESERVE src0_sel:WORD_1
	v_exp_f16_sdwa v119, v115 dst_sel:WORD_1 dst_unused:UNUSED_PRESERVE src0_sel:WORD_1
	v_exp_f16_sdwa v120, v116 dst_sel:WORD_1 dst_unused:UNUSED_PRESERVE src0_sel:WORD_1
	v_exp_f16_sdwa v121, v117 dst_sel:WORD_1 dst_unused:UNUSED_PRESERVE src0_sel:WORD_1
	v_pk_add_f16 v114, v222, v211 neg_lo:[0,1] neg_hi:[0,1]
	v_pk_add_f16 v97, v97, v118
	v_pk_add_f16 v96, v96, v119
	v_pk_add_f16 v95, v95, v120
	v_pk_add_f16 v94, v94, v121
	v_pk_fma_f16 v70, v90, v118, v70
	v_pk_fma_f16 v71, v91, v119, v71
	v_pk_fma_f16 v72, v92, v120, v72
	v_pk_fma_f16 v73, v93, v121, v73
	s_mov_b64 exec, s[78:79]
	buffer_load_dwordx4 v[6:9], v250, s[12:15], 0 offen offset:2048
	buffer_load_dwordx4 v[2:5], v250, s[12:15], 0 offen offset:2560
	s_mov_b64 exec, -1
	v_pk_add_f16 v115, v221, v212 neg_lo:[0,1] neg_hi:[0,1]
	v_pk_add_f16 v116, v220, v213 neg_lo:[0,1] neg_hi:[0,1]
	v_pk_add_f16 v117, v219, v214 neg_lo:[0,1] neg_hi:[0,1]
	v_exp_f16_sdwa v118, v114 dst_sel:WORD_0 dst_unused:UNUSED_PAD src0_sel:WORD_0
	v_exp_f16_sdwa v119, v115 dst_sel:WORD_0 dst_unused:UNUSED_PAD src0_sel:WORD_0
	v_exp_f16_sdwa v120, v116 dst_sel:WORD_0 dst_unused:UNUSED_PAD src0_sel:WORD_0
	v_exp_f16_sdwa v121, v117 dst_sel:WORD_0 dst_unused:UNUSED_PAD src0_sel:WORD_0
	v_exp_f16_sdwa v118, v114 dst_sel:WORD_1 dst_unused:UNUSED_PRESERVE src0_sel:WORD_1
	v_exp_f16_sdwa v119, v115 dst_sel:WORD_1 dst_unused:UNUSED_PRESERVE src0_sel:WORD_1
	v_exp_f16_sdwa v120, v116 dst_sel:WORD_1 dst_unused:UNUSED_PRESERVE src0_sel:WORD_1
	v_exp_f16_sdwa v121, v117 dst_sel:WORD_1 dst_unused:UNUSED_PRESERVE src0_sel:WORD_1
	v_pk_add_f16 v114, v226, v211 neg_lo:[0,1] neg_hi:[0,1]
	v_pk_add_f16 v97, v97, v118
	v_pk_add_f16 v94, v94, v121
	v_pk_add_f16 v95, v95, v120
	v_pk_add_f16 v96, v96, v119
	v_pk_fma_f16 v73, v25, v121, v73
	v_pk_fma_f16 v72, v24, v120, v72
	v_pk_fma_f16 v71, v23, v119, v71
	v_pk_fma_f16 v70, v22, v118, v70
	v_pk_add_f16 v115, v225, v212 neg_lo:[0,1] neg_hi:[0,1]
	v_pk_add_f16 v116, v224, v213 neg_lo:[0,1] neg_hi:[0,1]
	v_pk_add_f16 v117, v223, v214 neg_lo:[0,1] neg_hi:[0,1]
	v_exp_f16_sdwa v118, v114 dst_sel:WORD_0 dst_unused:UNUSED_PAD src0_sel:WORD_0
	v_exp_f16_sdwa v119, v115 dst_sel:WORD_0 dst_unused:UNUSED_PAD src0_sel:WORD_0
	v_exp_f16_sdwa v120, v116 dst_sel:WORD_0 dst_unused:UNUSED_PAD src0_sel:WORD_0
	v_exp_f16_sdwa v121, v117 dst_sel:WORD_0 dst_unused:UNUSED_PAD src0_sel:WORD_0
	v_exp_f16_sdwa v118, v114 dst_sel:WORD_1 dst_unused:UNUSED_PRESERVE src0_sel:WORD_1
	v_exp_f16_sdwa v119, v115 dst_sel:WORD_1 dst_unused:UNUSED_PRESERVE src0_sel:WORD_1
	v_exp_f16_sdwa v120, v116 dst_sel:WORD_1 dst_unused:UNUSED_PRESERVE src0_sel:WORD_1
	v_exp_f16_sdwa v121, v117 dst_sel:WORD_1 dst_unused:UNUSED_PRESERVE src0_sel:WORD_1
	v_pk_add_f16 v114, v162, v211 neg_lo:[0,1] neg_hi:[0,1]
	v_pk_add_f16 v97, v97, v118
	v_pk_add_f16 v96, v96, v119
	v_pk_add_f16 v95, v95, v120
	v_pk_add_f16 v94, v94, v121
	v_pk_fma_f16 v70, v34, v118, v70
	v_pk_fma_f16 v71, v35, v119, v71
	v_pk_fma_f16 v72, v36, v120, v72
	v_pk_fma_f16 v73, v37, v121, v73
	v_pk_add_f16 v115, v163, v212 neg_lo:[0,1] neg_hi:[0,1]
	v_pk_add_f16 v116, v164, v213 neg_lo:[0,1] neg_hi:[0,1]
	v_pk_add_f16 v117, v165, v214 neg_lo:[0,1] neg_hi:[0,1]
	v_exp_f16_sdwa v118, v114 dst_sel:WORD_0 dst_unused:UNUSED_PAD src0_sel:WORD_0
	v_exp_f16_sdwa v119, v115 dst_sel:WORD_0 dst_unused:UNUSED_PAD src0_sel:WORD_0
	v_exp_f16_sdwa v120, v116 dst_sel:WORD_0 dst_unused:UNUSED_PAD src0_sel:WORD_0
	v_exp_f16_sdwa v121, v117 dst_sel:WORD_0 dst_unused:UNUSED_PAD src0_sel:WORD_0
	v_exp_f16_sdwa v118, v114 dst_sel:WORD_1 dst_unused:UNUSED_PRESERVE src0_sel:WORD_1
	v_exp_f16_sdwa v119, v115 dst_sel:WORD_1 dst_unused:UNUSED_PRESERVE src0_sel:WORD_1
	v_exp_f16_sdwa v120, v116 dst_sel:WORD_1 dst_unused:UNUSED_PRESERVE src0_sel:WORD_1
	v_exp_f16_sdwa v121, v117 dst_sel:WORD_1 dst_unused:UNUSED_PRESERVE src0_sel:WORD_1
	v_pk_add_f16 v97, v97, v118
	v_pk_add_f16 v96, v96, v119
	v_rcp_f16_e32 v114, v97
	v_rcp_f16_sdwa v97, v97 dst_sel:DWORD dst_unused:UNUSED_PAD src0_sel:WORD_1
	v_pk_add_f16 v95, v95, v120
	v_rcp_f16_e32 v115, v96
	v_rcp_f16_sdwa v96, v96 dst_sel:DWORD dst_unused:UNUSED_PAD src0_sel:WORD_1
	v_pk_add_f16 v94, v94, v121
	v_rcp_f16_e32 v116, v95
	v_rcp_f16_sdwa v95, v95 dst_sel:DWORD dst_unused:UNUSED_PAD src0_sel:WORD_1
	v_rcp_f16_e32 v117, v94
	v_rcp_f16_sdwa v94, v94 dst_sel:DWORD dst_unused:UNUSED_PAD src0_sel:WORD_1
	v_pk_fma_f16 v70, v50, v118, v70
	v_pack_b32_f16 v97, v114, v97
	v_pk_fma_f16 v71, v51, v119, v71
	v_pk_mul_f16 v141, v70, v97
	v_pack_b32_f16 v70, v115, v96
	v_pk_fma_f16 v72, v52, v120, v72
	v_pk_mul_f16 v140, v71, v70
	v_pack_b32_f16 v70, v116, v95
	v_pk_fma_f16 v73, v53, v121, v73
	v_pk_mul_f16 v139, v72, v70
	v_pack_b32_f16 v70, v117, v94
	v_pk_mul_f16 v138, v73, v70
	s_waitcnt vmcnt(12)
	v_pk_mul_f16 v70, v160, v154 op_sel_hi:[0,1]
	v_pk_mul_f16 v73, v160, v157 op_sel_hi:[0,1]
	v_pk_mul_f16 v97, v158, v157 op_sel_hi:[0,1]
	v_pk_mul_f16 v117, v159, v157 op_sel_hi:[0,1]
	v_pk_mul_f16 v71, v160, v155 op_sel_hi:[0,1]
	v_pk_mul_f16 v72, v160, v156 op_sel_hi:[0,1]
	v_pk_mul_f16 v94, v158, v154 op_sel_hi:[0,1]
	v_pk_mul_f16 v95, v158, v155 op_sel_hi:[0,1]
	v_pk_mul_f16 v96, v158, v156 op_sel_hi:[0,1]
	v_pk_mul_f16 v114, v159, v154 op_sel_hi:[0,1]
	v_pk_mul_f16 v115, v159, v155 op_sel_hi:[0,1]
	v_pk_mul_f16 v116, v159, v156 op_sel_hi:[0,1]
	v_pk_fma_f16 v89, v89, v157, v73
	v_pk_fma_f16 v86, v86, v154, v70
	v_pk_fma_f16 v113, v113, v157, v73
	v_pk_fma_f16 v110, v110, v154, v70
	v_pk_fma_f16 v73, v129, v157, v73
	v_pk_fma_f16 v70, v126, v154, v70
	v_pk_fma_f16 v118, v57, v157, v97
	v_pk_fma_f16 v126, v77, v157, v97
	v_pk_fma_f16 v97, v101, v157, v97
	v_pk_fma_f16 v130, v29, v157, v117
	v_pk_fma_f16 v161, v41, v157, v117
	v_pk_fma_f16 v117, v61, v157, v117
	v_pk_maximum3_f16 v157, v89, v113, v73
	v_pk_fma_f16 v88, v88, v156, v72
	v_pk_fma_f16 v87, v87, v155, v71
	v_pk_fma_f16 v112, v112, v156, v72
	v_pk_fma_f16 v111, v111, v155, v71
	v_pk_fma_f16 v72, v128, v156, v72
	v_pk_fma_f16 v71, v127, v155, v71
	v_pk_fma_f16 v119, v56, v156, v96
	v_pk_fma_f16 v120, v55, v155, v95
	v_pk_fma_f16 v121, v54, v154, v94
	v_pk_fma_f16 v127, v76, v156, v96
	v_pk_fma_f16 v128, v75, v155, v95
	v_pk_fma_f16 v129, v74, v154, v94
	v_pk_fma_f16 v96, v100, v156, v96
	v_pk_fma_f16 v95, v99, v155, v95
	v_pk_fma_f16 v94, v98, v154, v94
	v_pk_fma_f16 v131, v28, v156, v116
	v_pk_fma_f16 v132, v27, v155, v115
	v_pk_fma_f16 v133, v26, v154, v114
	v_pk_fma_f16 v162, v40, v156, v116
	v_pk_fma_f16 v163, v39, v155, v115
	v_pk_fma_f16 v164, v38, v154, v114
	v_pk_fma_f16 v116, v60, v156, v116
	v_pk_fma_f16 v115, v59, v155, v115
	v_pk_fma_f16 v114, v58, v154, v114
	v_pk_maximum3_f16 v154, v86, v110, v70
	v_pk_maximum3_f16 v155, v87, v111, v71
	v_pk_maximum3_f16 v156, v88, v112, v72
	v_pk_maximum3_f16 v206, v118, v126, v97
	v_pk_maximum3_f16 v210, v130, v161, v117
	v_pk_maximum3_f16 v165, v121, v129, v94
	v_pk_maximum3_f16 v200, v120, v128, v95
	v_pk_maximum3_f16 v201, v119, v127, v96
	v_pk_maximum3_f16 v207, v133, v164, v114
	v_pk_maximum3_f16 v208, v132, v163, v115
	v_pk_maximum3_f16 v157, v157, v206, v210
	v_pk_maximum3_f16 v209, v131, v162, v116
	v_pk_maximum3_f16 v154, v154, v165, v207
	v_pk_maximum3_f16 v155, v155, v200, v208
	v_pk_maximum3_f16 v156, v156, v201, v209
	v_pk_add_f16 v89, v89, v157 neg_lo:[0,1] neg_hi:[0,1]
	v_pk_add_f16 v86, v86, v154 neg_lo:[0,1] neg_hi:[0,1]
	v_pk_add_f16 v87, v87, v155 neg_lo:[0,1] neg_hi:[0,1]
	v_pk_add_f16 v88, v88, v156 neg_lo:[0,1] neg_hi:[0,1]
	v_pk_add_f16 v110, v110, v154 neg_lo:[0,1] neg_hi:[0,1]
	v_exp_f16_sdwa v165, v86 dst_sel:WORD_0 dst_unused:UNUSED_PAD src0_sel:WORD_0
	v_exp_f16_sdwa v200, v87 dst_sel:WORD_0 dst_unused:UNUSED_PAD src0_sel:WORD_0
	v_exp_f16_sdwa v201, v88 dst_sel:WORD_0 dst_unused:UNUSED_PAD src0_sel:WORD_0
	v_exp_f16_sdwa v206, v89 dst_sel:WORD_0 dst_unused:UNUSED_PAD src0_sel:WORD_0
	v_exp_f16_sdwa v165, v86 dst_sel:WORD_1 dst_unused:UNUSED_PRESERVE src0_sel:WORD_1
	v_exp_f16_sdwa v200, v87 dst_sel:WORD_1 dst_unused:UNUSED_PRESERVE src0_sel:WORD_1
	v_exp_f16_sdwa v201, v88 dst_sel:WORD_1 dst_unused:UNUSED_PRESERVE src0_sel:WORD_1
	v_exp_f16_sdwa v206, v89 dst_sel:WORD_1 dst_unused:UNUSED_PRESERVE src0_sel:WORD_1
	v_pk_add_f16 v111, v111, v155 neg_lo:[0,1] neg_hi:[0,1]
	v_pk_add_f16 v89, v165, 0
	v_pk_fma_f16 v45, v45, v206, 0
	v_pk_add_f16 v86, v206, 0
	v_pk_add_f16 v87, v201, 0
	v_pk_add_f16 v88, v200, 0
	v_pk_fma_f16 v44, v44, v201, 0
	v_pk_fma_f16 v43, v43, v200, 0
	v_pk_fma_f16 v42, v42, v165, 0
	v_pk_add_f16 v112, v112, v156 neg_lo:[0,1] neg_hi:[0,1]
	v_pk_add_f16 v113, v113, v157 neg_lo:[0,1] neg_hi:[0,1]
	v_exp_f16_sdwa v165, v110 dst_sel:WORD_0 dst_unused:UNUSED_PAD src0_sel:WORD_0
	v_exp_f16_sdwa v200, v111 dst_sel:WORD_0 dst_unused:UNUSED_PAD src0_sel:WORD_0
	v_exp_f16_sdwa v201, v112 dst_sel:WORD_0 dst_unused:UNUSED_PAD src0_sel:WORD_0
	v_exp_f16_sdwa v206, v113 dst_sel:WORD_0 dst_unused:UNUSED_PAD src0_sel:WORD_0
	v_exp_f16_sdwa v165, v110 dst_sel:WORD_1 dst_unused:UNUSED_PRESERVE src0_sel:WORD_1
	v_exp_f16_sdwa v200, v111 dst_sel:WORD_1 dst_unused:UNUSED_PRESERVE src0_sel:WORD_1
	v_exp_f16_sdwa v201, v112 dst_sel:WORD_1 dst_unused:UNUSED_PRESERVE src0_sel:WORD_1
	v_exp_f16_sdwa v206, v113 dst_sel:WORD_1 dst_unused:UNUSED_PRESERVE src0_sel:WORD_1
	v_pk_add_f16 v89, v89, v165
	v_pk_fma_f16 v45, v69, v206, v45
	v_pk_add_f16 v69, v73, v157 neg_lo:[0,1] neg_hi:[0,1]
	v_pk_add_f16 v88, v88, v200
	v_pk_add_f16 v87, v87, v201
	v_pk_add_f16 v86, v86, v206
	v_pk_fma_f16 v42, v66, v165, v42
	v_pk_fma_f16 v43, v67, v200, v43
	v_pk_fma_f16 v44, v68, v201, v44
	v_pk_add_f16 v66, v70, v154 neg_lo:[0,1] neg_hi:[0,1]
	v_pk_add_f16 v67, v71, v155 neg_lo:[0,1] neg_hi:[0,1]
	v_pk_add_f16 v68, v72, v156 neg_lo:[0,1] neg_hi:[0,1]
	v_exp_f16_sdwa v70, v66 dst_sel:WORD_0 dst_unused:UNUSED_PAD src0_sel:WORD_0
	v_exp_f16_sdwa v71, v67 dst_sel:WORD_0 dst_unused:UNUSED_PAD src0_sel:WORD_0
	v_exp_f16_sdwa v72, v68 dst_sel:WORD_0 dst_unused:UNUSED_PAD src0_sel:WORD_0
	v_exp_f16_sdwa v73, v69 dst_sel:WORD_0 dst_unused:UNUSED_PAD src0_sel:WORD_0
	v_exp_f16_sdwa v70, v66 dst_sel:WORD_1 dst_unused:UNUSED_PRESERVE src0_sel:WORD_1
	v_exp_f16_sdwa v71, v67 dst_sel:WORD_1 dst_unused:UNUSED_PRESERVE src0_sel:WORD_1
	v_exp_f16_sdwa v72, v68 dst_sel:WORD_1 dst_unused:UNUSED_PRESERVE src0_sel:WORD_1
	v_exp_f16_sdwa v73, v69 dst_sel:WORD_1 dst_unused:UNUSED_PRESERVE src0_sel:WORD_1
	v_pk_add_f16 v69, v89, v70
	v_pk_add_f16 v66, v86, v73
	v_pk_add_f16 v67, v87, v72
	v_pk_add_f16 v68, v88, v71
	v_pk_fma_f16 v45, v93, v73, v45
	v_pk_fma_f16 v44, v92, v72, v44
	v_pk_fma_f16 v43, v91, v71, v43
	v_pk_fma_f16 v42, v90, v70, v42
	v_pk_add_f16 v70, v121, v154 neg_lo:[0,1] neg_hi:[0,1]
	v_pk_add_f16 v71, v120, v155 neg_lo:[0,1] neg_hi:[0,1]
	v_pk_add_f16 v72, v119, v156 neg_lo:[0,1] neg_hi:[0,1]
	v_pk_add_f16 v73, v118, v157 neg_lo:[0,1] neg_hi:[0,1]
	v_exp_f16_sdwa v86, v70 dst_sel:WORD_0 dst_unused:UNUSED_PAD src0_sel:WORD_0
	v_exp_f16_sdwa v87, v71 dst_sel:WORD_0 dst_unused:UNUSED_PAD src0_sel:WORD_0
	v_exp_f16_sdwa v88, v72 dst_sel:WORD_0 dst_unused:UNUSED_PAD src0_sel:WORD_0
	v_exp_f16_sdwa v89, v73 dst_sel:WORD_0 dst_unused:UNUSED_PAD src0_sel:WORD_0
	v_exp_f16_sdwa v86, v70 dst_sel:WORD_1 dst_unused:UNUSED_PRESERVE src0_sel:WORD_1
	v_exp_f16_sdwa v87, v71 dst_sel:WORD_1 dst_unused:UNUSED_PRESERVE src0_sel:WORD_1
	v_exp_f16_sdwa v88, v72 dst_sel:WORD_1 dst_unused:UNUSED_PRESERVE src0_sel:WORD_1
	v_exp_f16_sdwa v89, v73 dst_sel:WORD_1 dst_unused:UNUSED_PRESERVE src0_sel:WORD_1
	v_pk_add_f16 v70, v129, v154 neg_lo:[0,1] neg_hi:[0,1]
	v_pk_add_f16 v69, v69, v86
	v_pk_add_f16 v68, v68, v87
	v_pk_add_f16 v67, v67, v88
	v_pk_add_f16 v66, v66, v89
	v_pk_fma_f16 v42, v22, v86, v42
	v_pk_fma_f16 v43, v23, v87, v43
	v_pk_fma_f16 v44, v24, v88, v44
	v_pk_fma_f16 v45, v25, v89, v45
	v_pk_add_f16 v71, v128, v155 neg_lo:[0,1] neg_hi:[0,1]
	v_pk_add_f16 v72, v127, v156 neg_lo:[0,1] neg_hi:[0,1]
	v_pk_add_f16 v73, v126, v157 neg_lo:[0,1] neg_hi:[0,1]
	v_exp_f16_sdwa v86, v70 dst_sel:WORD_0 dst_unused:UNUSED_PAD src0_sel:WORD_0
	v_exp_f16_sdwa v87, v71 dst_sel:WORD_0 dst_unused:UNUSED_PAD src0_sel:WORD_0
	v_exp_f16_sdwa v88, v72 dst_sel:WORD_0 dst_unused:UNUSED_PAD src0_sel:WORD_0
	v_exp_f16_sdwa v89, v73 dst_sel:WORD_0 dst_unused:UNUSED_PAD src0_sel:WORD_0
	v_exp_f16_sdwa v86, v70 dst_sel:WORD_1 dst_unused:UNUSED_PRESERVE src0_sel:WORD_1
	v_exp_f16_sdwa v87, v71 dst_sel:WORD_1 dst_unused:UNUSED_PRESERVE src0_sel:WORD_1
	v_exp_f16_sdwa v88, v72 dst_sel:WORD_1 dst_unused:UNUSED_PRESERVE src0_sel:WORD_1
	v_exp_f16_sdwa v89, v73 dst_sel:WORD_1 dst_unused:UNUSED_PRESERVE src0_sel:WORD_1
	v_pk_add_f16 v70, v94, v154 neg_lo:[0,1] neg_hi:[0,1]
	v_pk_add_f16 v69, v69, v86
	v_pk_add_f16 v66, v66, v89
	v_pk_add_f16 v67, v67, v88
	v_pk_add_f16 v68, v68, v87
	v_pk_fma_f16 v45, v37, v89, v45
	v_pk_fma_f16 v44, v36, v88, v44
	v_pk_fma_f16 v43, v35, v87, v43
	v_pk_fma_f16 v42, v34, v86, v42
	v_pk_add_f16 v71, v95, v155 neg_lo:[0,1] neg_hi:[0,1]
	v_pk_add_f16 v72, v96, v156 neg_lo:[0,1] neg_hi:[0,1]
	v_pk_add_f16 v73, v97, v157 neg_lo:[0,1] neg_hi:[0,1]
	v_exp_f16_sdwa v86, v70 dst_sel:WORD_0 dst_unused:UNUSED_PAD src0_sel:WORD_0
	v_exp_f16_sdwa v87, v71 dst_sel:WORD_0 dst_unused:UNUSED_PAD src0_sel:WORD_0
	v_exp_f16_sdwa v88, v72 dst_sel:WORD_0 dst_unused:UNUSED_PAD src0_sel:WORD_0
	v_exp_f16_sdwa v89, v73 dst_sel:WORD_0 dst_unused:UNUSED_PAD src0_sel:WORD_0
	v_exp_f16_sdwa v86, v70 dst_sel:WORD_1 dst_unused:UNUSED_PRESERVE src0_sel:WORD_1
	v_exp_f16_sdwa v87, v71 dst_sel:WORD_1 dst_unused:UNUSED_PRESERVE src0_sel:WORD_1
	v_exp_f16_sdwa v88, v72 dst_sel:WORD_1 dst_unused:UNUSED_PRESERVE src0_sel:WORD_1
	v_exp_f16_sdwa v89, v73 dst_sel:WORD_1 dst_unused:UNUSED_PRESERVE src0_sel:WORD_1
	v_pk_add_f16 v70, v133, v154 neg_lo:[0,1] neg_hi:[0,1]
	v_pk_add_f16 v69, v69, v86
	v_pk_add_f16 v68, v68, v87
	v_pk_add_f16 v67, v67, v88
	v_pk_add_f16 v66, v66, v89
	v_pk_fma_f16 v42, v50, v86, v42
	v_pk_fma_f16 v43, v51, v87, v43
	v_pk_fma_f16 v44, v52, v88, v44
	v_pk_fma_f16 v45, v53, v89, v45
	v_pk_add_f16 v71, v132, v155 neg_lo:[0,1] neg_hi:[0,1]
	v_pk_add_f16 v72, v131, v156 neg_lo:[0,1] neg_hi:[0,1]
	v_pk_add_f16 v73, v130, v157 neg_lo:[0,1] neg_hi:[0,1]
	v_exp_f16_sdwa v86, v70 dst_sel:WORD_0 dst_unused:UNUSED_PAD src0_sel:WORD_0
	v_exp_f16_sdwa v87, v71 dst_sel:WORD_0 dst_unused:UNUSED_PAD src0_sel:WORD_0
	v_exp_f16_sdwa v88, v72 dst_sel:WORD_0 dst_unused:UNUSED_PAD src0_sel:WORD_0
	v_exp_f16_sdwa v89, v73 dst_sel:WORD_0 dst_unused:UNUSED_PAD src0_sel:WORD_0
	v_exp_f16_sdwa v86, v70 dst_sel:WORD_1 dst_unused:UNUSED_PRESERVE src0_sel:WORD_1
	v_exp_f16_sdwa v87, v71 dst_sel:WORD_1 dst_unused:UNUSED_PRESERVE src0_sel:WORD_1
	v_exp_f16_sdwa v88, v72 dst_sel:WORD_1 dst_unused:UNUSED_PRESERVE src0_sel:WORD_1
	v_exp_f16_sdwa v89, v73 dst_sel:WORD_1 dst_unused:UNUSED_PRESERVE src0_sel:WORD_1
	v_pk_add_f16 v70, v164, v154 neg_lo:[0,1] neg_hi:[0,1]
	v_pk_add_f16 v69, v69, v86
	v_pk_add_f16 v66, v66, v89
	v_pk_add_f16 v67, v67, v88
	v_pk_add_f16 v68, v68, v87
	v_pk_fma_f16 v45, v13, v89, v45
	v_pk_fma_f16 v44, v12, v88, v44
	v_pk_fma_f16 v43, v11, v87, v43
	v_pk_fma_f16 v42, v10, v86, v42
	v_pk_add_f16 v71, v163, v155 neg_lo:[0,1] neg_hi:[0,1]
	v_pk_add_f16 v72, v162, v156 neg_lo:[0,1] neg_hi:[0,1]
	v_pk_add_f16 v73, v161, v157 neg_lo:[0,1] neg_hi:[0,1]
	v_exp_f16_sdwa v86, v70 dst_sel:WORD_0 dst_unused:UNUSED_PAD src0_sel:WORD_0
	v_exp_f16_sdwa v87, v71 dst_sel:WORD_0 dst_unused:UNUSED_PAD src0_sel:WORD_0
	v_exp_f16_sdwa v88, v72 dst_sel:WORD_0 dst_unused:UNUSED_PAD src0_sel:WORD_0
	v_exp_f16_sdwa v89, v73 dst_sel:WORD_0 dst_unused:UNUSED_PAD src0_sel:WORD_0
	v_exp_f16_sdwa v86, v70 dst_sel:WORD_1 dst_unused:UNUSED_PRESERVE src0_sel:WORD_1
	v_exp_f16_sdwa v87, v71 dst_sel:WORD_1 dst_unused:UNUSED_PRESERVE src0_sel:WORD_1
	v_exp_f16_sdwa v88, v72 dst_sel:WORD_1 dst_unused:UNUSED_PRESERVE src0_sel:WORD_1
	v_exp_f16_sdwa v89, v73 dst_sel:WORD_1 dst_unused:UNUSED_PRESERVE src0_sel:WORD_1
	v_pk_add_f16 v70, v114, v154 neg_lo:[0,1] neg_hi:[0,1]
	v_pk_add_f16 v69, v69, v86
	v_pk_add_f16 v68, v68, v87
	v_pk_add_f16 v67, v67, v88
	v_pk_add_f16 v66, v66, v89
	v_pk_fma_f16 v42, v14, v86, v42
	v_pk_fma_f16 v43, v15, v87, v43
	v_pk_fma_f16 v44, v16, v88, v44
	v_pk_fma_f16 v45, v17, v89, v45
	v_pk_add_f16 v71, v115, v155 neg_lo:[0,1] neg_hi:[0,1]
	v_pk_add_f16 v72, v116, v156 neg_lo:[0,1] neg_hi:[0,1]
	v_pk_add_f16 v73, v117, v157 neg_lo:[0,1] neg_hi:[0,1]
	v_exp_f16_sdwa v86, v70 dst_sel:WORD_0 dst_unused:UNUSED_PAD src0_sel:WORD_0
	v_exp_f16_sdwa v87, v71 dst_sel:WORD_0 dst_unused:UNUSED_PAD src0_sel:WORD_0
	v_exp_f16_sdwa v88, v72 dst_sel:WORD_0 dst_unused:UNUSED_PAD src0_sel:WORD_0
	v_exp_f16_sdwa v89, v73 dst_sel:WORD_0 dst_unused:UNUSED_PAD src0_sel:WORD_0
	v_exp_f16_sdwa v86, v70 dst_sel:WORD_1 dst_unused:UNUSED_PRESERVE src0_sel:WORD_1
	v_exp_f16_sdwa v87, v71 dst_sel:WORD_1 dst_unused:UNUSED_PRESERVE src0_sel:WORD_1
	v_exp_f16_sdwa v88, v72 dst_sel:WORD_1 dst_unused:UNUSED_PRESERVE src0_sel:WORD_1
	v_exp_f16_sdwa v89, v73 dst_sel:WORD_1 dst_unused:UNUSED_PRESERVE src0_sel:WORD_1
	v_pk_add_f16 v69, v69, v86
	v_pk_add_f16 v68, v68, v87
	v_rcp_f16_e32 v70, v69
	v_rcp_f16_sdwa v69, v69 dst_sel:DWORD dst_unused:UNUSED_PAD src0_sel:WORD_1
	v_pk_add_f16 v67, v67, v88
	v_rcp_f16_e32 v71, v68
	v_rcp_f16_sdwa v68, v68 dst_sel:DWORD dst_unused:UNUSED_PAD src0_sel:WORD_1
	v_pk_add_f16 v66, v66, v89
	v_rcp_f16_e32 v72, v67
	v_rcp_f16_sdwa v67, v67 dst_sel:DWORD dst_unused:UNUSED_PAD src0_sel:WORD_1
	v_rcp_f16_e32 v73, v66
	v_rcp_f16_sdwa v66, v66 dst_sel:DWORD dst_unused:UNUSED_PAD src0_sel:WORD_1
	v_pk_fma_f16 v42, v18, v86, v42
	v_pack_b32_f16 v69, v70, v69
	v_pk_fma_f16 v43, v19, v87, v43
	v_pk_mul_f16 v97, v42, v69
	v_pack_b32_f16 v42, v71, v68
	v_pk_fma_f16 v44, v20, v88, v44
	v_pk_mul_f16 v96, v43, v42
	v_pack_b32_f16 v42, v72, v67
	v_pk_fma_f16 v45, v21, v89, v45
	v_pk_mul_f16 v95, v44, v42
	v_pack_b32_f16 v42, v73, v66
	v_pk_mul_f16 v94, v45, v42
	s_waitcnt vmcnt(6)
	v_pk_mul_f16 v45, v160, v153 op_sel_hi:[0,1]
	v_pk_mul_f16 v42, v160, v150 op_sel_hi:[0,1]
	v_pk_mul_f16 v43, v160, v151 op_sel_hi:[0,1]
	v_pk_mul_f16 v44, v160, v152 op_sel_hi:[0,1]
	v_pk_mul_f16 v69, v158, v153 op_sel_hi:[0,1]
	v_pk_mul_f16 v73, v159, v153 op_sel_hi:[0,1]
	v_pk_fma_f16 v57, v57, v153, v45
	v_pk_fma_f16 v77, v77, v153, v45
	v_pk_fma_f16 v45, v101, v153, v45
	v_pk_mul_f16 v66, v158, v150 op_sel_hi:[0,1]
	v_pk_maximum3_f16 v117, v57, v77, v45
	v_pk_mul_f16 v67, v158, v151 op_sel_hi:[0,1]
	v_pk_mul_f16 v68, v158, v152 op_sel_hi:[0,1]
	v_pk_mul_f16 v70, v159, v150 op_sel_hi:[0,1]
	v_pk_mul_f16 v71, v159, v151 op_sel_hi:[0,1]
	v_pk_mul_f16 v72, v159, v152 op_sel_hi:[0,1]
	v_pk_fma_f16 v56, v56, v152, v44
	v_pk_fma_f16 v55, v55, v151, v43
	v_pk_fma_f16 v54, v54, v150, v42
	v_pk_fma_f16 v76, v76, v152, v44
	v_pk_fma_f16 v75, v75, v151, v43
	v_pk_fma_f16 v74, v74, v150, v42
	v_pk_fma_f16 v44, v100, v152, v44
	v_pk_fma_f16 v43, v99, v151, v43
	v_pk_fma_f16 v42, v98, v150, v42
	v_pk_fma_f16 v86, v29, v153, v69
	v_pk_fma_f16 v90, v41, v153, v69
	v_pk_fma_f16 v69, v61, v153, v69
	v_pk_fma_f16 v98, v81, v153, v73
	v_pk_fma_f16 v110, v109, v153, v73
	v_pk_fma_f16 v73, v125, v153, v73
	v_pk_maximum3_f16 v114, v54, v74, v42
	v_pk_maximum3_f16 v115, v55, v75, v43
	v_pk_maximum3_f16 v116, v56, v76, v44
	v_pk_maximum3_f16 v121, v86, v90, v69
	v_pk_fma_f16 v87, v28, v152, v68
	v_pk_maximum3_f16 v129, v98, v110, v73
	v_pk_fma_f16 v88, v27, v151, v67
	v_pk_maximum3_f16 v117, v117, v121, v129
	v_pk_fma_f16 v89, v26, v150, v66
	v_pk_fma_f16 v91, v40, v152, v68
	v_pk_fma_f16 v92, v39, v151, v67
	v_pk_fma_f16 v93, v38, v150, v66
	v_pk_fma_f16 v68, v60, v152, v68
	v_pk_fma_f16 v67, v59, v151, v67
	v_pk_fma_f16 v66, v58, v150, v66
	v_pk_fma_f16 v99, v80, v152, v72
	v_pk_fma_f16 v100, v79, v151, v71
	v_pk_fma_f16 v101, v78, v150, v70
	v_pk_fma_f16 v111, v108, v152, v72
	v_pk_fma_f16 v112, v107, v151, v71
	v_pk_fma_f16 v113, v106, v150, v70
	v_pk_fma_f16 v72, v124, v152, v72
	v_pk_fma_f16 v71, v123, v151, v71
	v_pk_fma_f16 v70, v122, v150, v70
	v_pk_maximum3_f16 v118, v89, v93, v66
	v_pk_maximum3_f16 v119, v88, v92, v67
	v_pk_maximum3_f16 v120, v87, v91, v68
	v_pk_maximum3_f16 v127, v100, v112, v71
	v_pk_maximum3_f16 v128, v99, v111, v72
	v_pk_maximum3_f16 v126, v101, v113, v70
	v_pk_maximum3_f16 v114, v114, v118, v126
	v_pk_maximum3_f16 v115, v115, v119, v127
	v_pk_maximum3_f16 v116, v116, v120, v128
	v_pk_add_f16 v57, v57, v117 neg_lo:[0,1] neg_hi:[0,1]
	v_pk_add_f16 v54, v54, v114 neg_lo:[0,1] neg_hi:[0,1]
	v_pk_add_f16 v55, v55, v115 neg_lo:[0,1] neg_hi:[0,1]
	v_pk_add_f16 v56, v56, v116 neg_lo:[0,1] neg_hi:[0,1]
	v_pk_add_f16 v74, v74, v114 neg_lo:[0,1] neg_hi:[0,1]
	v_exp_f16_sdwa v118, v54 dst_sel:WORD_0 dst_unused:UNUSED_PAD src0_sel:WORD_0
	v_exp_f16_sdwa v119, v55 dst_sel:WORD_0 dst_unused:UNUSED_PAD src0_sel:WORD_0
	v_exp_f16_sdwa v120, v56 dst_sel:WORD_0 dst_unused:UNUSED_PAD src0_sel:WORD_0
	v_exp_f16_sdwa v121, v57 dst_sel:WORD_0 dst_unused:UNUSED_PAD src0_sel:WORD_0
	v_exp_f16_sdwa v118, v54 dst_sel:WORD_1 dst_unused:UNUSED_PRESERVE src0_sel:WORD_1
	v_exp_f16_sdwa v119, v55 dst_sel:WORD_1 dst_unused:UNUSED_PRESERVE src0_sel:WORD_1
	v_exp_f16_sdwa v120, v56 dst_sel:WORD_1 dst_unused:UNUSED_PRESERVE src0_sel:WORD_1
	v_exp_f16_sdwa v121, v57 dst_sel:WORD_1 dst_unused:UNUSED_PRESERVE src0_sel:WORD_1
	v_pk_add_f16 v75, v75, v115 neg_lo:[0,1] neg_hi:[0,1]
	v_pk_add_f16 v57, v118, 0
	v_pk_fma_f16 v25, v25, v121, 0
	v_pk_add_f16 v54, v121, 0
	v_pk_add_f16 v55, v120, 0
	v_pk_add_f16 v56, v119, 0
	v_pk_fma_f16 v24, v24, v120, 0
	v_pk_fma_f16 v23, v23, v119, 0
	v_pk_fma_f16 v22, v22, v118, 0
	v_pk_add_f16 v76, v76, v116 neg_lo:[0,1] neg_hi:[0,1]
	v_pk_add_f16 v77, v77, v117 neg_lo:[0,1] neg_hi:[0,1]
	v_exp_f16_sdwa v118, v74 dst_sel:WORD_0 dst_unused:UNUSED_PAD src0_sel:WORD_0
	v_exp_f16_sdwa v119, v75 dst_sel:WORD_0 dst_unused:UNUSED_PAD src0_sel:WORD_0
	v_exp_f16_sdwa v120, v76 dst_sel:WORD_0 dst_unused:UNUSED_PAD src0_sel:WORD_0
	v_exp_f16_sdwa v121, v77 dst_sel:WORD_0 dst_unused:UNUSED_PAD src0_sel:WORD_0
	v_exp_f16_sdwa v118, v74 dst_sel:WORD_1 dst_unused:UNUSED_PRESERVE src0_sel:WORD_1
	v_exp_f16_sdwa v119, v75 dst_sel:WORD_1 dst_unused:UNUSED_PRESERVE src0_sel:WORD_1
	v_exp_f16_sdwa v120, v76 dst_sel:WORD_1 dst_unused:UNUSED_PRESERVE src0_sel:WORD_1
	v_exp_f16_sdwa v121, v77 dst_sel:WORD_1 dst_unused:UNUSED_PRESERVE src0_sel:WORD_1
	v_pk_add_f16 v57, v57, v118
	v_pk_fma_f16 v25, v37, v121, v25
	v_pk_add_f16 v37, v45, v117 neg_lo:[0,1] neg_hi:[0,1]
	v_pk_add_f16 v56, v56, v119
	v_pk_add_f16 v55, v55, v120
	v_pk_add_f16 v54, v54, v121
	v_pk_fma_f16 v22, v34, v118, v22
	v_pk_fma_f16 v23, v35, v119, v23
	v_pk_fma_f16 v24, v36, v120, v24
	v_pk_add_f16 v34, v42, v114 neg_lo:[0,1] neg_hi:[0,1]
	v_pk_add_f16 v35, v43, v115 neg_lo:[0,1] neg_hi:[0,1]
	v_pk_add_f16 v36, v44, v116 neg_lo:[0,1] neg_hi:[0,1]
	v_exp_f16_sdwa v42, v34 dst_sel:WORD_0 dst_unused:UNUSED_PAD src0_sel:WORD_0
	v_exp_f16_sdwa v43, v35 dst_sel:WORD_0 dst_unused:UNUSED_PAD src0_sel:WORD_0
	v_exp_f16_sdwa v44, v36 dst_sel:WORD_0 dst_unused:UNUSED_PAD src0_sel:WORD_0
	v_exp_f16_sdwa v45, v37 dst_sel:WORD_0 dst_unused:UNUSED_PAD src0_sel:WORD_0
	v_exp_f16_sdwa v42, v34 dst_sel:WORD_1 dst_unused:UNUSED_PRESERVE src0_sel:WORD_1
	v_exp_f16_sdwa v43, v35 dst_sel:WORD_1 dst_unused:UNUSED_PRESERVE src0_sel:WORD_1
	v_exp_f16_sdwa v44, v36 dst_sel:WORD_1 dst_unused:UNUSED_PRESERVE src0_sel:WORD_1
	v_exp_f16_sdwa v45, v37 dst_sel:WORD_1 dst_unused:UNUSED_PRESERVE src0_sel:WORD_1
	v_pk_add_f16 v37, v57, v42
	v_pk_add_f16 v34, v54, v45
	v_pk_add_f16 v35, v55, v44
	v_pk_add_f16 v36, v56, v43
	v_pk_fma_f16 v25, v53, v45, v25
	v_pk_fma_f16 v24, v52, v44, v24
	v_pk_fma_f16 v23, v51, v43, v23
	v_pk_fma_f16 v22, v50, v42, v22
	v_pk_add_f16 v42, v89, v114 neg_lo:[0,1] neg_hi:[0,1]
	v_pk_add_f16 v43, v88, v115 neg_lo:[0,1] neg_hi:[0,1]
	v_pk_add_f16 v44, v87, v116 neg_lo:[0,1] neg_hi:[0,1]
	v_pk_add_f16 v45, v86, v117 neg_lo:[0,1] neg_hi:[0,1]
	v_exp_f16_sdwa v50, v42 dst_sel:WORD_0 dst_unused:UNUSED_PAD src0_sel:WORD_0
	v_exp_f16_sdwa v51, v43 dst_sel:WORD_0 dst_unused:UNUSED_PAD src0_sel:WORD_0
	v_exp_f16_sdwa v52, v44 dst_sel:WORD_0 dst_unused:UNUSED_PAD src0_sel:WORD_0
	v_exp_f16_sdwa v53, v45 dst_sel:WORD_0 dst_unused:UNUSED_PAD src0_sel:WORD_0
	v_exp_f16_sdwa v50, v42 dst_sel:WORD_1 dst_unused:UNUSED_PRESERVE src0_sel:WORD_1
	v_exp_f16_sdwa v51, v43 dst_sel:WORD_1 dst_unused:UNUSED_PRESERVE src0_sel:WORD_1
	v_exp_f16_sdwa v52, v44 dst_sel:WORD_1 dst_unused:UNUSED_PRESERVE src0_sel:WORD_1
	v_exp_f16_sdwa v53, v45 dst_sel:WORD_1 dst_unused:UNUSED_PRESERVE src0_sel:WORD_1
	v_pk_add_f16 v42, v93, v114 neg_lo:[0,1] neg_hi:[0,1]
	v_pk_add_f16 v37, v37, v50
	v_pk_add_f16 v36, v36, v51
	v_pk_add_f16 v35, v35, v52
	v_pk_add_f16 v34, v34, v53
	v_pk_fma_f16 v22, v10, v50, v22
	v_pk_fma_f16 v23, v11, v51, v23
	v_pk_fma_f16 v24, v12, v52, v24
	v_pk_fma_f16 v25, v13, v53, v25
	v_pk_add_f16 v43, v92, v115 neg_lo:[0,1] neg_hi:[0,1]
	v_pk_add_f16 v44, v91, v116 neg_lo:[0,1] neg_hi:[0,1]
	v_pk_add_f16 v45, v90, v117 neg_lo:[0,1] neg_hi:[0,1]
	v_exp_f16_sdwa v50, v42 dst_sel:WORD_0 dst_unused:UNUSED_PAD src0_sel:WORD_0
	v_exp_f16_sdwa v51, v43 dst_sel:WORD_0 dst_unused:UNUSED_PAD src0_sel:WORD_0
	v_exp_f16_sdwa v52, v44 dst_sel:WORD_0 dst_unused:UNUSED_PAD src0_sel:WORD_0
	v_exp_f16_sdwa v53, v45 dst_sel:WORD_0 dst_unused:UNUSED_PAD src0_sel:WORD_0
	v_exp_f16_sdwa v50, v42 dst_sel:WORD_1 dst_unused:UNUSED_PRESERVE src0_sel:WORD_1
	v_exp_f16_sdwa v51, v43 dst_sel:WORD_1 dst_unused:UNUSED_PRESERVE src0_sel:WORD_1
	v_exp_f16_sdwa v52, v44 dst_sel:WORD_1 dst_unused:UNUSED_PRESERVE src0_sel:WORD_1
	v_exp_f16_sdwa v53, v45 dst_sel:WORD_1 dst_unused:UNUSED_PRESERVE src0_sel:WORD_1
	v_pk_add_f16 v42, v66, v114 neg_lo:[0,1] neg_hi:[0,1]
	v_pk_add_f16 v37, v37, v50
	v_pk_add_f16 v34, v34, v53
	v_pk_add_f16 v35, v35, v52
	v_pk_add_f16 v36, v36, v51
	v_pk_fma_f16 v25, v17, v53, v25
	v_pk_fma_f16 v24, v16, v52, v24
	v_pk_fma_f16 v23, v15, v51, v23
	v_pk_fma_f16 v22, v14, v50, v22
	v_pk_add_f16 v43, v67, v115 neg_lo:[0,1] neg_hi:[0,1]
	v_pk_add_f16 v44, v68, v116 neg_lo:[0,1] neg_hi:[0,1]
	v_pk_add_f16 v45, v69, v117 neg_lo:[0,1] neg_hi:[0,1]
	v_exp_f16_sdwa v50, v42 dst_sel:WORD_0 dst_unused:UNUSED_PAD src0_sel:WORD_0
	v_exp_f16_sdwa v51, v43 dst_sel:WORD_0 dst_unused:UNUSED_PAD src0_sel:WORD_0
	v_exp_f16_sdwa v52, v44 dst_sel:WORD_0 dst_unused:UNUSED_PAD src0_sel:WORD_0
	v_exp_f16_sdwa v53, v45 dst_sel:WORD_0 dst_unused:UNUSED_PAD src0_sel:WORD_0
	v_exp_f16_sdwa v50, v42 dst_sel:WORD_1 dst_unused:UNUSED_PRESERVE src0_sel:WORD_1
	v_exp_f16_sdwa v51, v43 dst_sel:WORD_1 dst_unused:UNUSED_PRESERVE src0_sel:WORD_1
	v_exp_f16_sdwa v52, v44 dst_sel:WORD_1 dst_unused:UNUSED_PRESERVE src0_sel:WORD_1
	v_exp_f16_sdwa v53, v45 dst_sel:WORD_1 dst_unused:UNUSED_PRESERVE src0_sel:WORD_1
	v_pk_add_f16 v42, v101, v114 neg_lo:[0,1] neg_hi:[0,1]
	v_pk_add_f16 v37, v37, v50
	v_pk_add_f16 v36, v36, v51
	v_pk_add_f16 v35, v35, v52
	v_pk_add_f16 v34, v34, v53
	v_pk_fma_f16 v22, v18, v50, v22
	v_pk_fma_f16 v23, v19, v51, v23
	v_pk_fma_f16 v24, v20, v52, v24
	v_pk_fma_f16 v25, v21, v53, v25
	v_pk_add_f16 v43, v100, v115 neg_lo:[0,1] neg_hi:[0,1]
	v_pk_add_f16 v44, v99, v116 neg_lo:[0,1] neg_hi:[0,1]
	v_pk_add_f16 v45, v98, v117 neg_lo:[0,1] neg_hi:[0,1]
	v_exp_f16_sdwa v50, v42 dst_sel:WORD_0 dst_unused:UNUSED_PAD src0_sel:WORD_0
	v_exp_f16_sdwa v51, v43 dst_sel:WORD_0 dst_unused:UNUSED_PAD src0_sel:WORD_0
	v_exp_f16_sdwa v52, v44 dst_sel:WORD_0 dst_unused:UNUSED_PAD src0_sel:WORD_0
	v_exp_f16_sdwa v53, v45 dst_sel:WORD_0 dst_unused:UNUSED_PAD src0_sel:WORD_0
	v_exp_f16_sdwa v50, v42 dst_sel:WORD_1 dst_unused:UNUSED_PRESERVE src0_sel:WORD_1
	v_exp_f16_sdwa v51, v43 dst_sel:WORD_1 dst_unused:UNUSED_PRESERVE src0_sel:WORD_1
	v_exp_f16_sdwa v52, v44 dst_sel:WORD_1 dst_unused:UNUSED_PRESERVE src0_sel:WORD_1
	v_exp_f16_sdwa v53, v45 dst_sel:WORD_1 dst_unused:UNUSED_PRESERVE src0_sel:WORD_1
	v_pk_add_f16 v42, v113, v114 neg_lo:[0,1] neg_hi:[0,1]
	v_pk_add_f16 v37, v37, v50
	v_pk_add_f16 v34, v34, v53
	v_pk_add_f16 v35, v35, v52
	v_pk_add_f16 v36, v36, v51
	v_pk_fma_f16 v25, v33, v53, v25
	v_pk_fma_f16 v24, v32, v52, v24
	v_pk_fma_f16 v23, v31, v51, v23
	v_pk_fma_f16 v22, v30, v50, v22
	v_pk_add_f16 v43, v112, v115 neg_lo:[0,1] neg_hi:[0,1]
	v_pk_add_f16 v44, v111, v116 neg_lo:[0,1] neg_hi:[0,1]
	v_pk_add_f16 v45, v110, v117 neg_lo:[0,1] neg_hi:[0,1]
	v_exp_f16_sdwa v50, v42 dst_sel:WORD_0 dst_unused:UNUSED_PAD src0_sel:WORD_0
	v_exp_f16_sdwa v51, v43 dst_sel:WORD_0 dst_unused:UNUSED_PAD src0_sel:WORD_0
	v_exp_f16_sdwa v52, v44 dst_sel:WORD_0 dst_unused:UNUSED_PAD src0_sel:WORD_0
	v_exp_f16_sdwa v53, v45 dst_sel:WORD_0 dst_unused:UNUSED_PAD src0_sel:WORD_0
	v_exp_f16_sdwa v50, v42 dst_sel:WORD_1 dst_unused:UNUSED_PRESERVE src0_sel:WORD_1
	v_exp_f16_sdwa v51, v43 dst_sel:WORD_1 dst_unused:UNUSED_PRESERVE src0_sel:WORD_1
	v_exp_f16_sdwa v52, v44 dst_sel:WORD_1 dst_unused:UNUSED_PRESERVE src0_sel:WORD_1
	v_exp_f16_sdwa v53, v45 dst_sel:WORD_1 dst_unused:UNUSED_PRESERVE src0_sel:WORD_1
	v_pk_add_f16 v42, v70, v114 neg_lo:[0,1] neg_hi:[0,1]
	v_pk_add_f16 v37, v37, v50
	v_pk_add_f16 v36, v36, v51
	v_pk_add_f16 v35, v35, v52
	v_pk_add_f16 v34, v34, v53
	v_pk_fma_f16 v22, v46, v50, v22
	v_pk_fma_f16 v23, v47, v51, v23
	v_pk_fma_f16 v24, v48, v52, v24
	v_pk_fma_f16 v25, v49, v53, v25
	v_pk_add_f16 v43, v71, v115 neg_lo:[0,1] neg_hi:[0,1]
	v_pk_add_f16 v44, v72, v116 neg_lo:[0,1] neg_hi:[0,1]
	v_pk_add_f16 v45, v73, v117 neg_lo:[0,1] neg_hi:[0,1]
	v_exp_f16_sdwa v50, v42 dst_sel:WORD_0 dst_unused:UNUSED_PAD src0_sel:WORD_0
	v_exp_f16_sdwa v51, v43 dst_sel:WORD_0 dst_unused:UNUSED_PAD src0_sel:WORD_0
	v_exp_f16_sdwa v52, v44 dst_sel:WORD_0 dst_unused:UNUSED_PAD src0_sel:WORD_0
	v_exp_f16_sdwa v53, v45 dst_sel:WORD_0 dst_unused:UNUSED_PAD src0_sel:WORD_0
	v_exp_f16_sdwa v50, v42 dst_sel:WORD_1 dst_unused:UNUSED_PRESERVE src0_sel:WORD_1
	v_exp_f16_sdwa v51, v43 dst_sel:WORD_1 dst_unused:UNUSED_PRESERVE src0_sel:WORD_1
	v_exp_f16_sdwa v52, v44 dst_sel:WORD_1 dst_unused:UNUSED_PRESERVE src0_sel:WORD_1
	v_exp_f16_sdwa v53, v45 dst_sel:WORD_1 dst_unused:UNUSED_PRESERVE src0_sel:WORD_1
	v_pk_add_f16 v37, v37, v50
	v_pk_add_f16 v36, v36, v51
	v_rcp_f16_e32 v42, v37
	v_rcp_f16_sdwa v37, v37 dst_sel:DWORD dst_unused:UNUSED_PAD src0_sel:WORD_1
	v_pk_add_f16 v35, v35, v52
	v_rcp_f16_e32 v43, v36
	v_rcp_f16_sdwa v36, v36 dst_sel:DWORD dst_unused:UNUSED_PAD src0_sel:WORD_1
	v_pk_add_f16 v34, v34, v53
	v_pk_fma_f16 v22, v62, v50, v22
	v_rcp_f16_e32 v50, v35
	v_rcp_f16_sdwa v35, v35 dst_sel:DWORD dst_unused:UNUSED_PAD src0_sel:WORD_1
	v_pk_fma_f16 v23, v63, v51, v23
	v_rcp_f16_e32 v51, v34
	v_rcp_f16_sdwa v34, v34 dst_sel:DWORD dst_unused:UNUSED_PAD src0_sel:WORD_1
	v_pack_b32_f16 v37, v42, v37
	v_pk_mul_f16 v45, v22, v37
	v_pack_b32_f16 v22, v43, v36
	v_pk_fma_f16 v24, v64, v52, v24
	v_pk_mul_f16 v44, v23, v22
	v_pack_b32_f16 v22, v50, v35
	v_pk_fma_f16 v25, v65, v53, v25
	v_pk_mul_f16 v43, v24, v22
	v_pack_b32_f16 v22, v51, v34
	v_pk_mul_f16 v42, v25, v22
	s_waitcnt vmcnt(0)
	v_pk_mul_f16 v22, v160, v146 op_sel_hi:[0,1]
	v_pk_mul_f16 v23, v160, v147 op_sel_hi:[0,1]
	v_pk_mul_f16 v24, v160, v148 op_sel_hi:[0,1]
	v_pk_mul_f16 v25, v160, v149 op_sel_hi:[0,1]
	v_pk_mul_f16 v50, v159, v146 op_sel_hi:[0,1]
	v_pk_mul_f16 v51, v159, v147 op_sel_hi:[0,1]
	v_pk_mul_f16 v52, v159, v148 op_sel_hi:[0,1]
	v_pk_mul_f16 v53, v159, v149 op_sel_hi:[0,1]
	v_pk_mul_f16 v34, v158, v146 op_sel_hi:[0,1]
	v_pk_mul_f16 v35, v158, v147 op_sel_hi:[0,1]
	v_pk_mul_f16 v36, v158, v148 op_sel_hi:[0,1]
	v_pk_mul_f16 v37, v158, v149 op_sel_hi:[0,1]
	v_pk_fma_f16 v29, v29, v149, v25
	v_pk_fma_f16 v28, v28, v148, v24
	v_pk_fma_f16 v27, v27, v147, v23
	v_pk_fma_f16 v26, v26, v146, v22
	v_pk_fma_f16 v41, v41, v149, v25
	v_pk_fma_f16 v40, v40, v148, v24
	v_pk_fma_f16 v39, v39, v147, v23
	v_pk_fma_f16 v38, v38, v146, v22
	v_pk_fma_f16 v25, v61, v149, v25
	v_pk_fma_f16 v24, v60, v148, v24
	v_pk_fma_f16 v23, v59, v147, v23
	v_pk_fma_f16 v22, v58, v146, v22
	v_pk_fma_f16 v66, v137, v149, v53
	v_pk_fma_f16 v67, v136, v148, v52
	v_pk_fma_f16 v68, v135, v147, v51
	v_pk_fma_f16 v69, v134, v146, v50
	v_pk_fma_f16 v70, v145, v149, v53
	v_pk_fma_f16 v71, v144, v148, v52
	v_pk_fma_f16 v72, v143, v147, v51
	v_pk_fma_f16 v73, v142, v146, v50
	v_pk_fma_f16 v9, v9, v149, v53
	v_pk_fma_f16 v8, v8, v148, v52
	v_pk_fma_f16 v7, v7, v147, v51
	v_pk_fma_f16 v6, v6, v146, v50
	v_pk_maximum3_f16 v50, v26, v38, v22
	v_pk_maximum3_f16 v51, v27, v39, v23
	v_pk_maximum3_f16 v52, v28, v40, v24
	v_pk_maximum3_f16 v53, v29, v41, v25
	v_pk_fma_f16 v54, v81, v149, v37
	v_pk_fma_f16 v55, v80, v148, v36
	v_pk_fma_f16 v56, v79, v147, v35
	v_pk_fma_f16 v57, v78, v146, v34
	v_pk_fma_f16 v58, v109, v149, v37
	v_pk_fma_f16 v59, v108, v148, v36
	v_pk_fma_f16 v60, v107, v147, v35
	v_pk_fma_f16 v61, v106, v146, v34
	v_pk_fma_f16 v37, v125, v149, v37
	v_pk_fma_f16 v36, v124, v148, v36
	v_pk_fma_f16 v35, v123, v147, v35
	v_pk_fma_f16 v34, v122, v146, v34
	v_pk_maximum3_f16 v75, v56, v60, v35
	v_pk_maximum3_f16 v76, v55, v59, v36
	v_pk_maximum3_f16 v77, v54, v58, v37
	v_pk_maximum3_f16 v78, v69, v73, v6
	v_pk_maximum3_f16 v79, v68, v72, v7
	v_pk_maximum3_f16 v74, v57, v61, v34
	v_pk_maximum3_f16 v80, v67, v71, v8
	v_pk_maximum3_f16 v81, v66, v70, v9
	v_pk_maximum3_f16 v50, v50, v74, v78
	v_pk_maximum3_f16 v51, v51, v75, v79
	v_pk_maximum3_f16 v52, v52, v76, v80
	v_pk_maximum3_f16 v53, v53, v77, v81
	s_nop 0
	v_pk_add_f16 v26, v26, v50 neg_lo:[0,1] neg_hi:[0,1]
	v_pk_add_f16 v27, v27, v51 neg_lo:[0,1] neg_hi:[0,1]
	v_pk_add_f16 v28, v28, v52 neg_lo:[0,1] neg_hi:[0,1]
	v_pk_add_f16 v29, v29, v53 neg_lo:[0,1] neg_hi:[0,1]
	v_pk_add_f16 v38, v38, v50 neg_lo:[0,1] neg_hi:[0,1]
	v_exp_f16_sdwa v74, v26 dst_sel:WORD_0 dst_unused:UNUSED_PAD src0_sel:WORD_0
	v_exp_f16_sdwa v75, v27 dst_sel:WORD_0 dst_unused:UNUSED_PAD src0_sel:WORD_0
	v_exp_f16_sdwa v76, v28 dst_sel:WORD_0 dst_unused:UNUSED_PAD src0_sel:WORD_0
	v_exp_f16_sdwa v77, v29 dst_sel:WORD_0 dst_unused:UNUSED_PAD src0_sel:WORD_0
	v_exp_f16_sdwa v74, v26 dst_sel:WORD_1 dst_unused:UNUSED_PRESERVE src0_sel:WORD_1
	v_exp_f16_sdwa v75, v27 dst_sel:WORD_1 dst_unused:UNUSED_PRESERVE src0_sel:WORD_1
	v_exp_f16_sdwa v76, v28 dst_sel:WORD_1 dst_unused:UNUSED_PRESERVE src0_sel:WORD_1
	v_exp_f16_sdwa v77, v29 dst_sel:WORD_1 dst_unused:UNUSED_PRESERVE src0_sel:WORD_1
	v_pk_add_f16 v39, v39, v51 neg_lo:[0,1] neg_hi:[0,1]
	v_pk_add_f16 v26, v74, 0
	v_pk_add_f16 v27, v75, 0
	v_pk_add_f16 v28, v76, 0
	v_pk_add_f16 v29, v77, 0
	v_pk_fma_f16 v10, v10, v74, 0
	v_pk_fma_f16 v11, v11, v75, 0
	v_pk_fma_f16 v12, v12, v76, 0
	v_pk_fma_f16 v13, v13, v77, 0
	v_pk_add_f16 v40, v40, v52 neg_lo:[0,1] neg_hi:[0,1]
	v_pk_add_f16 v41, v41, v53 neg_lo:[0,1] neg_hi:[0,1]
	v_pk_add_f16 v6, v6, v50 neg_lo:[0,1] neg_hi:[0,1]
	v_exp_f16_sdwa v74, v38 dst_sel:WORD_0 dst_unused:UNUSED_PAD src0_sel:WORD_0
	v_exp_f16_sdwa v75, v39 dst_sel:WORD_0 dst_unused:UNUSED_PAD src0_sel:WORD_0
	v_exp_f16_sdwa v76, v40 dst_sel:WORD_0 dst_unused:UNUSED_PAD src0_sel:WORD_0
	v_exp_f16_sdwa v77, v41 dst_sel:WORD_0 dst_unused:UNUSED_PAD src0_sel:WORD_0
	v_exp_f16_sdwa v74, v38 dst_sel:WORD_1 dst_unused:UNUSED_PRESERVE src0_sel:WORD_1
	v_exp_f16_sdwa v75, v39 dst_sel:WORD_1 dst_unused:UNUSED_PRESERVE src0_sel:WORD_1
	v_exp_f16_sdwa v76, v40 dst_sel:WORD_1 dst_unused:UNUSED_PRESERVE src0_sel:WORD_1
	v_exp_f16_sdwa v77, v41 dst_sel:WORD_1 dst_unused:UNUSED_PRESERVE src0_sel:WORD_1
	v_pk_add_f16 v7, v7, v51 neg_lo:[0,1] neg_hi:[0,1]
	v_pk_add_f16 v29, v29, v77
	v_pk_add_f16 v28, v28, v76
	v_pk_add_f16 v27, v27, v75
	v_pk_add_f16 v26, v26, v74
	v_pk_fma_f16 v13, v17, v77, v13
	v_pk_fma_f16 v12, v16, v76, v12
	v_pk_fma_f16 v11, v15, v75, v11
	v_pk_fma_f16 v10, v14, v74, v10
	v_pk_add_f16 v14, v22, v50 neg_lo:[0,1] neg_hi:[0,1]
	v_pk_add_f16 v15, v23, v51 neg_lo:[0,1] neg_hi:[0,1]
	v_pk_add_f16 v16, v24, v52 neg_lo:[0,1] neg_hi:[0,1]
	v_pk_add_f16 v17, v25, v53 neg_lo:[0,1] neg_hi:[0,1]
	v_pk_add_f16 v8, v8, v52 neg_lo:[0,1] neg_hi:[0,1]
	v_exp_f16_sdwa v22, v14 dst_sel:WORD_0 dst_unused:UNUSED_PAD src0_sel:WORD_0
	v_exp_f16_sdwa v23, v15 dst_sel:WORD_0 dst_unused:UNUSED_PAD src0_sel:WORD_0
	v_exp_f16_sdwa v24, v16 dst_sel:WORD_0 dst_unused:UNUSED_PAD src0_sel:WORD_0
	v_exp_f16_sdwa v25, v17 dst_sel:WORD_0 dst_unused:UNUSED_PAD src0_sel:WORD_0
	v_exp_f16_sdwa v22, v14 dst_sel:WORD_1 dst_unused:UNUSED_PRESERVE src0_sel:WORD_1
	v_exp_f16_sdwa v23, v15 dst_sel:WORD_1 dst_unused:UNUSED_PRESERVE src0_sel:WORD_1
	v_exp_f16_sdwa v24, v16 dst_sel:WORD_1 dst_unused:UNUSED_PRESERVE src0_sel:WORD_1
	v_exp_f16_sdwa v25, v17 dst_sel:WORD_1 dst_unused:UNUSED_PRESERVE src0_sel:WORD_1
	v_pk_add_f16 v9, v9, v53 neg_lo:[0,1] neg_hi:[0,1]
	v_pk_add_f16 v14, v26, v22
	v_pk_add_f16 v15, v27, v23
	v_pk_add_f16 v16, v28, v24
	v_pk_add_f16 v17, v29, v25
	v_pk_fma_f16 v10, v18, v22, v10
	v_pk_fma_f16 v11, v19, v23, v11
	v_pk_fma_f16 v12, v20, v24, v12
	v_pk_fma_f16 v13, v21, v25, v13
	v_pk_add_f16 v18, v57, v50 neg_lo:[0,1] neg_hi:[0,1]
	v_pk_add_f16 v19, v56, v51 neg_lo:[0,1] neg_hi:[0,1]
	v_pk_add_f16 v20, v55, v52 neg_lo:[0,1] neg_hi:[0,1]
	v_pk_add_f16 v21, v54, v53 neg_lo:[0,1] neg_hi:[0,1]
	v_exp_f16_sdwa v22, v18 dst_sel:WORD_0 dst_unused:UNUSED_PAD src0_sel:WORD_0
	v_exp_f16_sdwa v23, v19 dst_sel:WORD_0 dst_unused:UNUSED_PAD src0_sel:WORD_0
	v_exp_f16_sdwa v24, v20 dst_sel:WORD_0 dst_unused:UNUSED_PAD src0_sel:WORD_0
	v_exp_f16_sdwa v25, v21 dst_sel:WORD_0 dst_unused:UNUSED_PAD src0_sel:WORD_0
	v_exp_f16_sdwa v22, v18 dst_sel:WORD_1 dst_unused:UNUSED_PRESERVE src0_sel:WORD_1
	v_exp_f16_sdwa v23, v19 dst_sel:WORD_1 dst_unused:UNUSED_PRESERVE src0_sel:WORD_1
	v_exp_f16_sdwa v24, v20 dst_sel:WORD_1 dst_unused:UNUSED_PRESERVE src0_sel:WORD_1
	v_exp_f16_sdwa v25, v21 dst_sel:WORD_1 dst_unused:UNUSED_PRESERVE src0_sel:WORD_1
	v_pk_add_f16 v18, v61, v50 neg_lo:[0,1] neg_hi:[0,1]
	v_pk_add_f16 v17, v17, v25
	v_pk_add_f16 v16, v16, v24
	v_pk_add_f16 v15, v15, v23
	v_pk_add_f16 v14, v14, v22
	v_pk_fma_f16 v13, v33, v25, v13
	v_pk_fma_f16 v12, v32, v24, v12
	v_pk_fma_f16 v11, v31, v23, v11
	v_pk_fma_f16 v10, v30, v22, v10
	v_pk_add_f16 v19, v60, v51 neg_lo:[0,1] neg_hi:[0,1]
	v_pk_add_f16 v20, v59, v52 neg_lo:[0,1] neg_hi:[0,1]
	v_pk_add_f16 v21, v58, v53 neg_lo:[0,1] neg_hi:[0,1]
	v_exp_f16_sdwa v22, v18 dst_sel:WORD_0 dst_unused:UNUSED_PAD src0_sel:WORD_0
	v_exp_f16_sdwa v23, v19 dst_sel:WORD_0 dst_unused:UNUSED_PAD src0_sel:WORD_0
	v_exp_f16_sdwa v24, v20 dst_sel:WORD_0 dst_unused:UNUSED_PAD src0_sel:WORD_0
	v_exp_f16_sdwa v25, v21 dst_sel:WORD_0 dst_unused:UNUSED_PAD src0_sel:WORD_0
	v_exp_f16_sdwa v22, v18 dst_sel:WORD_1 dst_unused:UNUSED_PRESERVE src0_sel:WORD_1
	v_exp_f16_sdwa v23, v19 dst_sel:WORD_1 dst_unused:UNUSED_PRESERVE src0_sel:WORD_1
	v_exp_f16_sdwa v24, v20 dst_sel:WORD_1 dst_unused:UNUSED_PRESERVE src0_sel:WORD_1
	v_exp_f16_sdwa v25, v21 dst_sel:WORD_1 dst_unused:UNUSED_PRESERVE src0_sel:WORD_1
	v_pk_add_f16 v18, v34, v50 neg_lo:[0,1] neg_hi:[0,1]
	v_pk_add_f16 v14, v14, v22
	v_pk_add_f16 v15, v15, v23
	v_pk_add_f16 v16, v16, v24
	v_pk_add_f16 v17, v17, v25
	v_pk_fma_f16 v10, v46, v22, v10
	v_pk_fma_f16 v11, v47, v23, v11
	v_pk_fma_f16 v12, v48, v24, v12
	v_pk_fma_f16 v13, v49, v25, v13
	v_pk_add_f16 v19, v35, v51 neg_lo:[0,1] neg_hi:[0,1]
	v_pk_add_f16 v20, v36, v52 neg_lo:[0,1] neg_hi:[0,1]
	v_pk_add_f16 v21, v37, v53 neg_lo:[0,1] neg_hi:[0,1]
	v_exp_f16_sdwa v22, v18 dst_sel:WORD_0 dst_unused:UNUSED_PAD src0_sel:WORD_0
	v_exp_f16_sdwa v23, v19 dst_sel:WORD_0 dst_unused:UNUSED_PAD src0_sel:WORD_0
	v_exp_f16_sdwa v24, v20 dst_sel:WORD_0 dst_unused:UNUSED_PAD src0_sel:WORD_0
	v_exp_f16_sdwa v25, v21 dst_sel:WORD_0 dst_unused:UNUSED_PAD src0_sel:WORD_0
	v_exp_f16_sdwa v22, v18 dst_sel:WORD_1 dst_unused:UNUSED_PRESERVE src0_sel:WORD_1
	v_exp_f16_sdwa v23, v19 dst_sel:WORD_1 dst_unused:UNUSED_PRESERVE src0_sel:WORD_1
	v_exp_f16_sdwa v24, v20 dst_sel:WORD_1 dst_unused:UNUSED_PRESERVE src0_sel:WORD_1
	v_exp_f16_sdwa v25, v21 dst_sel:WORD_1 dst_unused:UNUSED_PRESERVE src0_sel:WORD_1
	v_pk_add_f16 v18, v69, v50 neg_lo:[0,1] neg_hi:[0,1]
	v_pk_add_f16 v17, v17, v25
	v_pk_add_f16 v16, v16, v24
	v_pk_add_f16 v15, v15, v23
	v_pk_add_f16 v14, v14, v22
	v_pk_fma_f16 v13, v65, v25, v13
	v_pk_fma_f16 v12, v64, v24, v12
	v_pk_fma_f16 v11, v63, v23, v11
	v_pk_fma_f16 v10, v62, v22, v10
	v_pk_add_f16 v19, v68, v51 neg_lo:[0,1] neg_hi:[0,1]
	v_pk_add_f16 v20, v67, v52 neg_lo:[0,1] neg_hi:[0,1]
	v_pk_add_f16 v21, v66, v53 neg_lo:[0,1] neg_hi:[0,1]
	v_exp_f16_sdwa v22, v18 dst_sel:WORD_0 dst_unused:UNUSED_PAD src0_sel:WORD_0
	v_exp_f16_sdwa v23, v19 dst_sel:WORD_0 dst_unused:UNUSED_PAD src0_sel:WORD_0
	v_exp_f16_sdwa v24, v20 dst_sel:WORD_0 dst_unused:UNUSED_PAD src0_sel:WORD_0
	v_exp_f16_sdwa v25, v21 dst_sel:WORD_0 dst_unused:UNUSED_PAD src0_sel:WORD_0
	v_exp_f16_sdwa v22, v18 dst_sel:WORD_1 dst_unused:UNUSED_PRESERVE src0_sel:WORD_1
	v_exp_f16_sdwa v23, v19 dst_sel:WORD_1 dst_unused:UNUSED_PRESERVE src0_sel:WORD_1
	v_exp_f16_sdwa v24, v20 dst_sel:WORD_1 dst_unused:UNUSED_PRESERVE src0_sel:WORD_1
	v_exp_f16_sdwa v25, v21 dst_sel:WORD_1 dst_unused:UNUSED_PRESERVE src0_sel:WORD_1
	v_pk_add_f16 v18, v73, v50 neg_lo:[0,1] neg_hi:[0,1]
	v_pk_add_f16 v14, v14, v22
	v_pk_add_f16 v15, v15, v23
	v_pk_add_f16 v16, v16, v24
	v_pk_add_f16 v17, v17, v25
	v_pk_fma_f16 v10, v82, v22, v10
	v_pk_fma_f16 v11, v83, v23, v11
	v_pk_fma_f16 v12, v84, v24, v12
	v_pk_fma_f16 v13, v85, v25, v13
	v_pk_add_f16 v19, v72, v51 neg_lo:[0,1] neg_hi:[0,1]
	v_pk_add_f16 v20, v71, v52 neg_lo:[0,1] neg_hi:[0,1]
	v_pk_add_f16 v21, v70, v53 neg_lo:[0,1] neg_hi:[0,1]
	v_exp_f16_sdwa v22, v18 dst_sel:WORD_0 dst_unused:UNUSED_PAD src0_sel:WORD_0
	v_exp_f16_sdwa v23, v19 dst_sel:WORD_0 dst_unused:UNUSED_PAD src0_sel:WORD_0
	v_exp_f16_sdwa v24, v20 dst_sel:WORD_0 dst_unused:UNUSED_PAD src0_sel:WORD_0
	v_exp_f16_sdwa v25, v21 dst_sel:WORD_0 dst_unused:UNUSED_PAD src0_sel:WORD_0
	v_exp_f16_sdwa v22, v18 dst_sel:WORD_1 dst_unused:UNUSED_PRESERVE src0_sel:WORD_1
	v_exp_f16_sdwa v23, v19 dst_sel:WORD_1 dst_unused:UNUSED_PRESERVE src0_sel:WORD_1
	v_exp_f16_sdwa v24, v20 dst_sel:WORD_1 dst_unused:UNUSED_PRESERVE src0_sel:WORD_1
	v_exp_f16_sdwa v25, v21 dst_sel:WORD_1 dst_unused:UNUSED_PRESERVE src0_sel:WORD_1
	s_nop 0
	v_pk_add_f16 v17, v17, v25
	v_pk_add_f16 v16, v16, v24
	v_pk_add_f16 v15, v15, v23
	v_pk_add_f16 v14, v14, v22
	v_pk_fma_f16 v21, v105, v25, v13
	v_pk_fma_f16 v20, v104, v24, v12
	v_pk_fma_f16 v19, v103, v23, v11
	v_pk_fma_f16 v18, v102, v22, v10
	v_mov_b32_e32 v13, v5
	v_mov_b32_e32 v12, v4
	v_mov_b32_e32 v11, v3
	v_mov_b32_e32 v10, v2
	v_exp_f16_sdwa v22, v6 dst_sel:WORD_0 dst_unused:UNUSED_PAD src0_sel:WORD_0
	v_exp_f16_sdwa v23, v7 dst_sel:WORD_0 dst_unused:UNUSED_PAD src0_sel:WORD_0
	v_exp_f16_sdwa v24, v8 dst_sel:WORD_0 dst_unused:UNUSED_PAD src0_sel:WORD_0
	v_exp_f16_sdwa v25, v9 dst_sel:WORD_0 dst_unused:UNUSED_PAD src0_sel:WORD_0
	v_exp_f16_sdwa v22, v6 dst_sel:WORD_1 dst_unused:UNUSED_PRESERVE src0_sel:WORD_1
	v_exp_f16_sdwa v23, v7 dst_sel:WORD_1 dst_unused:UNUSED_PRESERVE src0_sel:WORD_1
	v_exp_f16_sdwa v24, v8 dst_sel:WORD_1 dst_unused:UNUSED_PRESERVE src0_sel:WORD_1
	v_exp_f16_sdwa v25, v9 dst_sel:WORD_1 dst_unused:UNUSED_PRESERVE src0_sel:WORD_1
	s_nop 0

.Lmyf_C3_7:
	s_mov_b64 exec, -1
	s_waitcnt vmcnt(21)
	v_cvt_f16_f32_e32 v206, v155
	v_cvt_f16_f32_e32 v208, v154
	v_cvt_f16_f32_e32 v207, v156
	v_add_u32_e32 v251, 0x48000, v200
	buffer_load_dwordx4 v[154:157], v251, s[12:15], 0 offen
	s_mov_b64 s[4:5], 0
	s_waitcnt vmcnt(3)
	s_mul_i32 s84, s81, s83
	s_add_i32 s84, s84, s82
	s_mul_i32 s84, s84, 0x60000
	s_lshl_b32 s85, s92, 3
	s_add_u32 s85, s85, s94
	s_mul_i32 s85, s85, 1536
	s_add_u32 s84, s84, s85
	s_add_u32 s88, s86, s84
	s_addc_u32 s89, s87, 0
	s_load_dword s90, s[88:89], 0x0
	s_load_dword s90, s[88:89], 0x80
	s_load_dword s90, s[88:89], 0x100
	s_load_dword s90, s[88:89], 0x180
	s_load_dword s90, s[88:89], 0x200
	s_load_dword s90, s[88:89], 0x280
	s_load_dword s90, s[88:89], 0x300
	s_load_dword s90, s[88:89], 0x380
	s_load_dword s90, s[88:89], 0x400
	s_load_dword s90, s[88:89], 0x480
	s_load_dword s90, s[88:89], 0x500
	s_load_dword s90, s[88:89], 0x580
	v_pk_mul_f16 v216, v208, v213 op_sel_hi:[0,1]
	v_pk_mul_f16 v220, v206, v213 op_sel_hi:[0,1]
	v_pk_mul_f16 v224, v207, v213 op_sel_hi:[0,1]
	v_pk_mul_f16 v209, v208, v210 op_sel_hi:[0,1]
	v_pk_mul_f16 v214, v208, v211 op_sel_hi:[0,1]
	v_pk_mul_f16 v215, v208, v212 op_sel_hi:[0,1]
	v_pk_mul_f16 v217, v206, v210 op_sel_hi:[0,1]
	s_mov_b64 exec, s[64:65]
	buffer_load_dwordx4 v[34:37], v245, s[12:15], 0 offen
	buffer_load_dwordx4 v[18:21], v245, s[12:15], 0 offen offset:512
	s_mov_b64 exec, -1
	v_pk_mul_f16 v218, v206, v211 op_sel_hi:[0,1]
	v_pk_mul_f16 v219, v206, v212 op_sel_hi:[0,1]
	v_pk_mul_f16 v221, v207, v210 op_sel_hi:[0,1]
	v_pk_mul_f16 v222, v207, v211 op_sel_hi:[0,1]
	v_pk_mul_f16 v223, v207, v212 op_sel_hi:[0,1]
	v_pk_fma_f16 v125, v125, v213, v216
	v_pk_fma_f16 v141, v141, v213, v220
	v_pk_fma_f16 v149, v149, v213, v224
	v_pk_fma_f16 v225, v97, v213, v216
	v_pk_fma_f16 v229, v121, v213, v220
	v_pk_fma_f16 v233, v137, v213, v224
	v_pk_fma_f16 v216, v65, v213, v216
	v_pk_fma_f16 v220, v81, v213, v220
	buffer_load_dwordx4 v[46:49], v246, s[12:15], 0 offen offset:512
	buffer_load_dwordx4 v[22:25], v246, s[12:15], 0 offen offset:1024
	v_pk_fma_f16 v213, v105, v213, v224
	v_pk_maximum3_f16 v224, v125, v141, v149
	v_pk_fma_f16 v124, v124, v212, v215
	v_pk_fma_f16 v123, v123, v211, v214
	v_pk_fma_f16 v122, v122, v210, v209
	v_pk_fma_f16 v140, v140, v212, v219
	v_pk_fma_f16 v139, v139, v211, v218
	v_pk_fma_f16 v138, v138, v210, v217
	v_pk_fma_f16 v148, v148, v212, v223
	v_pk_fma_f16 v147, v147, v211, v222
	v_pk_fma_f16 v146, v146, v210, v221
	v_pk_fma_f16 v226, v96, v212, v215
	v_pk_fma_f16 v227, v95, v211, v214
	v_pk_fma_f16 v228, v94, v210, v209
	v_pk_fma_f16 v230, v120, v212, v219
	v_pk_fma_f16 v231, v119, v211, v218
	s_mov_b64 exec, s[66:67]
	buffer_load_dwordx4 v[66:69], v246, s[12:15], 0 offen offset:2048
	buffer_load_dwordx4 v[26:29], v246, s[12:15], 0 offen offset:2560
	s_mov_b64 exec, -1
	v_pk_fma_f16 v232, v118, v210, v217
	v_pk_fma_f16 v234, v136, v212, v223
	v_pk_fma_f16 v235, v135, v211, v222
	v_pk_fma_f16 v236, v134, v210, v221
	v_pk_fma_f16 v215, v64, v212, v215
	v_pk_fma_f16 v214, v63, v211, v214
	v_pk_fma_f16 v209, v62, v210, v209
	v_pk_fma_f16 v219, v80, v212, v219
	v_pk_fma_f16 v218, v79, v211, v218
	v_pk_fma_f16 v217, v78, v210, v217
	v_pk_fma_f16 v212, v104, v212, v223
	v_pk_fma_f16 v211, v103, v211, v222
	v_pk_fma_f16 v210, v102, v210, v221
	v_pk_maximum3_f16 v221, v122, v138, v146
	v_pk_maximum3_f16 v222, v123, v139, v147
	v_pk_maximum3_f16 v223, v124, v140, v148
	v_pk_maximum3_f16 v240, v225, v229, v233
	v_pk_maximum3_f16 v244, v216, v220, v213
	v_pk_maximum3_f16 v237, v228, v232, v236
	v_pk_maximum3_f16 v238, v227, v231, v235
	v_pk_maximum3_f16 v239, v226, v230, v234
	v_pk_maximum3_f16 v241, v209, v217, v210
	v_pk_maximum3_f16 v242, v214, v218, v211
	v_pk_maximum3_f16 v224, v224, v240, v244
	v_pk_maximum3_f16 v243, v215, v219, v212
	v_pk_maximum3_f16 v221, v221, v237, v241
	v_pk_maximum3_f16 v222, v222, v238, v242
	v_pk_maximum3_f16 v223, v223, v239, v243
	v_pk_add_f16 v125, v125, v224 neg_lo:[0,1] neg_hi:[0,1]
	s_mov_b64 exec, s[64:65]
	buffer_load_dwordx4 v[86:89], v247, s[12:15], 0 offen
	buffer_load_dwordx4 v[38:41], v247, s[12:15], 0 offen offset:512
	s_mov_b64 exec, -1
	v_pk_add_f16 v122, v122, v221 neg_lo:[0,1] neg_hi:[0,1]
	v_pk_add_f16 v123, v123, v222 neg_lo:[0,1] neg_hi:[0,1]
	v_pk_add_f16 v124, v124, v223 neg_lo:[0,1] neg_hi:[0,1]
	v_pk_add_f16 v138, v138, v221 neg_lo:[0,1] neg_hi:[0,1]
	v_exp_f16_sdwa v237, v122 dst_sel:WORD_0 dst_unused:UNUSED_PAD src0_sel:WORD_0
	v_exp_f16_sdwa v238, v123 dst_sel:WORD_0 dst_unused:UNUSED_PAD src0_sel:WORD_0
	v_exp_f16_sdwa v239, v124 dst_sel:WORD_0 dst_unused:UNUSED_PAD src0_sel:WORD_0
	v_exp_f16_sdwa v240, v125 dst_sel:WORD_0 dst_unused:UNUSED_PAD src0_sel:WORD_0
	v_exp_f16_sdwa v237, v122 dst_sel:WORD_1 dst_unused:UNUSED_PRESERVE src0_sel:WORD_1
	v_exp_f16_sdwa v238, v123 dst_sel:WORD_1 dst_unused:UNUSED_PRESERVE src0_sel:WORD_1
	v_exp_f16_sdwa v239, v124 dst_sel:WORD_1 dst_unused:UNUSED_PRESERVE src0_sel:WORD_1
	v_exp_f16_sdwa v240, v125 dst_sel:WORD_1 dst_unused:UNUSED_PRESERVE src0_sel:WORD_1
	v_pk_add_f16 v139, v139, v222 neg_lo:[0,1] neg_hi:[0,1]
	v_pk_add_f16 v125, v237, 0
	v_pk_fma_f16 v85, v85, v240, 0
	v_pk_add_f16 v122, v240, 0
	v_pk_add_f16 v123, v239, 0
	v_pk_add_f16 v124, v238, 0
	v_pk_fma_f16 v84, v84, v239, 0
	v_pk_fma_f16 v83, v83, v238, 0
	v_pk_fma_f16 v82, v82, v237, 0
	v_pk_add_f16 v140, v140, v223 neg_lo:[0,1] neg_hi:[0,1]
	buffer_load_dwordx4 v[114:117], v248, s[12:15], 0 offen offset:512
	buffer_load_dwordx4 v[50:53], v248, s[12:15], 0 offen offset:1024
	v_pk_add_f16 v141, v141, v224 neg_lo:[0,1] neg_hi:[0,1]
	v_exp_f16_sdwa v237, v138 dst_sel:WORD_0 dst_unused:UNUSED_PAD src0_sel:WORD_0
	v_exp_f16_sdwa v238, v139 dst_sel:WORD_0 dst_unused:UNUSED_PAD src0_sel:WORD_0
	v_exp_f16_sdwa v239, v140 dst_sel:WORD_0 dst_unused:UNUSED_PAD src0_sel:WORD_0
	v_exp_f16_sdwa v240, v141 dst_sel:WORD_0 dst_unused:UNUSED_PAD src0_sel:WORD_0
	v_exp_f16_sdwa v237, v138 dst_sel:WORD_1 dst_unused:UNUSED_PRESERVE src0_sel:WORD_1
	v_exp_f16_sdwa v238, v139 dst_sel:WORD_1 dst_unused:UNUSED_PRESERVE src0_sel:WORD_1
	v_exp_f16_sdwa v239, v140 dst_sel:WORD_1 dst_unused:UNUSED_PRESERVE src0_sel:WORD_1
	v_exp_f16_sdwa v240, v141 dst_sel:WORD_1 dst_unused:UNUSED_PRESERVE src0_sel:WORD_1
	v_pk_add_f16 v125, v125, v237
	v_pk_fma_f16 v85, v109, v240, v85
	v_pk_add_f16 v109, v149, v224 neg_lo:[0,1] neg_hi:[0,1]
	v_pk_add_f16 v124, v124, v238
	v_pk_add_f16 v123, v123, v239
	v_pk_add_f16 v122, v122, v240
	v_pk_fma_f16 v82, v106, v237, v82
	v_pk_fma_f16 v83, v107, v238, v83
	v_pk_fma_f16 v84, v108, v239, v84
	v_pk_add_f16 v106, v146, v221 neg_lo:[0,1] neg_hi:[0,1]
	v_pk_add_f16 v107, v147, v222 neg_lo:[0,1] neg_hi:[0,1]
	v_pk_add_f16 v108, v148, v223 neg_lo:[0,1] neg_hi:[0,1]
	v_exp_f16_sdwa v138, v106 dst_sel:WORD_0 dst_unused:UNUSED_PAD src0_sel:WORD_0
	v_exp_f16_sdwa v139, v107 dst_sel:WORD_0 dst_unused:UNUSED_PAD src0_sel:WORD_0
	v_exp_f16_sdwa v140, v108 dst_sel:WORD_0 dst_unused:UNUSED_PAD src0_sel:WORD_0
	v_exp_f16_sdwa v141, v109 dst_sel:WORD_0 dst_unused:UNUSED_PAD src0_sel:WORD_0
	v_exp_f16_sdwa v138, v106 dst_sel:WORD_1 dst_unused:UNUSED_PRESERVE src0_sel:WORD_1
	v_exp_f16_sdwa v139, v107 dst_sel:WORD_1 dst_unused:UNUSED_PRESERVE src0_sel:WORD_1
	v_exp_f16_sdwa v140, v108 dst_sel:WORD_1 dst_unused:UNUSED_PRESERVE src0_sel:WORD_1
	v_exp_f16_sdwa v141, v109 dst_sel:WORD_1 dst_unused:UNUSED_PRESERVE src0_sel:WORD_1
	v_pk_add_f16 v109, v125, v138
	v_pk_add_f16 v106, v122, v141
	s_mov_b64 exec, s[66:67]
	buffer_load_dwordx4 v[130:133], v248, s[12:15], 0 offen offset:2048
	buffer_load_dwordx4 v[70:73], v248, s[12:15], 0 offen offset:2560
	s_mov_b64 exec, -1
	v_pk_add_f16 v107, v123, v140
	v_pk_add_f16 v108, v124, v139
	v_pk_fma_f16 v85, v129, v141, v85
	v_pk_fma_f16 v84, v128, v140, v84
	v_pk_fma_f16 v83, v127, v139, v83
	v_pk_fma_f16 v82, v126, v138, v82
	v_pk_add_f16 v122, v228, v221 neg_lo:[0,1] neg_hi:[0,1]
	v_pk_add_f16 v123, v227, v222 neg_lo:[0,1] neg_hi:[0,1]
	v_pk_add_f16 v124, v226, v223 neg_lo:[0,1] neg_hi:[0,1]
	v_pk_add_f16 v125, v225, v224 neg_lo:[0,1] neg_hi:[0,1]
	v_exp_f16_sdwa v126, v122 dst_sel:WORD_0 dst_unused:UNUSED_PAD src0_sel:WORD_0
	v_exp_f16_sdwa v127, v123 dst_sel:WORD_0 dst_unused:UNUSED_PAD src0_sel:WORD_0
	v_exp_f16_sdwa v128, v124 dst_sel:WORD_0 dst_unused:UNUSED_PAD src0_sel:WORD_0
	v_exp_f16_sdwa v129, v125 dst_sel:WORD_0 dst_unused:UNUSED_PAD src0_sel:WORD_0
	v_exp_f16_sdwa v126, v122 dst_sel:WORD_1 dst_unused:UNUSED_PRESERVE src0_sel:WORD_1
	v_exp_f16_sdwa v127, v123 dst_sel:WORD_1 dst_unused:UNUSED_PRESERVE src0_sel:WORD_1
	v_exp_f16_sdwa v128, v124 dst_sel:WORD_1 dst_unused:UNUSED_PRESERVE src0_sel:WORD_1
	v_exp_f16_sdwa v129, v125 dst_sel:WORD_1 dst_unused:UNUSED_PRESERVE src0_sel:WORD_1
	v_pk_add_f16 v122, v232, v221 neg_lo:[0,1] neg_hi:[0,1]
	v_pk_add_f16 v109, v109, v126
	v_pk_add_f16 v108, v108, v127
	v_pk_add_f16 v107, v107, v128
	s_mov_b64 exec, s[76:77]
	buffer_load_dwordx4 v[142:145], v249, s[12:15], 0 offen
	buffer_load_dwordx4 v[90:93], v249, s[12:15], 0 offen offset:512
	s_mov_b64 exec, -1
	v_pk_add_f16 v106, v106, v129
	v_pk_fma_f16 v82, v54, v126, v82
	v_pk_fma_f16 v83, v55, v127, v83
	v_pk_fma_f16 v84, v56, v128, v84
	v_pk_fma_f16 v85, v57, v129, v85
	v_pk_add_f16 v123, v231, v222 neg_lo:[0,1] neg_hi:[0,1]
	v_pk_add_f16 v124, v230, v223 neg_lo:[0,1] neg_hi:[0,1]
	v_pk_add_f16 v125, v229, v224 neg_lo:[0,1] neg_hi:[0,1]
	v_exp_f16_sdwa v126, v122 dst_sel:WORD_0 dst_unused:UNUSED_PAD src0_sel:WORD_0
	v_exp_f16_sdwa v127, v123 dst_sel:WORD_0 dst_unused:UNUSED_PAD src0_sel:WORD_0
	v_exp_f16_sdwa v128, v124 dst_sel:WORD_0 dst_unused:UNUSED_PAD src0_sel:WORD_0
	v_exp_f16_sdwa v129, v125 dst_sel:WORD_0 dst_unused:UNUSED_PAD src0_sel:WORD_0
	v_exp_f16_sdwa v126, v122 dst_sel:WORD_1 dst_unused:UNUSED_PRESERVE src0_sel:WORD_1
	v_exp_f16_sdwa v127, v123 dst_sel:WORD_1 dst_unused:UNUSED_PRESERVE src0_sel:WORD_1
	v_exp_f16_sdwa v128, v124 dst_sel:WORD_1 dst_unused:UNUSED_PRESERVE src0_sel:WORD_1
	v_exp_f16_sdwa v129, v125 dst_sel:WORD_1 dst_unused:UNUSED_PRESERVE src0_sel:WORD_1
	v_pk_add_f16 v122, v236, v221 neg_lo:[0,1] neg_hi:[0,1]
	v_pk_add_f16 v109, v109, v126
	v_pk_add_f16 v106, v106, v129
	v_pk_add_f16 v107, v107, v128
	v_pk_add_f16 v108, v108, v127
	v_pk_fma_f16 v85, v77, v129, v85
	v_pk_fma_f16 v84, v76, v128, v84
	s_mov_b64 exec, s[70:71]
	buffer_load_dwordx4 v[150:153], v250, s[12:15], 0 offen offset:512
	buffer_load_dwordx4 v[110:113], v250, s[12:15], 0 offen offset:1024
	s_mov_b64 exec, -1
	v_pk_fma_f16 v83, v75, v127, v83
	v_pk_fma_f16 v82, v74, v126, v82
	v_pk_add_f16 v123, v235, v222 neg_lo:[0,1] neg_hi:[0,1]
	v_pk_add_f16 v124, v234, v223 neg_lo:[0,1] neg_hi:[0,1]
	v_pk_add_f16 v125, v233, v224 neg_lo:[0,1] neg_hi:[0,1]
	v_exp_f16_sdwa v126, v122 dst_sel:WORD_0 dst_unused:UNUSED_PAD src0_sel:WORD_0
	v_exp_f16_sdwa v127, v123 dst_sel:WORD_0 dst_unused:UNUSED_PAD src0_sel:WORD_0
	v_exp_f16_sdwa v128, v124 dst_sel:WORD_0 dst_unused:UNUSED_PAD src0_sel:WORD_0
	v_exp_f16_sdwa v129, v125 dst_sel:WORD_0 dst_unused:UNUSED_PAD src0_sel:WORD_0
	v_exp_f16_sdwa v126, v122 dst_sel:WORD_1 dst_unused:UNUSED_PRESERVE src0_sel:WORD_1
	v_exp_f16_sdwa v127, v123 dst_sel:WORD_1 dst_unused:UNUSED_PRESERVE src0_sel:WORD_1
	v_exp_f16_sdwa v128, v124 dst_sel:WORD_1 dst_unused:UNUSED_PRESERVE src0_sel:WORD_1
	v_exp_f16_sdwa v129, v125 dst_sel:WORD_1 dst_unused:UNUSED_PRESERVE src0_sel:WORD_1
	v_pk_add_f16 v122, v209, v221 neg_lo:[0,1] neg_hi:[0,1]
	v_pk_add_f16 v109, v109, v126
	v_pk_add_f16 v108, v108, v127
	v_pk_add_f16 v107, v107, v128
	v_pk_add_f16 v106, v106, v129
	v_pk_fma_f16 v82, v98, v126, v82
	v_pk_fma_f16 v83, v99, v127, v83
	v_pk_fma_f16 v84, v100, v128, v84
	v_pk_fma_f16 v85, v101, v129, v85
	s_mov_b64 exec, s[78:79]
	buffer_load_dwordx4 v[14:17], v250, s[12:15], 0 offen offset:2048
	buffer_load_dwordx4 v[10:13], v250, s[12:15], 0 offen offset:2560
	s_mov_b64 exec, -1
	v_pk_add_f16 v123, v214, v222 neg_lo:[0,1] neg_hi:[0,1]
	v_pk_add_f16 v124, v215, v223 neg_lo:[0,1] neg_hi:[0,1]
	v_pk_add_f16 v125, v216, v224 neg_lo:[0,1] neg_hi:[0,1]
	v_exp_f16_sdwa v126, v122 dst_sel:WORD_0 dst_unused:UNUSED_PAD src0_sel:WORD_0
	v_exp_f16_sdwa v127, v123 dst_sel:WORD_0 dst_unused:UNUSED_PAD src0_sel:WORD_0
	v_exp_f16_sdwa v128, v124 dst_sel:WORD_0 dst_unused:UNUSED_PAD src0_sel:WORD_0
	v_exp_f16_sdwa v129, v125 dst_sel:WORD_0 dst_unused:UNUSED_PAD src0_sel:WORD_0
	v_exp_f16_sdwa v126, v122 dst_sel:WORD_1 dst_unused:UNUSED_PRESERVE src0_sel:WORD_1
	v_exp_f16_sdwa v127, v123 dst_sel:WORD_1 dst_unused:UNUSED_PRESERVE src0_sel:WORD_1
	v_exp_f16_sdwa v128, v124 dst_sel:WORD_1 dst_unused:UNUSED_PRESERVE src0_sel:WORD_1
	v_exp_f16_sdwa v129, v125 dst_sel:WORD_1 dst_unused:UNUSED_PRESERVE src0_sel:WORD_1
	v_pk_add_f16 v122, v217, v221 neg_lo:[0,1] neg_hi:[0,1]
	v_pk_add_f16 v109, v109, v126
	v_pk_add_f16 v106, v106, v129
	v_pk_add_f16 v107, v107, v128
	v_pk_add_f16 v108, v108, v127
	v_pk_fma_f16 v85, v33, v129, v85
	v_pk_fma_f16 v84, v32, v128, v84
	v_pk_fma_f16 v83, v31, v127, v83
	v_pk_fma_f16 v82, v30, v126, v82
	v_pk_add_f16 v123, v218, v222 neg_lo:[0,1] neg_hi:[0,1]
	v_pk_add_f16 v124, v219, v223 neg_lo:[0,1] neg_hi:[0,1]
	v_pk_add_f16 v125, v220, v224 neg_lo:[0,1] neg_hi:[0,1]
	v_exp_f16_sdwa v126, v122 dst_sel:WORD_0 dst_unused:UNUSED_PAD src0_sel:WORD_0
	v_exp_f16_sdwa v127, v123 dst_sel:WORD_0 dst_unused:UNUSED_PAD src0_sel:WORD_0
	v_exp_f16_sdwa v128, v124 dst_sel:WORD_0 dst_unused:UNUSED_PAD src0_sel:WORD_0
	v_exp_f16_sdwa v129, v125 dst_sel:WORD_0 dst_unused:UNUSED_PAD src0_sel:WORD_0
	v_exp_f16_sdwa v126, v122 dst_sel:WORD_1 dst_unused:UNUSED_PRESERVE src0_sel:WORD_1
	v_exp_f16_sdwa v127, v123 dst_sel:WORD_1 dst_unused:UNUSED_PRESERVE src0_sel:WORD_1
	v_exp_f16_sdwa v128, v124 dst_sel:WORD_1 dst_unused:UNUSED_PRESERVE src0_sel:WORD_1
	v_exp_f16_sdwa v129, v125 dst_sel:WORD_1 dst_unused:UNUSED_PRESERVE src0_sel:WORD_1
	v_pk_add_f16 v122, v210, v221 neg_lo:[0,1] neg_hi:[0,1]
	v_pk_add_f16 v109, v109, v126
	v_pk_add_f16 v108, v108, v127
	v_pk_add_f16 v107, v107, v128
	v_pk_add_f16 v106, v106, v129
	v_pk_fma_f16 v82, v42, v126, v82
	v_pk_fma_f16 v83, v43, v127, v83
	v_pk_fma_f16 v84, v44, v128, v84
	v_pk_fma_f16 v85, v45, v129, v85
	v_pk_add_f16 v123, v211, v222 neg_lo:[0,1] neg_hi:[0,1]
	v_pk_add_f16 v124, v212, v223 neg_lo:[0,1] neg_hi:[0,1]
	v_pk_add_f16 v125, v213, v224 neg_lo:[0,1] neg_hi:[0,1]
	v_exp_f16_sdwa v126, v122 dst_sel:WORD_0 dst_unused:UNUSED_PAD src0_sel:WORD_0
	v_exp_f16_sdwa v127, v123 dst_sel:WORD_0 dst_unused:UNUSED_PAD src0_sel:WORD_0
	v_exp_f16_sdwa v128, v124 dst_sel:WORD_0 dst_unused:UNUSED_PAD src0_sel:WORD_0
	v_exp_f16_sdwa v129, v125 dst_sel:WORD_0 dst_unused:UNUSED_PAD src0_sel:WORD_0
	v_exp_f16_sdwa v126, v122 dst_sel:WORD_1 dst_unused:UNUSED_PRESERVE src0_sel:WORD_1
	v_exp_f16_sdwa v127, v123 dst_sel:WORD_1 dst_unused:UNUSED_PRESERVE src0_sel:WORD_1
	v_exp_f16_sdwa v128, v124 dst_sel:WORD_1 dst_unused:UNUSED_PRESERVE src0_sel:WORD_1
	v_exp_f16_sdwa v129, v125 dst_sel:WORD_1 dst_unused:UNUSED_PRESERVE src0_sel:WORD_1
	v_pk_add_f16 v109, v109, v126
	v_pk_add_f16 v108, v108, v127
	v_rcp_f16_e32 v122, v109
	v_rcp_f16_sdwa v109, v109 dst_sel:DWORD dst_unused:UNUSED_PAD src0_sel:WORD_1
	v_pk_add_f16 v107, v107, v128
	v_rcp_f16_e32 v123, v108
	v_rcp_f16_sdwa v108, v108 dst_sel:DWORD dst_unused:UNUSED_PAD src0_sel:WORD_1
	v_pk_add_f16 v106, v106, v129
	v_rcp_f16_e32 v124, v107
	v_rcp_f16_sdwa v107, v107 dst_sel:DWORD dst_unused:UNUSED_PAD src0_sel:WORD_1
	v_rcp_f16_e32 v125, v106
	v_rcp_f16_sdwa v106, v106 dst_sel:DWORD dst_unused:UNUSED_PAD src0_sel:WORD_1
	v_pk_fma_f16 v82, v58, v126, v82
	v_pack_b32_f16 v109, v122, v109
	v_pk_fma_f16 v83, v59, v127, v83
	v_pk_mul_f16 v141, v82, v109
	v_pack_b32_f16 v82, v123, v108
	v_pk_fma_f16 v84, v60, v128, v84
	v_pk_mul_f16 v140, v83, v82
	v_pack_b32_f16 v82, v124, v107
	v_pk_fma_f16 v85, v61, v129, v85
	v_pk_mul_f16 v139, v84, v82
	v_pack_b32_f16 v82, v125, v106
	v_pk_mul_f16 v138, v85, v82
	s_waitcnt vmcnt(12)
	v_pk_mul_f16 v85, v208, v165 op_sel_hi:[0,1]
	v_pk_mul_f16 v109, v206, v165 op_sel_hi:[0,1]
	v_pk_mul_f16 v122, v207, v162 op_sel_hi:[0,1]
	v_pk_mul_f16 v125, v207, v165 op_sel_hi:[0,1]
	v_pk_mul_f16 v82, v208, v162 op_sel_hi:[0,1]
	v_pk_mul_f16 v83, v208, v163 op_sel_hi:[0,1]
	v_pk_mul_f16 v84, v208, v164 op_sel_hi:[0,1]
	v_pk_mul_f16 v106, v206, v162 op_sel_hi:[0,1]
	v_pk_mul_f16 v107, v206, v163 op_sel_hi:[0,1]
	v_pk_mul_f16 v108, v206, v164 op_sel_hi:[0,1]
	v_pk_mul_f16 v123, v207, v163 op_sel_hi:[0,1]
	v_pk_mul_f16 v124, v207, v164 op_sel_hi:[0,1]
	v_pk_fma_f16 v97, v97, v165, v85
	v_pk_fma_f16 v121, v121, v165, v109
	v_pk_fma_f16 v126, v137, v165, v125
	v_pk_fma_f16 v129, v134, v162, v122
	v_pk_fma_f16 v134, v65, v165, v85
	v_pk_fma_f16 v146, v81, v165, v109
	v_pk_fma_f16 v209, v105, v165, v125
	v_pk_fma_f16 v85, v37, v165, v85
	v_pk_fma_f16 v109, v49, v165, v109
	v_pk_fma_f16 v125, v69, v165, v125
	v_pk_maximum3_f16 v165, v97, v121, v126
	v_pk_fma_f16 v96, v96, v164, v84
	v_pk_fma_f16 v95, v95, v163, v83
	v_pk_fma_f16 v94, v94, v162, v82
	v_pk_fma_f16 v120, v120, v164, v108
	v_pk_fma_f16 v119, v119, v163, v107
	v_pk_fma_f16 v118, v118, v162, v106
	v_pk_fma_f16 v127, v136, v164, v124
	v_pk_fma_f16 v128, v135, v163, v123
	v_pk_fma_f16 v135, v64, v164, v84
	v_pk_fma_f16 v136, v63, v163, v83
	v_pk_fma_f16 v137, v62, v162, v82
	v_pk_fma_f16 v147, v80, v164, v108
	v_pk_fma_f16 v148, v79, v163, v107
	v_pk_fma_f16 v149, v78, v162, v106
	v_pk_fma_f16 v210, v104, v164, v124
	v_pk_fma_f16 v211, v103, v163, v123
	v_pk_fma_f16 v212, v102, v162, v122
	v_pk_fma_f16 v84, v36, v164, v84
	v_pk_fma_f16 v83, v35, v163, v83
	v_pk_fma_f16 v82, v34, v162, v82
	v_pk_fma_f16 v108, v48, v164, v108
	v_pk_fma_f16 v107, v47, v163, v107
	v_pk_fma_f16 v106, v46, v162, v106
	v_pk_fma_f16 v124, v68, v164, v124
	v_pk_fma_f16 v123, v67, v163, v123
	v_pk_fma_f16 v122, v66, v162, v122
	v_pk_maximum3_f16 v162, v94, v118, v129
	v_pk_maximum3_f16 v163, v95, v119, v128
	v_pk_maximum3_f16 v164, v96, v120, v127
	v_pk_maximum3_f16 v216, v134, v146, v209
	v_pk_maximum3_f16 v220, v85, v109, v125
	v_pk_maximum3_f16 v213, v137, v149, v212
	v_pk_maximum3_f16 v214, v136, v148, v211
	v_pk_maximum3_f16 v215, v135, v147, v210
	v_pk_maximum3_f16 v217, v82, v106, v122
	v_pk_maximum3_f16 v218, v83, v107, v123
	v_pk_maximum3_f16 v165, v165, v216, v220
	v_pk_maximum3_f16 v219, v84, v108, v124
	v_pk_maximum3_f16 v162, v162, v213, v217
	v_pk_maximum3_f16 v163, v163, v214, v218
	v_pk_maximum3_f16 v164, v164, v215, v219
	v_pk_add_f16 v97, v97, v165 neg_lo:[0,1] neg_hi:[0,1]
	v_pk_add_f16 v94, v94, v162 neg_lo:[0,1] neg_hi:[0,1]
	v_pk_add_f16 v95, v95, v163 neg_lo:[0,1] neg_hi:[0,1]
	v_pk_add_f16 v96, v96, v164 neg_lo:[0,1] neg_hi:[0,1]
	v_pk_add_f16 v118, v118, v162 neg_lo:[0,1] neg_hi:[0,1]
	v_exp_f16_sdwa v213, v94 dst_sel:WORD_0 dst_unused:UNUSED_PAD src0_sel:WORD_0
	v_exp_f16_sdwa v214, v95 dst_sel:WORD_0 dst_unused:UNUSED_PAD src0_sel:WORD_0
	v_exp_f16_sdwa v215, v96 dst_sel:WORD_0 dst_unused:UNUSED_PAD src0_sel:WORD_0
	v_exp_f16_sdwa v216, v97 dst_sel:WORD_0 dst_unused:UNUSED_PAD src0_sel:WORD_0
	v_exp_f16_sdwa v213, v94 dst_sel:WORD_1 dst_unused:UNUSED_PRESERVE src0_sel:WORD_1
	v_exp_f16_sdwa v214, v95 dst_sel:WORD_1 dst_unused:UNUSED_PRESERVE src0_sel:WORD_1
	v_exp_f16_sdwa v215, v96 dst_sel:WORD_1 dst_unused:UNUSED_PRESERVE src0_sel:WORD_1
	v_exp_f16_sdwa v216, v97 dst_sel:WORD_1 dst_unused:UNUSED_PRESERVE src0_sel:WORD_1
	v_pk_add_f16 v119, v119, v163 neg_lo:[0,1] neg_hi:[0,1]
	v_pk_add_f16 v97, v213, 0
	v_pk_fma_f16 v57, v57, v216, 0
	v_pk_add_f16 v94, v216, 0
	v_pk_add_f16 v95, v215, 0
	v_pk_add_f16 v96, v214, 0
	v_pk_fma_f16 v56, v56, v215, 0
	v_pk_fma_f16 v55, v55, v214, 0
	v_pk_fma_f16 v54, v54, v213, 0
	v_pk_add_f16 v120, v120, v164 neg_lo:[0,1] neg_hi:[0,1]
	v_pk_add_f16 v121, v121, v165 neg_lo:[0,1] neg_hi:[0,1]
	v_pk_add_f16 v82, v82, v162 neg_lo:[0,1] neg_hi:[0,1]
	v_exp_f16_sdwa v213, v118 dst_sel:WORD_0 dst_unused:UNUSED_PAD src0_sel:WORD_0
	v_exp_f16_sdwa v214, v119 dst_sel:WORD_0 dst_unused:UNUSED_PAD src0_sel:WORD_0
	v_exp_f16_sdwa v215, v120 dst_sel:WORD_0 dst_unused:UNUSED_PAD src0_sel:WORD_0
	v_exp_f16_sdwa v216, v121 dst_sel:WORD_0 dst_unused:UNUSED_PAD src0_sel:WORD_0
	v_exp_f16_sdwa v213, v118 dst_sel:WORD_1 dst_unused:UNUSED_PRESERVE src0_sel:WORD_1
	v_exp_f16_sdwa v214, v119 dst_sel:WORD_1 dst_unused:UNUSED_PRESERVE src0_sel:WORD_1
	v_exp_f16_sdwa v215, v120 dst_sel:WORD_1 dst_unused:UNUSED_PRESERVE src0_sel:WORD_1
	v_exp_f16_sdwa v216, v121 dst_sel:WORD_1 dst_unused:UNUSED_PRESERVE src0_sel:WORD_1
	v_pk_add_f16 v83, v83, v163 neg_lo:[0,1] neg_hi:[0,1]
	v_pk_add_f16 v97, v97, v213
	v_pk_fma_f16 v57, v77, v216, v57
	v_pk_add_f16 v77, v126, v165 neg_lo:[0,1] neg_hi:[0,1]
	v_pk_add_f16 v96, v96, v214
	v_pk_add_f16 v95, v95, v215
	v_pk_add_f16 v94, v94, v216
	v_pk_fma_f16 v54, v74, v213, v54
	v_pk_fma_f16 v55, v75, v214, v55
	v_pk_fma_f16 v56, v76, v215, v56
	v_pk_add_f16 v74, v129, v162 neg_lo:[0,1] neg_hi:[0,1]
	v_pk_add_f16 v75, v128, v163 neg_lo:[0,1] neg_hi:[0,1]
	v_pk_add_f16 v76, v127, v164 neg_lo:[0,1] neg_hi:[0,1]
	v_pk_add_f16 v84, v84, v164 neg_lo:[0,1] neg_hi:[0,1]
	v_exp_f16_sdwa v118, v74 dst_sel:WORD_0 dst_unused:UNUSED_PAD src0_sel:WORD_0
	v_exp_f16_sdwa v119, v75 dst_sel:WORD_0 dst_unused:UNUSED_PAD src0_sel:WORD_0
	v_exp_f16_sdwa v120, v76 dst_sel:WORD_0 dst_unused:UNUSED_PAD src0_sel:WORD_0
	v_exp_f16_sdwa v121, v77 dst_sel:WORD_0 dst_unused:UNUSED_PAD src0_sel:WORD_0
	v_exp_f16_sdwa v118, v74 dst_sel:WORD_1 dst_unused:UNUSED_PRESERVE src0_sel:WORD_1
	v_exp_f16_sdwa v119, v75 dst_sel:WORD_1 dst_unused:UNUSED_PRESERVE src0_sel:WORD_1
	v_exp_f16_sdwa v120, v76 dst_sel:WORD_1 dst_unused:UNUSED_PRESERVE src0_sel:WORD_1
	v_exp_f16_sdwa v121, v77 dst_sel:WORD_1 dst_unused:UNUSED_PRESERVE src0_sel:WORD_1
	v_pk_add_f16 v85, v85, v165 neg_lo:[0,1] neg_hi:[0,1]
	v_pk_add_f16 v77, v97, v118
	v_pk_add_f16 v74, v94, v121
	v_pk_add_f16 v75, v95, v120
	v_pk_add_f16 v76, v96, v119
	v_pk_fma_f16 v57, v101, v121, v57
	v_pk_fma_f16 v56, v100, v120, v56
	v_pk_fma_f16 v55, v99, v119, v55
	v_pk_fma_f16 v54, v98, v118, v54
	v_pk_add_f16 v94, v137, v162 neg_lo:[0,1] neg_hi:[0,1]
	v_pk_add_f16 v95, v136, v163 neg_lo:[0,1] neg_hi:[0,1]
	v_pk_add_f16 v96, v135, v164 neg_lo:[0,1] neg_hi:[0,1]
	v_pk_add_f16 v97, v134, v165 neg_lo:[0,1] neg_hi:[0,1]
	v_exp_f16_sdwa v98, v94 dst_sel:WORD_0 dst_unused:UNUSED_PAD src0_sel:WORD_0
	v_exp_f16_sdwa v99, v95 dst_sel:WORD_0 dst_unused:UNUSED_PAD src0_sel:WORD_0
	v_exp_f16_sdwa v100, v96 dst_sel:WORD_0 dst_unused:UNUSED_PAD src0_sel:WORD_0
	v_exp_f16_sdwa v101, v97 dst_sel:WORD_0 dst_unused:UNUSED_PAD src0_sel:WORD_0
	v_exp_f16_sdwa v98, v94 dst_sel:WORD_1 dst_unused:UNUSED_PRESERVE src0_sel:WORD_1
	v_exp_f16_sdwa v99, v95 dst_sel:WORD_1 dst_unused:UNUSED_PRESERVE src0_sel:WORD_1
	v_exp_f16_sdwa v100, v96 dst_sel:WORD_1 dst_unused:UNUSED_PRESERVE src0_sel:WORD_1
	v_exp_f16_sdwa v101, v97 dst_sel:WORD_1 dst_unused:UNUSED_PRESERVE src0_sel:WORD_1
	v_pk_add_f16 v94, v149, v162 neg_lo:[0,1] neg_hi:[0,1]
	v_pk_add_f16 v77, v77, v98
	v_pk_add_f16 v76, v76, v99
	v_pk_add_f16 v75, v75, v100
	v_pk_add_f16 v74, v74, v101
	v_pk_fma_f16 v54, v30, v98, v54
	v_pk_fma_f16 v55, v31, v99, v55
	v_pk_fma_f16 v56, v32, v100, v56
	v_pk_fma_f16 v57, v33, v101, v57
	v_pk_add_f16 v95, v148, v163 neg_lo:[0,1] neg_hi:[0,1]
	v_pk_add_f16 v96, v147, v164 neg_lo:[0,1] neg_hi:[0,1]
	v_pk_add_f16 v97, v146, v165 neg_lo:[0,1] neg_hi:[0,1]
	v_exp_f16_sdwa v98, v94 dst_sel:WORD_0 dst_unused:UNUSED_PAD src0_sel:WORD_0
	v_exp_f16_sdwa v99, v95 dst_sel:WORD_0 dst_unused:UNUSED_PAD src0_sel:WORD_0
	v_exp_f16_sdwa v100, v96 dst_sel:WORD_0 dst_unused:UNUSED_PAD src0_sel:WORD_0
	v_exp_f16_sdwa v101, v97 dst_sel:WORD_0 dst_unused:UNUSED_PAD src0_sel:WORD_0
	v_exp_f16_sdwa v98, v94 dst_sel:WORD_1 dst_unused:UNUSED_PRESERVE src0_sel:WORD_1
	v_exp_f16_sdwa v99, v95 dst_sel:WORD_1 dst_unused:UNUSED_PRESERVE src0_sel:WORD_1
	v_exp_f16_sdwa v100, v96 dst_sel:WORD_1 dst_unused:UNUSED_PRESERVE src0_sel:WORD_1
	v_exp_f16_sdwa v101, v97 dst_sel:WORD_1 dst_unused:UNUSED_PRESERVE src0_sel:WORD_1
	v_pk_add_f16 v94, v212, v162 neg_lo:[0,1] neg_hi:[0,1]
	v_pk_add_f16 v77, v77, v98
	v_pk_add_f16 v74, v74, v101
	v_pk_add_f16 v75, v75, v100
	v_pk_add_f16 v76, v76, v99
	v_pk_fma_f16 v57, v45, v101, v57
	v_pk_fma_f16 v56, v44, v100, v56
	v_pk_fma_f16 v55, v43, v99, v55
	v_pk_fma_f16 v54, v42, v98, v54
	v_pk_add_f16 v95, v211, v163 neg_lo:[0,1] neg_hi:[0,1]
	v_pk_add_f16 v96, v210, v164 neg_lo:[0,1] neg_hi:[0,1]
	v_pk_add_f16 v97, v209, v165 neg_lo:[0,1] neg_hi:[0,1]
	v_exp_f16_sdwa v98, v94 dst_sel:WORD_0 dst_unused:UNUSED_PAD src0_sel:WORD_0
	v_exp_f16_sdwa v99, v95 dst_sel:WORD_0 dst_unused:UNUSED_PAD src0_sel:WORD_0
	v_exp_f16_sdwa v100, v96 dst_sel:WORD_0 dst_unused:UNUSED_PAD src0_sel:WORD_0
	v_exp_f16_sdwa v101, v97 dst_sel:WORD_0 dst_unused:UNUSED_PAD src0_sel:WORD_0
	v_exp_f16_sdwa v98, v94 dst_sel:WORD_1 dst_unused:UNUSED_PRESERVE src0_sel:WORD_1
	v_exp_f16_sdwa v99, v95 dst_sel:WORD_1 dst_unused:UNUSED_PRESERVE src0_sel:WORD_1
	v_exp_f16_sdwa v100, v96 dst_sel:WORD_1 dst_unused:UNUSED_PRESERVE src0_sel:WORD_1
	v_exp_f16_sdwa v101, v97 dst_sel:WORD_1 dst_unused:UNUSED_PRESERVE src0_sel:WORD_1
	v_exp_f16_sdwa v94, v82 dst_sel:WORD_0 dst_unused:UNUSED_PAD src0_sel:WORD_0
	v_exp_f16_sdwa v95, v83 dst_sel:WORD_0 dst_unused:UNUSED_PAD src0_sel:WORD_0
	v_exp_f16_sdwa v96, v84 dst_sel:WORD_0 dst_unused:UNUSED_PAD src0_sel:WORD_0
	v_exp_f16_sdwa v97, v85 dst_sel:WORD_0 dst_unused:UNUSED_PAD src0_sel:WORD_0
	v_exp_f16_sdwa v94, v82 dst_sel:WORD_1 dst_unused:UNUSED_PRESERVE src0_sel:WORD_1
	v_exp_f16_sdwa v95, v83 dst_sel:WORD_1 dst_unused:UNUSED_PRESERVE src0_sel:WORD_1
	v_exp_f16_sdwa v96, v84 dst_sel:WORD_1 dst_unused:UNUSED_PRESERVE src0_sel:WORD_1
	v_exp_f16_sdwa v97, v85 dst_sel:WORD_1 dst_unused:UNUSED_PRESERVE src0_sel:WORD_1
	v_pk_add_f16 v82, v106, v162 neg_lo:[0,1] neg_hi:[0,1]
	v_pk_add_f16 v77, v77, v98
	v_pk_add_f16 v76, v76, v99
	v_pk_add_f16 v75, v75, v100
	v_pk_add_f16 v74, v74, v101
	v_pk_fma_f16 v54, v58, v98, v54
	v_pk_fma_f16 v55, v59, v99, v55
	v_pk_fma_f16 v56, v60, v100, v56
	v_pk_fma_f16 v57, v61, v101, v57
	v_pk_add_f16 v77, v77, v94
	v_pk_add_f16 v74, v74, v97
	v_pk_add_f16 v75, v75, v96
	v_pk_add_f16 v76, v76, v95
	v_pk_fma_f16 v57, v21, v97, v57
	v_pk_fma_f16 v56, v20, v96, v56
	v_pk_fma_f16 v55, v19, v95, v55
	v_pk_fma_f16 v54, v18, v94, v54
	v_pk_add_f16 v83, v107, v163 neg_lo:[0,1] neg_hi:[0,1]
	v_pk_add_f16 v84, v108, v164 neg_lo:[0,1] neg_hi:[0,1]
	v_pk_add_f16 v85, v109, v165 neg_lo:[0,1] neg_hi:[0,1]
	v_exp_f16_sdwa v94, v82 dst_sel:WORD_0 dst_unused:UNUSED_PAD src0_sel:WORD_0
	v_exp_f16_sdwa v95, v83 dst_sel:WORD_0 dst_unused:UNUSED_PAD src0_sel:WORD_0
	v_exp_f16_sdwa v96, v84 dst_sel:WORD_0 dst_unused:UNUSED_PAD src0_sel:WORD_0
	v_exp_f16_sdwa v97, v85 dst_sel:WORD_0 dst_unused:UNUSED_PAD src0_sel:WORD_0
	v_exp_f16_sdwa v94, v82 dst_sel:WORD_1 dst_unused:UNUSED_PRESERVE src0_sel:WORD_1
	v_exp_f16_sdwa v95, v83 dst_sel:WORD_1 dst_unused:UNUSED_PRESERVE src0_sel:WORD_1
	v_exp_f16_sdwa v96, v84 dst_sel:WORD_1 dst_unused:UNUSED_PRESERVE src0_sel:WORD_1
	v_exp_f16_sdwa v97, v85 dst_sel:WORD_1 dst_unused:UNUSED_PRESERVE src0_sel:WORD_1
	v_pk_add_f16 v82, v122, v162 neg_lo:[0,1] neg_hi:[0,1]
	v_pk_add_f16 v77, v77, v94
	v_pk_add_f16 v76, v76, v95
	v_pk_add_f16 v75, v75, v96
	v_pk_add_f16 v74, v74, v97
	v_pk_fma_f16 v54, v22, v94, v54
	v_pk_fma_f16 v55, v23, v95, v55
	v_pk_fma_f16 v56, v24, v96, v56
	v_pk_fma_f16 v57, v25, v97, v57
	v_pk_add_f16 v83, v123, v163 neg_lo:[0,1] neg_hi:[0,1]
	v_pk_add_f16 v84, v124, v164 neg_lo:[0,1] neg_hi:[0,1]
	v_pk_add_f16 v85, v125, v165 neg_lo:[0,1] neg_hi:[0,1]
	v_exp_f16_sdwa v94, v82 dst_sel:WORD_0 dst_unused:UNUSED_PAD src0_sel:WORD_0
	v_exp_f16_sdwa v95, v83 dst_sel:WORD_0 dst_unused:UNUSED_PAD src0_sel:WORD_0
	v_exp_f16_sdwa v96, v84 dst_sel:WORD_0 dst_unused:UNUSED_PAD src0_sel:WORD_0
	v_exp_f16_sdwa v97, v85 dst_sel:WORD_0 dst_unused:UNUSED_PAD src0_sel:WORD_0
	v_exp_f16_sdwa v94, v82 dst_sel:WORD_1 dst_unused:UNUSED_PRESERVE src0_sel:WORD_1
	v_exp_f16_sdwa v95, v83 dst_sel:WORD_1 dst_unused:UNUSED_PRESERVE src0_sel:WORD_1
	v_exp_f16_sdwa v96, v84 dst_sel:WORD_1 dst_unused:UNUSED_PRESERVE src0_sel:WORD_1
	v_exp_f16_sdwa v97, v85 dst_sel:WORD_1 dst_unused:UNUSED_PRESERVE src0_sel:WORD_1
	v_pk_add_f16 v77, v77, v94
	v_pk_add_f16 v76, v76, v95
	v_rcp_f16_e32 v82, v77
	v_rcp_f16_sdwa v77, v77 dst_sel:DWORD dst_unused:UNUSED_PAD src0_sel:WORD_1
	v_pk_add_f16 v75, v75, v96
	v_rcp_f16_e32 v83, v76
	v_rcp_f16_sdwa v76, v76 dst_sel:DWORD dst_unused:UNUSED_PAD src0_sel:WORD_1
	v_pk_add_f16 v74, v74, v97
	v_rcp_f16_e32 v84, v75
	v_rcp_f16_sdwa v75, v75 dst_sel:DWORD dst_unused:UNUSED_PAD src0_sel:WORD_1
	v_rcp_f16_e32 v85, v74
	v_rcp_f16_sdwa v74, v74 dst_sel:DWORD dst_unused:UNUSED_PAD src0_sel:WORD_1
	v_pk_fma_f16 v54, v26, v94, v54
	v_pack_b32_f16 v77, v82, v77
	v_pk_fma_f16 v57, v29, v97, v57
	v_pk_fma_f16 v55, v27, v95, v55
	v_pk_mul_f16 v97, v54, v77
	v_pack_b32_f16 v54, v83, v76
	v_pk_fma_f16 v56, v28, v96, v56
	v_pk_mul_f16 v96, v55, v54
	v_pack_b32_f16 v54, v84, v75
	v_pk_mul_f16 v95, v56, v54
	v_pack_b32_f16 v54, v85, v74
	v_pk_mul_f16 v94, v57, v54
	s_waitcnt vmcnt(6)
	v_pk_mul_f16 v57, v208, v161 op_sel_hi:[0,1]
	v_pk_mul_f16 v77, v206, v161 op_sel_hi:[0,1]
	v_pk_mul_f16 v85, v207, v161 op_sel_hi:[0,1]
	v_pk_mul_f16 v54, v208, v158 op_sel_hi:[0,1]
	v_pk_mul_f16 v55, v208, v159 op_sel_hi:[0,1]
	v_pk_mul_f16 v56, v208, v160 op_sel_hi:[0,1]
	v_pk_mul_f16 v74, v206, v158 op_sel_hi:[0,1]
	v_pk_mul_f16 v75, v206, v159 op_sel_hi:[0,1]
	v_pk_mul_f16 v76, v206, v160 op_sel_hi:[0,1]
	v_pk_mul_f16 v82, v207, v158 op_sel_hi:[0,1]
	v_pk_mul_f16 v83, v207, v159 op_sel_hi:[0,1]
	v_pk_mul_f16 v84, v207, v160 op_sel_hi:[0,1]
	v_pk_fma_f16 v65, v65, v161, v57
	v_pk_fma_f16 v81, v81, v161, v77
	v_pk_fma_f16 v98, v105, v161, v85
	v_pk_fma_f16 v64, v64, v160, v56
	v_pk_maximum3_f16 v125, v65, v81, v98
	v_pk_fma_f16 v63, v63, v159, v55
	v_pk_fma_f16 v62, v62, v158, v54
	v_pk_fma_f16 v80, v80, v160, v76
	v_pk_fma_f16 v79, v79, v159, v75
	v_pk_fma_f16 v78, v78, v158, v74
	v_pk_fma_f16 v99, v104, v160, v84
	v_pk_fma_f16 v100, v103, v159, v83
	v_pk_fma_f16 v101, v102, v158, v82
	v_pk_fma_f16 v102, v37, v161, v57
	v_pk_fma_f16 v106, v49, v161, v77
	v_pk_fma_f16 v118, v69, v161, v85
	v_pk_fma_f16 v57, v89, v161, v57
	v_pk_fma_f16 v77, v117, v161, v77
	v_pk_fma_f16 v85, v133, v161, v85
	v_pk_maximum3_f16 v122, v62, v78, v101
	v_pk_maximum3_f16 v123, v63, v79, v100
	v_pk_maximum3_f16 v124, v64, v80, v99
	v_pk_maximum3_f16 v129, v102, v106, v118
	v_pk_fma_f16 v103, v36, v160, v56
	v_pk_maximum3_f16 v137, v57, v77, v85
	v_pk_fma_f16 v104, v35, v159, v55
	v_pk_maximum3_f16 v125, v125, v129, v137
	v_pk_fma_f16 v105, v34, v158, v54
	v_pk_fma_f16 v107, v48, v160, v76
	v_pk_fma_f16 v108, v47, v159, v75
	v_pk_fma_f16 v109, v46, v158, v74
	v_pk_fma_f16 v119, v68, v160, v84
	v_pk_fma_f16 v120, v67, v159, v83
	v_pk_fma_f16 v121, v66, v158, v82
	v_pk_fma_f16 v56, v88, v160, v56
	v_pk_fma_f16 v55, v87, v159, v55
	v_pk_fma_f16 v54, v86, v158, v54
	v_pk_fma_f16 v76, v116, v160, v76
	v_pk_fma_f16 v75, v115, v159, v75
	v_pk_fma_f16 v74, v114, v158, v74
	v_pk_fma_f16 v84, v132, v160, v84
	v_pk_fma_f16 v83, v131, v159, v83
	v_pk_fma_f16 v82, v130, v158, v82
	v_pk_maximum3_f16 v126, v105, v109, v121
	v_pk_maximum3_f16 v127, v104, v108, v120
	v_pk_maximum3_f16 v128, v103, v107, v119
	v_pk_maximum3_f16 v135, v55, v75, v83
	v_pk_maximum3_f16 v136, v56, v76, v84
	v_pk_maximum3_f16 v134, v54, v74, v82
	v_pk_maximum3_f16 v122, v122, v126, v134
	v_pk_maximum3_f16 v123, v123, v127, v135
	v_pk_maximum3_f16 v124, v124, v128, v136
	v_pk_add_f16 v65, v65, v125 neg_lo:[0,1] neg_hi:[0,1]
	v_pk_add_f16 v62, v62, v122 neg_lo:[0,1] neg_hi:[0,1]
	v_pk_add_f16 v63, v63, v123 neg_lo:[0,1] neg_hi:[0,1]
	v_pk_add_f16 v64, v64, v124 neg_lo:[0,1] neg_hi:[0,1]
	v_pk_add_f16 v78, v78, v122 neg_lo:[0,1] neg_hi:[0,1]
	v_exp_f16_sdwa v126, v62 dst_sel:WORD_0 dst_unused:UNUSED_PAD src0_sel:WORD_0
	v_exp_f16_sdwa v127, v63 dst_sel:WORD_0 dst_unused:UNUSED_PAD src0_sel:WORD_0
	v_exp_f16_sdwa v128, v64 dst_sel:WORD_0 dst_unused:UNUSED_PAD src0_sel:WORD_0
	v_exp_f16_sdwa v129, v65 dst_sel:WORD_0 dst_unused:UNUSED_PAD src0_sel:WORD_0
	v_exp_f16_sdwa v126, v62 dst_sel:WORD_1 dst_unused:UNUSED_PRESERVE src0_sel:WORD_1
	v_exp_f16_sdwa v127, v63 dst_sel:WORD_1 dst_unused:UNUSED_PRESERVE src0_sel:WORD_1
	v_exp_f16_sdwa v128, v64 dst_sel:WORD_1 dst_unused:UNUSED_PRESERVE src0_sel:WORD_1
	v_exp_f16_sdwa v129, v65 dst_sel:WORD_1 dst_unused:UNUSED_PRESERVE src0_sel:WORD_1
	v_pk_add_f16 v79, v79, v123 neg_lo:[0,1] neg_hi:[0,1]
	v_pk_add_f16 v65, v126, 0
	v_pk_fma_f16 v33, v33, v129, 0
	v_pk_add_f16 v62, v129, 0
	v_pk_add_f16 v63, v128, 0
	v_pk_add_f16 v64, v127, 0
	v_pk_fma_f16 v32, v32, v128, 0
	v_pk_fma_f16 v31, v31, v127, 0
	v_pk_fma_f16 v30, v30, v126, 0
	v_pk_add_f16 v80, v80, v124 neg_lo:[0,1] neg_hi:[0,1]
	v_pk_add_f16 v81, v81, v125 neg_lo:[0,1] neg_hi:[0,1]
	v_pk_add_f16 v54, v54, v122 neg_lo:[0,1] neg_hi:[0,1]
	v_exp_f16_sdwa v126, v78 dst_sel:WORD_0 dst_unused:UNUSED_PAD src0_sel:WORD_0
	v_exp_f16_sdwa v127, v79 dst_sel:WORD_0 dst_unused:UNUSED_PAD src0_sel:WORD_0
	v_exp_f16_sdwa v128, v80 dst_sel:WORD_0 dst_unused:UNUSED_PAD src0_sel:WORD_0
	v_exp_f16_sdwa v129, v81 dst_sel:WORD_0 dst_unused:UNUSED_PAD src0_sel:WORD_0
	v_exp_f16_sdwa v126, v78 dst_sel:WORD_1 dst_unused:UNUSED_PRESERVE src0_sel:WORD_1
	v_exp_f16_sdwa v127, v79 dst_sel:WORD_1 dst_unused:UNUSED_PRESERVE src0_sel:WORD_1
	v_exp_f16_sdwa v128, v80 dst_sel:WORD_1 dst_unused:UNUSED_PRESERVE src0_sel:WORD_1
	v_exp_f16_sdwa v129, v81 dst_sel:WORD_1 dst_unused:UNUSED_PRESERVE src0_sel:WORD_1
	v_pk_add_f16 v55, v55, v123 neg_lo:[0,1] neg_hi:[0,1]
	v_pk_add_f16 v65, v65, v126
	v_pk_fma_f16 v33, v45, v129, v33
	v_pk_add_f16 v45, v98, v125 neg_lo:[0,1] neg_hi:[0,1]
	v_pk_add_f16 v64, v64, v127
	v_pk_add_f16 v63, v63, v128
	v_pk_add_f16 v62, v62, v129
	v_pk_fma_f16 v30, v42, v126, v30
	v_pk_fma_f16 v31, v43, v127, v31
	v_pk_fma_f16 v32, v44, v128, v32
	v_pk_add_f16 v42, v101, v122 neg_lo:[0,1] neg_hi:[0,1]
	v_pk_add_f16 v43, v100, v123 neg_lo:[0,1] neg_hi:[0,1]
	v_pk_add_f16 v44, v99, v124 neg_lo:[0,1] neg_hi:[0,1]
	v_pk_add_f16 v56, v56, v124 neg_lo:[0,1] neg_hi:[0,1]
	v_exp_f16_sdwa v78, v42 dst_sel:WORD_0 dst_unused:UNUSED_PAD src0_sel:WORD_0
	v_exp_f16_sdwa v79, v43 dst_sel:WORD_0 dst_unused:UNUSED_PAD src0_sel:WORD_0
	v_exp_f16_sdwa v80, v44 dst_sel:WORD_0 dst_unused:UNUSED_PAD src0_sel:WORD_0
	v_exp_f16_sdwa v81, v45 dst_sel:WORD_0 dst_unused:UNUSED_PAD src0_sel:WORD_0
	v_exp_f16_sdwa v78, v42 dst_sel:WORD_1 dst_unused:UNUSED_PRESERVE src0_sel:WORD_1
	v_exp_f16_sdwa v79, v43 dst_sel:WORD_1 dst_unused:UNUSED_PRESERVE src0_sel:WORD_1
	v_exp_f16_sdwa v80, v44 dst_sel:WORD_1 dst_unused:UNUSED_PRESERVE src0_sel:WORD_1
	v_exp_f16_sdwa v81, v45 dst_sel:WORD_1 dst_unused:UNUSED_PRESERVE src0_sel:WORD_1
	v_pk_add_f16 v57, v57, v125 neg_lo:[0,1] neg_hi:[0,1]
	v_pk_add_f16 v45, v65, v78
	v_pk_add_f16 v42, v62, v81
	v_pk_add_f16 v43, v63, v80
	v_pk_add_f16 v44, v64, v79
	v_pk_fma_f16 v33, v61, v81, v33
	v_pk_fma_f16 v32, v60, v80, v32
	v_pk_fma_f16 v31, v59, v79, v31
	v_pk_fma_f16 v30, v58, v78, v30
	v_pk_add_f16 v58, v105, v122 neg_lo:[0,1] neg_hi:[0,1]
	v_pk_add_f16 v59, v104, v123 neg_lo:[0,1] neg_hi:[0,1]
	v_pk_add_f16 v60, v103, v124 neg_lo:[0,1] neg_hi:[0,1]
	v_pk_add_f16 v61, v102, v125 neg_lo:[0,1] neg_hi:[0,1]
	v_exp_f16_sdwa v62, v58 dst_sel:WORD_0 dst_unused:UNUSED_PAD src0_sel:WORD_0
	v_exp_f16_sdwa v63, v59 dst_sel:WORD_0 dst_unused:UNUSED_PAD src0_sel:WORD_0
	v_exp_f16_sdwa v64, v60 dst_sel:WORD_0 dst_unused:UNUSED_PAD src0_sel:WORD_0
	v_exp_f16_sdwa v65, v61 dst_sel:WORD_0 dst_unused:UNUSED_PAD src0_sel:WORD_0
	v_exp_f16_sdwa v62, v58 dst_sel:WORD_1 dst_unused:UNUSED_PRESERVE src0_sel:WORD_1
	v_exp_f16_sdwa v63, v59 dst_sel:WORD_1 dst_unused:UNUSED_PRESERVE src0_sel:WORD_1
	v_exp_f16_sdwa v64, v60 dst_sel:WORD_1 dst_unused:UNUSED_PRESERVE src0_sel:WORD_1
	v_exp_f16_sdwa v65, v61 dst_sel:WORD_1 dst_unused:UNUSED_PRESERVE src0_sel:WORD_1
	v_pk_add_f16 v58, v109, v122 neg_lo:[0,1] neg_hi:[0,1]
	v_pk_add_f16 v45, v45, v62
	v_pk_add_f16 v44, v44, v63
	v_pk_add_f16 v43, v43, v64
	v_pk_add_f16 v42, v42, v65
	v_pk_fma_f16 v30, v18, v62, v30
	v_pk_fma_f16 v31, v19, v63, v31
	v_pk_fma_f16 v32, v20, v64, v32
	v_pk_fma_f16 v33, v21, v65, v33
	v_pk_add_f16 v59, v108, v123 neg_lo:[0,1] neg_hi:[0,1]
	v_pk_add_f16 v60, v107, v124 neg_lo:[0,1] neg_hi:[0,1]
	v_pk_add_f16 v61, v106, v125 neg_lo:[0,1] neg_hi:[0,1]
	v_exp_f16_sdwa v62, v58 dst_sel:WORD_0 dst_unused:UNUSED_PAD src0_sel:WORD_0
	v_exp_f16_sdwa v63, v59 dst_sel:WORD_0 dst_unused:UNUSED_PAD src0_sel:WORD_0
	v_exp_f16_sdwa v64, v60 dst_sel:WORD_0 dst_unused:UNUSED_PAD src0_sel:WORD_0
	v_exp_f16_sdwa v65, v61 dst_sel:WORD_0 dst_unused:UNUSED_PAD src0_sel:WORD_0
	v_exp_f16_sdwa v62, v58 dst_sel:WORD_1 dst_unused:UNUSED_PRESERVE src0_sel:WORD_1
	v_exp_f16_sdwa v63, v59 dst_sel:WORD_1 dst_unused:UNUSED_PRESERVE src0_sel:WORD_1
	v_exp_f16_sdwa v64, v60 dst_sel:WORD_1 dst_unused:UNUSED_PRESERVE src0_sel:WORD_1
	v_exp_f16_sdwa v65, v61 dst_sel:WORD_1 dst_unused:UNUSED_PRESERVE src0_sel:WORD_1
	v_pk_add_f16 v58, v121, v122 neg_lo:[0,1] neg_hi:[0,1]
	v_pk_add_f16 v45, v45, v62
	v_pk_add_f16 v42, v42, v65
	v_pk_add_f16 v43, v43, v64
	v_pk_add_f16 v44, v44, v63
	v_pk_fma_f16 v33, v25, v65, v33
	v_pk_fma_f16 v32, v24, v64, v32
	v_pk_fma_f16 v31, v23, v63, v31
	v_pk_fma_f16 v30, v22, v62, v30
	v_pk_add_f16 v59, v120, v123 neg_lo:[0,1] neg_hi:[0,1]
	v_pk_add_f16 v60, v119, v124 neg_lo:[0,1] neg_hi:[0,1]
	v_pk_add_f16 v61, v118, v125 neg_lo:[0,1] neg_hi:[0,1]
	v_exp_f16_sdwa v62, v58 dst_sel:WORD_0 dst_unused:UNUSED_PAD src0_sel:WORD_0
	v_exp_f16_sdwa v63, v59 dst_sel:WORD_0 dst_unused:UNUSED_PAD src0_sel:WORD_0
	v_exp_f16_sdwa v64, v60 dst_sel:WORD_0 dst_unused:UNUSED_PAD src0_sel:WORD_0
	v_exp_f16_sdwa v65, v61 dst_sel:WORD_0 dst_unused:UNUSED_PAD src0_sel:WORD_0
	v_exp_f16_sdwa v62, v58 dst_sel:WORD_1 dst_unused:UNUSED_PRESERVE src0_sel:WORD_1
	v_exp_f16_sdwa v63, v59 dst_sel:WORD_1 dst_unused:UNUSED_PRESERVE src0_sel:WORD_1
	v_exp_f16_sdwa v64, v60 dst_sel:WORD_1 dst_unused:UNUSED_PRESERVE src0_sel:WORD_1
	v_exp_f16_sdwa v65, v61 dst_sel:WORD_1 dst_unused:UNUSED_PRESERVE src0_sel:WORD_1
	v_exp_f16_sdwa v58, v54 dst_sel:WORD_0 dst_unused:UNUSED_PAD src0_sel:WORD_0
	v_exp_f16_sdwa v59, v55 dst_sel:WORD_0 dst_unused:UNUSED_PAD src0_sel:WORD_0
	v_exp_f16_sdwa v60, v56 dst_sel:WORD_0 dst_unused:UNUSED_PAD src0_sel:WORD_0
	v_exp_f16_sdwa v61, v57 dst_sel:WORD_0 dst_unused:UNUSED_PAD src0_sel:WORD_0
	v_exp_f16_sdwa v58, v54 dst_sel:WORD_1 dst_unused:UNUSED_PRESERVE src0_sel:WORD_1
	v_exp_f16_sdwa v59, v55 dst_sel:WORD_1 dst_unused:UNUSED_PRESERVE src0_sel:WORD_1
	v_exp_f16_sdwa v60, v56 dst_sel:WORD_1 dst_unused:UNUSED_PRESERVE src0_sel:WORD_1
	v_exp_f16_sdwa v61, v57 dst_sel:WORD_1 dst_unused:UNUSED_PRESERVE src0_sel:WORD_1
	v_pk_add_f16 v54, v74, v122 neg_lo:[0,1] neg_hi:[0,1]
	v_pk_add_f16 v45, v45, v62
	v_pk_add_f16 v44, v44, v63
	v_pk_add_f16 v43, v43, v64
	v_pk_add_f16 v42, v42, v65
	v_pk_fma_f16 v30, v26, v62, v30
	v_pk_fma_f16 v31, v27, v63, v31
	v_pk_fma_f16 v32, v28, v64, v32
	v_pk_fma_f16 v33, v29, v65, v33
	v_pk_add_f16 v45, v45, v58
	v_pk_add_f16 v42, v42, v61
	v_pk_add_f16 v43, v43, v60
	v_pk_add_f16 v44, v44, v59
	v_pk_fma_f16 v33, v41, v61, v33
	v_pk_fma_f16 v32, v40, v60, v32
	v_pk_fma_f16 v31, v39, v59, v31
	v_pk_fma_f16 v30, v38, v58, v30
	v_pk_add_f16 v55, v75, v123 neg_lo:[0,1] neg_hi:[0,1]
	v_pk_add_f16 v56, v76, v124 neg_lo:[0,1] neg_hi:[0,1]
	v_pk_add_f16 v57, v77, v125 neg_lo:[0,1] neg_hi:[0,1]
	v_exp_f16_sdwa v58, v54 dst_sel:WORD_0 dst_unused:UNUSED_PAD src0_sel:WORD_0
	v_exp_f16_sdwa v59, v55 dst_sel:WORD_0 dst_unused:UNUSED_PAD src0_sel:WORD_0
	v_exp_f16_sdwa v60, v56 dst_sel:WORD_0 dst_unused:UNUSED_PAD src0_sel:WORD_0
	v_exp_f16_sdwa v61, v57 dst_sel:WORD_0 dst_unused:UNUSED_PAD src0_sel:WORD_0
	v_exp_f16_sdwa v58, v54 dst_sel:WORD_1 dst_unused:UNUSED_PRESERVE src0_sel:WORD_1
	v_exp_f16_sdwa v59, v55 dst_sel:WORD_1 dst_unused:UNUSED_PRESERVE src0_sel:WORD_1
	v_exp_f16_sdwa v60, v56 dst_sel:WORD_1 dst_unused:UNUSED_PRESERVE src0_sel:WORD_1
	v_exp_f16_sdwa v61, v57 dst_sel:WORD_1 dst_unused:UNUSED_PRESERVE src0_sel:WORD_1
	v_pk_add_f16 v54, v82, v122 neg_lo:[0,1] neg_hi:[0,1]
	v_pk_add_f16 v45, v45, v58
	v_pk_add_f16 v44, v44, v59
	v_pk_add_f16 v43, v43, v60
	v_pk_add_f16 v42, v42, v61
	v_pk_fma_f16 v30, v50, v58, v30
	v_pk_fma_f16 v31, v51, v59, v31
	v_pk_fma_f16 v32, v52, v60, v32
	v_pk_fma_f16 v33, v53, v61, v33
	v_pk_add_f16 v55, v83, v123 neg_lo:[0,1] neg_hi:[0,1]
	v_pk_add_f16 v56, v84, v124 neg_lo:[0,1] neg_hi:[0,1]
	v_pk_add_f16 v57, v85, v125 neg_lo:[0,1] neg_hi:[0,1]
	v_exp_f16_sdwa v58, v54 dst_sel:WORD_0 dst_unused:UNUSED_PAD src0_sel:WORD_0
	v_exp_f16_sdwa v59, v55 dst_sel:WORD_0 dst_unused:UNUSED_PAD src0_sel:WORD_0
	v_exp_f16_sdwa v60, v56 dst_sel:WORD_0 dst_unused:UNUSED_PAD src0_sel:WORD_0
	v_exp_f16_sdwa v61, v57 dst_sel:WORD_0 dst_unused:UNUSED_PAD src0_sel:WORD_0
	v_exp_f16_sdwa v58, v54 dst_sel:WORD_1 dst_unused:UNUSED_PRESERVE src0_sel:WORD_1
	v_exp_f16_sdwa v59, v55 dst_sel:WORD_1 dst_unused:UNUSED_PRESERVE src0_sel:WORD_1
	v_exp_f16_sdwa v60, v56 dst_sel:WORD_1 dst_unused:UNUSED_PRESERVE src0_sel:WORD_1
	v_exp_f16_sdwa v61, v57 dst_sel:WORD_1 dst_unused:UNUSED_PRESERVE src0_sel:WORD_1
	v_pk_add_f16 v45, v45, v58
	v_pk_add_f16 v44, v44, v59
	v_rcp_f16_e32 v54, v45
	v_rcp_f16_sdwa v45, v45 dst_sel:DWORD dst_unused:UNUSED_PAD src0_sel:WORD_1
	v_pk_add_f16 v43, v43, v60
	v_rcp_f16_e32 v55, v44
	v_rcp_f16_sdwa v44, v44 dst_sel:DWORD dst_unused:UNUSED_PAD src0_sel:WORD_1
	v_pk_add_f16 v42, v42, v61
	v_rcp_f16_e32 v56, v43
	v_rcp_f16_sdwa v43, v43 dst_sel:DWORD dst_unused:UNUSED_PAD src0_sel:WORD_1
	v_rcp_f16_e32 v57, v42
	v_rcp_f16_sdwa v42, v42 dst_sel:DWORD dst_unused:UNUSED_PAD src0_sel:WORD_1
	v_pk_fma_f16 v30, v70, v58, v30
	v_pack_b32_f16 v45, v54, v45
	v_pk_fma_f16 v31, v71, v59, v31
	v_pk_mul_f16 v45, v30, v45
	v_pack_b32_f16 v30, v55, v44
	v_pk_fma_f16 v32, v72, v60, v32
	v_pk_mul_f16 v44, v31, v30
	v_pack_b32_f16 v30, v56, v43
	v_pk_fma_f16 v33, v73, v61, v33
	v_pk_mul_f16 v43, v32, v30
	v_pack_b32_f16 v30, v57, v42
	v_pk_mul_f16 v42, v33, v30
	s_waitcnt vmcnt(0)
	v_pk_mul_f16 v30, v208, v154 op_sel_hi:[0,1]
	v_pk_mul_f16 v31, v208, v155 op_sel_hi:[0,1]
	v_pk_mul_f16 v32, v208, v156 op_sel_hi:[0,1]
	v_pk_mul_f16 v33, v208, v157 op_sel_hi:[0,1]
	v_pk_mul_f16 v54, v206, v154 op_sel_hi:[0,1]
	v_pk_mul_f16 v55, v206, v155 op_sel_hi:[0,1]
	v_pk_mul_f16 v56, v206, v156 op_sel_hi:[0,1]
	v_pk_mul_f16 v57, v206, v157 op_sel_hi:[0,1]
	v_pk_mul_f16 v58, v207, v154 op_sel_hi:[0,1]
	v_pk_mul_f16 v59, v207, v155 op_sel_hi:[0,1]
	v_pk_mul_f16 v60, v207, v156 op_sel_hi:[0,1]
	v_pk_mul_f16 v61, v207, v157 op_sel_hi:[0,1]
	v_pk_fma_f16 v37, v37, v157, v33
	v_pk_fma_f16 v36, v36, v156, v32
	v_pk_fma_f16 v35, v35, v155, v31
	v_pk_fma_f16 v34, v34, v154, v30
	v_pk_fma_f16 v49, v49, v157, v57
	v_pk_fma_f16 v48, v48, v156, v56
	v_pk_fma_f16 v47, v47, v155, v55
	v_pk_fma_f16 v46, v46, v154, v54
	v_pk_fma_f16 v62, v69, v157, v61
	v_pk_fma_f16 v63, v68, v156, v60
	v_pk_fma_f16 v64, v67, v155, v59
	v_pk_fma_f16 v65, v66, v154, v58
	v_pk_fma_f16 v66, v89, v157, v33
	v_pk_fma_f16 v67, v88, v156, v32
	v_pk_fma_f16 v68, v87, v155, v31
	v_pk_fma_f16 v69, v86, v154, v30
	v_pk_fma_f16 v74, v117, v157, v57
	v_pk_fma_f16 v75, v116, v156, v56
	v_pk_fma_f16 v76, v115, v155, v55
	v_pk_fma_f16 v77, v114, v154, v54
	v_pk_fma_f16 v78, v133, v157, v61
	v_pk_fma_f16 v79, v132, v156, v60
	v_pk_fma_f16 v80, v131, v155, v59
	v_pk_fma_f16 v81, v130, v154, v58
	v_pk_fma_f16 v61, v17, v157, v61
	v_pk_fma_f16 v60, v16, v156, v60
	v_pk_fma_f16 v59, v15, v155, v59
	v_pk_fma_f16 v58, v14, v154, v58
	v_pk_maximum3_f16 v14, v34, v46, v65
	v_pk_maximum3_f16 v15, v35, v47, v64
	v_pk_maximum3_f16 v16, v36, v48, v63
	v_pk_maximum3_f16 v17, v37, v49, v62
	v_pk_maximum3_f16 v82, v69, v77, v81
	v_pk_maximum3_f16 v83, v68, v76, v80
	v_pk_maximum3_f16 v84, v67, v75, v79
	v_pk_maximum3_f16 v85, v66, v74, v78
	v_pk_fma_f16 v33, v145, v157, v33
	v_pk_fma_f16 v32, v144, v156, v32
	v_pk_fma_f16 v31, v143, v155, v31
	v_pk_fma_f16 v30, v142, v154, v30
	v_pk_fma_f16 v57, v153, v157, v57
	v_pk_fma_f16 v56, v152, v156, v56
	v_pk_fma_f16 v55, v151, v155, v55
	v_pk_fma_f16 v54, v150, v154, v54
	v_pk_maximum3_f16 v87, v31, v55, v59
	v_pk_maximum3_f16 v88, v32, v56, v60
	v_pk_maximum3_f16 v89, v33, v57, v61
	v_pk_maximum3_f16 v86, v30, v54, v58
	v_pk_maximum3_f16 v15, v15, v83, v87
	v_pk_maximum3_f16 v16, v16, v84, v88
	v_pk_maximum3_f16 v17, v17, v85, v89
	v_pk_maximum3_f16 v14, v14, v82, v86
	v_xor_b32_e32 v82, 0x80008000, v17
	v_xor_b32_e32 v83, 0x80008000, v16
	v_xor_b32_e32 v84, 0x80008000, v15
	v_xor_b32_e32 v85, 0x80008000, v14
	v_pk_add_f16 v14, v34, v85
	v_pk_add_f16 v15, v35, v84
	v_pk_add_f16 v16, v36, v83
	v_pk_add_f16 v17, v37, v82
	v_exp_f16_sdwa v34, v14 dst_sel:WORD_0 dst_unused:UNUSED_PAD src0_sel:WORD_0
	v_exp_f16_sdwa v35, v15 dst_sel:WORD_0 dst_unused:UNUSED_PAD src0_sel:WORD_0
	v_exp_f16_sdwa v36, v16 dst_sel:WORD_0 dst_unused:UNUSED_PAD src0_sel:WORD_0
	v_exp_f16_sdwa v37, v17 dst_sel:WORD_0 dst_unused:UNUSED_PAD src0_sel:WORD_0
	v_exp_f16_sdwa v34, v14 dst_sel:WORD_1 dst_unused:UNUSED_PRESERVE src0_sel:WORD_1
	v_exp_f16_sdwa v35, v15 dst_sel:WORD_1 dst_unused:UNUSED_PRESERVE src0_sel:WORD_1
	v_exp_f16_sdwa v36, v16 dst_sel:WORD_1 dst_unused:UNUSED_PRESERVE src0_sel:WORD_1
	v_exp_f16_sdwa v37, v17 dst_sel:WORD_1 dst_unused:UNUSED_PRESERVE src0_sel:WORD_1
	v_pk_add_f16 v14, v34, 0
	v_pk_add_f16 v15, v35, 0
	v_pk_add_f16 v16, v36, 0
	v_pk_add_f16 v17, v37, 0
	v_pk_fma_f16 v18, v18, v34, 0
	v_pk_fma_f16 v19, v19, v35, 0
	v_pk_fma_f16 v20, v20, v36, 0
	v_pk_fma_f16 v21, v21, v37, 0
	v_pk_add_f16 v34, v46, v85
	v_pk_add_f16 v35, v47, v84
	v_pk_add_f16 v36, v48, v83
	v_pk_add_f16 v37, v49, v82
	v_exp_f16_sdwa v46, v34 dst_sel:WORD_0 dst_unused:UNUSED_PAD src0_sel:WORD_0
	v_exp_f16_sdwa v47, v35 dst_sel:WORD_0 dst_unused:UNUSED_PAD src0_sel:WORD_0
	v_exp_f16_sdwa v48, v36 dst_sel:WORD_0 dst_unused:UNUSED_PAD src0_sel:WORD_0
	v_exp_f16_sdwa v49, v37 dst_sel:WORD_0 dst_unused:UNUSED_PAD src0_sel:WORD_0
	v_exp_f16_sdwa v46, v34 dst_sel:WORD_1 dst_unused:UNUSED_PRESERVE src0_sel:WORD_1
	v_exp_f16_sdwa v47, v35 dst_sel:WORD_1 dst_unused:UNUSED_PRESERVE src0_sel:WORD_1
	v_exp_f16_sdwa v48, v36 dst_sel:WORD_1 dst_unused:UNUSED_PRESERVE src0_sel:WORD_1
	v_exp_f16_sdwa v49, v37 dst_sel:WORD_1 dst_unused:UNUSED_PRESERVE src0_sel:WORD_1
	s_nop 0
	v_pk_add_f16 v17, v17, v49
	v_pk_add_f16 v16, v16, v48
	v_pk_add_f16 v15, v15, v47
	v_pk_add_f16 v14, v14, v46
	v_pk_fma_f16 v21, v25, v49, v21
	v_pk_fma_f16 v20, v24, v48, v20
	v_pk_fma_f16 v19, v23, v47, v19
	v_pk_fma_f16 v18, v22, v46, v18
	v_pk_add_f16 v22, v65, v85
	v_pk_add_f16 v23, v64, v84
	v_pk_add_f16 v24, v63, v83
	v_pk_add_f16 v25, v62, v82
	v_exp_f16_sdwa v34, v22 dst_sel:WORD_0 dst_unused:UNUSED_PAD src0_sel:WORD_0
	v_exp_f16_sdwa v35, v23 dst_sel:WORD_0 dst_unused:UNUSED_PAD src0_sel:WORD_0
	v_exp_f16_sdwa v36, v24 dst_sel:WORD_0 dst_unused:UNUSED_PAD src0_sel:WORD_0
	v_exp_f16_sdwa v37, v25 dst_sel:WORD_0 dst_unused:UNUSED_PAD src0_sel:WORD_0
	v_exp_f16_sdwa v34, v22 dst_sel:WORD_1 dst_unused:UNUSED_PRESERVE src0_sel:WORD_1
	v_exp_f16_sdwa v35, v23 dst_sel:WORD_1 dst_unused:UNUSED_PRESERVE src0_sel:WORD_1
	v_exp_f16_sdwa v36, v24 dst_sel:WORD_1 dst_unused:UNUSED_PRESERVE src0_sel:WORD_1
	v_exp_f16_sdwa v37, v25 dst_sel:WORD_1 dst_unused:UNUSED_PRESERVE src0_sel:WORD_1
	v_pk_add_f16 v22, v69, v85
	v_pk_add_f16 v14, v14, v34
	v_pk_add_f16 v15, v15, v35
	v_pk_add_f16 v16, v16, v36
	v_pk_add_f16 v17, v17, v37
	v_pk_fma_f16 v18, v26, v34, v18
	v_pk_fma_f16 v19, v27, v35, v19
	v_pk_fma_f16 v20, v28, v36, v20
	v_pk_fma_f16 v21, v29, v37, v21
	v_pk_add_f16 v23, v68, v84
	v_pk_add_f16 v24, v67, v83
	v_pk_add_f16 v25, v66, v82
	v_exp_f16_sdwa v26, v22 dst_sel:WORD_0 dst_unused:UNUSED_PAD src0_sel:WORD_0
	v_exp_f16_sdwa v27, v23 dst_sel:WORD_0 dst_unused:UNUSED_PAD src0_sel:WORD_0
	v_exp_f16_sdwa v28, v24 dst_sel:WORD_0 dst_unused:UNUSED_PAD src0_sel:WORD_0
	v_exp_f16_sdwa v29, v25 dst_sel:WORD_0 dst_unused:UNUSED_PAD src0_sel:WORD_0
	v_exp_f16_sdwa v26, v22 dst_sel:WORD_1 dst_unused:UNUSED_PRESERVE src0_sel:WORD_1
	v_exp_f16_sdwa v27, v23 dst_sel:WORD_1 dst_unused:UNUSED_PRESERVE src0_sel:WORD_1
	v_exp_f16_sdwa v28, v24 dst_sel:WORD_1 dst_unused:UNUSED_PRESERVE src0_sel:WORD_1
	v_exp_f16_sdwa v29, v25 dst_sel:WORD_1 dst_unused:UNUSED_PRESERVE src0_sel:WORD_1
	v_pk_add_f16 v22, v77, v85
	v_pk_add_f16 v17, v17, v29
	v_pk_add_f16 v16, v16, v28
	v_pk_add_f16 v15, v15, v27
	v_pk_add_f16 v14, v14, v26
	v_pk_fma_f16 v21, v41, v29, v21
	v_pk_fma_f16 v20, v40, v28, v20
	v_pk_fma_f16 v19, v39, v27, v19
	v_pk_fma_f16 v18, v38, v26, v18
	v_pk_add_f16 v23, v76, v84
	v_pk_add_f16 v24, v75, v83
	v_pk_add_f16 v25, v74, v82
	v_exp_f16_sdwa v26, v22 dst_sel:WORD_0 dst_unused:UNUSED_PAD src0_sel:WORD_0
	v_exp_f16_sdwa v27, v23 dst_sel:WORD_0 dst_unused:UNUSED_PAD src0_sel:WORD_0
	v_exp_f16_sdwa v28, v24 dst_sel:WORD_0 dst_unused:UNUSED_PAD src0_sel:WORD_0
	v_exp_f16_sdwa v29, v25 dst_sel:WORD_0 dst_unused:UNUSED_PAD src0_sel:WORD_0
	v_exp_f16_sdwa v26, v22 dst_sel:WORD_1 dst_unused:UNUSED_PRESERVE src0_sel:WORD_1
	v_exp_f16_sdwa v27, v23 dst_sel:WORD_1 dst_unused:UNUSED_PRESERVE src0_sel:WORD_1
	v_exp_f16_sdwa v28, v24 dst_sel:WORD_1 dst_unused:UNUSED_PRESERVE src0_sel:WORD_1
	v_exp_f16_sdwa v29, v25 dst_sel:WORD_1 dst_unused:UNUSED_PRESERVE src0_sel:WORD_1
	v_pk_add_f16 v22, v81, v85
	v_pk_add_f16 v14, v14, v26
	v_pk_add_f16 v15, v15, v27
	v_pk_add_f16 v16, v16, v28
	v_pk_add_f16 v17, v17, v29
	v_pk_fma_f16 v18, v50, v26, v18
	v_pk_fma_f16 v19, v51, v27, v19
	v_pk_fma_f16 v20, v52, v28, v20
	v_pk_fma_f16 v21, v53, v29, v21
	v_pk_add_f16 v23, v80, v84
	v_pk_add_f16 v24, v79, v83
	v_pk_add_f16 v25, v78, v82
	v_exp_f16_sdwa v26, v22 dst_sel:WORD_0 dst_unused:UNUSED_PAD src0_sel:WORD_0
	v_exp_f16_sdwa v27, v23 dst_sel:WORD_0 dst_unused:UNUSED_PAD src0_sel:WORD_0
	v_exp_f16_sdwa v28, v24 dst_sel:WORD_0 dst_unused:UNUSED_PAD src0_sel:WORD_0
	v_exp_f16_sdwa v29, v25 dst_sel:WORD_0 dst_unused:UNUSED_PAD src0_sel:WORD_0
	v_exp_f16_sdwa v26, v22 dst_sel:WORD_1 dst_unused:UNUSED_PRESERVE src0_sel:WORD_1
	v_exp_f16_sdwa v27, v23 dst_sel:WORD_1 dst_unused:UNUSED_PRESERVE src0_sel:WORD_1
	v_exp_f16_sdwa v28, v24 dst_sel:WORD_1 dst_unused:UNUSED_PRESERVE src0_sel:WORD_1
	v_exp_f16_sdwa v29, v25 dst_sel:WORD_1 dst_unused:UNUSED_PRESERVE src0_sel:WORD_1
	v_pk_add_f16 v22, v30, v85
	v_pk_add_f16 v17, v17, v29
	v_pk_add_f16 v16, v16, v28
	v_pk_add_f16 v15, v15, v27
	v_pk_add_f16 v14, v14, v26
	v_pk_fma_f16 v21, v73, v29, v21
	v_pk_fma_f16 v20, v72, v28, v20
	v_pk_fma_f16 v19, v71, v27, v19
	v_pk_fma_f16 v18, v70, v26, v18
	v_pk_add_f16 v23, v31, v84
	v_pk_add_f16 v24, v32, v83
	v_pk_add_f16 v25, v33, v82
	v_exp_f16_sdwa v26, v22 dst_sel:WORD_0 dst_unused:UNUSED_PAD src0_sel:WORD_0
	v_exp_f16_sdwa v27, v23 dst_sel:WORD_0 dst_unused:UNUSED_PAD src0_sel:WORD_0
	v_exp_f16_sdwa v28, v24 dst_sel:WORD_0 dst_unused:UNUSED_PAD src0_sel:WORD_0
	v_exp_f16_sdwa v29, v25 dst_sel:WORD_0 dst_unused:UNUSED_PAD src0_sel:WORD_0
	v_exp_f16_sdwa v26, v22 dst_sel:WORD_1 dst_unused:UNUSED_PRESERVE src0_sel:WORD_1
	v_exp_f16_sdwa v27, v23 dst_sel:WORD_1 dst_unused:UNUSED_PRESERVE src0_sel:WORD_1
	v_exp_f16_sdwa v28, v24 dst_sel:WORD_1 dst_unused:UNUSED_PRESERVE src0_sel:WORD_1
	v_exp_f16_sdwa v29, v25 dst_sel:WORD_1 dst_unused:UNUSED_PRESERVE src0_sel:WORD_1
	v_pk_add_f16 v22, v54, v85
	v_pk_add_f16 v14, v14, v26
	v_pk_add_f16 v15, v15, v27
	v_pk_add_f16 v16, v16, v28
	v_pk_add_f16 v17, v17, v29
	v_pk_fma_f16 v18, v90, v26, v18
	v_pk_fma_f16 v19, v91, v27, v19
	v_pk_fma_f16 v20, v92, v28, v20
	v_pk_fma_f16 v21, v93, v29, v21
	v_pk_add_f16 v23, v55, v84
	v_pk_add_f16 v24, v56, v83
	v_pk_add_f16 v25, v57, v82
	v_exp_f16_sdwa v26, v22 dst_sel:WORD_0 dst_unused:UNUSED_PAD src0_sel:WORD_0
	v_exp_f16_sdwa v27, v23 dst_sel:WORD_0 dst_unused:UNUSED_PAD src0_sel:WORD_0
	v_exp_f16_sdwa v28, v24 dst_sel:WORD_0 dst_unused:UNUSED_PAD src0_sel:WORD_0
	v_exp_f16_sdwa v29, v25 dst_sel:WORD_0 dst_unused:UNUSED_PAD src0_sel:WORD_0
	v_exp_f16_sdwa v26, v22 dst_sel:WORD_1 dst_unused:UNUSED_PRESERVE src0_sel:WORD_1
	v_exp_f16_sdwa v27, v23 dst_sel:WORD_1 dst_unused:UNUSED_PRESERVE src0_sel:WORD_1
	v_exp_f16_sdwa v28, v24 dst_sel:WORD_1 dst_unused:UNUSED_PRESERVE src0_sel:WORD_1
	v_exp_f16_sdwa v29, v25 dst_sel:WORD_1 dst_unused:UNUSED_PRESERVE src0_sel:WORD_1
	s_nop 0
	v_pk_add_f16 v17, v17, v29
	v_pk_add_f16 v16, v16, v28
	v_pk_add_f16 v15, v15, v27
	v_pk_add_f16 v14, v14, v26
	v_pk_fma_f16 v21, v113, v29, v21
	v_pk_fma_f16 v20, v112, v28, v20
	v_pk_fma_f16 v19, v111, v27, v19
	v_pk_fma_f16 v18, v110, v26, v18
	v_pk_add_f16 v26, v58, v85
	v_pk_add_f16 v27, v59, v84
	v_pk_add_f16 v28, v60, v83
	v_pk_add_f16 v29, v61, v82
	v_exp_f16_sdwa v22, v26 dst_sel:WORD_0 dst_unused:UNUSED_PAD src0_sel:WORD_0
	v_exp_f16_sdwa v23, v27 dst_sel:WORD_0 dst_unused:UNUSED_PAD src0_sel:WORD_0
	v_exp_f16_sdwa v24, v28 dst_sel:WORD_0 dst_unused:UNUSED_PAD src0_sel:WORD_0
	v_exp_f16_sdwa v25, v29 dst_sel:WORD_0 dst_unused:UNUSED_PAD src0_sel:WORD_0
	v_exp_f16_sdwa v22, v26 dst_sel:WORD_1 dst_unused:UNUSED_PRESERVE src0_sel:WORD_1
	v_exp_f16_sdwa v23, v27 dst_sel:WORD_1 dst_unused:UNUSED_PRESERVE src0_sel:WORD_1
	v_exp_f16_sdwa v24, v28 dst_sel:WORD_1 dst_unused:UNUSED_PRESERVE src0_sel:WORD_1
	v_exp_f16_sdwa v25, v29 dst_sel:WORD_1 dst_unused:UNUSED_PRESERVE src0_sel:WORD_1
	s_nop 0

_Z7k_stageILi0ELi4EEv8AttnArgsPKDF16_PKfPDF16_iii:
	s_load_dwordx2 s[86:87], s[0:1], 0x70
	s_load_dwordx2 s[82:83], s[0:1], 0x88
	s_lshr_b32 s92, s2, 3
	s_mov_b32 s81, s3
	s_load_dwordx16 s[64:79], s[0:1], 0x0
	v_readfirstlane_b32 s94, v0
	s_nop 0
	s_lshr_b32 s94, s94, 6
	s_load_dwordx4 s[8:11], s[0:1], 0x70
	s_load_dwordx2 s[20:21], s[0:1], 0x80
	s_load_dwordx4 s[12:15], s[0:1], 0x88
	s_lshl_b32 s5, s2, 5
	s_waitcnt lgkmcnt(0)
	s_and_b32 s15, s5, 0xe0
	s_lshr_b32 s5, s2, 3
	s_add_i32 s15, s15, s5
	s_and_b32 s2, s2, 56
	v_readfirstlane_b32 s4, v0
	v_and_b32_e32 v1, 15, v0
	s_cmp_lt_i32 s14, 1
	v_bfe_u32 v158, v0, 4, 2
	s_cbranch_scc1 .LBB5_79
	s_bfe_u32 s5, s4, 0x10006
	s_lshl_b32 s6, s5, 4
	s_mul_i32 s16, s3, 40
	s_mul_hi_i32 s7, s3, 40
	s_add_u32 s22, s0, s16
	s_addc_u32 s23, s1, s7
	s_load_dwordx4 s[16:19], s[22:23], 0x0
	s_load_dwordx2 s[0:1], s[22:23], 0x10
	v_or_b32_e32 v159, s6, v1
	v_lshlrev_b32_e32 v18, 5, v159
	s_waitcnt lgkmcnt(0)
	global_load_dwordx4 v[230:233], v18, s[18:19]
	global_load_dwordx4 v[234:237], v18, s[0:1]
	global_load_dwordx4 v[238:241], v18, s[18:19] offset:16
	global_load_dwordx4 v[242:245], v18, s[0:1] offset:16
	v_bfe_u32 v21, v0, 7, 1
	v_lshrrev_b32_e32 v19, 4, v0
	v_lshlrev_b16_e32 v23, 2, v21
	v_lshrrev_b32_e32 v18, 5, v0
	v_lshrrev_b32_e32 v20, 6, v0
	v_and_b32_e32 v24, 3, v19
	v_bitop3_b16 v19, v23, v19, 3 bitop3:0xf8
	s_movk_i32 s0, 0x3000
	v_and_b32_e32 v18, 4, v18
	v_and_b32_e32 v22, 4, v20
	v_lshlrev_b32_e32 v20, 12, v20
	v_lshlrev_b32_e32 v21, 11, v21
	v_and_b32_e32 v19, 0xffff, v19
	s_bitcmp1_b32 s4, 6
	v_or_b32_e32 v161, v18, v158
	v_and_or_b32 v162, s15, 56, v22
	v_bitop3_b16 v23, v23, 8, v24 bitop3:0xfe
	v_lshlrev_b32_e32 v24, 3, v22
	v_lshl_or_b32 v22, v22, 12, v21
	v_or3_b32 v163, v20, v21, s0
	v_bitop3_b32 v18, v18, v159, v158 bitop3:0x36
	v_bitop3_b32 v19, s6, v19, v1 bitop3:0x36
	s_cselect_b64 s[24:25], -1, 0
	s_and_b32 s0, s15, 0x1ffc0
	s_movk_i32 s1, 0x2000
	v_lshl_or_b32 v168, v18, 4, v22
	v_lshlrev_b32_e32 v18, 4, v19
	v_or_b32_e32 v19, s0, v162
	v_add3_u32 v170, v22, v18, s1
	v_lshl_or_b32 v18, v19, 6, s2
	v_add_u32_e32 v18, v161, v18
	v_mul_u32_u24_e32 v18, 0x600, v18
	v_and_b32_e32 v20, 0xffff, v23
	v_lshl_or_b32 v18, s5, 8, v18
	v_lshlrev_b32_e32 v160, 9, v158
	v_bitop3_b32 v20, s6, v20, v1 bitop3:0x36
	v_lshl_or_b32 v18, v1, 4, v18
	v_add_u32_e32 v164, -1, v162
	v_add_u32_e32 v165, 4, v162
	v_or3_b32 v166, v161, v24, 8
	v_or_b32_e32 v167, 0x1000, v22
	v_lshl_or_b32 v169, v20, 4, v160
	s_and_b32 s17, s17, 0xffff
	s_mov_b32 s19, 0x20000
	s_mov_b32 s18, 0x1800000
	v_add_u32_e32 v171, 0xfffe7c00, v18
	s_mov_b32 s30, s2
	s_mov_b32 s93, 0
	s_branch .LBB5_4
.LBB5_2:
	s_waitcnt lgkmcnt(0)
	v_cvt_f16_f32_e32 v180, s7
	v_cvt_f16_f32_e32 v182, s6
	v_cvt_f16_f32_e32 v181, s28
	s_waitcnt vmcnt(3)
	s_cmp_lg_u32 s14, 1
	s_cbranch_scc1 .Lmysw5_1
	s_mul_i32 s84, s81, s83
	s_add_i32 s84, s84, s82
	s_mul_i32 s84, s84, 0x60000
	s_lshl_b32 s85, s92, 3
	s_add_u32 s85, s85, s94
	s_mul_i32 s85, s85, 1536
	s_add_u32 s84, s84, s85
	s_add_u32 s88, s86, s84
	s_addc_u32 s89, s87, 0
	s_load_dword s90, s[88:89], 0x0
	s_load_dword s90, s[88:89], 0x80
	s_load_dword s90, s[88:89], 0x100
	s_load_dword s90, s[88:89], 0x180
	s_load_dword s90, s[88:89], 0x200
	s_load_dword s90, s[88:89], 0x280
	s_load_dword s90, s[88:89], 0x300
	s_load_dword s90, s[88:89], 0x380
	s_load_dword s90, s[88:89], 0x400
	s_load_dword s90, s[88:89], 0x480
	s_load_dword s90, s[88:89], 0x500
	s_load_dword s90, s[88:89], 0x580
.Lmysw5_1:
	v_pk_mul_f16 v183, v182, v184 op_sel_hi:[0,1]
	v_pk_mul_f16 v190, v182, v187 op_sel_hi:[0,1]
	v_pk_mul_f16 v194, v180, v187 op_sel_hi:[0,1]
	v_pk_mul_f16 v198, v181, v187 op_sel_hi:[0,1]
	v_pk_mul_f16 v188, v182, v185 op_sel_hi:[0,1]
	v_pk_mul_f16 v189, v182, v186 op_sel_hi:[0,1]
	v_pk_mul_f16 v191, v180, v184 op_sel_hi:[0,1]
	s_mov_b64 exec, s[64:65]
	buffer_load_dwordx4 v[18:21], v224, s[16:19], 0 offen
	buffer_load_dwordx4 v[6:9], v224, s[16:19], 0 offen offset:512
	s_mov_b64 exec, -1
	v_pk_mul_f16 v192, v180, v185 op_sel_hi:[0,1]
	v_pk_mul_f16 v193, v180, v186 op_sel_hi:[0,1]
	v_pk_mul_f16 v195, v181, v184 op_sel_hi:[0,1]
	v_pk_mul_f16 v196, v181, v185 op_sel_hi:[0,1]
	v_pk_mul_f16 v197, v181, v186 op_sel_hi:[0,1]
	v_pk_fma_f16 v113, v113, v187, v190
	v_pk_fma_f16 v110, v110, v184, v183
	v_pk_fma_f16 v129, v129, v187, v190
	v_pk_fma_f16 v126, v126, v184, v183
	v_pk_fma_f16 v137, v137, v187, v190
	v_pk_fma_f16 v134, v134, v184, v183
	v_pk_fma_f16 v183, v85, v187, v194
	v_pk_fma_f16 v199, v109, v187, v194
	buffer_load_dwordx4 v[30:33], v225, s[16:19], 0 offen offset:512
	buffer_load_dwordx4 v[10:13], v225, s[16:19], 0 offen offset:1024
	v_pk_fma_f16 v194, v125, v187, v194
	v_pk_fma_f16 v203, v53, v187, v198
	v_pk_fma_f16 v207, v69, v187, v198
	v_pk_fma_f16 v187, v97, v187, v198
	v_pk_maximum3_f16 v198, v113, v129, v137
	v_pk_fma_f16 v112, v112, v186, v189
	v_pk_fma_f16 v111, v111, v185, v188
	v_pk_fma_f16 v128, v128, v186, v189
	v_pk_fma_f16 v127, v127, v185, v188
	v_pk_fma_f16 v136, v136, v186, v189
	v_pk_fma_f16 v135, v135, v185, v188
	v_pk_fma_f16 v188, v84, v186, v193
	v_pk_fma_f16 v189, v83, v185, v192
	v_pk_fma_f16 v190, v82, v184, v191
	v_pk_fma_f16 v200, v108, v186, v193
	v_pk_fma_f16 v201, v107, v185, v192
	s_mov_b64 exec, s[66:67]
	buffer_load_dwordx4 v[54:57], v225, s[16:19], 0 offen offset:2048
	buffer_load_dwordx4 v[14:17], v225, s[16:19], 0 offen offset:2560
	s_mov_b64 exec, -1
	v_pk_fma_f16 v202, v106, v184, v191
	v_pk_fma_f16 v193, v124, v186, v193
	v_pk_fma_f16 v192, v123, v185, v192
	v_pk_fma_f16 v191, v122, v184, v191
	v_pk_fma_f16 v204, v52, v186, v197
	v_pk_fma_f16 v205, v51, v185, v196
	v_pk_fma_f16 v206, v50, v184, v195
	v_pk_fma_f16 v208, v68, v186, v197
	v_pk_fma_f16 v209, v67, v185, v196
	v_pk_fma_f16 v210, v66, v184, v195
	v_pk_fma_f16 v186, v96, v186, v197
	v_pk_fma_f16 v185, v95, v185, v196
	v_pk_fma_f16 v184, v94, v184, v195
	v_pk_maximum3_f16 v195, v110, v126, v134
	v_pk_maximum3_f16 v196, v111, v127, v135
	v_pk_maximum3_f16 v197, v112, v128, v136
	v_pk_maximum3_f16 v214, v183, v199, v194
	v_pk_maximum3_f16 v218, v203, v207, v187
	v_pk_maximum3_f16 v211, v190, v202, v191
	v_pk_maximum3_f16 v212, v189, v201, v192
	v_pk_maximum3_f16 v213, v188, v200, v193
	v_pk_maximum3_f16 v215, v206, v210, v184
	v_pk_maximum3_f16 v216, v205, v209, v185
	v_pk_maximum3_f16 v198, v198, v214, v218
	v_pk_maximum3_f16 v217, v204, v208, v186
	v_pk_maximum3_f16 v195, v195, v211, v215
	v_pk_maximum3_f16 v196, v196, v212, v216
	v_pk_maximum3_f16 v197, v197, v213, v217
	v_pk_add_f16 v113, v113, v198 neg_lo:[0,1] neg_hi:[0,1]
	s_mov_b64 exec, s[64:65]
	buffer_load_dwordx4 v[74:77], v226, s[16:19], 0 offen
	buffer_load_dwordx4 v[26:29], v226, s[16:19], 0 offen offset:512
	s_mov_b64 exec, -1
	v_pk_add_f16 v110, v110, v195 neg_lo:[0,1] neg_hi:[0,1]
	v_pk_add_f16 v111, v111, v196 neg_lo:[0,1] neg_hi:[0,1]
	v_pk_add_f16 v112, v112, v197 neg_lo:[0,1] neg_hi:[0,1]
	v_pk_add_f16 v126, v126, v195 neg_lo:[0,1] neg_hi:[0,1]
	v_exp_f16_sdwa v211, v110 dst_sel:WORD_0 dst_unused:UNUSED_PAD src0_sel:WORD_0
	v_exp_f16_sdwa v212, v111 dst_sel:WORD_0 dst_unused:UNUSED_PAD src0_sel:WORD_0
	v_exp_f16_sdwa v213, v112 dst_sel:WORD_0 dst_unused:UNUSED_PAD src0_sel:WORD_0
	v_exp_f16_sdwa v214, v113 dst_sel:WORD_0 dst_unused:UNUSED_PAD src0_sel:WORD_0
	v_exp_f16_sdwa v211, v110 dst_sel:WORD_1 dst_unused:UNUSED_PRESERVE src0_sel:WORD_1
	v_exp_f16_sdwa v212, v111 dst_sel:WORD_1 dst_unused:UNUSED_PRESERVE src0_sel:WORD_1
	v_exp_f16_sdwa v213, v112 dst_sel:WORD_1 dst_unused:UNUSED_PRESERVE src0_sel:WORD_1
	v_exp_f16_sdwa v214, v113 dst_sel:WORD_1 dst_unused:UNUSED_PRESERVE src0_sel:WORD_1
	v_pk_add_f16 v127, v127, v196 neg_lo:[0,1] neg_hi:[0,1]
	v_pk_add_f16 v113, v211, 0
	v_pk_fma_f16 v81, v81, v214, 0
	v_pk_add_f16 v110, v214, 0
	v_pk_add_f16 v111, v213, 0
	v_pk_add_f16 v112, v212, 0
	v_pk_fma_f16 v80, v80, v213, 0
	v_pk_fma_f16 v79, v79, v212, 0
	v_pk_fma_f16 v78, v78, v211, 0
	v_pk_add_f16 v128, v128, v197 neg_lo:[0,1] neg_hi:[0,1]
	buffer_load_dwordx4 v[98:101], v227, s[16:19], 0 offen offset:512
	buffer_load_dwordx4 v[38:41], v227, s[16:19], 0 offen offset:1024
	v_pk_add_f16 v129, v129, v198 neg_lo:[0,1] neg_hi:[0,1]
	v_exp_f16_sdwa v211, v126 dst_sel:WORD_0 dst_unused:UNUSED_PAD src0_sel:WORD_0
	v_exp_f16_sdwa v212, v127 dst_sel:WORD_0 dst_unused:UNUSED_PAD src0_sel:WORD_0
	v_exp_f16_sdwa v213, v128 dst_sel:WORD_0 dst_unused:UNUSED_PAD src0_sel:WORD_0
	v_exp_f16_sdwa v214, v129 dst_sel:WORD_0 dst_unused:UNUSED_PAD src0_sel:WORD_0
	v_exp_f16_sdwa v211, v126 dst_sel:WORD_1 dst_unused:UNUSED_PRESERVE src0_sel:WORD_1
	v_exp_f16_sdwa v212, v127 dst_sel:WORD_1 dst_unused:UNUSED_PRESERVE src0_sel:WORD_1
	v_exp_f16_sdwa v213, v128 dst_sel:WORD_1 dst_unused:UNUSED_PRESERVE src0_sel:WORD_1
	v_exp_f16_sdwa v214, v129 dst_sel:WORD_1 dst_unused:UNUSED_PRESERVE src0_sel:WORD_1
	v_pk_add_f16 v113, v113, v211
	v_pk_fma_f16 v81, v105, v214, v81
	v_pk_add_f16 v105, v137, v198 neg_lo:[0,1] neg_hi:[0,1]
	v_pk_add_f16 v112, v112, v212
	v_pk_add_f16 v111, v111, v213
	v_pk_add_f16 v110, v110, v214
	v_pk_fma_f16 v78, v102, v211, v78
	v_pk_fma_f16 v79, v103, v212, v79
	v_pk_fma_f16 v80, v104, v213, v80
	v_pk_add_f16 v102, v134, v195 neg_lo:[0,1] neg_hi:[0,1]
	v_pk_add_f16 v103, v135, v196 neg_lo:[0,1] neg_hi:[0,1]
	v_pk_add_f16 v104, v136, v197 neg_lo:[0,1] neg_hi:[0,1]
	v_exp_f16_sdwa v126, v102 dst_sel:WORD_0 dst_unused:UNUSED_PAD src0_sel:WORD_0
	v_exp_f16_sdwa v127, v103 dst_sel:WORD_0 dst_unused:UNUSED_PAD src0_sel:WORD_0
	v_exp_f16_sdwa v128, v104 dst_sel:WORD_0 dst_unused:UNUSED_PAD src0_sel:WORD_0
	v_exp_f16_sdwa v129, v105 dst_sel:WORD_0 dst_unused:UNUSED_PAD src0_sel:WORD_0
	v_exp_f16_sdwa v126, v102 dst_sel:WORD_1 dst_unused:UNUSED_PRESERVE src0_sel:WORD_1
	v_exp_f16_sdwa v127, v103 dst_sel:WORD_1 dst_unused:UNUSED_PRESERVE src0_sel:WORD_1
	v_exp_f16_sdwa v128, v104 dst_sel:WORD_1 dst_unused:UNUSED_PRESERVE src0_sel:WORD_1
	v_exp_f16_sdwa v129, v105 dst_sel:WORD_1 dst_unused:UNUSED_PRESERVE src0_sel:WORD_1
	v_pk_add_f16 v105, v113, v126
	v_pk_add_f16 v102, v110, v129
	s_mov_b64 exec, s[66:67]
	buffer_load_dwordx4 v[118:121], v227, s[16:19], 0 offen offset:2048
	buffer_load_dwordx4 v[58:61], v227, s[16:19], 0 offen offset:2560
	s_mov_b64 exec, -1
	v_pk_add_f16 v103, v111, v128
	v_pk_add_f16 v104, v112, v127
	v_pk_fma_f16 v81, v117, v129, v81
	v_pk_fma_f16 v80, v116, v128, v80
	v_pk_fma_f16 v79, v115, v127, v79
	v_pk_fma_f16 v78, v114, v126, v78
	v_pk_add_f16 v110, v190, v195 neg_lo:[0,1] neg_hi:[0,1]
	v_pk_add_f16 v111, v189, v196 neg_lo:[0,1] neg_hi:[0,1]
	v_pk_add_f16 v112, v188, v197 neg_lo:[0,1] neg_hi:[0,1]
	v_pk_add_f16 v113, v183, v198 neg_lo:[0,1] neg_hi:[0,1]
	v_exp_f16_sdwa v114, v110 dst_sel:WORD_0 dst_unused:UNUSED_PAD src0_sel:WORD_0
	v_exp_f16_sdwa v115, v111 dst_sel:WORD_0 dst_unused:UNUSED_PAD src0_sel:WORD_0
	v_exp_f16_sdwa v116, v112 dst_sel:WORD_0 dst_unused:UNUSED_PAD src0_sel:WORD_0
	v_exp_f16_sdwa v117, v113 dst_sel:WORD_0 dst_unused:UNUSED_PAD src0_sel:WORD_0
	v_exp_f16_sdwa v114, v110 dst_sel:WORD_1 dst_unused:UNUSED_PRESERVE src0_sel:WORD_1
	v_exp_f16_sdwa v115, v111 dst_sel:WORD_1 dst_unused:UNUSED_PRESERVE src0_sel:WORD_1
	v_exp_f16_sdwa v116, v112 dst_sel:WORD_1 dst_unused:UNUSED_PRESERVE src0_sel:WORD_1
	v_exp_f16_sdwa v117, v113 dst_sel:WORD_1 dst_unused:UNUSED_PRESERVE src0_sel:WORD_1
	v_pk_add_f16 v110, v202, v195 neg_lo:[0,1] neg_hi:[0,1]
	v_pk_add_f16 v105, v105, v114
	v_pk_add_f16 v104, v104, v115
	v_pk_add_f16 v103, v103, v116
	s_mov_b64 exec, s[76:77]
	buffer_load_dwordx4 v[130:133], v228, s[16:19], 0 offen
	buffer_load_dwordx4 v[70:73], v228, s[16:19], 0 offen offset:512
	s_mov_b64 exec, -1
	v_pk_add_f16 v102, v102, v117
	v_pk_fma_f16 v78, v42, v114, v78
	v_pk_fma_f16 v79, v43, v115, v79
	v_pk_fma_f16 v80, v44, v116, v80
	v_pk_fma_f16 v81, v45, v117, v81
	v_pk_add_f16 v111, v201, v196 neg_lo:[0,1] neg_hi:[0,1]
	v_pk_add_f16 v112, v200, v197 neg_lo:[0,1] neg_hi:[0,1]
	v_pk_add_f16 v113, v199, v198 neg_lo:[0,1] neg_hi:[0,1]
	v_exp_f16_sdwa v114, v110 dst_sel:WORD_0 dst_unused:UNUSED_PAD src0_sel:WORD_0
	v_exp_f16_sdwa v115, v111 dst_sel:WORD_0 dst_unused:UNUSED_PAD src0_sel:WORD_0
	v_exp_f16_sdwa v116, v112 dst_sel:WORD_0 dst_unused:UNUSED_PAD src0_sel:WORD_0
	v_exp_f16_sdwa v117, v113 dst_sel:WORD_0 dst_unused:UNUSED_PAD src0_sel:WORD_0
	v_exp_f16_sdwa v114, v110 dst_sel:WORD_1 dst_unused:UNUSED_PRESERVE src0_sel:WORD_1
	v_exp_f16_sdwa v115, v111 dst_sel:WORD_1 dst_unused:UNUSED_PRESERVE src0_sel:WORD_1
	v_exp_f16_sdwa v116, v112 dst_sel:WORD_1 dst_unused:UNUSED_PRESERVE src0_sel:WORD_1
	v_exp_f16_sdwa v117, v113 dst_sel:WORD_1 dst_unused:UNUSED_PRESERVE src0_sel:WORD_1
	v_pk_add_f16 v110, v191, v195 neg_lo:[0,1] neg_hi:[0,1]
	v_pk_add_f16 v105, v105, v114
	v_pk_add_f16 v102, v102, v117
	v_pk_add_f16 v103, v103, v116
	v_pk_add_f16 v104, v104, v115
	v_pk_fma_f16 v81, v65, v117, v81
	v_pk_fma_f16 v80, v64, v116, v80
	s_mov_b64 exec, s[70:71]
	buffer_load_dwordx4 v[138:141], v229, s[16:19], 0 offen offset:512
	buffer_load_dwordx4 v[90:93], v229, s[16:19], 0 offen offset:1024
	s_mov_b64 exec, -1
	v_pk_fma_f16 v79, v63, v115, v79
	v_pk_fma_f16 v78, v62, v114, v78
	v_pk_add_f16 v111, v192, v196 neg_lo:[0,1] neg_hi:[0,1]
	v_pk_add_f16 v112, v193, v197 neg_lo:[0,1] neg_hi:[0,1]
	v_pk_add_f16 v113, v194, v198 neg_lo:[0,1] neg_hi:[0,1]
	v_exp_f16_sdwa v114, v110 dst_sel:WORD_0 dst_unused:UNUSED_PAD src0_sel:WORD_0
	v_exp_f16_sdwa v115, v111 dst_sel:WORD_0 dst_unused:UNUSED_PAD src0_sel:WORD_0
	v_exp_f16_sdwa v116, v112 dst_sel:WORD_0 dst_unused:UNUSED_PAD src0_sel:WORD_0
	v_exp_f16_sdwa v117, v113 dst_sel:WORD_0 dst_unused:UNUSED_PAD src0_sel:WORD_0
	v_exp_f16_sdwa v114, v110 dst_sel:WORD_1 dst_unused:UNUSED_PRESERVE src0_sel:WORD_1
	v_exp_f16_sdwa v115, v111 dst_sel:WORD_1 dst_unused:UNUSED_PRESERVE src0_sel:WORD_1
	v_exp_f16_sdwa v116, v112 dst_sel:WORD_1 dst_unused:UNUSED_PRESERVE src0_sel:WORD_1
	v_exp_f16_sdwa v117, v113 dst_sel:WORD_1 dst_unused:UNUSED_PRESERVE src0_sel:WORD_1
	v_pk_add_f16 v110, v206, v195 neg_lo:[0,1] neg_hi:[0,1]
	v_pk_add_f16 v105, v105, v114
	v_pk_add_f16 v104, v104, v115
	v_pk_add_f16 v103, v103, v116
	v_pk_add_f16 v102, v102, v117
	v_pk_fma_f16 v78, v86, v114, v78
	v_pk_fma_f16 v79, v87, v115, v79
	v_pk_fma_f16 v80, v88, v116, v80
	v_pk_fma_f16 v81, v89, v117, v81
	s_mov_b64 exec, s[78:79]
	buffer_load_dwordx4 v[142:145], v229, s[16:19], 0 offen offset:2048
	buffer_load_dwordx4 v[2:5], v229, s[16:19], 0 offen offset:2560
	s_mov_b64 exec, -1
	v_pk_add_f16 v111, v205, v196 neg_lo:[0,1] neg_hi:[0,1]
	v_pk_add_f16 v112, v204, v197 neg_lo:[0,1] neg_hi:[0,1]
	v_pk_add_f16 v113, v203, v198 neg_lo:[0,1] neg_hi:[0,1]
	v_exp_f16_sdwa v114, v110 dst_sel:WORD_0 dst_unused:UNUSED_PAD src0_sel:WORD_0
	v_exp_f16_sdwa v115, v111 dst_sel:WORD_0 dst_unused:UNUSED_PAD src0_sel:WORD_0
	v_exp_f16_sdwa v116, v112 dst_sel:WORD_0 dst_unused:UNUSED_PAD src0_sel:WORD_0
	v_exp_f16_sdwa v117, v113 dst_sel:WORD_0 dst_unused:UNUSED_PAD src0_sel:WORD_0
	v_exp_f16_sdwa v114, v110 dst_sel:WORD_1 dst_unused:UNUSED_PRESERVE src0_sel:WORD_1
	v_exp_f16_sdwa v115, v111 dst_sel:WORD_1 dst_unused:UNUSED_PRESERVE src0_sel:WORD_1
	v_exp_f16_sdwa v116, v112 dst_sel:WORD_1 dst_unused:UNUSED_PRESERVE src0_sel:WORD_1
	v_exp_f16_sdwa v117, v113 dst_sel:WORD_1 dst_unused:UNUSED_PRESERVE src0_sel:WORD_1
	v_pk_add_f16 v110, v210, v195 neg_lo:[0,1] neg_hi:[0,1]
	v_pk_add_f16 v105, v105, v114
	v_pk_add_f16 v102, v102, v117
	v_pk_add_f16 v103, v103, v116
	v_pk_add_f16 v104, v104, v115
	v_pk_fma_f16 v81, v25, v117, v81
	v_pk_fma_f16 v80, v24, v116, v80
	v_pk_fma_f16 v79, v23, v115, v79
	v_pk_fma_f16 v78, v22, v114, v78
	v_pk_add_f16 v111, v209, v196 neg_lo:[0,1] neg_hi:[0,1]
	v_pk_add_f16 v112, v208, v197 neg_lo:[0,1] neg_hi:[0,1]
	v_pk_add_f16 v113, v207, v198 neg_lo:[0,1] neg_hi:[0,1]
	v_exp_f16_sdwa v114, v110 dst_sel:WORD_0 dst_unused:UNUSED_PAD src0_sel:WORD_0
	v_exp_f16_sdwa v115, v111 dst_sel:WORD_0 dst_unused:UNUSED_PAD src0_sel:WORD_0
	v_exp_f16_sdwa v116, v112 dst_sel:WORD_0 dst_unused:UNUSED_PAD src0_sel:WORD_0
	v_exp_f16_sdwa v117, v113 dst_sel:WORD_0 dst_unused:UNUSED_PAD src0_sel:WORD_0
	v_exp_f16_sdwa v114, v110 dst_sel:WORD_1 dst_unused:UNUSED_PRESERVE src0_sel:WORD_1
	v_exp_f16_sdwa v115, v111 dst_sel:WORD_1 dst_unused:UNUSED_PRESERVE src0_sel:WORD_1
	v_exp_f16_sdwa v116, v112 dst_sel:WORD_1 dst_unused:UNUSED_PRESERVE src0_sel:WORD_1
	v_exp_f16_sdwa v117, v113 dst_sel:WORD_1 dst_unused:UNUSED_PRESERVE src0_sel:WORD_1
	v_pk_add_f16 v110, v184, v195 neg_lo:[0,1] neg_hi:[0,1]
	v_pk_add_f16 v105, v105, v114
	v_pk_add_f16 v104, v104, v115
	v_pk_add_f16 v103, v103, v116
	v_pk_add_f16 v102, v102, v117
	v_pk_fma_f16 v78, v34, v114, v78
	v_pk_fma_f16 v79, v35, v115, v79
	v_pk_fma_f16 v80, v36, v116, v80
	v_pk_fma_f16 v81, v37, v117, v81
	v_pk_add_f16 v111, v185, v196 neg_lo:[0,1] neg_hi:[0,1]
	v_pk_add_f16 v112, v186, v197 neg_lo:[0,1] neg_hi:[0,1]
	v_pk_add_f16 v113, v187, v198 neg_lo:[0,1] neg_hi:[0,1]
	v_exp_f16_sdwa v114, v110 dst_sel:WORD_0 dst_unused:UNUSED_PAD src0_sel:WORD_0
	v_exp_f16_sdwa v115, v111 dst_sel:WORD_0 dst_unused:UNUSED_PAD src0_sel:WORD_0
	v_exp_f16_sdwa v116, v112 dst_sel:WORD_0 dst_unused:UNUSED_PAD src0_sel:WORD_0
	v_exp_f16_sdwa v117, v113 dst_sel:WORD_0 dst_unused:UNUSED_PAD src0_sel:WORD_0
	v_exp_f16_sdwa v114, v110 dst_sel:WORD_1 dst_unused:UNUSED_PRESERVE src0_sel:WORD_1
	v_exp_f16_sdwa v115, v111 dst_sel:WORD_1 dst_unused:UNUSED_PRESERVE src0_sel:WORD_1
	v_exp_f16_sdwa v116, v112 dst_sel:WORD_1 dst_unused:UNUSED_PRESERVE src0_sel:WORD_1
	v_exp_f16_sdwa v117, v113 dst_sel:WORD_1 dst_unused:UNUSED_PRESERVE src0_sel:WORD_1
	v_pk_add_f16 v105, v105, v114
	v_pk_add_f16 v104, v104, v115
	v_rcp_f16_e32 v110, v105
	v_rcp_f16_sdwa v105, v105 dst_sel:DWORD dst_unused:UNUSED_PAD src0_sel:WORD_1
	v_pk_add_f16 v103, v103, v116
	v_rcp_f16_e32 v111, v104
	v_rcp_f16_sdwa v104, v104 dst_sel:DWORD dst_unused:UNUSED_PAD src0_sel:WORD_1
	v_pk_add_f16 v102, v102, v117
	v_rcp_f16_e32 v112, v103
	v_rcp_f16_sdwa v103, v103 dst_sel:DWORD dst_unused:UNUSED_PAD src0_sel:WORD_1
	v_rcp_f16_e32 v113, v102
	v_rcp_f16_sdwa v102, v102 dst_sel:DWORD dst_unused:UNUSED_PAD src0_sel:WORD_1
	v_pk_fma_f16 v78, v46, v114, v78
	v_pack_b32_f16 v105, v110, v105
	v_pk_fma_f16 v79, v47, v115, v79
	v_pk_mul_f16 v110, v78, v105
	v_pack_b32_f16 v78, v111, v104
	v_pk_fma_f16 v80, v48, v116, v80
	v_pk_mul_f16 v111, v79, v78
	v_pack_b32_f16 v78, v112, v103
	v_pk_fma_f16 v81, v49, v117, v81
	v_pk_mul_f16 v112, v80, v78
	v_pack_b32_f16 v78, v113, v102
	v_pk_mul_f16 v113, v81, v78
	s_waitcnt vmcnt(12)
	v_pk_mul_f16 v78, v182, v154 op_sel_hi:[0,1]
	v_pk_mul_f16 v81, v182, v157 op_sel_hi:[0,1]
	v_pk_mul_f16 v102, v180, v154 op_sel_hi:[0,1]
	v_pk_mul_f16 v114, v181, v154 op_sel_hi:[0,1]
	v_pk_mul_f16 v79, v182, v155 op_sel_hi:[0,1]
	v_pk_mul_f16 v80, v182, v156 op_sel_hi:[0,1]
	v_pk_mul_f16 v103, v180, v155 op_sel_hi:[0,1]
	v_pk_mul_f16 v104, v180, v156 op_sel_hi:[0,1]
	v_pk_mul_f16 v105, v180, v157 op_sel_hi:[0,1]
	v_pk_mul_f16 v115, v181, v155 op_sel_hi:[0,1]
	v_pk_mul_f16 v116, v181, v156 op_sel_hi:[0,1]
	v_pk_mul_f16 v117, v181, v157 op_sel_hi:[0,1]
	v_pk_fma_f16 v85, v85, v157, v81
	v_pk_fma_f16 v82, v82, v154, v78
	v_pk_fma_f16 v109, v109, v157, v81
	v_pk_fma_f16 v106, v106, v154, v78
	v_pk_fma_f16 v81, v125, v157, v81
	v_pk_fma_f16 v78, v122, v154, v78
	v_pk_fma_f16 v125, v50, v154, v102
	v_pk_fma_f16 v129, v66, v154, v102
	v_pk_fma_f16 v102, v94, v154, v102
	v_pk_fma_f16 v137, v18, v154, v114
	v_pk_fma_f16 v186, v30, v154, v114
	v_pk_fma_f16 v114, v54, v154, v114
	v_pk_maximum3_f16 v154, v82, v106, v78
	v_pk_fma_f16 v84, v84, v156, v80
	v_pk_fma_f16 v83, v83, v155, v79
	v_pk_fma_f16 v108, v108, v156, v80
	v_pk_fma_f16 v107, v107, v155, v79
	v_pk_fma_f16 v80, v124, v156, v80
	v_pk_fma_f16 v79, v123, v155, v79
	v_pk_fma_f16 v122, v53, v157, v105
	v_pk_fma_f16 v123, v52, v156, v104
	v_pk_fma_f16 v124, v51, v155, v103
	v_pk_fma_f16 v126, v69, v157, v105
	v_pk_fma_f16 v127, v68, v156, v104
	v_pk_fma_f16 v128, v67, v155, v103
	v_pk_fma_f16 v105, v97, v157, v105
	v_pk_fma_f16 v104, v96, v156, v104
	v_pk_fma_f16 v103, v95, v155, v103
	v_pk_fma_f16 v134, v21, v157, v117
	v_pk_fma_f16 v135, v20, v156, v116
	v_pk_fma_f16 v136, v19, v155, v115
	v_pk_fma_f16 v183, v33, v157, v117
	v_pk_fma_f16 v184, v32, v156, v116
	v_pk_fma_f16 v185, v31, v155, v115
	v_pk_fma_f16 v117, v57, v157, v117
	v_pk_fma_f16 v116, v56, v156, v116
	v_pk_fma_f16 v115, v55, v155, v115
	v_pk_maximum3_f16 v155, v83, v107, v79
	v_pk_maximum3_f16 v156, v84, v108, v80
	v_pk_maximum3_f16 v157, v85, v109, v81
	v_pk_maximum3_f16 v187, v125, v129, v102
	v_pk_maximum3_f16 v191, v137, v186, v114
	v_pk_maximum3_f16 v188, v124, v128, v103
	v_pk_maximum3_f16 v189, v123, v127, v104
	v_pk_maximum3_f16 v190, v122, v126, v105
	v_pk_maximum3_f16 v192, v136, v185, v115
	v_pk_maximum3_f16 v193, v135, v184, v116
	v_pk_maximum3_f16 v154, v154, v187, v191
	v_pk_maximum3_f16 v194, v134, v183, v117
	v_pk_maximum3_f16 v155, v155, v188, v192
	v_pk_maximum3_f16 v156, v156, v189, v193
	v_pk_maximum3_f16 v157, v157, v190, v194
	v_pk_add_f16 v82, v82, v154 neg_lo:[0,1] neg_hi:[0,1]
	v_pk_add_f16 v83, v83, v155 neg_lo:[0,1] neg_hi:[0,1]
	v_pk_add_f16 v84, v84, v156 neg_lo:[0,1] neg_hi:[0,1]
	v_pk_add_f16 v85, v85, v157 neg_lo:[0,1] neg_hi:[0,1]
	v_pk_add_f16 v106, v106, v154 neg_lo:[0,1] neg_hi:[0,1]
	v_exp_f16_sdwa v187, v82 dst_sel:WORD_0 dst_unused:UNUSED_PAD src0_sel:WORD_0
	v_exp_f16_sdwa v188, v83 dst_sel:WORD_0 dst_unused:UNUSED_PAD src0_sel:WORD_0
	v_exp_f16_sdwa v189, v84 dst_sel:WORD_0 dst_unused:UNUSED_PAD src0_sel:WORD_0
	v_exp_f16_sdwa v190, v85 dst_sel:WORD_0 dst_unused:UNUSED_PAD src0_sel:WORD_0
	v_exp_f16_sdwa v187, v82 dst_sel:WORD_1 dst_unused:UNUSED_PRESERVE src0_sel:WORD_1
	v_exp_f16_sdwa v188, v83 dst_sel:WORD_1 dst_unused:UNUSED_PRESERVE src0_sel:WORD_1
	v_exp_f16_sdwa v189, v84 dst_sel:WORD_1 dst_unused:UNUSED_PRESERVE src0_sel:WORD_1
	v_exp_f16_sdwa v190, v85 dst_sel:WORD_1 dst_unused:UNUSED_PRESERVE src0_sel:WORD_1
	v_pk_add_f16 v107, v107, v155 neg_lo:[0,1] neg_hi:[0,1]
	v_pk_add_f16 v82, v190, 0
	v_pk_fma_f16 v42, v42, v187, 0
	v_pk_add_f16 v83, v189, 0
	v_pk_add_f16 v84, v188, 0
	v_pk_add_f16 v85, v187, 0
	v_pk_fma_f16 v45, v45, v190, 0
	v_pk_fma_f16 v44, v44, v189, 0
	v_pk_fma_f16 v43, v43, v188, 0
	v_pk_add_f16 v108, v108, v156 neg_lo:[0,1] neg_hi:[0,1]
	v_pk_add_f16 v109, v109, v157 neg_lo:[0,1] neg_hi:[0,1]
	v_exp_f16_sdwa v187, v106 dst_sel:WORD_0 dst_unused:UNUSED_PAD src0_sel:WORD_0
	v_exp_f16_sdwa v188, v107 dst_sel:WORD_0 dst_unused:UNUSED_PAD src0_sel:WORD_0
	v_exp_f16_sdwa v189, v108 dst_sel:WORD_0 dst_unused:UNUSED_PAD src0_sel:WORD_0
	v_exp_f16_sdwa v190, v109 dst_sel:WORD_0 dst_unused:UNUSED_PAD src0_sel:WORD_0
	v_exp_f16_sdwa v187, v106 dst_sel:WORD_1 dst_unused:UNUSED_PRESERVE src0_sel:WORD_1
	v_exp_f16_sdwa v188, v107 dst_sel:WORD_1 dst_unused:UNUSED_PRESERVE src0_sel:WORD_1
	v_exp_f16_sdwa v189, v108 dst_sel:WORD_1 dst_unused:UNUSED_PRESERVE src0_sel:WORD_1
	v_exp_f16_sdwa v190, v109 dst_sel:WORD_1 dst_unused:UNUSED_PRESERVE src0_sel:WORD_1
	s_nop 0
	v_pk_add_f16 v82, v82, v190
	v_pk_fma_f16 v42, v62, v187, v42
	v_pk_add_f16 v62, v78, v154 neg_lo:[0,1] neg_hi:[0,1]
	v_pk_add_f16 v85, v85, v187
	v_pk_add_f16 v84, v84, v188
	v_pk_add_f16 v83, v83, v189
	v_pk_fma_f16 v43, v63, v188, v43
	v_pk_fma_f16 v44, v64, v189, v44
	v_pk_fma_f16 v45, v65, v190, v45
	v_pk_add_f16 v63, v79, v155 neg_lo:[0,1] neg_hi:[0,1]
	v_pk_add_f16 v64, v80, v156 neg_lo:[0,1] neg_hi:[0,1]
	v_pk_add_f16 v65, v81, v157 neg_lo:[0,1] neg_hi:[0,1]
	v_exp_f16_sdwa v78, v62 dst_sel:WORD_0 dst_unused:UNUSED_PAD src0_sel:WORD_0
	v_exp_f16_sdwa v79, v63 dst_sel:WORD_0 dst_unused:UNUSED_PAD src0_sel:WORD_0
	v_exp_f16_sdwa v80, v64 dst_sel:WORD_0 dst_unused:UNUSED_PAD src0_sel:WORD_0
	v_exp_f16_sdwa v81, v65 dst_sel:WORD_0 dst_unused:UNUSED_PAD src0_sel:WORD_0
	v_exp_f16_sdwa v78, v62 dst_sel:WORD_1 dst_unused:UNUSED_PRESERVE src0_sel:WORD_1
	v_exp_f16_sdwa v79, v63 dst_sel:WORD_1 dst_unused:UNUSED_PRESERVE src0_sel:WORD_1
	v_exp_f16_sdwa v80, v64 dst_sel:WORD_1 dst_unused:UNUSED_PRESERVE src0_sel:WORD_1
	v_exp_f16_sdwa v81, v65 dst_sel:WORD_1 dst_unused:UNUSED_PRESERVE src0_sel:WORD_1
	s_nop 0
	v_pk_add_f16 v62, v82, v81
	v_pk_add_f16 v63, v83, v80
	v_pk_add_f16 v64, v84, v79
	v_pk_add_f16 v65, v85, v78
	v_pk_fma_f16 v45, v89, v81, v45
	v_pk_fma_f16 v44, v88, v80, v44
	v_pk_fma_f16 v43, v87, v79, v43
	v_pk_fma_f16 v42, v86, v78, v42
	v_pk_add_f16 v78, v125, v154 neg_lo:[0,1] neg_hi:[0,1]
	v_pk_add_f16 v79, v124, v155 neg_lo:[0,1] neg_hi:[0,1]
	v_pk_add_f16 v80, v123, v156 neg_lo:[0,1] neg_hi:[0,1]
	v_pk_add_f16 v81, v122, v157 neg_lo:[0,1] neg_hi:[0,1]
	v_exp_f16_sdwa v82, v78 dst_sel:WORD_0 dst_unused:UNUSED_PAD src0_sel:WORD_0
	v_exp_f16_sdwa v83, v79 dst_sel:WORD_0 dst_unused:UNUSED_PAD src0_sel:WORD_0
	v_exp_f16_sdwa v84, v80 dst_sel:WORD_0 dst_unused:UNUSED_PAD src0_sel:WORD_0
	v_exp_f16_sdwa v85, v81 dst_sel:WORD_0 dst_unused:UNUSED_PAD src0_sel:WORD_0
	v_exp_f16_sdwa v82, v78 dst_sel:WORD_1 dst_unused:UNUSED_PRESERVE src0_sel:WORD_1
	v_exp_f16_sdwa v83, v79 dst_sel:WORD_1 dst_unused:UNUSED_PRESERVE src0_sel:WORD_1
	v_exp_f16_sdwa v84, v80 dst_sel:WORD_1 dst_unused:UNUSED_PRESERVE src0_sel:WORD_1
	v_exp_f16_sdwa v85, v81 dst_sel:WORD_1 dst_unused:UNUSED_PRESERVE src0_sel:WORD_1
	v_pk_add_f16 v78, v129, v154 neg_lo:[0,1] neg_hi:[0,1]
	v_pk_add_f16 v62, v62, v85
	v_pk_add_f16 v65, v65, v82
	v_pk_add_f16 v64, v64, v83
	v_pk_add_f16 v63, v63, v84
	v_pk_fma_f16 v42, v22, v82, v42
	v_pk_fma_f16 v43, v23, v83, v43
	v_pk_fma_f16 v44, v24, v84, v44
	v_pk_fma_f16 v45, v25, v85, v45
	v_pk_add_f16 v79, v128, v155 neg_lo:[0,1] neg_hi:[0,1]
	v_pk_add_f16 v80, v127, v156 neg_lo:[0,1] neg_hi:[0,1]
	v_pk_add_f16 v81, v126, v157 neg_lo:[0,1] neg_hi:[0,1]
	v_exp_f16_sdwa v82, v78 dst_sel:WORD_0 dst_unused:UNUSED_PAD src0_sel:WORD_0
	v_exp_f16_sdwa v83, v79 dst_sel:WORD_0 dst_unused:UNUSED_PAD src0_sel:WORD_0
	v_exp_f16_sdwa v84, v80 dst_sel:WORD_0 dst_unused:UNUSED_PAD src0_sel:WORD_0
	v_exp_f16_sdwa v85, v81 dst_sel:WORD_0 dst_unused:UNUSED_PAD src0_sel:WORD_0
	v_exp_f16_sdwa v82, v78 dst_sel:WORD_1 dst_unused:UNUSED_PRESERVE src0_sel:WORD_1
	v_exp_f16_sdwa v83, v79 dst_sel:WORD_1 dst_unused:UNUSED_PRESERVE src0_sel:WORD_1
	v_exp_f16_sdwa v84, v80 dst_sel:WORD_1 dst_unused:UNUSED_PRESERVE src0_sel:WORD_1
	v_exp_f16_sdwa v85, v81 dst_sel:WORD_1 dst_unused:UNUSED_PRESERVE src0_sel:WORD_1
	v_pk_add_f16 v78, v102, v154 neg_lo:[0,1] neg_hi:[0,1]
	v_pk_add_f16 v62, v62, v85
	v_pk_add_f16 v63, v63, v84
	v_pk_add_f16 v64, v64, v83
	v_pk_add_f16 v65, v65, v82
	v_pk_fma_f16 v45, v37, v85, v45
	v_pk_fma_f16 v44, v36, v84, v44
	v_pk_fma_f16 v43, v35, v83, v43
	v_pk_fma_f16 v42, v34, v82, v42
	v_pk_add_f16 v79, v103, v155 neg_lo:[0,1] neg_hi:[0,1]
	v_pk_add_f16 v80, v104, v156 neg_lo:[0,1] neg_hi:[0,1]
	v_pk_add_f16 v81, v105, v157 neg_lo:[0,1] neg_hi:[0,1]
	v_exp_f16_sdwa v82, v78 dst_sel:WORD_0 dst_unused:UNUSED_PAD src0_sel:WORD_0
	v_exp_f16_sdwa v83, v79 dst_sel:WORD_0 dst_unused:UNUSED_PAD src0_sel:WORD_0
	v_exp_f16_sdwa v84, v80 dst_sel:WORD_0 dst_unused:UNUSED_PAD src0_sel:WORD_0
	v_exp_f16_sdwa v85, v81 dst_sel:WORD_0 dst_unused:UNUSED_PAD src0_sel:WORD_0
	v_exp_f16_sdwa v82, v78 dst_sel:WORD_1 dst_unused:UNUSED_PRESERVE src0_sel:WORD_1
	v_exp_f16_sdwa v83, v79 dst_sel:WORD_1 dst_unused:UNUSED_PRESERVE src0_sel:WORD_1
	v_exp_f16_sdwa v84, v80 dst_sel:WORD_1 dst_unused:UNUSED_PRESERVE src0_sel:WORD_1
	v_exp_f16_sdwa v85, v81 dst_sel:WORD_1 dst_unused:UNUSED_PRESERVE src0_sel:WORD_1
	v_pk_add_f16 v78, v137, v154 neg_lo:[0,1] neg_hi:[0,1]
	v_pk_add_f16 v62, v62, v85
	v_pk_add_f16 v65, v65, v82
	v_pk_add_f16 v64, v64, v83
	v_pk_add_f16 v63, v63, v84
	v_pk_fma_f16 v42, v46, v82, v42
	v_pk_fma_f16 v43, v47, v83, v43
	v_pk_fma_f16 v44, v48, v84, v44
	v_pk_fma_f16 v45, v49, v85, v45
	v_pk_add_f16 v79, v136, v155 neg_lo:[0,1] neg_hi:[0,1]
	v_pk_add_f16 v80, v135, v156 neg_lo:[0,1] neg_hi:[0,1]
	v_pk_add_f16 v81, v134, v157 neg_lo:[0,1] neg_hi:[0,1]
	v_exp_f16_sdwa v82, v78 dst_sel:WORD_0 dst_unused:UNUSED_PAD src0_sel:WORD_0
	v_exp_f16_sdwa v83, v79 dst_sel:WORD_0 dst_unused:UNUSED_PAD src0_sel:WORD_0
	v_exp_f16_sdwa v84, v80 dst_sel:WORD_0 dst_unused:UNUSED_PAD src0_sel:WORD_0
	v_exp_f16_sdwa v85, v81 dst_sel:WORD_0 dst_unused:UNUSED_PAD src0_sel:WORD_0
	v_exp_f16_sdwa v82, v78 dst_sel:WORD_1 dst_unused:UNUSED_PRESERVE src0_sel:WORD_1
	v_exp_f16_sdwa v83, v79 dst_sel:WORD_1 dst_unused:UNUSED_PRESERVE src0_sel:WORD_1
	v_exp_f16_sdwa v84, v80 dst_sel:WORD_1 dst_unused:UNUSED_PRESERVE src0_sel:WORD_1
	v_exp_f16_sdwa v85, v81 dst_sel:WORD_1 dst_unused:UNUSED_PRESERVE src0_sel:WORD_1
	v_pk_add_f16 v78, v186, v154 neg_lo:[0,1] neg_hi:[0,1]
	v_pk_add_f16 v62, v62, v85
	v_pk_add_f16 v63, v63, v84
	v_pk_add_f16 v64, v64, v83
	v_pk_add_f16 v65, v65, v82
	v_pk_fma_f16 v45, v9, v85, v45
	v_pk_fma_f16 v44, v8, v84, v44
	v_pk_fma_f16 v43, v7, v83, v43
	v_pk_fma_f16 v42, v6, v82, v42
	v_pk_add_f16 v79, v185, v155 neg_lo:[0,1] neg_hi:[0,1]
	v_pk_add_f16 v80, v184, v156 neg_lo:[0,1] neg_hi:[0,1]
	v_pk_add_f16 v81, v183, v157 neg_lo:[0,1] neg_hi:[0,1]
	v_exp_f16_sdwa v82, v78 dst_sel:WORD_0 dst_unused:UNUSED_PAD src0_sel:WORD_0
	v_exp_f16_sdwa v83, v79 dst_sel:WORD_0 dst_unused:UNUSED_PAD src0_sel:WORD_0
	v_exp_f16_sdwa v84, v80 dst_sel:WORD_0 dst_unused:UNUSED_PAD src0_sel:WORD_0
	v_exp_f16_sdwa v85, v81 dst_sel:WORD_0 dst_unused:UNUSED_PAD src0_sel:WORD_0
	v_exp_f16_sdwa v82, v78 dst_sel:WORD_1 dst_unused:UNUSED_PRESERVE src0_sel:WORD_1
	v_exp_f16_sdwa v83, v79 dst_sel:WORD_1 dst_unused:UNUSED_PRESERVE src0_sel:WORD_1
	v_exp_f16_sdwa v84, v80 dst_sel:WORD_1 dst_unused:UNUSED_PRESERVE src0_sel:WORD_1
	v_exp_f16_sdwa v85, v81 dst_sel:WORD_1 dst_unused:UNUSED_PRESERVE src0_sel:WORD_1
	v_pk_add_f16 v78, v114, v154 neg_lo:[0,1] neg_hi:[0,1]
	v_pk_add_f16 v62, v62, v85
	v_pk_add_f16 v65, v65, v82
	v_pk_add_f16 v64, v64, v83
	v_pk_add_f16 v63, v63, v84
	v_pk_fma_f16 v42, v10, v82, v42
	v_pk_fma_f16 v43, v11, v83, v43
	v_pk_fma_f16 v44, v12, v84, v44
	v_pk_fma_f16 v45, v13, v85, v45
	v_pk_add_f16 v79, v115, v155 neg_lo:[0,1] neg_hi:[0,1]
	v_pk_add_f16 v80, v116, v156 neg_lo:[0,1] neg_hi:[0,1]
	v_pk_add_f16 v81, v117, v157 neg_lo:[0,1] neg_hi:[0,1]
	v_exp_f16_sdwa v82, v78 dst_sel:WORD_0 dst_unused:UNUSED_PAD src0_sel:WORD_0
	v_exp_f16_sdwa v83, v79 dst_sel:WORD_0 dst_unused:UNUSED_PAD src0_sel:WORD_0
	v_exp_f16_sdwa v84, v80 dst_sel:WORD_0 dst_unused:UNUSED_PAD src0_sel:WORD_0
	v_exp_f16_sdwa v85, v81 dst_sel:WORD_0 dst_unused:UNUSED_PAD src0_sel:WORD_0
	v_exp_f16_sdwa v82, v78 dst_sel:WORD_1 dst_unused:UNUSED_PRESERVE src0_sel:WORD_1
	v_exp_f16_sdwa v83, v79 dst_sel:WORD_1 dst_unused:UNUSED_PRESERVE src0_sel:WORD_1
	v_exp_f16_sdwa v84, v80 dst_sel:WORD_1 dst_unused:UNUSED_PRESERVE src0_sel:WORD_1
	v_exp_f16_sdwa v85, v81 dst_sel:WORD_1 dst_unused:UNUSED_PRESERVE src0_sel:WORD_1
	s_nop 0
	v_pk_add_f16 v62, v62, v85
	v_pk_add_f16 v63, v63, v84
	v_pk_add_f16 v64, v64, v83
	v_pk_add_f16 v65, v65, v82
	v_rcp_f16_e32 v81, v62
	v_rcp_f16_sdwa v62, v62 dst_sel:DWORD dst_unused:UNUSED_PAD src0_sel:WORD_1
	v_rcp_f16_e32 v78, v65
	v_rcp_f16_sdwa v65, v65 dst_sel:DWORD dst_unused:UNUSED_PAD src0_sel:WORD_1
	v_rcp_f16_e32 v79, v64
	v_rcp_f16_sdwa v64, v64 dst_sel:DWORD dst_unused:UNUSED_PAD src0_sel:WORD_1
	v_rcp_f16_e32 v80, v63
	v_rcp_f16_sdwa v63, v63 dst_sel:DWORD dst_unused:UNUSED_PAD src0_sel:WORD_1
	v_pk_fma_f16 v45, v17, v85, v45
	v_pack_b32_f16 v62, v81, v62
	v_pk_fma_f16 v44, v16, v84, v44
	v_pk_fma_f16 v43, v15, v83, v43
	v_pk_fma_f16 v42, v14, v82, v42
	v_pack_b32_f16 v65, v78, v65
	v_pack_b32_f16 v64, v79, v64
	v_pack_b32_f16 v63, v80, v63
	v_pk_mul_f16 v45, v45, v62
	s_waitcnt vmcnt(6)
	v_pk_mul_f16 v62, v182, v150 op_sel_hi:[0,1]
	v_pk_mul_f16 v42, v42, v65
	v_pk_mul_f16 v43, v43, v64
	v_pk_mul_f16 v44, v44, v63
	v_pk_mul_f16 v63, v182, v151 op_sel_hi:[0,1]
	v_pk_mul_f16 v64, v182, v152 op_sel_hi:[0,1]
	v_pk_mul_f16 v65, v182, v153 op_sel_hi:[0,1]
	v_pk_mul_f16 v78, v180, v150 op_sel_hi:[0,1]
	v_pk_mul_f16 v82, v181, v150 op_sel_hi:[0,1]
	v_pk_fma_f16 v50, v50, v150, v62
	v_pk_fma_f16 v66, v66, v150, v62
	v_pk_fma_f16 v62, v94, v150, v62
	v_pk_mul_f16 v79, v180, v151 op_sel_hi:[0,1]
	v_pk_maximum3_f16 v114, v50, v66, v62
	v_pk_mul_f16 v80, v180, v152 op_sel_hi:[0,1]
	v_pk_mul_f16 v81, v180, v153 op_sel_hi:[0,1]
	v_pk_mul_f16 v83, v181, v151 op_sel_hi:[0,1]
	v_pk_mul_f16 v84, v181, v152 op_sel_hi:[0,1]
	v_pk_mul_f16 v85, v181, v153 op_sel_hi:[0,1]
	v_pk_fma_f16 v53, v53, v153, v65
	v_pk_fma_f16 v52, v52, v152, v64
	v_pk_fma_f16 v51, v51, v151, v63
	v_pk_fma_f16 v69, v69, v153, v65
	v_pk_fma_f16 v68, v68, v152, v64
	v_pk_fma_f16 v67, v67, v151, v63
	v_pk_fma_f16 v65, v97, v153, v65
	v_pk_fma_f16 v64, v96, v152, v64
	v_pk_fma_f16 v63, v95, v151, v63
	v_pk_fma_f16 v89, v18, v150, v78
	v_pk_fma_f16 v97, v30, v150, v78
	v_pk_fma_f16 v78, v54, v150, v78
	v_pk_fma_f16 v105, v74, v150, v82
	v_pk_fma_f16 v109, v98, v150, v82
	v_pk_fma_f16 v82, v118, v150, v82
	v_pk_maximum3_f16 v115, v51, v67, v63
	v_pk_maximum3_f16 v116, v52, v68, v64
	v_pk_maximum3_f16 v117, v53, v69, v65
	v_pk_maximum3_f16 v122, v89, v97, v78
	v_pk_fma_f16 v86, v21, v153, v81
	v_pk_maximum3_f16 v126, v105, v109, v82
	v_pk_fma_f16 v87, v20, v152, v80
	v_pk_maximum3_f16 v114, v114, v122, v126
	v_pk_fma_f16 v88, v19, v151, v79
	v_pk_fma_f16 v94, v33, v153, v81
	v_pk_fma_f16 v95, v32, v152, v80
	v_pk_fma_f16 v96, v31, v151, v79
	v_pk_fma_f16 v81, v57, v153, v81
	v_pk_fma_f16 v80, v56, v152, v80
	v_pk_fma_f16 v79, v55, v151, v79
	v_pk_fma_f16 v102, v77, v153, v85
	v_pk_fma_f16 v103, v76, v152, v84
	v_pk_fma_f16 v104, v75, v151, v83
	v_pk_fma_f16 v106, v101, v153, v85
	v_pk_fma_f16 v107, v100, v152, v84
	v_pk_fma_f16 v108, v99, v151, v83
	v_pk_fma_f16 v85, v121, v153, v85
	v_pk_fma_f16 v84, v120, v152, v84
	v_pk_fma_f16 v83, v119, v151, v83
	v_pk_maximum3_f16 v123, v88, v96, v79
	v_pk_maximum3_f16 v124, v87, v95, v80
	v_pk_maximum3_f16 v125, v86, v94, v81
	v_pk_maximum3_f16 v128, v103, v107, v84
	v_pk_maximum3_f16 v129, v102, v106, v85
	v_pk_maximum3_f16 v127, v104, v108, v83
	v_pk_maximum3_f16 v115, v115, v123, v127
	v_pk_maximum3_f16 v116, v116, v124, v128
	v_pk_maximum3_f16 v117, v117, v125, v129
	v_pk_add_f16 v50, v50, v114 neg_lo:[0,1] neg_hi:[0,1]
	v_pk_add_f16 v51, v51, v115 neg_lo:[0,1] neg_hi:[0,1]
	v_pk_add_f16 v52, v52, v116 neg_lo:[0,1] neg_hi:[0,1]
	v_pk_add_f16 v53, v53, v117 neg_lo:[0,1] neg_hi:[0,1]
	v_pk_add_f16 v66, v66, v114 neg_lo:[0,1] neg_hi:[0,1]
	v_exp_f16_sdwa v122, v50 dst_sel:WORD_0 dst_unused:UNUSED_PAD src0_sel:WORD_0
	v_exp_f16_sdwa v123, v51 dst_sel:WORD_0 dst_unused:UNUSED_PAD src0_sel:WORD_0
	v_exp_f16_sdwa v124, v52 dst_sel:WORD_0 dst_unused:UNUSED_PAD src0_sel:WORD_0
	v_exp_f16_sdwa v125, v53 dst_sel:WORD_0 dst_unused:UNUSED_PAD src0_sel:WORD_0
	v_exp_f16_sdwa v122, v50 dst_sel:WORD_1 dst_unused:UNUSED_PRESERVE src0_sel:WORD_1
	v_exp_f16_sdwa v123, v51 dst_sel:WORD_1 dst_unused:UNUSED_PRESERVE src0_sel:WORD_1
	v_exp_f16_sdwa v124, v52 dst_sel:WORD_1 dst_unused:UNUSED_PRESERVE src0_sel:WORD_1
	v_exp_f16_sdwa v125, v53 dst_sel:WORD_1 dst_unused:UNUSED_PRESERVE src0_sel:WORD_1
	v_pk_add_f16 v67, v67, v115 neg_lo:[0,1] neg_hi:[0,1]
	v_pk_add_f16 v50, v125, 0
	v_pk_fma_f16 v22, v22, v122, 0
	v_pk_add_f16 v51, v124, 0
	v_pk_add_f16 v52, v123, 0
	v_pk_add_f16 v53, v122, 0
	v_pk_fma_f16 v23, v23, v123, 0
	v_pk_fma_f16 v24, v24, v124, 0
	v_pk_fma_f16 v25, v25, v125, 0
	v_pk_add_f16 v68, v68, v116 neg_lo:[0,1] neg_hi:[0,1]
	v_pk_add_f16 v69, v69, v117 neg_lo:[0,1] neg_hi:[0,1]
	v_exp_f16_sdwa v122, v66 dst_sel:WORD_0 dst_unused:UNUSED_PAD src0_sel:WORD_0
	v_exp_f16_sdwa v123, v67 dst_sel:WORD_0 dst_unused:UNUSED_PAD src0_sel:WORD_0
	v_exp_f16_sdwa v124, v68 dst_sel:WORD_0 dst_unused:UNUSED_PAD src0_sel:WORD_0
	v_exp_f16_sdwa v125, v69 dst_sel:WORD_0 dst_unused:UNUSED_PAD src0_sel:WORD_0
	v_exp_f16_sdwa v122, v66 dst_sel:WORD_1 dst_unused:UNUSED_PRESERVE src0_sel:WORD_1
	v_exp_f16_sdwa v123, v67 dst_sel:WORD_1 dst_unused:UNUSED_PRESERVE src0_sel:WORD_1
	v_exp_f16_sdwa v124, v68 dst_sel:WORD_1 dst_unused:UNUSED_PRESERVE src0_sel:WORD_1
	v_exp_f16_sdwa v125, v69 dst_sel:WORD_1 dst_unused:UNUSED_PRESERVE src0_sel:WORD_1
	s_nop 0
	v_pk_add_f16 v50, v50, v125
	v_pk_fma_f16 v22, v34, v122, v22
	v_pk_add_f16 v34, v62, v114 neg_lo:[0,1] neg_hi:[0,1]
	v_pk_add_f16 v53, v53, v122
	v_pk_add_f16 v52, v52, v123
	v_pk_add_f16 v51, v51, v124
	v_pk_fma_f16 v25, v37, v125, v25
	v_pk_fma_f16 v24, v36, v124, v24
	v_pk_fma_f16 v23, v35, v123, v23
	v_pk_add_f16 v35, v63, v115 neg_lo:[0,1] neg_hi:[0,1]
	v_pk_add_f16 v36, v64, v116 neg_lo:[0,1] neg_hi:[0,1]
	v_pk_add_f16 v37, v65, v117 neg_lo:[0,1] neg_hi:[0,1]
	v_exp_f16_sdwa v62, v34 dst_sel:WORD_0 dst_unused:UNUSED_PAD src0_sel:WORD_0
	v_exp_f16_sdwa v63, v35 dst_sel:WORD_0 dst_unused:UNUSED_PAD src0_sel:WORD_0
	v_exp_f16_sdwa v64, v36 dst_sel:WORD_0 dst_unused:UNUSED_PAD src0_sel:WORD_0
	v_exp_f16_sdwa v65, v37 dst_sel:WORD_0 dst_unused:UNUSED_PAD src0_sel:WORD_0
	v_exp_f16_sdwa v62, v34 dst_sel:WORD_1 dst_unused:UNUSED_PRESERVE src0_sel:WORD_1
	v_exp_f16_sdwa v63, v35 dst_sel:WORD_1 dst_unused:UNUSED_PRESERVE src0_sel:WORD_1
	v_exp_f16_sdwa v64, v36 dst_sel:WORD_1 dst_unused:UNUSED_PRESERVE src0_sel:WORD_1
	v_exp_f16_sdwa v65, v37 dst_sel:WORD_1 dst_unused:UNUSED_PRESERVE src0_sel:WORD_1
	s_nop 0
	v_pk_add_f16 v34, v50, v65
	v_pk_add_f16 v35, v51, v64
	v_pk_add_f16 v36, v52, v63
	v_pk_add_f16 v37, v53, v62
	v_pk_fma_f16 v22, v46, v62, v22
	v_pk_fma_f16 v23, v47, v63, v23
	v_pk_fma_f16 v24, v48, v64, v24
	v_pk_fma_f16 v25, v49, v65, v25
	v_pk_add_f16 v46, v89, v114 neg_lo:[0,1] neg_hi:[0,1]
	v_pk_add_f16 v47, v88, v115 neg_lo:[0,1] neg_hi:[0,1]
	v_pk_add_f16 v48, v87, v116 neg_lo:[0,1] neg_hi:[0,1]
	v_pk_add_f16 v49, v86, v117 neg_lo:[0,1] neg_hi:[0,1]
	v_exp_f16_sdwa v50, v46 dst_sel:WORD_0 dst_unused:UNUSED_PAD src0_sel:WORD_0
	v_exp_f16_sdwa v51, v47 dst_sel:WORD_0 dst_unused:UNUSED_PAD src0_sel:WORD_0
	v_exp_f16_sdwa v52, v48 dst_sel:WORD_0 dst_unused:UNUSED_PAD src0_sel:WORD_0
	v_exp_f16_sdwa v53, v49 dst_sel:WORD_0 dst_unused:UNUSED_PAD src0_sel:WORD_0
	v_exp_f16_sdwa v50, v46 dst_sel:WORD_1 dst_unused:UNUSED_PRESERVE src0_sel:WORD_1
	v_exp_f16_sdwa v51, v47 dst_sel:WORD_1 dst_unused:UNUSED_PRESERVE src0_sel:WORD_1
	v_exp_f16_sdwa v52, v48 dst_sel:WORD_1 dst_unused:UNUSED_PRESERVE src0_sel:WORD_1
	v_exp_f16_sdwa v53, v49 dst_sel:WORD_1 dst_unused:UNUSED_PRESERVE src0_sel:WORD_1
	v_pk_add_f16 v46, v97, v114 neg_lo:[0,1] neg_hi:[0,1]
	v_pk_add_f16 v34, v34, v53
	v_pk_add_f16 v37, v37, v50
	v_pk_add_f16 v36, v36, v51
	v_pk_add_f16 v35, v35, v52
	v_pk_fma_f16 v25, v9, v53, v25
	v_pk_fma_f16 v24, v8, v52, v24
	v_pk_fma_f16 v23, v7, v51, v23
	v_pk_fma_f16 v22, v6, v50, v22
	v_pk_add_f16 v47, v96, v115 neg_lo:[0,1] neg_hi:[0,1]
	v_pk_add_f16 v48, v95, v116 neg_lo:[0,1] neg_hi:[0,1]
	v_pk_add_f16 v49, v94, v117 neg_lo:[0,1] neg_hi:[0,1]
	v_exp_f16_sdwa v50, v46 dst_sel:WORD_0 dst_unused:UNUSED_PAD src0_sel:WORD_0
	v_exp_f16_sdwa v51, v47 dst_sel:WORD_0 dst_unused:UNUSED_PAD src0_sel:WORD_0
	v_exp_f16_sdwa v52, v48 dst_sel:WORD_0 dst_unused:UNUSED_PAD src0_sel:WORD_0
	v_exp_f16_sdwa v53, v49 dst_sel:WORD_0 dst_unused:UNUSED_PAD src0_sel:WORD_0
	v_exp_f16_sdwa v50, v46 dst_sel:WORD_1 dst_unused:UNUSED_PRESERVE src0_sel:WORD_1
	v_exp_f16_sdwa v51, v47 dst_sel:WORD_1 dst_unused:UNUSED_PRESERVE src0_sel:WORD_1
	v_exp_f16_sdwa v52, v48 dst_sel:WORD_1 dst_unused:UNUSED_PRESERVE src0_sel:WORD_1
	v_exp_f16_sdwa v53, v49 dst_sel:WORD_1 dst_unused:UNUSED_PRESERVE src0_sel:WORD_1
	v_pk_add_f16 v46, v78, v114 neg_lo:[0,1] neg_hi:[0,1]
	v_pk_add_f16 v34, v34, v53
	v_pk_add_f16 v35, v35, v52
	v_pk_add_f16 v36, v36, v51
	v_pk_add_f16 v37, v37, v50
	v_pk_fma_f16 v22, v10, v50, v22
	v_pk_fma_f16 v23, v11, v51, v23
	v_pk_fma_f16 v24, v12, v52, v24
	v_pk_fma_f16 v25, v13, v53, v25
	v_pk_add_f16 v47, v79, v115 neg_lo:[0,1] neg_hi:[0,1]
	v_pk_add_f16 v48, v80, v116 neg_lo:[0,1] neg_hi:[0,1]
	v_pk_add_f16 v49, v81, v117 neg_lo:[0,1] neg_hi:[0,1]
	v_exp_f16_sdwa v50, v46 dst_sel:WORD_0 dst_unused:UNUSED_PAD src0_sel:WORD_0
	v_exp_f16_sdwa v51, v47 dst_sel:WORD_0 dst_unused:UNUSED_PAD src0_sel:WORD_0
	v_exp_f16_sdwa v52, v48 dst_sel:WORD_0 dst_unused:UNUSED_PAD src0_sel:WORD_0
	v_exp_f16_sdwa v53, v49 dst_sel:WORD_0 dst_unused:UNUSED_PAD src0_sel:WORD_0
	v_exp_f16_sdwa v50, v46 dst_sel:WORD_1 dst_unused:UNUSED_PRESERVE src0_sel:WORD_1
	v_exp_f16_sdwa v51, v47 dst_sel:WORD_1 dst_unused:UNUSED_PRESERVE src0_sel:WORD_1
	v_exp_f16_sdwa v52, v48 dst_sel:WORD_1 dst_unused:UNUSED_PRESERVE src0_sel:WORD_1
	v_exp_f16_sdwa v53, v49 dst_sel:WORD_1 dst_unused:UNUSED_PRESERVE src0_sel:WORD_1
	v_pk_add_f16 v46, v105, v114 neg_lo:[0,1] neg_hi:[0,1]
	v_pk_add_f16 v34, v34, v53
	v_pk_add_f16 v37, v37, v50
	v_pk_add_f16 v36, v36, v51
	v_pk_add_f16 v35, v35, v52
	v_pk_fma_f16 v25, v17, v53, v25
	v_pk_fma_f16 v24, v16, v52, v24
	v_pk_fma_f16 v23, v15, v51, v23
	v_pk_fma_f16 v22, v14, v50, v22
	v_pk_add_f16 v47, v104, v115 neg_lo:[0,1] neg_hi:[0,1]
	v_pk_add_f16 v48, v103, v116 neg_lo:[0,1] neg_hi:[0,1]
	v_pk_add_f16 v49, v102, v117 neg_lo:[0,1] neg_hi:[0,1]
	v_exp_f16_sdwa v50, v46 dst_sel:WORD_0 dst_unused:UNUSED_PAD src0_sel:WORD_0
	v_exp_f16_sdwa v51, v47 dst_sel:WORD_0 dst_unused:UNUSED_PAD src0_sel:WORD_0
	v_exp_f16_sdwa v52, v48 dst_sel:WORD_0 dst_unused:UNUSED_PAD src0_sel:WORD_0
	v_exp_f16_sdwa v53, v49 dst_sel:WORD_0 dst_unused:UNUSED_PAD src0_sel:WORD_0
	v_exp_f16_sdwa v50, v46 dst_sel:WORD_1 dst_unused:UNUSED_PRESERVE src0_sel:WORD_1
	v_exp_f16_sdwa v51, v47 dst_sel:WORD_1 dst_unused:UNUSED_PRESERVE src0_sel:WORD_1
	v_exp_f16_sdwa v52, v48 dst_sel:WORD_1 dst_unused:UNUSED_PRESERVE src0_sel:WORD_1
	v_exp_f16_sdwa v53, v49 dst_sel:WORD_1 dst_unused:UNUSED_PRESERVE src0_sel:WORD_1
	v_pk_add_f16 v46, v109, v114 neg_lo:[0,1] neg_hi:[0,1]
	v_pk_add_f16 v34, v34, v53
	v_pk_add_f16 v35, v35, v52
	v_pk_add_f16 v36, v36, v51
	v_pk_add_f16 v37, v37, v50
	v_pk_fma_f16 v22, v26, v50, v22
	v_pk_fma_f16 v23, v27, v51, v23
	v_pk_fma_f16 v24, v28, v52, v24
	v_pk_fma_f16 v25, v29, v53, v25
	v_pk_add_f16 v47, v108, v115 neg_lo:[0,1] neg_hi:[0,1]
	v_pk_add_f16 v48, v107, v116 neg_lo:[0,1] neg_hi:[0,1]
	v_pk_add_f16 v49, v106, v117 neg_lo:[0,1] neg_hi:[0,1]
	v_exp_f16_sdwa v50, v46 dst_sel:WORD_0 dst_unused:UNUSED_PAD src0_sel:WORD_0
	v_exp_f16_sdwa v51, v47 dst_sel:WORD_0 dst_unused:UNUSED_PAD src0_sel:WORD_0
	v_exp_f16_sdwa v52, v48 dst_sel:WORD_0 dst_unused:UNUSED_PAD src0_sel:WORD_0
	v_exp_f16_sdwa v53, v49 dst_sel:WORD_0 dst_unused:UNUSED_PAD src0_sel:WORD_0
	v_exp_f16_sdwa v50, v46 dst_sel:WORD_1 dst_unused:UNUSED_PRESERVE src0_sel:WORD_1
	v_exp_f16_sdwa v51, v47 dst_sel:WORD_1 dst_unused:UNUSED_PRESERVE src0_sel:WORD_1
	v_exp_f16_sdwa v52, v48 dst_sel:WORD_1 dst_unused:UNUSED_PRESERVE src0_sel:WORD_1
	v_exp_f16_sdwa v53, v49 dst_sel:WORD_1 dst_unused:UNUSED_PRESERVE src0_sel:WORD_1
	v_pk_add_f16 v46, v82, v114 neg_lo:[0,1] neg_hi:[0,1]
	v_pk_add_f16 v34, v34, v53
	v_pk_add_f16 v37, v37, v50
	v_pk_add_f16 v36, v36, v51
	v_pk_add_f16 v35, v35, v52
	v_pk_fma_f16 v25, v41, v53, v25
	v_pk_fma_f16 v24, v40, v52, v24
	v_pk_fma_f16 v23, v39, v51, v23
	v_pk_fma_f16 v22, v38, v50, v22
	v_pk_add_f16 v47, v83, v115 neg_lo:[0,1] neg_hi:[0,1]
	v_pk_add_f16 v48, v84, v116 neg_lo:[0,1] neg_hi:[0,1]
	v_pk_add_f16 v49, v85, v117 neg_lo:[0,1] neg_hi:[0,1]
	v_exp_f16_sdwa v50, v46 dst_sel:WORD_0 dst_unused:UNUSED_PAD src0_sel:WORD_0
	v_exp_f16_sdwa v51, v47 dst_sel:WORD_0 dst_unused:UNUSED_PAD src0_sel:WORD_0
	v_exp_f16_sdwa v52, v48 dst_sel:WORD_0 dst_unused:UNUSED_PAD src0_sel:WORD_0
	v_exp_f16_sdwa v53, v49 dst_sel:WORD_0 dst_unused:UNUSED_PAD src0_sel:WORD_0
	v_exp_f16_sdwa v50, v46 dst_sel:WORD_1 dst_unused:UNUSED_PRESERVE src0_sel:WORD_1
	v_exp_f16_sdwa v51, v47 dst_sel:WORD_1 dst_unused:UNUSED_PRESERVE src0_sel:WORD_1
	v_exp_f16_sdwa v52, v48 dst_sel:WORD_1 dst_unused:UNUSED_PRESERVE src0_sel:WORD_1
	v_exp_f16_sdwa v53, v49 dst_sel:WORD_1 dst_unused:UNUSED_PRESERVE src0_sel:WORD_1
	s_nop 0
	v_pk_add_f16 v34, v34, v53
	v_pk_add_f16 v35, v35, v52
	v_rcp_f16_e32 v48, v34
	v_rcp_f16_sdwa v34, v34 dst_sel:DWORD dst_unused:UNUSED_PAD src0_sel:WORD_1
	v_pk_add_f16 v36, v36, v51
	v_rcp_f16_e32 v49, v35
	v_rcp_f16_sdwa v35, v35 dst_sel:DWORD dst_unused:UNUSED_PAD src0_sel:WORD_1
	v_pk_add_f16 v37, v37, v50
	v_rcp_f16_e32 v47, v36
	v_rcp_f16_sdwa v36, v36 dst_sel:DWORD dst_unused:UNUSED_PAD src0_sel:WORD_1
	v_rcp_f16_e32 v46, v37
	v_rcp_f16_sdwa v37, v37 dst_sel:DWORD dst_unused:UNUSED_PAD src0_sel:WORD_1
	v_pk_fma_f16 v25, v61, v53, v25
	v_pack_b32_f16 v34, v48, v34
	v_pk_fma_f16 v24, v60, v52, v24
	v_pk_mul_f16 v25, v25, v34
	v_pack_b32_f16 v34, v49, v35
	v_pk_fma_f16 v23, v59, v51, v23
	v_pk_mul_f16 v24, v24, v34
	v_pack_b32_f16 v34, v47, v36
	v_pk_fma_f16 v22, v58, v50, v22
	v_pk_mul_f16 v23, v23, v34
	v_pack_b32_f16 v34, v46, v37
	v_pk_mul_f16 v22, v22, v34
	s_waitcnt vmcnt(0)
	v_pk_mul_f16 v34, v182, v146 op_sel_hi:[0,1]
	v_pk_mul_f16 v35, v182, v147 op_sel_hi:[0,1]
	v_pk_mul_f16 v36, v182, v148 op_sel_hi:[0,1]
	v_pk_mul_f16 v37, v182, v149 op_sel_hi:[0,1]
	v_pk_mul_f16 v46, v180, v146 op_sel_hi:[0,1]
	v_pk_mul_f16 v47, v180, v147 op_sel_hi:[0,1]
	v_pk_mul_f16 v48, v180, v148 op_sel_hi:[0,1]
	v_pk_mul_f16 v49, v180, v149 op_sel_hi:[0,1]
	v_pk_mul_f16 v50, v181, v146 op_sel_hi:[0,1]
	v_pk_mul_f16 v51, v181, v147 op_sel_hi:[0,1]
	v_pk_mul_f16 v52, v181, v148 op_sel_hi:[0,1]
	v_pk_mul_f16 v53, v181, v149 op_sel_hi:[0,1]
	v_pk_fma_f16 v21, v21, v149, v37
	v_pk_fma_f16 v20, v20, v148, v36
	v_pk_fma_f16 v19, v19, v147, v35
	v_pk_fma_f16 v18, v18, v146, v34
	v_pk_fma_f16 v33, v33, v149, v37
	v_pk_fma_f16 v32, v32, v148, v36
	v_pk_fma_f16 v31, v31, v147, v35
	v_pk_fma_f16 v30, v30, v146, v34
	v_pk_fma_f16 v37, v57, v149, v37
	v_pk_fma_f16 v36, v56, v148, v36
	v_pk_fma_f16 v35, v55, v147, v35
	v_pk_fma_f16 v34, v54, v146, v34
	v_pk_maximum3_f16 v79, v19, v31, v35
	v_pk_maximum3_f16 v80, v20, v32, v36
	v_pk_maximum3_f16 v81, v21, v33, v37
	v_pk_fma_f16 v54, v77, v149, v49
	v_pk_maximum3_f16 v78, v18, v30, v34
	v_pk_fma_f16 v55, v76, v148, v48
	v_pk_fma_f16 v56, v75, v147, v47
	v_pk_fma_f16 v57, v74, v146, v46
	v_pk_fma_f16 v62, v101, v149, v49
	v_pk_fma_f16 v63, v100, v148, v48
	v_pk_fma_f16 v64, v99, v147, v47
	v_pk_fma_f16 v65, v98, v146, v46
	v_pk_fma_f16 v49, v121, v149, v49
	v_pk_fma_f16 v48, v120, v148, v48
	v_pk_fma_f16 v47, v119, v147, v47
	v_pk_fma_f16 v46, v118, v146, v46
	v_pk_fma_f16 v66, v133, v149, v53
	v_pk_fma_f16 v67, v132, v148, v52
	v_pk_fma_f16 v68, v131, v147, v51
	v_pk_fma_f16 v69, v130, v146, v50
	v_pk_fma_f16 v74, v141, v149, v53
	v_pk_fma_f16 v75, v140, v148, v52
	v_pk_fma_f16 v76, v139, v147, v51
	v_pk_fma_f16 v77, v138, v146, v50
	v_pk_fma_f16 v53, v145, v149, v53
	v_pk_fma_f16 v52, v144, v148, v52
	v_pk_fma_f16 v51, v143, v147, v51
	v_pk_fma_f16 v50, v142, v146, v50
	v_pk_maximum3_f16 v82, v57, v65, v46
	v_pk_maximum3_f16 v83, v56, v64, v47
	v_pk_maximum3_f16 v84, v55, v63, v48
	v_pk_maximum3_f16 v85, v54, v62, v49
	v_pk_maximum3_f16 v87, v68, v76, v51
	v_pk_maximum3_f16 v86, v69, v77, v50
	v_pk_maximum3_f16 v88, v67, v75, v52
	v_pk_maximum3_f16 v89, v66, v74, v53
	v_pk_maximum3_f16 v78, v78, v82, v86
	v_pk_maximum3_f16 v79, v79, v83, v87
	v_pk_maximum3_f16 v80, v80, v84, v88
	v_pk_maximum3_f16 v81, v81, v85, v89
	s_nop 0
	v_pk_add_f16 v18, v18, v78 neg_lo:[0,1] neg_hi:[0,1]
	v_pk_add_f16 v19, v19, v79 neg_lo:[0,1] neg_hi:[0,1]
	v_pk_add_f16 v20, v20, v80 neg_lo:[0,1] neg_hi:[0,1]
	v_pk_add_f16 v21, v21, v81 neg_lo:[0,1] neg_hi:[0,1]
	v_pk_add_f16 v30, v30, v78 neg_lo:[0,1] neg_hi:[0,1]
	v_exp_f16_sdwa v82, v18 dst_sel:WORD_0 dst_unused:UNUSED_PAD src0_sel:WORD_0
	v_exp_f16_sdwa v83, v19 dst_sel:WORD_0 dst_unused:UNUSED_PAD src0_sel:WORD_0
	v_exp_f16_sdwa v84, v20 dst_sel:WORD_0 dst_unused:UNUSED_PAD src0_sel:WORD_0
	v_exp_f16_sdwa v85, v21 dst_sel:WORD_0 dst_unused:UNUSED_PAD src0_sel:WORD_0
	v_exp_f16_sdwa v82, v18 dst_sel:WORD_1 dst_unused:UNUSED_PRESERVE src0_sel:WORD_1
	v_exp_f16_sdwa v83, v19 dst_sel:WORD_1 dst_unused:UNUSED_PRESERVE src0_sel:WORD_1
	v_exp_f16_sdwa v84, v20 dst_sel:WORD_1 dst_unused:UNUSED_PRESERVE src0_sel:WORD_1
	v_exp_f16_sdwa v85, v21 dst_sel:WORD_1 dst_unused:UNUSED_PRESERVE src0_sel:WORD_1
	v_pk_add_f16 v31, v31, v79 neg_lo:[0,1] neg_hi:[0,1]
	v_pk_add_f16 v18, v82, 0
	v_pk_add_f16 v19, v83, 0
	v_pk_add_f16 v20, v84, 0
	v_pk_add_f16 v21, v85, 0
	v_pk_fma_f16 v6, v6, v82, 0
	v_pk_fma_f16 v7, v7, v83, 0
	v_pk_fma_f16 v8, v8, v84, 0
	v_pk_fma_f16 v9, v9, v85, 0
	v_pk_add_f16 v32, v32, v80 neg_lo:[0,1] neg_hi:[0,1]
	v_pk_add_f16 v33, v33, v81 neg_lo:[0,1] neg_hi:[0,1]
	v_exp_f16_sdwa v82, v30 dst_sel:WORD_0 dst_unused:UNUSED_PAD src0_sel:WORD_0
	v_exp_f16_sdwa v83, v31 dst_sel:WORD_0 dst_unused:UNUSED_PAD src0_sel:WORD_0
	v_exp_f16_sdwa v84, v32 dst_sel:WORD_0 dst_unused:UNUSED_PAD src0_sel:WORD_0
	v_exp_f16_sdwa v85, v33 dst_sel:WORD_0 dst_unused:UNUSED_PAD src0_sel:WORD_0
	v_exp_f16_sdwa v82, v30 dst_sel:WORD_1 dst_unused:UNUSED_PRESERVE src0_sel:WORD_1
	v_exp_f16_sdwa v83, v31 dst_sel:WORD_1 dst_unused:UNUSED_PRESERVE src0_sel:WORD_1
	v_exp_f16_sdwa v84, v32 dst_sel:WORD_1 dst_unused:UNUSED_PRESERVE src0_sel:WORD_1
	v_exp_f16_sdwa v85, v33 dst_sel:WORD_1 dst_unused:UNUSED_PRESERVE src0_sel:WORD_1
	s_nop 0
	v_pk_add_f16 v21, v21, v85
	v_pk_add_f16 v20, v20, v84
	v_pk_add_f16 v19, v19, v83
	v_pk_add_f16 v18, v18, v82
	v_pk_fma_f16 v9, v13, v85, v9
	v_pk_fma_f16 v8, v12, v84, v8
	v_pk_fma_f16 v7, v11, v83, v7
	v_pk_fma_f16 v6, v10, v82, v6
	v_pk_add_f16 v10, v34, v78 neg_lo:[0,1] neg_hi:[0,1]
	v_pk_add_f16 v11, v35, v79 neg_lo:[0,1] neg_hi:[0,1]
	v_pk_add_f16 v12, v36, v80 neg_lo:[0,1] neg_hi:[0,1]
	v_pk_add_f16 v13, v37, v81 neg_lo:[0,1] neg_hi:[0,1]
	v_exp_f16_sdwa v30, v10 dst_sel:WORD_0 dst_unused:UNUSED_PAD src0_sel:WORD_0
	v_exp_f16_sdwa v31, v11 dst_sel:WORD_0 dst_unused:UNUSED_PAD src0_sel:WORD_0
	v_exp_f16_sdwa v32, v12 dst_sel:WORD_0 dst_unused:UNUSED_PAD src0_sel:WORD_0
	v_exp_f16_sdwa v33, v13 dst_sel:WORD_0 dst_unused:UNUSED_PAD src0_sel:WORD_0
	v_exp_f16_sdwa v30, v10 dst_sel:WORD_1 dst_unused:UNUSED_PRESERVE src0_sel:WORD_1
	v_exp_f16_sdwa v31, v11 dst_sel:WORD_1 dst_unused:UNUSED_PRESERVE src0_sel:WORD_1
	v_exp_f16_sdwa v32, v12 dst_sel:WORD_1 dst_unused:UNUSED_PRESERVE src0_sel:WORD_1
	v_exp_f16_sdwa v33, v13 dst_sel:WORD_1 dst_unused:UNUSED_PRESERVE src0_sel:WORD_1
	v_pk_add_f16 v10, v18, v30
	v_pk_add_f16 v11, v19, v31
	v_pk_add_f16 v12, v20, v32
	v_pk_add_f16 v13, v21, v33
	v_pk_fma_f16 v6, v14, v30, v6
	v_pk_fma_f16 v7, v15, v31, v7
	v_pk_fma_f16 v8, v16, v32, v8
	v_pk_fma_f16 v9, v17, v33, v9
	v_pk_add_f16 v14, v57, v78 neg_lo:[0,1] neg_hi:[0,1]
	v_pk_add_f16 v15, v56, v79 neg_lo:[0,1] neg_hi:[0,1]
	v_pk_add_f16 v16, v55, v80 neg_lo:[0,1] neg_hi:[0,1]
	v_pk_add_f16 v17, v54, v81 neg_lo:[0,1] neg_hi:[0,1]
	v_exp_f16_sdwa v18, v14 dst_sel:WORD_0 dst_unused:UNUSED_PAD src0_sel:WORD_0
	v_exp_f16_sdwa v19, v15 dst_sel:WORD_0 dst_unused:UNUSED_PAD src0_sel:WORD_0
	v_exp_f16_sdwa v20, v16 dst_sel:WORD_0 dst_unused:UNUSED_PAD src0_sel:WORD_0
	v_exp_f16_sdwa v21, v17 dst_sel:WORD_0 dst_unused:UNUSED_PAD src0_sel:WORD_0
	v_exp_f16_sdwa v18, v14 dst_sel:WORD_1 dst_unused:UNUSED_PRESERVE src0_sel:WORD_1
	v_exp_f16_sdwa v19, v15 dst_sel:WORD_1 dst_unused:UNUSED_PRESERVE src0_sel:WORD_1
	v_exp_f16_sdwa v20, v16 dst_sel:WORD_1 dst_unused:UNUSED_PRESERVE src0_sel:WORD_1
	v_exp_f16_sdwa v21, v17 dst_sel:WORD_1 dst_unused:UNUSED_PRESERVE src0_sel:WORD_1
	v_pk_add_f16 v14, v65, v78 neg_lo:[0,1] neg_hi:[0,1]
	v_pk_add_f16 v13, v13, v21
	v_pk_add_f16 v12, v12, v20
	v_pk_add_f16 v11, v11, v19
	v_pk_add_f16 v10, v10, v18
	v_pk_fma_f16 v9, v29, v21, v9
	v_pk_fma_f16 v8, v28, v20, v8
	v_pk_fma_f16 v7, v27, v19, v7
	v_pk_fma_f16 v6, v26, v18, v6
	v_pk_add_f16 v15, v64, v79 neg_lo:[0,1] neg_hi:[0,1]
	v_pk_add_f16 v16, v63, v80 neg_lo:[0,1] neg_hi:[0,1]
	v_pk_add_f16 v17, v62, v81 neg_lo:[0,1] neg_hi:[0,1]
	v_exp_f16_sdwa v18, v14 dst_sel:WORD_0 dst_unused:UNUSED_PAD src0_sel:WORD_0
	v_exp_f16_sdwa v19, v15 dst_sel:WORD_0 dst_unused:UNUSED_PAD src0_sel:WORD_0
	v_exp_f16_sdwa v20, v16 dst_sel:WORD_0 dst_unused:UNUSED_PAD src0_sel:WORD_0
	v_exp_f16_sdwa v21, v17 dst_sel:WORD_0 dst_unused:UNUSED_PAD src0_sel:WORD_0
	v_exp_f16_sdwa v18, v14 dst_sel:WORD_1 dst_unused:UNUSED_PRESERVE src0_sel:WORD_1
	v_exp_f16_sdwa v19, v15 dst_sel:WORD_1 dst_unused:UNUSED_PRESERVE src0_sel:WORD_1
	v_exp_f16_sdwa v20, v16 dst_sel:WORD_1 dst_unused:UNUSED_PRESERVE src0_sel:WORD_1
	v_exp_f16_sdwa v21, v17 dst_sel:WORD_1 dst_unused:UNUSED_PRESERVE src0_sel:WORD_1
	v_pk_add_f16 v14, v46, v78 neg_lo:[0,1] neg_hi:[0,1]
	v_pk_add_f16 v10, v10, v18
	v_pk_add_f16 v11, v11, v19
	v_pk_add_f16 v12, v12, v20
	v_pk_add_f16 v13, v13, v21
	v_pk_fma_f16 v6, v38, v18, v6
	v_pk_fma_f16 v7, v39, v19, v7
	v_pk_fma_f16 v8, v40, v20, v8
	v_pk_fma_f16 v9, v41, v21, v9
	v_pk_add_f16 v15, v47, v79 neg_lo:[0,1] neg_hi:[0,1]
	v_pk_add_f16 v16, v48, v80 neg_lo:[0,1] neg_hi:[0,1]
	v_pk_add_f16 v17, v49, v81 neg_lo:[0,1] neg_hi:[0,1]
	v_exp_f16_sdwa v18, v14 dst_sel:WORD_0 dst_unused:UNUSED_PAD src0_sel:WORD_0
	v_exp_f16_sdwa v19, v15 dst_sel:WORD_0 dst_unused:UNUSED_PAD src0_sel:WORD_0
	v_exp_f16_sdwa v20, v16 dst_sel:WORD_0 dst_unused:UNUSED_PAD src0_sel:WORD_0
	v_exp_f16_sdwa v21, v17 dst_sel:WORD_0 dst_unused:UNUSED_PAD src0_sel:WORD_0
	v_exp_f16_sdwa v18, v14 dst_sel:WORD_1 dst_unused:UNUSED_PRESERVE src0_sel:WORD_1
	v_exp_f16_sdwa v19, v15 dst_sel:WORD_1 dst_unused:UNUSED_PRESERVE src0_sel:WORD_1
	v_exp_f16_sdwa v20, v16 dst_sel:WORD_1 dst_unused:UNUSED_PRESERVE src0_sel:WORD_1
	v_exp_f16_sdwa v21, v17 dst_sel:WORD_1 dst_unused:UNUSED_PRESERVE src0_sel:WORD_1
	v_pk_add_f16 v14, v69, v78 neg_lo:[0,1] neg_hi:[0,1]
	v_pk_add_f16 v13, v13, v21
	v_pk_add_f16 v12, v12, v20
	v_pk_add_f16 v11, v11, v19
	v_pk_add_f16 v10, v10, v18
	v_pk_fma_f16 v9, v61, v21, v9
	v_pk_fma_f16 v8, v60, v20, v8
	v_pk_fma_f16 v7, v59, v19, v7
	v_pk_fma_f16 v6, v58, v18, v6
	v_pk_add_f16 v15, v68, v79 neg_lo:[0,1] neg_hi:[0,1]
	v_pk_add_f16 v16, v67, v80 neg_lo:[0,1] neg_hi:[0,1]
	v_pk_add_f16 v17, v66, v81 neg_lo:[0,1] neg_hi:[0,1]
	v_exp_f16_sdwa v18, v14 dst_sel:WORD_0 dst_unused:UNUSED_PAD src0_sel:WORD_0
	v_exp_f16_sdwa v19, v15 dst_sel:WORD_0 dst_unused:UNUSED_PAD src0_sel:WORD_0
	v_exp_f16_sdwa v20, v16 dst_sel:WORD_0 dst_unused:UNUSED_PAD src0_sel:WORD_0
	v_exp_f16_sdwa v21, v17 dst_sel:WORD_0 dst_unused:UNUSED_PAD src0_sel:WORD_0
	v_exp_f16_sdwa v18, v14 dst_sel:WORD_1 dst_unused:UNUSED_PRESERVE src0_sel:WORD_1
	v_exp_f16_sdwa v19, v15 dst_sel:WORD_1 dst_unused:UNUSED_PRESERVE src0_sel:WORD_1
	v_exp_f16_sdwa v20, v16 dst_sel:WORD_1 dst_unused:UNUSED_PRESERVE src0_sel:WORD_1
	v_exp_f16_sdwa v21, v17 dst_sel:WORD_1 dst_unused:UNUSED_PRESERVE src0_sel:WORD_1
	v_pk_add_f16 v10, v10, v18
	v_pk_add_f16 v11, v11, v19
	v_pk_add_f16 v12, v12, v20
	v_pk_add_f16 v13, v13, v21
	v_pk_fma_f16 v14, v70, v18, v6
	v_pk_fma_f16 v15, v71, v19, v7
	v_pk_fma_f16 v16, v72, v20, v8
	v_pk_fma_f16 v17, v73, v21, v9
	v_pk_add_f16 v6, v77, v78 neg_lo:[0,1] neg_hi:[0,1]
	v_pk_add_f16 v7, v76, v79 neg_lo:[0,1] neg_hi:[0,1]
	v_pk_add_f16 v8, v75, v80 neg_lo:[0,1] neg_hi:[0,1]
	v_pk_add_f16 v9, v74, v81 neg_lo:[0,1] neg_hi:[0,1]
	v_exp_f16_sdwa v18, v6 dst_sel:WORD_0 dst_unused:UNUSED_PAD src0_sel:WORD_0
	v_exp_f16_sdwa v19, v7 dst_sel:WORD_0 dst_unused:UNUSED_PAD src0_sel:WORD_0
	v_exp_f16_sdwa v20, v8 dst_sel:WORD_0 dst_unused:UNUSED_PAD src0_sel:WORD_0
	v_exp_f16_sdwa v21, v9 dst_sel:WORD_0 dst_unused:UNUSED_PAD src0_sel:WORD_0
	v_exp_f16_sdwa v18, v6 dst_sel:WORD_1 dst_unused:UNUSED_PRESERVE src0_sel:WORD_1
	v_exp_f16_sdwa v19, v7 dst_sel:WORD_1 dst_unused:UNUSED_PRESERVE src0_sel:WORD_1
	v_exp_f16_sdwa v20, v8 dst_sel:WORD_1 dst_unused:UNUSED_PRESERVE src0_sel:WORD_1
	v_exp_f16_sdwa v21, v9 dst_sel:WORD_1 dst_unused:UNUSED_PRESERVE src0_sel:WORD_1
	s_nop 0
	v_pk_add_f16 v9, v13, v21
	v_pk_add_f16 v8, v12, v20
	v_pk_add_f16 v7, v11, v19
	v_pk_add_f16 v6, v10, v18
	v_pk_fma_f16 v13, v93, v21, v17
	v_pk_fma_f16 v12, v92, v20, v16
	v_pk_fma_f16 v11, v91, v19, v15
	v_pk_fma_f16 v10, v90, v18, v14
	v_pk_add_f16 v18, v50, v78 neg_lo:[0,1] neg_hi:[0,1]
	v_pk_add_f16 v19, v51, v79 neg_lo:[0,1] neg_hi:[0,1]
	v_pk_add_f16 v20, v52, v80 neg_lo:[0,1] neg_hi:[0,1]
	v_pk_add_f16 v21, v53, v81 neg_lo:[0,1] neg_hi:[0,1]
	v_exp_f16_sdwa v14, v18 dst_sel:WORD_0 dst_unused:UNUSED_PAD src0_sel:WORD_0
	v_exp_f16_sdwa v17, v19 dst_sel:WORD_0 dst_unused:UNUSED_PAD src0_sel:WORD_0
	v_exp_f16_sdwa v15, v20 dst_sel:WORD_0 dst_unused:UNUSED_PAD src0_sel:WORD_0
	v_exp_f16_sdwa v16, v21 dst_sel:WORD_0 dst_unused:UNUSED_PAD src0_sel:WORD_0
	v_exp_f16_sdwa v14, v18 dst_sel:WORD_1 dst_unused:UNUSED_PRESERVE src0_sel:WORD_1
	v_exp_f16_sdwa v17, v19 dst_sel:WORD_1 dst_unused:UNUSED_PRESERVE src0_sel:WORD_1
	v_exp_f16_sdwa v15, v20 dst_sel:WORD_1 dst_unused:UNUSED_PRESERVE src0_sel:WORD_1
	v_exp_f16_sdwa v16, v21 dst_sel:WORD_1 dst_unused:UNUSED_PRESERVE src0_sel:WORD_1
	s_nop 0

.Lmyf_D1_7:
	s_mov_b64 exec, -1
	s_waitcnt lgkmcnt(0)
	v_cvt_f16_f32_e32 v183, s27
	v_cvt_f16_f32_e32 v185, s26
	v_cvt_f16_f32_e32 v184, s31
	s_mov_b64 s[4:5], 0
	s_waitcnt vmcnt(3)
	s_cmp_lg_u32 s14, 1
	s_cbranch_scc1 .Lmysw5_0
	s_mul_i32 s84, s81, s83
	s_add_i32 s84, s84, s82
	s_mul_i32 s84, s84, 0x60000
	s_lshl_b32 s85, s92, 3
	s_add_u32 s85, s85, s94
	s_mul_i32 s85, s85, 1536
	s_add_u32 s84, s84, s85
	s_add_u32 s88, s86, s84
	s_addc_u32 s89, s87, 0
	s_load_dword s90, s[88:89], 0x0
	s_load_dword s90, s[88:89], 0x80
	s_load_dword s90, s[88:89], 0x100
	s_load_dword s90, s[88:89], 0x180
	s_load_dword s90, s[88:89], 0x200
	s_load_dword s90, s[88:89], 0x280
	s_load_dword s90, s[88:89], 0x300
	s_load_dword s90, s[88:89], 0x380
	s_load_dword s90, s[88:89], 0x400
	s_load_dword s90, s[88:89], 0x480
	s_load_dword s90, s[88:89], 0x500
	s_load_dword s90, s[88:89], 0x580
.Lmysw5_0:
	v_pk_mul_f16 v193, v185, v189 op_sel_hi:[0,1]
	v_pk_mul_f16 v197, v183, v189 op_sel_hi:[0,1]
	v_pk_mul_f16 v201, v184, v189 op_sel_hi:[0,1]
	v_pk_mul_f16 v190, v185, v186 op_sel_hi:[0,1]
	v_pk_mul_f16 v191, v185, v187 op_sel_hi:[0,1]
	v_pk_mul_f16 v192, v185, v188 op_sel_hi:[0,1]
	v_pk_mul_f16 v194, v183, v186 op_sel_hi:[0,1]
	s_mov_b64 exec, s[64:65]
	buffer_load_dwordx4 v[18:21], v224, s[16:19], 0 offen
	buffer_load_dwordx4 v[6:9], v224, s[16:19], 0 offen offset:512
	s_mov_b64 exec, -1
	v_pk_mul_f16 v195, v183, v187 op_sel_hi:[0,1]
	v_pk_mul_f16 v196, v183, v188 op_sel_hi:[0,1]
	v_pk_mul_f16 v198, v184, v186 op_sel_hi:[0,1]
	v_pk_mul_f16 v199, v184, v187 op_sel_hi:[0,1]
	v_pk_mul_f16 v200, v184, v188 op_sel_hi:[0,1]
	v_pk_fma_f16 v113, v113, v189, v193
	v_pk_fma_f16 v129, v129, v189, v197
	v_pk_fma_f16 v137, v137, v189, v201
	v_pk_fma_f16 v202, v85, v189, v193
	v_pk_fma_f16 v206, v109, v189, v197
	v_pk_fma_f16 v210, v125, v189, v201
	v_pk_fma_f16 v193, v53, v189, v193
	v_pk_fma_f16 v197, v69, v189, v197
	buffer_load_dwordx4 v[34:37], v225, s[16:19], 0 offen offset:512
	buffer_load_dwordx4 v[10:13], v225, s[16:19], 0 offen offset:1024
	v_pk_fma_f16 v189, v97, v189, v201
	v_pk_maximum3_f16 v201, v113, v129, v137
	v_pk_fma_f16 v112, v112, v188, v192
	v_pk_fma_f16 v111, v111, v187, v191
	v_pk_fma_f16 v110, v110, v186, v190
	v_pk_fma_f16 v128, v128, v188, v196
	v_pk_fma_f16 v127, v127, v187, v195
	v_pk_fma_f16 v126, v126, v186, v194
	v_pk_fma_f16 v136, v136, v188, v200
	v_pk_fma_f16 v135, v135, v187, v199
	v_pk_fma_f16 v134, v134, v186, v198
	v_pk_fma_f16 v203, v84, v188, v192
	v_pk_fma_f16 v204, v83, v187, v191
	v_pk_fma_f16 v205, v82, v186, v190
	v_pk_fma_f16 v207, v108, v188, v196
	v_pk_fma_f16 v208, v107, v187, v195
	s_mov_b64 exec, s[66:67]
	buffer_load_dwordx4 v[54:57], v225, s[16:19], 0 offen offset:2048
	buffer_load_dwordx4 v[14:17], v225, s[16:19], 0 offen offset:2560
	s_mov_b64 exec, -1
	v_pk_fma_f16 v209, v106, v186, v194
	v_pk_fma_f16 v211, v124, v188, v200
	v_pk_fma_f16 v212, v123, v187, v199
	v_pk_fma_f16 v213, v122, v186, v198
	v_pk_fma_f16 v192, v52, v188, v192
	v_pk_fma_f16 v191, v51, v187, v191
	v_pk_fma_f16 v190, v50, v186, v190
	v_pk_fma_f16 v196, v68, v188, v196
	v_pk_fma_f16 v195, v67, v187, v195
	v_pk_fma_f16 v194, v66, v186, v194
	v_pk_fma_f16 v188, v96, v188, v200
	v_pk_fma_f16 v187, v95, v187, v199
	v_pk_fma_f16 v186, v94, v186, v198
	v_pk_maximum3_f16 v198, v110, v126, v134
	v_pk_maximum3_f16 v199, v111, v127, v135
	v_pk_maximum3_f16 v200, v112, v128, v136
	v_pk_maximum3_f16 v217, v202, v206, v210
	v_pk_maximum3_f16 v221, v193, v197, v189
	v_pk_maximum3_f16 v214, v205, v209, v213
	v_pk_maximum3_f16 v215, v204, v208, v212
	v_pk_maximum3_f16 v216, v203, v207, v211
	v_pk_maximum3_f16 v218, v190, v194, v186
	v_pk_maximum3_f16 v219, v191, v195, v187
	v_pk_maximum3_f16 v201, v201, v217, v221
	v_pk_maximum3_f16 v220, v192, v196, v188
	v_pk_maximum3_f16 v198, v198, v214, v218
	v_pk_maximum3_f16 v199, v199, v215, v219
	v_pk_maximum3_f16 v200, v200, v216, v220
	v_pk_add_f16 v113, v113, v201 neg_lo:[0,1] neg_hi:[0,1]
	s_mov_b64 exec, s[64:65]
	buffer_load_dwordx4 v[74:77], v226, s[16:19], 0 offen
	buffer_load_dwordx4 v[26:29], v226, s[16:19], 0 offen offset:512
	s_mov_b64 exec, -1
	v_pk_add_f16 v110, v110, v198 neg_lo:[0,1] neg_hi:[0,1]
	v_pk_add_f16 v111, v111, v199 neg_lo:[0,1] neg_hi:[0,1]
	v_pk_add_f16 v112, v112, v200 neg_lo:[0,1] neg_hi:[0,1]
	v_pk_add_f16 v126, v126, v198 neg_lo:[0,1] neg_hi:[0,1]
	v_exp_f16_sdwa v214, v110 dst_sel:WORD_0 dst_unused:UNUSED_PAD src0_sel:WORD_0
	v_exp_f16_sdwa v215, v111 dst_sel:WORD_0 dst_unused:UNUSED_PAD src0_sel:WORD_0
	v_exp_f16_sdwa v216, v112 dst_sel:WORD_0 dst_unused:UNUSED_PAD src0_sel:WORD_0
	v_exp_f16_sdwa v217, v113 dst_sel:WORD_0 dst_unused:UNUSED_PAD src0_sel:WORD_0
	v_exp_f16_sdwa v214, v110 dst_sel:WORD_1 dst_unused:UNUSED_PRESERVE src0_sel:WORD_1
	v_exp_f16_sdwa v215, v111 dst_sel:WORD_1 dst_unused:UNUSED_PRESERVE src0_sel:WORD_1
	v_exp_f16_sdwa v216, v112 dst_sel:WORD_1 dst_unused:UNUSED_PRESERVE src0_sel:WORD_1
	v_exp_f16_sdwa v217, v113 dst_sel:WORD_1 dst_unused:UNUSED_PRESERVE src0_sel:WORD_1
	v_pk_add_f16 v127, v127, v199 neg_lo:[0,1] neg_hi:[0,1]
	v_pk_add_f16 v113, v214, 0
	v_pk_fma_f16 v73, v73, v217, 0
	v_pk_add_f16 v110, v217, 0
	v_pk_add_f16 v111, v216, 0
	v_pk_add_f16 v112, v215, 0
	v_pk_fma_f16 v72, v72, v216, 0
	v_pk_fma_f16 v71, v71, v215, 0
	v_pk_fma_f16 v70, v70, v214, 0
	v_pk_add_f16 v128, v128, v200 neg_lo:[0,1] neg_hi:[0,1]
	buffer_load_dwordx4 v[102:105], v227, s[16:19], 0 offen offset:512
	buffer_load_dwordx4 v[38:41], v227, s[16:19], 0 offen offset:1024
	v_pk_add_f16 v129, v129, v201 neg_lo:[0,1] neg_hi:[0,1]
	v_exp_f16_sdwa v214, v126 dst_sel:WORD_0 dst_unused:UNUSED_PAD src0_sel:WORD_0
	v_exp_f16_sdwa v215, v127 dst_sel:WORD_0 dst_unused:UNUSED_PAD src0_sel:WORD_0
	v_exp_f16_sdwa v216, v128 dst_sel:WORD_0 dst_unused:UNUSED_PAD src0_sel:WORD_0
	v_exp_f16_sdwa v217, v129 dst_sel:WORD_0 dst_unused:UNUSED_PAD src0_sel:WORD_0
	v_exp_f16_sdwa v214, v126 dst_sel:WORD_1 dst_unused:UNUSED_PRESERVE src0_sel:WORD_1
	v_exp_f16_sdwa v215, v127 dst_sel:WORD_1 dst_unused:UNUSED_PRESERVE src0_sel:WORD_1
	v_exp_f16_sdwa v216, v128 dst_sel:WORD_1 dst_unused:UNUSED_PRESERVE src0_sel:WORD_1
	v_exp_f16_sdwa v217, v129 dst_sel:WORD_1 dst_unused:UNUSED_PRESERVE src0_sel:WORD_1
	v_pk_add_f16 v113, v113, v214
	v_pk_fma_f16 v73, v101, v217, v73
	v_pk_add_f16 v101, v137, v201 neg_lo:[0,1] neg_hi:[0,1]
	v_pk_add_f16 v112, v112, v215
	v_pk_add_f16 v111, v111, v216
	v_pk_add_f16 v110, v110, v217
	v_pk_fma_f16 v70, v98, v214, v70
	v_pk_fma_f16 v71, v99, v215, v71
	v_pk_fma_f16 v72, v100, v216, v72
	v_pk_add_f16 v98, v134, v198 neg_lo:[0,1] neg_hi:[0,1]
	v_pk_add_f16 v99, v135, v199 neg_lo:[0,1] neg_hi:[0,1]
	v_pk_add_f16 v100, v136, v200 neg_lo:[0,1] neg_hi:[0,1]
	v_exp_f16_sdwa v126, v98 dst_sel:WORD_0 dst_unused:UNUSED_PAD src0_sel:WORD_0
	v_exp_f16_sdwa v127, v99 dst_sel:WORD_0 dst_unused:UNUSED_PAD src0_sel:WORD_0
	v_exp_f16_sdwa v128, v100 dst_sel:WORD_0 dst_unused:UNUSED_PAD src0_sel:WORD_0
	v_exp_f16_sdwa v129, v101 dst_sel:WORD_0 dst_unused:UNUSED_PAD src0_sel:WORD_0
	v_exp_f16_sdwa v126, v98 dst_sel:WORD_1 dst_unused:UNUSED_PRESERVE src0_sel:WORD_1
	v_exp_f16_sdwa v127, v99 dst_sel:WORD_1 dst_unused:UNUSED_PRESERVE src0_sel:WORD_1
	v_exp_f16_sdwa v128, v100 dst_sel:WORD_1 dst_unused:UNUSED_PRESERVE src0_sel:WORD_1
	v_exp_f16_sdwa v129, v101 dst_sel:WORD_1 dst_unused:UNUSED_PRESERVE src0_sel:WORD_1
	v_pk_add_f16 v101, v113, v126
	v_pk_add_f16 v98, v110, v129
	s_mov_b64 exec, s[66:67]
	buffer_load_dwordx4 v[118:121], v227, s[16:19], 0 offen offset:2048
	buffer_load_dwordx4 v[58:61], v227, s[16:19], 0 offen offset:2560
	s_mov_b64 exec, -1
	v_pk_add_f16 v99, v111, v128
	v_pk_add_f16 v100, v112, v127
	v_pk_fma_f16 v73, v117, v129, v73
	v_pk_fma_f16 v72, v116, v128, v72
	v_pk_fma_f16 v71, v115, v127, v71
	v_pk_fma_f16 v70, v114, v126, v70
	v_pk_add_f16 v110, v205, v198 neg_lo:[0,1] neg_hi:[0,1]
	v_pk_add_f16 v111, v204, v199 neg_lo:[0,1] neg_hi:[0,1]
	v_pk_add_f16 v112, v203, v200 neg_lo:[0,1] neg_hi:[0,1]
	v_pk_add_f16 v113, v202, v201 neg_lo:[0,1] neg_hi:[0,1]
	v_exp_f16_sdwa v114, v110 dst_sel:WORD_0 dst_unused:UNUSED_PAD src0_sel:WORD_0
	v_exp_f16_sdwa v115, v111 dst_sel:WORD_0 dst_unused:UNUSED_PAD src0_sel:WORD_0
	v_exp_f16_sdwa v116, v112 dst_sel:WORD_0 dst_unused:UNUSED_PAD src0_sel:WORD_0
	v_exp_f16_sdwa v117, v113 dst_sel:WORD_0 dst_unused:UNUSED_PAD src0_sel:WORD_0
	v_exp_f16_sdwa v114, v110 dst_sel:WORD_1 dst_unused:UNUSED_PRESERVE src0_sel:WORD_1
	v_exp_f16_sdwa v115, v111 dst_sel:WORD_1 dst_unused:UNUSED_PRESERVE src0_sel:WORD_1
	v_exp_f16_sdwa v116, v112 dst_sel:WORD_1 dst_unused:UNUSED_PRESERVE src0_sel:WORD_1
	v_exp_f16_sdwa v117, v113 dst_sel:WORD_1 dst_unused:UNUSED_PRESERVE src0_sel:WORD_1
	v_pk_add_f16 v110, v209, v198 neg_lo:[0,1] neg_hi:[0,1]
	v_pk_add_f16 v101, v101, v114
	v_pk_add_f16 v100, v100, v115
	v_pk_add_f16 v99, v99, v116
	s_mov_b64 exec, s[76:77]
	buffer_load_dwordx4 v[130:133], v228, s[16:19], 0 offen
	buffer_load_dwordx4 v[78:81], v228, s[16:19], 0 offen offset:512
	s_mov_b64 exec, -1
	v_pk_add_f16 v98, v98, v117
	v_pk_fma_f16 v70, v42, v114, v70
	v_pk_fma_f16 v71, v43, v115, v71
	v_pk_fma_f16 v72, v44, v116, v72
	v_pk_fma_f16 v73, v45, v117, v73
	v_pk_add_f16 v111, v208, v199 neg_lo:[0,1] neg_hi:[0,1]
	v_pk_add_f16 v112, v207, v200 neg_lo:[0,1] neg_hi:[0,1]
	v_pk_add_f16 v113, v206, v201 neg_lo:[0,1] neg_hi:[0,1]
	v_exp_f16_sdwa v114, v110 dst_sel:WORD_0 dst_unused:UNUSED_PAD src0_sel:WORD_0
	v_exp_f16_sdwa v115, v111 dst_sel:WORD_0 dst_unused:UNUSED_PAD src0_sel:WORD_0
	v_exp_f16_sdwa v116, v112 dst_sel:WORD_0 dst_unused:UNUSED_PAD src0_sel:WORD_0
	v_exp_f16_sdwa v117, v113 dst_sel:WORD_0 dst_unused:UNUSED_PAD src0_sel:WORD_0
	v_exp_f16_sdwa v114, v110 dst_sel:WORD_1 dst_unused:UNUSED_PRESERVE src0_sel:WORD_1
	v_exp_f16_sdwa v115, v111 dst_sel:WORD_1 dst_unused:UNUSED_PRESERVE src0_sel:WORD_1
	v_exp_f16_sdwa v116, v112 dst_sel:WORD_1 dst_unused:UNUSED_PRESERVE src0_sel:WORD_1
	v_exp_f16_sdwa v117, v113 dst_sel:WORD_1 dst_unused:UNUSED_PRESERVE src0_sel:WORD_1
	v_pk_add_f16 v110, v213, v198 neg_lo:[0,1] neg_hi:[0,1]
	v_pk_add_f16 v101, v101, v114
	v_pk_add_f16 v98, v98, v117
	v_pk_add_f16 v99, v99, v116
	v_pk_add_f16 v100, v100, v115
	v_pk_fma_f16 v73, v65, v117, v73
	v_pk_fma_f16 v72, v64, v116, v72
	s_mov_b64 exec, s[70:71]
	buffer_load_dwordx4 v[138:141], v229, s[16:19], 0 offen offset:512
	buffer_load_dwordx4 v[90:93], v229, s[16:19], 0 offen offset:1024
	s_mov_b64 exec, -1
	v_pk_fma_f16 v71, v63, v115, v71
	v_pk_fma_f16 v70, v62, v114, v70
	v_pk_add_f16 v111, v212, v199 neg_lo:[0,1] neg_hi:[0,1]
	v_pk_add_f16 v112, v211, v200 neg_lo:[0,1] neg_hi:[0,1]
	v_pk_add_f16 v113, v210, v201 neg_lo:[0,1] neg_hi:[0,1]
	v_exp_f16_sdwa v114, v110 dst_sel:WORD_0 dst_unused:UNUSED_PAD src0_sel:WORD_0
	v_exp_f16_sdwa v115, v111 dst_sel:WORD_0 dst_unused:UNUSED_PAD src0_sel:WORD_0
	v_exp_f16_sdwa v116, v112 dst_sel:WORD_0 dst_unused:UNUSED_PAD src0_sel:WORD_0
	v_exp_f16_sdwa v117, v113 dst_sel:WORD_0 dst_unused:UNUSED_PAD src0_sel:WORD_0
	v_exp_f16_sdwa v114, v110 dst_sel:WORD_1 dst_unused:UNUSED_PRESERVE src0_sel:WORD_1
	v_exp_f16_sdwa v115, v111 dst_sel:WORD_1 dst_unused:UNUSED_PRESERVE src0_sel:WORD_1
	v_exp_f16_sdwa v116, v112 dst_sel:WORD_1 dst_unused:UNUSED_PRESERVE src0_sel:WORD_1
	v_exp_f16_sdwa v117, v113 dst_sel:WORD_1 dst_unused:UNUSED_PRESERVE src0_sel:WORD_1
	v_pk_add_f16 v110, v190, v198 neg_lo:[0,1] neg_hi:[0,1]
	v_pk_add_f16 v101, v101, v114
	v_pk_add_f16 v100, v100, v115
	v_pk_add_f16 v99, v99, v116
	v_pk_add_f16 v98, v98, v117
	v_pk_fma_f16 v70, v86, v114, v70
	v_pk_fma_f16 v71, v87, v115, v71
	v_pk_fma_f16 v72, v88, v116, v72
	v_pk_fma_f16 v73, v89, v117, v73
	s_mov_b64 exec, s[78:79]
	buffer_load_dwordx4 v[142:145], v229, s[16:19], 0 offen offset:2048
	buffer_load_dwordx4 v[2:5], v229, s[16:19], 0 offen offset:2560
	s_mov_b64 exec, -1
	v_pk_add_f16 v111, v191, v199 neg_lo:[0,1] neg_hi:[0,1]
	v_pk_add_f16 v112, v192, v200 neg_lo:[0,1] neg_hi:[0,1]
	v_pk_add_f16 v113, v193, v201 neg_lo:[0,1] neg_hi:[0,1]
	v_exp_f16_sdwa v114, v110 dst_sel:WORD_0 dst_unused:UNUSED_PAD src0_sel:WORD_0
	v_exp_f16_sdwa v115, v111 dst_sel:WORD_0 dst_unused:UNUSED_PAD src0_sel:WORD_0
	v_exp_f16_sdwa v116, v112 dst_sel:WORD_0 dst_unused:UNUSED_PAD src0_sel:WORD_0
	v_exp_f16_sdwa v117, v113 dst_sel:WORD_0 dst_unused:UNUSED_PAD src0_sel:WORD_0
	v_exp_f16_sdwa v114, v110 dst_sel:WORD_1 dst_unused:UNUSED_PRESERVE src0_sel:WORD_1
	v_exp_f16_sdwa v115, v111 dst_sel:WORD_1 dst_unused:UNUSED_PRESERVE src0_sel:WORD_1
	v_exp_f16_sdwa v116, v112 dst_sel:WORD_1 dst_unused:UNUSED_PRESERVE src0_sel:WORD_1
	v_exp_f16_sdwa v117, v113 dst_sel:WORD_1 dst_unused:UNUSED_PRESERVE src0_sel:WORD_1
	v_pk_add_f16 v110, v194, v198 neg_lo:[0,1] neg_hi:[0,1]
	v_pk_add_f16 v101, v101, v114
	v_pk_add_f16 v98, v98, v117
	v_pk_add_f16 v99, v99, v116
	v_pk_add_f16 v100, v100, v115
	v_pk_fma_f16 v73, v25, v117, v73
	v_pk_fma_f16 v72, v24, v116, v72
	v_pk_fma_f16 v71, v23, v115, v71
	v_pk_fma_f16 v70, v22, v114, v70
	v_pk_add_f16 v111, v195, v199 neg_lo:[0,1] neg_hi:[0,1]
	v_pk_add_f16 v112, v196, v200 neg_lo:[0,1] neg_hi:[0,1]
	v_pk_add_f16 v113, v197, v201 neg_lo:[0,1] neg_hi:[0,1]
	v_exp_f16_sdwa v114, v110 dst_sel:WORD_0 dst_unused:UNUSED_PAD src0_sel:WORD_0
	v_exp_f16_sdwa v115, v111 dst_sel:WORD_0 dst_unused:UNUSED_PAD src0_sel:WORD_0
	v_exp_f16_sdwa v116, v112 dst_sel:WORD_0 dst_unused:UNUSED_PAD src0_sel:WORD_0
	v_exp_f16_sdwa v117, v113 dst_sel:WORD_0 dst_unused:UNUSED_PAD src0_sel:WORD_0
	v_exp_f16_sdwa v114, v110 dst_sel:WORD_1 dst_unused:UNUSED_PRESERVE src0_sel:WORD_1
	v_exp_f16_sdwa v115, v111 dst_sel:WORD_1 dst_unused:UNUSED_PRESERVE src0_sel:WORD_1
	v_exp_f16_sdwa v116, v112 dst_sel:WORD_1 dst_unused:UNUSED_PRESERVE src0_sel:WORD_1
	v_exp_f16_sdwa v117, v113 dst_sel:WORD_1 dst_unused:UNUSED_PRESERVE src0_sel:WORD_1
	v_pk_add_f16 v110, v186, v198 neg_lo:[0,1] neg_hi:[0,1]
	v_pk_add_f16 v101, v101, v114
	v_pk_add_f16 v100, v100, v115
	v_pk_add_f16 v99, v99, v116
	v_pk_add_f16 v98, v98, v117
	v_pk_fma_f16 v70, v30, v114, v70
	v_pk_fma_f16 v71, v31, v115, v71
	v_pk_fma_f16 v72, v32, v116, v72
	v_pk_fma_f16 v73, v33, v117, v73
	v_pk_add_f16 v111, v187, v199 neg_lo:[0,1] neg_hi:[0,1]
	v_pk_add_f16 v112, v188, v200 neg_lo:[0,1] neg_hi:[0,1]
	v_pk_add_f16 v113, v189, v201 neg_lo:[0,1] neg_hi:[0,1]
	v_exp_f16_sdwa v114, v110 dst_sel:WORD_0 dst_unused:UNUSED_PAD src0_sel:WORD_0
	v_exp_f16_sdwa v115, v111 dst_sel:WORD_0 dst_unused:UNUSED_PAD src0_sel:WORD_0
	v_exp_f16_sdwa v116, v112 dst_sel:WORD_0 dst_unused:UNUSED_PAD src0_sel:WORD_0
	v_exp_f16_sdwa v117, v113 dst_sel:WORD_0 dst_unused:UNUSED_PAD src0_sel:WORD_0
	v_exp_f16_sdwa v114, v110 dst_sel:WORD_1 dst_unused:UNUSED_PRESERVE src0_sel:WORD_1
	v_exp_f16_sdwa v115, v111 dst_sel:WORD_1 dst_unused:UNUSED_PRESERVE src0_sel:WORD_1
	v_exp_f16_sdwa v116, v112 dst_sel:WORD_1 dst_unused:UNUSED_PRESERVE src0_sel:WORD_1
	v_exp_f16_sdwa v117, v113 dst_sel:WORD_1 dst_unused:UNUSED_PRESERVE src0_sel:WORD_1
	v_pk_add_f16 v101, v101, v114
	v_pk_add_f16 v100, v100, v115
	v_rcp_f16_e32 v110, v101
	v_rcp_f16_sdwa v101, v101 dst_sel:DWORD dst_unused:UNUSED_PAD src0_sel:WORD_1
	v_pk_add_f16 v99, v99, v116
	v_rcp_f16_e32 v111, v100
	v_rcp_f16_sdwa v100, v100 dst_sel:DWORD dst_unused:UNUSED_PAD src0_sel:WORD_1
	v_pk_add_f16 v98, v98, v117
	v_rcp_f16_e32 v112, v99
	v_rcp_f16_sdwa v99, v99 dst_sel:DWORD dst_unused:UNUSED_PAD src0_sel:WORD_1
	v_rcp_f16_e32 v113, v98
	v_rcp_f16_sdwa v98, v98 dst_sel:DWORD dst_unused:UNUSED_PAD src0_sel:WORD_1
	v_pk_fma_f16 v70, v46, v114, v70
	v_pack_b32_f16 v101, v110, v101
	v_pk_fma_f16 v71, v47, v115, v71
	v_pk_mul_f16 v110, v70, v101
	v_pack_b32_f16 v70, v111, v100
	v_pk_fma_f16 v72, v48, v116, v72
	v_pk_mul_f16 v111, v71, v70
	v_pack_b32_f16 v70, v112, v99
	v_pk_fma_f16 v73, v49, v117, v73
	v_pk_mul_f16 v112, v72, v70
	v_pack_b32_f16 v70, v113, v98
	v_pk_mul_f16 v113, v73, v70
	s_waitcnt vmcnt(12)
	v_pk_mul_f16 v70, v185, v154 op_sel_hi:[0,1]
	v_pk_mul_f16 v98, v183, v154 op_sel_hi:[0,1]
	v_pk_mul_f16 v114, v184, v154 op_sel_hi:[0,1]
	v_pk_mul_f16 v71, v185, v155 op_sel_hi:[0,1]
	v_pk_mul_f16 v72, v185, v156 op_sel_hi:[0,1]
	v_pk_mul_f16 v73, v185, v157 op_sel_hi:[0,1]
	v_pk_mul_f16 v99, v183, v155 op_sel_hi:[0,1]
	v_pk_mul_f16 v100, v183, v156 op_sel_hi:[0,1]
	v_pk_mul_f16 v101, v183, v157 op_sel_hi:[0,1]
	v_pk_mul_f16 v115, v184, v155 op_sel_hi:[0,1]
	v_pk_mul_f16 v116, v184, v156 op_sel_hi:[0,1]
	v_pk_mul_f16 v117, v184, v157 op_sel_hi:[0,1]
	v_pk_fma_f16 v82, v82, v154, v70
	v_pk_fma_f16 v106, v106, v154, v98
	v_pk_fma_f16 v122, v122, v154, v114
	v_pk_fma_f16 v129, v50, v154, v70
	v_pk_fma_f16 v137, v66, v154, v98
	v_pk_fma_f16 v189, v94, v154, v114
	v_pk_fma_f16 v70, v18, v154, v70
	v_pk_fma_f16 v98, v34, v154, v98
	v_pk_fma_f16 v114, v54, v154, v114
	v_pk_maximum3_f16 v154, v82, v106, v122
	v_pk_fma_f16 v85, v85, v157, v73
	v_pk_fma_f16 v84, v84, v156, v72
	v_pk_fma_f16 v83, v83, v155, v71
	v_pk_fma_f16 v109, v109, v157, v101
	v_pk_fma_f16 v108, v108, v156, v100
	v_pk_fma_f16 v107, v107, v155, v99
	v_pk_fma_f16 v125, v125, v157, v117
	v_pk_fma_f16 v124, v124, v156, v116
	v_pk_fma_f16 v123, v123, v155, v115
	v_pk_fma_f16 v126, v53, v157, v73
	v_pk_fma_f16 v127, v52, v156, v72
	v_pk_fma_f16 v128, v51, v155, v71
	v_pk_fma_f16 v134, v69, v157, v101
	v_pk_fma_f16 v135, v68, v156, v100
	v_pk_fma_f16 v136, v67, v155, v99
	v_pk_fma_f16 v186, v97, v157, v117
	v_pk_fma_f16 v187, v96, v156, v116
	v_pk_fma_f16 v188, v95, v155, v115
	v_pk_fma_f16 v73, v21, v157, v73
	v_pk_fma_f16 v72, v20, v156, v72
	v_pk_fma_f16 v71, v19, v155, v71
	v_pk_fma_f16 v101, v37, v157, v101
	v_pk_fma_f16 v100, v36, v156, v100
	v_pk_fma_f16 v99, v35, v155, v99
	v_pk_fma_f16 v117, v57, v157, v117
	v_pk_fma_f16 v116, v56, v156, v116
	v_pk_fma_f16 v115, v55, v155, v115
	v_pk_maximum3_f16 v155, v83, v107, v123
	v_pk_maximum3_f16 v156, v84, v108, v124
	v_pk_maximum3_f16 v157, v85, v109, v125
	v_pk_maximum3_f16 v190, v129, v137, v189
	v_pk_maximum3_f16 v194, v70, v98, v114
	v_pk_maximum3_f16 v191, v128, v136, v188
	v_pk_maximum3_f16 v192, v127, v135, v187
	v_pk_maximum3_f16 v193, v126, v134, v186
	v_pk_maximum3_f16 v195, v71, v99, v115
	v_pk_maximum3_f16 v196, v72, v100, v116
	v_pk_maximum3_f16 v154, v154, v190, v194
	v_pk_maximum3_f16 v197, v73, v101, v117
	v_pk_maximum3_f16 v155, v155, v191, v195
	v_pk_maximum3_f16 v156, v156, v192, v196
	v_pk_maximum3_f16 v157, v157, v193, v197
	v_pk_add_f16 v82, v82, v154 neg_lo:[0,1] neg_hi:[0,1]
	v_pk_add_f16 v83, v83, v155 neg_lo:[0,1] neg_hi:[0,1]
	v_pk_add_f16 v84, v84, v156 neg_lo:[0,1] neg_hi:[0,1]
	v_pk_add_f16 v85, v85, v157 neg_lo:[0,1] neg_hi:[0,1]
	v_pk_add_f16 v106, v106, v154 neg_lo:[0,1] neg_hi:[0,1]
	v_exp_f16_sdwa v190, v82 dst_sel:WORD_0 dst_unused:UNUSED_PAD src0_sel:WORD_0
	v_exp_f16_sdwa v191, v83 dst_sel:WORD_0 dst_unused:UNUSED_PAD src0_sel:WORD_0
	v_exp_f16_sdwa v192, v84 dst_sel:WORD_0 dst_unused:UNUSED_PAD src0_sel:WORD_0
	v_exp_f16_sdwa v193, v85 dst_sel:WORD_0 dst_unused:UNUSED_PAD src0_sel:WORD_0
	v_exp_f16_sdwa v190, v82 dst_sel:WORD_1 dst_unused:UNUSED_PRESERVE src0_sel:WORD_1
	v_exp_f16_sdwa v191, v83 dst_sel:WORD_1 dst_unused:UNUSED_PRESERVE src0_sel:WORD_1
	v_exp_f16_sdwa v192, v84 dst_sel:WORD_1 dst_unused:UNUSED_PRESERVE src0_sel:WORD_1
	v_exp_f16_sdwa v193, v85 dst_sel:WORD_1 dst_unused:UNUSED_PRESERVE src0_sel:WORD_1
	v_pk_add_f16 v107, v107, v155 neg_lo:[0,1] neg_hi:[0,1]
	v_pk_add_f16 v82, v193, 0
	v_pk_fma_f16 v42, v42, v190, 0
	v_pk_add_f16 v83, v192, 0
	v_pk_add_f16 v84, v191, 0
	v_pk_add_f16 v85, v190, 0
	v_pk_fma_f16 v45, v45, v193, 0
	v_pk_fma_f16 v44, v44, v192, 0
	v_pk_fma_f16 v43, v43, v191, 0
	v_pk_add_f16 v108, v108, v156 neg_lo:[0,1] neg_hi:[0,1]
	v_pk_add_f16 v109, v109, v157 neg_lo:[0,1] neg_hi:[0,1]
	v_pk_add_f16 v70, v70, v154 neg_lo:[0,1] neg_hi:[0,1]
	v_exp_f16_sdwa v190, v106 dst_sel:WORD_0 dst_unused:UNUSED_PAD src0_sel:WORD_0
	v_exp_f16_sdwa v191, v107 dst_sel:WORD_0 dst_unused:UNUSED_PAD src0_sel:WORD_0
	v_exp_f16_sdwa v192, v108 dst_sel:WORD_0 dst_unused:UNUSED_PAD src0_sel:WORD_0
	v_exp_f16_sdwa v193, v109 dst_sel:WORD_0 dst_unused:UNUSED_PAD src0_sel:WORD_0
	v_exp_f16_sdwa v190, v106 dst_sel:WORD_1 dst_unused:UNUSED_PRESERVE src0_sel:WORD_1
	v_exp_f16_sdwa v191, v107 dst_sel:WORD_1 dst_unused:UNUSED_PRESERVE src0_sel:WORD_1
	v_exp_f16_sdwa v192, v108 dst_sel:WORD_1 dst_unused:UNUSED_PRESERVE src0_sel:WORD_1
	v_exp_f16_sdwa v193, v109 dst_sel:WORD_1 dst_unused:UNUSED_PRESERVE src0_sel:WORD_1
	v_pk_add_f16 v71, v71, v155 neg_lo:[0,1] neg_hi:[0,1]
	v_pk_add_f16 v82, v82, v193
	v_pk_fma_f16 v42, v62, v190, v42
	v_pk_add_f16 v62, v122, v154 neg_lo:[0,1] neg_hi:[0,1]
	v_pk_add_f16 v85, v85, v190
	v_pk_add_f16 v84, v84, v191
	v_pk_add_f16 v83, v83, v192
	v_pk_fma_f16 v43, v63, v191, v43
	v_pk_fma_f16 v44, v64, v192, v44
	v_pk_fma_f16 v45, v65, v193, v45
	v_pk_add_f16 v63, v123, v155 neg_lo:[0,1] neg_hi:[0,1]
	v_pk_add_f16 v64, v124, v156 neg_lo:[0,1] neg_hi:[0,1]
	v_pk_add_f16 v65, v125, v157 neg_lo:[0,1] neg_hi:[0,1]
	v_pk_add_f16 v72, v72, v156 neg_lo:[0,1] neg_hi:[0,1]
	v_exp_f16_sdwa v106, v62 dst_sel:WORD_0 dst_unused:UNUSED_PAD src0_sel:WORD_0
	v_exp_f16_sdwa v107, v63 dst_sel:WORD_0 dst_unused:UNUSED_PAD src0_sel:WORD_0
	v_exp_f16_sdwa v108, v64 dst_sel:WORD_0 dst_unused:UNUSED_PAD src0_sel:WORD_0
	v_exp_f16_sdwa v109, v65 dst_sel:WORD_0 dst_unused:UNUSED_PAD src0_sel:WORD_0
	v_exp_f16_sdwa v106, v62 dst_sel:WORD_1 dst_unused:UNUSED_PRESERVE src0_sel:WORD_1
	v_exp_f16_sdwa v107, v63 dst_sel:WORD_1 dst_unused:UNUSED_PRESERVE src0_sel:WORD_1
	v_exp_f16_sdwa v108, v64 dst_sel:WORD_1 dst_unused:UNUSED_PRESERVE src0_sel:WORD_1
	v_exp_f16_sdwa v109, v65 dst_sel:WORD_1 dst_unused:UNUSED_PRESERVE src0_sel:WORD_1
	v_pk_add_f16 v73, v73, v157 neg_lo:[0,1] neg_hi:[0,1]
	v_pk_add_f16 v62, v82, v109
	v_pk_add_f16 v63, v83, v108
	v_pk_add_f16 v64, v84, v107
	v_pk_add_f16 v65, v85, v106
	v_pk_fma_f16 v45, v89, v109, v45
	v_pk_fma_f16 v44, v88, v108, v44
	v_pk_fma_f16 v43, v87, v107, v43
	v_pk_fma_f16 v42, v86, v106, v42
	v_pk_add_f16 v82, v129, v154 neg_lo:[0,1] neg_hi:[0,1]
	v_pk_add_f16 v83, v128, v155 neg_lo:[0,1] neg_hi:[0,1]
	v_pk_add_f16 v84, v127, v156 neg_lo:[0,1] neg_hi:[0,1]
	v_pk_add_f16 v85, v126, v157 neg_lo:[0,1] neg_hi:[0,1]
	v_exp_f16_sdwa v86, v82 dst_sel:WORD_0 dst_unused:UNUSED_PAD src0_sel:WORD_0
	v_exp_f16_sdwa v87, v83 dst_sel:WORD_0 dst_unused:UNUSED_PAD src0_sel:WORD_0
	v_exp_f16_sdwa v88, v84 dst_sel:WORD_0 dst_unused:UNUSED_PAD src0_sel:WORD_0
	v_exp_f16_sdwa v89, v85 dst_sel:WORD_0 dst_unused:UNUSED_PAD src0_sel:WORD_0
	v_exp_f16_sdwa v86, v82 dst_sel:WORD_1 dst_unused:UNUSED_PRESERVE src0_sel:WORD_1
	v_exp_f16_sdwa v87, v83 dst_sel:WORD_1 dst_unused:UNUSED_PRESERVE src0_sel:WORD_1
	v_exp_f16_sdwa v88, v84 dst_sel:WORD_1 dst_unused:UNUSED_PRESERVE src0_sel:WORD_1
	v_exp_f16_sdwa v89, v85 dst_sel:WORD_1 dst_unused:UNUSED_PRESERVE src0_sel:WORD_1
	v_pk_add_f16 v82, v137, v154 neg_lo:[0,1] neg_hi:[0,1]
	v_pk_add_f16 v62, v62, v89
	v_pk_add_f16 v65, v65, v86
	v_pk_add_f16 v64, v64, v87
	v_pk_add_f16 v63, v63, v88
	v_pk_fma_f16 v42, v22, v86, v42
	v_pk_fma_f16 v43, v23, v87, v43
	v_pk_fma_f16 v44, v24, v88, v44
	v_pk_fma_f16 v45, v25, v89, v45
	v_pk_add_f16 v83, v136, v155 neg_lo:[0,1] neg_hi:[0,1]
	v_pk_add_f16 v84, v135, v156 neg_lo:[0,1] neg_hi:[0,1]
	v_pk_add_f16 v85, v134, v157 neg_lo:[0,1] neg_hi:[0,1]
	v_exp_f16_sdwa v86, v82 dst_sel:WORD_0 dst_unused:UNUSED_PAD src0_sel:WORD_0
	v_exp_f16_sdwa v87, v83 dst_sel:WORD_0 dst_unused:UNUSED_PAD src0_sel:WORD_0
	v_exp_f16_sdwa v88, v84 dst_sel:WORD_0 dst_unused:UNUSED_PAD src0_sel:WORD_0
	v_exp_f16_sdwa v89, v85 dst_sel:WORD_0 dst_unused:UNUSED_PAD src0_sel:WORD_0
	v_exp_f16_sdwa v86, v82 dst_sel:WORD_1 dst_unused:UNUSED_PRESERVE src0_sel:WORD_1
	v_exp_f16_sdwa v87, v83 dst_sel:WORD_1 dst_unused:UNUSED_PRESERVE src0_sel:WORD_1
	v_exp_f16_sdwa v88, v84 dst_sel:WORD_1 dst_unused:UNUSED_PRESERVE src0_sel:WORD_1
	v_exp_f16_sdwa v89, v85 dst_sel:WORD_1 dst_unused:UNUSED_PRESERVE src0_sel:WORD_1
	v_pk_add_f16 v82, v189, v154 neg_lo:[0,1] neg_hi:[0,1]
	v_pk_add_f16 v62, v62, v89
	v_pk_add_f16 v63, v63, v88
	v_pk_add_f16 v64, v64, v87
	v_pk_add_f16 v65, v65, v86
	v_pk_fma_f16 v45, v33, v89, v45
	v_pk_fma_f16 v44, v32, v88, v44
	v_pk_fma_f16 v43, v31, v87, v43
	v_pk_fma_f16 v42, v30, v86, v42
	v_pk_add_f16 v83, v188, v155 neg_lo:[0,1] neg_hi:[0,1]
	v_pk_add_f16 v84, v187, v156 neg_lo:[0,1] neg_hi:[0,1]
	v_pk_add_f16 v85, v186, v157 neg_lo:[0,1] neg_hi:[0,1]
	v_exp_f16_sdwa v86, v82 dst_sel:WORD_0 dst_unused:UNUSED_PAD src0_sel:WORD_0
	v_exp_f16_sdwa v87, v83 dst_sel:WORD_0 dst_unused:UNUSED_PAD src0_sel:WORD_0
	v_exp_f16_sdwa v88, v84 dst_sel:WORD_0 dst_unused:UNUSED_PAD src0_sel:WORD_0
	v_exp_f16_sdwa v89, v85 dst_sel:WORD_0 dst_unused:UNUSED_PAD src0_sel:WORD_0
	v_exp_f16_sdwa v86, v82 dst_sel:WORD_1 dst_unused:UNUSED_PRESERVE src0_sel:WORD_1
	v_exp_f16_sdwa v87, v83 dst_sel:WORD_1 dst_unused:UNUSED_PRESERVE src0_sel:WORD_1
	v_exp_f16_sdwa v88, v84 dst_sel:WORD_1 dst_unused:UNUSED_PRESERVE src0_sel:WORD_1
	v_exp_f16_sdwa v89, v85 dst_sel:WORD_1 dst_unused:UNUSED_PRESERVE src0_sel:WORD_1
	v_exp_f16_sdwa v82, v70 dst_sel:WORD_0 dst_unused:UNUSED_PAD src0_sel:WORD_0
	v_exp_f16_sdwa v83, v71 dst_sel:WORD_0 dst_unused:UNUSED_PAD src0_sel:WORD_0
	v_exp_f16_sdwa v84, v72 dst_sel:WORD_0 dst_unused:UNUSED_PAD src0_sel:WORD_0
	v_exp_f16_sdwa v85, v73 dst_sel:WORD_0 dst_unused:UNUSED_PAD src0_sel:WORD_0
	v_exp_f16_sdwa v82, v70 dst_sel:WORD_1 dst_unused:UNUSED_PRESERVE src0_sel:WORD_1
	v_exp_f16_sdwa v83, v71 dst_sel:WORD_1 dst_unused:UNUSED_PRESERVE src0_sel:WORD_1
	v_exp_f16_sdwa v84, v72 dst_sel:WORD_1 dst_unused:UNUSED_PRESERVE src0_sel:WORD_1
	v_exp_f16_sdwa v85, v73 dst_sel:WORD_1 dst_unused:UNUSED_PRESERVE src0_sel:WORD_1
	v_pk_add_f16 v70, v98, v154 neg_lo:[0,1] neg_hi:[0,1]
	v_pk_add_f16 v62, v62, v89
	v_pk_add_f16 v65, v65, v86
	v_pk_add_f16 v64, v64, v87
	v_pk_add_f16 v63, v63, v88
	v_pk_fma_f16 v42, v46, v86, v42
	v_pk_fma_f16 v43, v47, v87, v43
	v_pk_fma_f16 v44, v48, v88, v44
	v_pk_fma_f16 v45, v49, v89, v45
	v_pk_add_f16 v62, v62, v85
	v_pk_add_f16 v63, v63, v84
	v_pk_add_f16 v64, v64, v83
	v_pk_add_f16 v65, v65, v82
	v_pk_fma_f16 v45, v9, v85, v45
	v_pk_fma_f16 v44, v8, v84, v44
	v_pk_fma_f16 v43, v7, v83, v43
	v_pk_fma_f16 v42, v6, v82, v42
	v_pk_add_f16 v71, v99, v155 neg_lo:[0,1] neg_hi:[0,1]
	v_pk_add_f16 v72, v100, v156 neg_lo:[0,1] neg_hi:[0,1]
	v_pk_add_f16 v73, v101, v157 neg_lo:[0,1] neg_hi:[0,1]
	v_exp_f16_sdwa v82, v70 dst_sel:WORD_0 dst_unused:UNUSED_PAD src0_sel:WORD_0
	v_exp_f16_sdwa v83, v71 dst_sel:WORD_0 dst_unused:UNUSED_PAD src0_sel:WORD_0
	v_exp_f16_sdwa v84, v72 dst_sel:WORD_0 dst_unused:UNUSED_PAD src0_sel:WORD_0
	v_exp_f16_sdwa v85, v73 dst_sel:WORD_0 dst_unused:UNUSED_PAD src0_sel:WORD_0
	v_exp_f16_sdwa v82, v70 dst_sel:WORD_1 dst_unused:UNUSED_PRESERVE src0_sel:WORD_1
	v_exp_f16_sdwa v83, v71 dst_sel:WORD_1 dst_unused:UNUSED_PRESERVE src0_sel:WORD_1
	v_exp_f16_sdwa v84, v72 dst_sel:WORD_1 dst_unused:UNUSED_PRESERVE src0_sel:WORD_1
	v_exp_f16_sdwa v85, v73 dst_sel:WORD_1 dst_unused:UNUSED_PRESERVE src0_sel:WORD_1
	v_pk_add_f16 v70, v114, v154 neg_lo:[0,1] neg_hi:[0,1]
	v_pk_add_f16 v62, v62, v85
	v_pk_add_f16 v65, v65, v82
	v_pk_add_f16 v64, v64, v83
	v_pk_add_f16 v63, v63, v84
	v_pk_fma_f16 v42, v10, v82, v42
	v_pk_fma_f16 v43, v11, v83, v43
	v_pk_fma_f16 v44, v12, v84, v44
	v_pk_fma_f16 v45, v13, v85, v45
	v_pk_add_f16 v71, v115, v155 neg_lo:[0,1] neg_hi:[0,1]
	v_pk_add_f16 v72, v116, v156 neg_lo:[0,1] neg_hi:[0,1]
	v_pk_add_f16 v73, v117, v157 neg_lo:[0,1] neg_hi:[0,1]
	v_exp_f16_sdwa v82, v70 dst_sel:WORD_0 dst_unused:UNUSED_PAD src0_sel:WORD_0
	v_exp_f16_sdwa v83, v71 dst_sel:WORD_0 dst_unused:UNUSED_PAD src0_sel:WORD_0
	v_exp_f16_sdwa v84, v72 dst_sel:WORD_0 dst_unused:UNUSED_PAD src0_sel:WORD_0
	v_exp_f16_sdwa v85, v73 dst_sel:WORD_0 dst_unused:UNUSED_PAD src0_sel:WORD_0
	v_exp_f16_sdwa v82, v70 dst_sel:WORD_1 dst_unused:UNUSED_PRESERVE src0_sel:WORD_1
	v_exp_f16_sdwa v83, v71 dst_sel:WORD_1 dst_unused:UNUSED_PRESERVE src0_sel:WORD_1
	v_exp_f16_sdwa v84, v72 dst_sel:WORD_1 dst_unused:UNUSED_PRESERVE src0_sel:WORD_1
	v_exp_f16_sdwa v85, v73 dst_sel:WORD_1 dst_unused:UNUSED_PRESERVE src0_sel:WORD_1
	s_nop 0
	v_pk_add_f16 v62, v62, v85
	v_pk_add_f16 v63, v63, v84
	v_pk_add_f16 v64, v64, v83
	v_pk_add_f16 v65, v65, v82
	v_rcp_f16_e32 v73, v62
	v_rcp_f16_sdwa v62, v62 dst_sel:DWORD dst_unused:UNUSED_PAD src0_sel:WORD_1
	v_rcp_f16_e32 v70, v65
	v_rcp_f16_sdwa v65, v65 dst_sel:DWORD dst_unused:UNUSED_PAD src0_sel:WORD_1
	v_rcp_f16_e32 v71, v64
	v_rcp_f16_sdwa v64, v64 dst_sel:DWORD dst_unused:UNUSED_PAD src0_sel:WORD_1
	v_rcp_f16_e32 v72, v63
	v_rcp_f16_sdwa v63, v63 dst_sel:DWORD dst_unused:UNUSED_PAD src0_sel:WORD_1
	v_pk_fma_f16 v45, v17, v85, v45
	v_pack_b32_f16 v62, v73, v62
	v_pk_fma_f16 v44, v16, v84, v44
	v_pk_fma_f16 v43, v15, v83, v43
	v_pk_fma_f16 v42, v14, v82, v42
	v_pack_b32_f16 v65, v70, v65
	v_pack_b32_f16 v64, v71, v64
	v_pack_b32_f16 v63, v72, v63
	v_pk_mul_f16 v45, v45, v62
	s_waitcnt vmcnt(6)
	v_pk_mul_f16 v62, v185, v150 op_sel_hi:[0,1]
	v_pk_mul_f16 v70, v183, v150 op_sel_hi:[0,1]
	v_pk_mul_f16 v82, v184, v150 op_sel_hi:[0,1]
	v_pk_mul_f16 v42, v42, v65
	v_pk_mul_f16 v43, v43, v64
	v_pk_mul_f16 v44, v44, v63
	v_pk_mul_f16 v63, v185, v151 op_sel_hi:[0,1]
	v_pk_mul_f16 v64, v185, v152 op_sel_hi:[0,1]
	v_pk_mul_f16 v65, v185, v153 op_sel_hi:[0,1]
	v_pk_mul_f16 v71, v183, v151 op_sel_hi:[0,1]
	v_pk_mul_f16 v72, v183, v152 op_sel_hi:[0,1]
	v_pk_mul_f16 v73, v183, v153 op_sel_hi:[0,1]
	v_pk_mul_f16 v83, v184, v151 op_sel_hi:[0,1]
	v_pk_mul_f16 v84, v184, v152 op_sel_hi:[0,1]
	v_pk_mul_f16 v85, v184, v153 op_sel_hi:[0,1]
	v_pk_fma_f16 v50, v50, v150, v62
	v_pk_fma_f16 v66, v66, v150, v70
	v_pk_fma_f16 v89, v94, v150, v82
	v_pk_fma_f16 v53, v53, v153, v65
	v_pk_maximum3_f16 v114, v50, v66, v89
	v_pk_fma_f16 v52, v52, v152, v64
	v_pk_fma_f16 v51, v51, v151, v63
	v_pk_fma_f16 v69, v69, v153, v73
	v_pk_fma_f16 v68, v68, v152, v72
	v_pk_fma_f16 v67, v67, v151, v71
	v_pk_fma_f16 v86, v97, v153, v85
	v_pk_fma_f16 v87, v96, v152, v84
	v_pk_fma_f16 v88, v95, v151, v83
	v_pk_fma_f16 v97, v18, v150, v62
	v_pk_fma_f16 v101, v34, v150, v70
	v_pk_fma_f16 v109, v54, v150, v82
	v_pk_fma_f16 v62, v74, v150, v62
	v_pk_fma_f16 v70, v102, v150, v70
	v_pk_fma_f16 v82, v118, v150, v82
	v_pk_maximum3_f16 v115, v51, v67, v88
	v_pk_maximum3_f16 v116, v52, v68, v87
	v_pk_maximum3_f16 v117, v53, v69, v86
	v_pk_maximum3_f16 v122, v97, v101, v109
	v_pk_fma_f16 v94, v21, v153, v65
	v_pk_maximum3_f16 v126, v62, v70, v82
	v_pk_fma_f16 v95, v20, v152, v64
	v_pk_maximum3_f16 v114, v114, v122, v126
	v_pk_fma_f16 v96, v19, v151, v63
	v_pk_fma_f16 v98, v37, v153, v73
	v_pk_fma_f16 v99, v36, v152, v72
	v_pk_fma_f16 v100, v35, v151, v71
	v_pk_fma_f16 v106, v57, v153, v85
	v_pk_fma_f16 v107, v56, v152, v84
	v_pk_fma_f16 v108, v55, v151, v83
	v_pk_fma_f16 v65, v77, v153, v65
	v_pk_fma_f16 v64, v76, v152, v64
	v_pk_fma_f16 v63, v75, v151, v63
	v_pk_fma_f16 v73, v105, v153, v73
	v_pk_fma_f16 v72, v104, v152, v72
	v_pk_fma_f16 v71, v103, v151, v71
	v_pk_fma_f16 v85, v121, v153, v85
	v_pk_fma_f16 v84, v120, v152, v84
	v_pk_fma_f16 v83, v119, v151, v83
	v_pk_maximum3_f16 v123, v96, v100, v108
	v_pk_maximum3_f16 v124, v95, v99, v107
	v_pk_maximum3_f16 v125, v94, v98, v106
	v_pk_maximum3_f16 v128, v64, v72, v84
	v_pk_maximum3_f16 v129, v65, v73, v85
	v_pk_maximum3_f16 v127, v63, v71, v83
	v_pk_maximum3_f16 v115, v115, v123, v127
	v_pk_maximum3_f16 v116, v116, v124, v128
	v_pk_maximum3_f16 v117, v117, v125, v129
	v_pk_add_f16 v50, v50, v114 neg_lo:[0,1] neg_hi:[0,1]
	v_pk_add_f16 v51, v51, v115 neg_lo:[0,1] neg_hi:[0,1]
	v_pk_add_f16 v52, v52, v116 neg_lo:[0,1] neg_hi:[0,1]
	v_pk_add_f16 v53, v53, v117 neg_lo:[0,1] neg_hi:[0,1]
	v_pk_add_f16 v66, v66, v114 neg_lo:[0,1] neg_hi:[0,1]
	v_exp_f16_sdwa v122, v50 dst_sel:WORD_0 dst_unused:UNUSED_PAD src0_sel:WORD_0
	v_exp_f16_sdwa v123, v51 dst_sel:WORD_0 dst_unused:UNUSED_PAD src0_sel:WORD_0
	v_exp_f16_sdwa v124, v52 dst_sel:WORD_0 dst_unused:UNUSED_PAD src0_sel:WORD_0
	v_exp_f16_sdwa v125, v53 dst_sel:WORD_0 dst_unused:UNUSED_PAD src0_sel:WORD_0
	v_exp_f16_sdwa v122, v50 dst_sel:WORD_1 dst_unused:UNUSED_PRESERVE src0_sel:WORD_1
	v_exp_f16_sdwa v123, v51 dst_sel:WORD_1 dst_unused:UNUSED_PRESERVE src0_sel:WORD_1
	v_exp_f16_sdwa v124, v52 dst_sel:WORD_1 dst_unused:UNUSED_PRESERVE src0_sel:WORD_1
	v_exp_f16_sdwa v125, v53 dst_sel:WORD_1 dst_unused:UNUSED_PRESERVE src0_sel:WORD_1
	v_pk_add_f16 v67, v67, v115 neg_lo:[0,1] neg_hi:[0,1]
	v_pk_add_f16 v50, v125, 0
	v_pk_fma_f16 v22, v22, v122, 0
	v_pk_add_f16 v51, v124, 0
	v_pk_add_f16 v52, v123, 0
	v_pk_add_f16 v53, v122, 0
	v_pk_fma_f16 v23, v23, v123, 0
	v_pk_fma_f16 v24, v24, v124, 0
	v_pk_fma_f16 v25, v25, v125, 0
	v_pk_add_f16 v68, v68, v116 neg_lo:[0,1] neg_hi:[0,1]
	v_pk_add_f16 v69, v69, v117 neg_lo:[0,1] neg_hi:[0,1]
	v_exp_f16_sdwa v122, v66 dst_sel:WORD_0 dst_unused:UNUSED_PAD src0_sel:WORD_0
	v_exp_f16_sdwa v123, v67 dst_sel:WORD_0 dst_unused:UNUSED_PAD src0_sel:WORD_0
	v_exp_f16_sdwa v124, v68 dst_sel:WORD_0 dst_unused:UNUSED_PAD src0_sel:WORD_0
	v_exp_f16_sdwa v125, v69 dst_sel:WORD_0 dst_unused:UNUSED_PAD src0_sel:WORD_0
	v_exp_f16_sdwa v122, v66 dst_sel:WORD_1 dst_unused:UNUSED_PRESERVE src0_sel:WORD_1
	v_exp_f16_sdwa v123, v67 dst_sel:WORD_1 dst_unused:UNUSED_PRESERVE src0_sel:WORD_1
	v_exp_f16_sdwa v124, v68 dst_sel:WORD_1 dst_unused:UNUSED_PRESERVE src0_sel:WORD_1
	v_exp_f16_sdwa v125, v69 dst_sel:WORD_1 dst_unused:UNUSED_PRESERVE src0_sel:WORD_1
	s_nop 0
	v_pk_add_f16 v50, v50, v125
	v_pk_fma_f16 v22, v30, v122, v22
	v_pk_add_f16 v30, v89, v114 neg_lo:[0,1] neg_hi:[0,1]
	v_pk_add_f16 v53, v53, v122
	v_pk_add_f16 v52, v52, v123
	v_pk_add_f16 v51, v51, v124
	v_pk_fma_f16 v25, v33, v125, v25
	v_pk_fma_f16 v24, v32, v124, v24
	v_pk_fma_f16 v23, v31, v123, v23
	v_pk_add_f16 v31, v88, v115 neg_lo:[0,1] neg_hi:[0,1]
	v_pk_add_f16 v32, v87, v116 neg_lo:[0,1] neg_hi:[0,1]
	v_pk_add_f16 v33, v86, v117 neg_lo:[0,1] neg_hi:[0,1]
	v_exp_f16_sdwa v66, v30 dst_sel:WORD_0 dst_unused:UNUSED_PAD src0_sel:WORD_0
	v_exp_f16_sdwa v67, v31 dst_sel:WORD_0 dst_unused:UNUSED_PAD src0_sel:WORD_0
	v_exp_f16_sdwa v68, v32 dst_sel:WORD_0 dst_unused:UNUSED_PAD src0_sel:WORD_0
	v_exp_f16_sdwa v69, v33 dst_sel:WORD_0 dst_unused:UNUSED_PAD src0_sel:WORD_0
	v_exp_f16_sdwa v66, v30 dst_sel:WORD_1 dst_unused:UNUSED_PRESERVE src0_sel:WORD_1
	v_exp_f16_sdwa v67, v31 dst_sel:WORD_1 dst_unused:UNUSED_PRESERVE src0_sel:WORD_1
	v_exp_f16_sdwa v68, v32 dst_sel:WORD_1 dst_unused:UNUSED_PRESERVE src0_sel:WORD_1
	v_exp_f16_sdwa v69, v33 dst_sel:WORD_1 dst_unused:UNUSED_PRESERVE src0_sel:WORD_1
	s_nop 0
	v_pk_add_f16 v30, v50, v69
	v_pk_add_f16 v31, v51, v68
	v_pk_add_f16 v32, v52, v67
	v_pk_add_f16 v33, v53, v66
	v_pk_fma_f16 v22, v46, v66, v22
	v_pk_fma_f16 v23, v47, v67, v23
	v_pk_fma_f16 v24, v48, v68, v24
	v_pk_fma_f16 v25, v49, v69, v25
	v_pk_add_f16 v46, v97, v114 neg_lo:[0,1] neg_hi:[0,1]
	v_pk_add_f16 v47, v96, v115 neg_lo:[0,1] neg_hi:[0,1]
	v_pk_add_f16 v48, v95, v116 neg_lo:[0,1] neg_hi:[0,1]
	v_pk_add_f16 v49, v94, v117 neg_lo:[0,1] neg_hi:[0,1]
	v_exp_f16_sdwa v50, v46 dst_sel:WORD_0 dst_unused:UNUSED_PAD src0_sel:WORD_0
	v_exp_f16_sdwa v51, v47 dst_sel:WORD_0 dst_unused:UNUSED_PAD src0_sel:WORD_0
	v_exp_f16_sdwa v52, v48 dst_sel:WORD_0 dst_unused:UNUSED_PAD src0_sel:WORD_0
	v_exp_f16_sdwa v53, v49 dst_sel:WORD_0 dst_unused:UNUSED_PAD src0_sel:WORD_0
	v_exp_f16_sdwa v50, v46 dst_sel:WORD_1 dst_unused:UNUSED_PRESERVE src0_sel:WORD_1
	v_exp_f16_sdwa v51, v47 dst_sel:WORD_1 dst_unused:UNUSED_PRESERVE src0_sel:WORD_1
	v_exp_f16_sdwa v52, v48 dst_sel:WORD_1 dst_unused:UNUSED_PRESERVE src0_sel:WORD_1
	v_exp_f16_sdwa v53, v49 dst_sel:WORD_1 dst_unused:UNUSED_PRESERVE src0_sel:WORD_1
	v_pk_add_f16 v46, v101, v114 neg_lo:[0,1] neg_hi:[0,1]
	v_pk_add_f16 v30, v30, v53
	v_pk_add_f16 v33, v33, v50
	v_pk_add_f16 v32, v32, v51
	v_pk_add_f16 v31, v31, v52
	v_pk_fma_f16 v25, v9, v53, v25
	v_pk_fma_f16 v24, v8, v52, v24
	v_pk_fma_f16 v23, v7, v51, v23
	v_pk_fma_f16 v22, v6, v50, v22
	v_pk_add_f16 v47, v100, v115 neg_lo:[0,1] neg_hi:[0,1]
	v_pk_add_f16 v48, v99, v116 neg_lo:[0,1] neg_hi:[0,1]
	v_pk_add_f16 v49, v98, v117 neg_lo:[0,1] neg_hi:[0,1]
	v_exp_f16_sdwa v50, v46 dst_sel:WORD_0 dst_unused:UNUSED_PAD src0_sel:WORD_0
	v_exp_f16_sdwa v51, v47 dst_sel:WORD_0 dst_unused:UNUSED_PAD src0_sel:WORD_0
	v_exp_f16_sdwa v52, v48 dst_sel:WORD_0 dst_unused:UNUSED_PAD src0_sel:WORD_0
	v_exp_f16_sdwa v53, v49 dst_sel:WORD_0 dst_unused:UNUSED_PAD src0_sel:WORD_0
	v_exp_f16_sdwa v50, v46 dst_sel:WORD_1 dst_unused:UNUSED_PRESERVE src0_sel:WORD_1
	v_exp_f16_sdwa v51, v47 dst_sel:WORD_1 dst_unused:UNUSED_PRESERVE src0_sel:WORD_1
	v_exp_f16_sdwa v52, v48 dst_sel:WORD_1 dst_unused:UNUSED_PRESERVE src0_sel:WORD_1
	v_exp_f16_sdwa v53, v49 dst_sel:WORD_1 dst_unused:UNUSED_PRESERVE src0_sel:WORD_1
	v_pk_add_f16 v46, v109, v114 neg_lo:[0,1] neg_hi:[0,1]
	v_pk_add_f16 v30, v30, v53
	v_pk_add_f16 v31, v31, v52
	v_pk_add_f16 v32, v32, v51
	v_pk_add_f16 v33, v33, v50
	v_pk_fma_f16 v22, v10, v50, v22
	v_pk_fma_f16 v23, v11, v51, v23
	v_pk_fma_f16 v24, v12, v52, v24
	v_pk_fma_f16 v25, v13, v53, v25
	v_pk_add_f16 v47, v108, v115 neg_lo:[0,1] neg_hi:[0,1]
	v_pk_add_f16 v48, v107, v116 neg_lo:[0,1] neg_hi:[0,1]
	v_pk_add_f16 v49, v106, v117 neg_lo:[0,1] neg_hi:[0,1]
	v_exp_f16_sdwa v50, v46 dst_sel:WORD_0 dst_unused:UNUSED_PAD src0_sel:WORD_0
	v_exp_f16_sdwa v51, v47 dst_sel:WORD_0 dst_unused:UNUSED_PAD src0_sel:WORD_0
	v_exp_f16_sdwa v52, v48 dst_sel:WORD_0 dst_unused:UNUSED_PAD src0_sel:WORD_0
	v_exp_f16_sdwa v53, v49 dst_sel:WORD_0 dst_unused:UNUSED_PAD src0_sel:WORD_0
	v_exp_f16_sdwa v50, v46 dst_sel:WORD_1 dst_unused:UNUSED_PRESERVE src0_sel:WORD_1
	v_exp_f16_sdwa v51, v47 dst_sel:WORD_1 dst_unused:UNUSED_PRESERVE src0_sel:WORD_1
	v_exp_f16_sdwa v52, v48 dst_sel:WORD_1 dst_unused:UNUSED_PRESERVE src0_sel:WORD_1
	v_exp_f16_sdwa v53, v49 dst_sel:WORD_1 dst_unused:UNUSED_PRESERVE src0_sel:WORD_1
	v_pk_add_f16 v46, v62, v114 neg_lo:[0,1] neg_hi:[0,1]
	v_pk_add_f16 v30, v30, v53
	v_pk_add_f16 v33, v33, v50
	v_pk_add_f16 v32, v32, v51
	v_pk_add_f16 v31, v31, v52
	v_pk_fma_f16 v25, v17, v53, v25
	v_pk_fma_f16 v24, v16, v52, v24
	v_pk_fma_f16 v23, v15, v51, v23
	v_pk_fma_f16 v22, v14, v50, v22
	v_pk_add_f16 v47, v63, v115 neg_lo:[0,1] neg_hi:[0,1]
	v_pk_add_f16 v48, v64, v116 neg_lo:[0,1] neg_hi:[0,1]
	v_pk_add_f16 v49, v65, v117 neg_lo:[0,1] neg_hi:[0,1]
	v_exp_f16_sdwa v50, v46 dst_sel:WORD_0 dst_unused:UNUSED_PAD src0_sel:WORD_0
	v_exp_f16_sdwa v51, v47 dst_sel:WORD_0 dst_unused:UNUSED_PAD src0_sel:WORD_0
	v_exp_f16_sdwa v52, v48 dst_sel:WORD_0 dst_unused:UNUSED_PAD src0_sel:WORD_0
	v_exp_f16_sdwa v53, v49 dst_sel:WORD_0 dst_unused:UNUSED_PAD src0_sel:WORD_0
	v_exp_f16_sdwa v50, v46 dst_sel:WORD_1 dst_unused:UNUSED_PRESERVE src0_sel:WORD_1
	v_exp_f16_sdwa v51, v47 dst_sel:WORD_1 dst_unused:UNUSED_PRESERVE src0_sel:WORD_1
	v_exp_f16_sdwa v52, v48 dst_sel:WORD_1 dst_unused:UNUSED_PRESERVE src0_sel:WORD_1
	v_exp_f16_sdwa v53, v49 dst_sel:WORD_1 dst_unused:UNUSED_PRESERVE src0_sel:WORD_1
	v_pk_add_f16 v46, v70, v114 neg_lo:[0,1] neg_hi:[0,1]
	v_pk_add_f16 v30, v30, v53
	v_pk_add_f16 v31, v31, v52
	v_pk_add_f16 v32, v32, v51
	v_pk_add_f16 v33, v33, v50
	v_pk_fma_f16 v22, v26, v50, v22
	v_pk_fma_f16 v23, v27, v51, v23
	v_pk_fma_f16 v24, v28, v52, v24
	v_pk_fma_f16 v25, v29, v53, v25
	v_pk_add_f16 v47, v71, v115 neg_lo:[0,1] neg_hi:[0,1]
	v_pk_add_f16 v48, v72, v116 neg_lo:[0,1] neg_hi:[0,1]
	v_pk_add_f16 v49, v73, v117 neg_lo:[0,1] neg_hi:[0,1]
	v_exp_f16_sdwa v50, v46 dst_sel:WORD_0 dst_unused:UNUSED_PAD src0_sel:WORD_0
	v_exp_f16_sdwa v51, v47 dst_sel:WORD_0 dst_unused:UNUSED_PAD src0_sel:WORD_0
	v_exp_f16_sdwa v52, v48 dst_sel:WORD_0 dst_unused:UNUSED_PAD src0_sel:WORD_0
	v_exp_f16_sdwa v53, v49 dst_sel:WORD_0 dst_unused:UNUSED_PAD src0_sel:WORD_0
	v_exp_f16_sdwa v50, v46 dst_sel:WORD_1 dst_unused:UNUSED_PRESERVE src0_sel:WORD_1
	v_exp_f16_sdwa v51, v47 dst_sel:WORD_1 dst_unused:UNUSED_PRESERVE src0_sel:WORD_1
	v_exp_f16_sdwa v52, v48 dst_sel:WORD_1 dst_unused:UNUSED_PRESERVE src0_sel:WORD_1
	v_exp_f16_sdwa v53, v49 dst_sel:WORD_1 dst_unused:UNUSED_PRESERVE src0_sel:WORD_1
	v_pk_add_f16 v46, v82, v114 neg_lo:[0,1] neg_hi:[0,1]
	v_pk_add_f16 v30, v30, v53
	v_pk_add_f16 v33, v33, v50
	v_pk_add_f16 v32, v32, v51
	v_pk_add_f16 v31, v31, v52
	v_pk_fma_f16 v25, v41, v53, v25
	v_pk_fma_f16 v24, v40, v52, v24
	v_pk_fma_f16 v23, v39, v51, v23
	v_pk_fma_f16 v22, v38, v50, v22
	v_pk_add_f16 v47, v83, v115 neg_lo:[0,1] neg_hi:[0,1]
	v_pk_add_f16 v48, v84, v116 neg_lo:[0,1] neg_hi:[0,1]
	v_pk_add_f16 v49, v85, v117 neg_lo:[0,1] neg_hi:[0,1]
	v_exp_f16_sdwa v50, v46 dst_sel:WORD_0 dst_unused:UNUSED_PAD src0_sel:WORD_0
	v_exp_f16_sdwa v51, v47 dst_sel:WORD_0 dst_unused:UNUSED_PAD src0_sel:WORD_0
	v_exp_f16_sdwa v52, v48 dst_sel:WORD_0 dst_unused:UNUSED_PAD src0_sel:WORD_0
	v_exp_f16_sdwa v53, v49 dst_sel:WORD_0 dst_unused:UNUSED_PAD src0_sel:WORD_0
	v_exp_f16_sdwa v50, v46 dst_sel:WORD_1 dst_unused:UNUSED_PRESERVE src0_sel:WORD_1
	v_exp_f16_sdwa v51, v47 dst_sel:WORD_1 dst_unused:UNUSED_PRESERVE src0_sel:WORD_1
	v_exp_f16_sdwa v52, v48 dst_sel:WORD_1 dst_unused:UNUSED_PRESERVE src0_sel:WORD_1
	v_exp_f16_sdwa v53, v49 dst_sel:WORD_1 dst_unused:UNUSED_PRESERVE src0_sel:WORD_1
	s_nop 0
	v_pk_add_f16 v30, v30, v53
	v_pk_add_f16 v31, v31, v52
	v_rcp_f16_e32 v48, v30
	v_rcp_f16_sdwa v30, v30 dst_sel:DWORD dst_unused:UNUSED_PAD src0_sel:WORD_1
	v_pk_add_f16 v32, v32, v51
	v_rcp_f16_e32 v49, v31
	v_rcp_f16_sdwa v31, v31 dst_sel:DWORD dst_unused:UNUSED_PAD src0_sel:WORD_1
	v_pk_add_f16 v33, v33, v50
	v_rcp_f16_e32 v47, v32
	v_rcp_f16_sdwa v32, v32 dst_sel:DWORD dst_unused:UNUSED_PAD src0_sel:WORD_1
	v_rcp_f16_e32 v46, v33
	v_rcp_f16_sdwa v33, v33 dst_sel:DWORD dst_unused:UNUSED_PAD src0_sel:WORD_1
	v_pk_fma_f16 v25, v61, v53, v25
	v_pack_b32_f16 v30, v48, v30
	v_pk_fma_f16 v24, v60, v52, v24
	v_pk_mul_f16 v25, v25, v30
	v_pack_b32_f16 v30, v49, v31
	v_pk_fma_f16 v23, v59, v51, v23
	v_pk_mul_f16 v24, v24, v30
	v_pack_b32_f16 v30, v47, v32
	v_pk_fma_f16 v22, v58, v50, v22
	v_pk_mul_f16 v23, v23, v30
	v_pack_b32_f16 v30, v46, v33
	v_pk_mul_f16 v22, v22, v30
	s_waitcnt vmcnt(0)
	v_pk_mul_f16 v30, v185, v146 op_sel_hi:[0,1]
	v_pk_mul_f16 v31, v185, v147 op_sel_hi:[0,1]
	v_pk_mul_f16 v32, v185, v148 op_sel_hi:[0,1]
	v_pk_mul_f16 v33, v185, v149 op_sel_hi:[0,1]
	v_pk_mul_f16 v46, v183, v146 op_sel_hi:[0,1]
	v_pk_mul_f16 v47, v183, v147 op_sel_hi:[0,1]
	v_pk_mul_f16 v48, v183, v148 op_sel_hi:[0,1]
	v_pk_mul_f16 v49, v183, v149 op_sel_hi:[0,1]
	v_pk_mul_f16 v50, v184, v146 op_sel_hi:[0,1]
	v_pk_mul_f16 v51, v184, v147 op_sel_hi:[0,1]
	v_pk_mul_f16 v52, v184, v148 op_sel_hi:[0,1]
	v_pk_mul_f16 v53, v184, v149 op_sel_hi:[0,1]
	v_pk_fma_f16 v21, v21, v149, v33
	v_pk_fma_f16 v20, v20, v148, v32
	v_pk_fma_f16 v19, v19, v147, v31
	v_pk_fma_f16 v18, v18, v146, v30
	v_pk_fma_f16 v37, v37, v149, v49
	v_pk_fma_f16 v36, v36, v148, v48
	v_pk_fma_f16 v35, v35, v147, v47
	v_pk_fma_f16 v34, v34, v146, v46
	v_pk_fma_f16 v57, v57, v149, v53
	v_pk_fma_f16 v56, v56, v148, v52
	v_pk_fma_f16 v55, v55, v147, v51
	v_pk_fma_f16 v54, v54, v146, v50
	v_pk_fma_f16 v62, v77, v149, v33
	v_pk_fma_f16 v63, v76, v148, v32
	v_pk_fma_f16 v64, v75, v147, v31
	v_pk_fma_f16 v65, v74, v146, v30
	v_pk_maximum3_f16 v74, v18, v34, v54
	v_pk_maximum3_f16 v75, v19, v35, v55
	v_pk_maximum3_f16 v76, v20, v36, v56
	v_pk_maximum3_f16 v77, v21, v37, v57
	v_pk_fma_f16 v66, v105, v149, v49
	v_pk_fma_f16 v67, v104, v148, v48
	v_pk_fma_f16 v68, v103, v147, v47
	v_pk_fma_f16 v69, v102, v146, v46
	v_pk_fma_f16 v70, v121, v149, v53
	v_pk_fma_f16 v71, v120, v148, v52
	v_pk_fma_f16 v72, v119, v147, v51
	v_pk_fma_f16 v73, v118, v146, v50
	v_pk_fma_f16 v33, v133, v149, v33
	v_pk_fma_f16 v32, v132, v148, v32
	v_pk_fma_f16 v31, v131, v147, v31
	v_pk_fma_f16 v30, v130, v146, v30
	v_pk_fma_f16 v49, v141, v149, v49
	v_pk_fma_f16 v48, v140, v148, v48
	v_pk_fma_f16 v47, v139, v147, v47
	v_pk_fma_f16 v46, v138, v146, v46
	v_pk_fma_f16 v53, v145, v149, v53
	v_pk_fma_f16 v52, v144, v148, v52
	v_pk_fma_f16 v51, v143, v147, v51
	v_pk_fma_f16 v50, v142, v146, v50
	v_pk_maximum3_f16 v82, v65, v69, v73
	v_pk_maximum3_f16 v83, v64, v68, v72
	v_pk_maximum3_f16 v84, v63, v67, v71
	v_pk_maximum3_f16 v85, v62, v66, v70
	v_pk_maximum3_f16 v87, v31, v47, v51
	v_pk_maximum3_f16 v86, v30, v46, v50
	v_pk_maximum3_f16 v88, v32, v48, v52
	v_pk_maximum3_f16 v89, v33, v49, v53
	v_pk_maximum3_f16 v74, v74, v82, v86
	v_pk_maximum3_f16 v75, v75, v83, v87
	v_pk_maximum3_f16 v76, v76, v84, v88
	v_pk_maximum3_f16 v77, v77, v85, v89
	s_nop 0
	v_pk_add_f16 v18, v18, v74 neg_lo:[0,1] neg_hi:[0,1]
	v_pk_add_f16 v19, v19, v75 neg_lo:[0,1] neg_hi:[0,1]
	v_pk_add_f16 v20, v20, v76 neg_lo:[0,1] neg_hi:[0,1]
	v_pk_add_f16 v21, v21, v77 neg_lo:[0,1] neg_hi:[0,1]
	v_pk_add_f16 v34, v34, v74 neg_lo:[0,1] neg_hi:[0,1]
	v_exp_f16_sdwa v82, v18 dst_sel:WORD_0 dst_unused:UNUSED_PAD src0_sel:WORD_0
	v_exp_f16_sdwa v83, v19 dst_sel:WORD_0 dst_unused:UNUSED_PAD src0_sel:WORD_0
	v_exp_f16_sdwa v84, v20 dst_sel:WORD_0 dst_unused:UNUSED_PAD src0_sel:WORD_0
	v_exp_f16_sdwa v85, v21 dst_sel:WORD_0 dst_unused:UNUSED_PAD src0_sel:WORD_0
	v_exp_f16_sdwa v82, v18 dst_sel:WORD_1 dst_unused:UNUSED_PRESERVE src0_sel:WORD_1
	v_exp_f16_sdwa v83, v19 dst_sel:WORD_1 dst_unused:UNUSED_PRESERVE src0_sel:WORD_1
	v_exp_f16_sdwa v84, v20 dst_sel:WORD_1 dst_unused:UNUSED_PRESERVE src0_sel:WORD_1
	v_exp_f16_sdwa v85, v21 dst_sel:WORD_1 dst_unused:UNUSED_PRESERVE src0_sel:WORD_1
	v_pk_add_f16 v35, v35, v75 neg_lo:[0,1] neg_hi:[0,1]
	v_pk_add_f16 v18, v82, 0
	v_pk_add_f16 v19, v83, 0
	v_pk_add_f16 v20, v84, 0
	v_pk_add_f16 v21, v85, 0
	v_pk_fma_f16 v6, v6, v82, 0
	v_pk_fma_f16 v7, v7, v83, 0
	v_pk_fma_f16 v8, v8, v84, 0
	v_pk_fma_f16 v9, v9, v85, 0
	v_pk_add_f16 v36, v36, v76 neg_lo:[0,1] neg_hi:[0,1]
	v_pk_add_f16 v37, v37, v77 neg_lo:[0,1] neg_hi:[0,1]
	v_exp_f16_sdwa v82, v34 dst_sel:WORD_0 dst_unused:UNUSED_PAD src0_sel:WORD_0
	v_exp_f16_sdwa v83, v35 dst_sel:WORD_0 dst_unused:UNUSED_PAD src0_sel:WORD_0
	v_exp_f16_sdwa v84, v36 dst_sel:WORD_0 dst_unused:UNUSED_PAD src0_sel:WORD_0
	v_exp_f16_sdwa v85, v37 dst_sel:WORD_0 dst_unused:UNUSED_PAD src0_sel:WORD_0
	v_exp_f16_sdwa v82, v34 dst_sel:WORD_1 dst_unused:UNUSED_PRESERVE src0_sel:WORD_1
	v_exp_f16_sdwa v83, v35 dst_sel:WORD_1 dst_unused:UNUSED_PRESERVE src0_sel:WORD_1
	v_exp_f16_sdwa v84, v36 dst_sel:WORD_1 dst_unused:UNUSED_PRESERVE src0_sel:WORD_1
	v_exp_f16_sdwa v85, v37 dst_sel:WORD_1 dst_unused:UNUSED_PRESERVE src0_sel:WORD_1
	s_nop 0
	v_pk_add_f16 v21, v21, v85
	v_pk_add_f16 v20, v20, v84
	v_pk_add_f16 v19, v19, v83
	v_pk_add_f16 v18, v18, v82
	v_pk_fma_f16 v9, v13, v85, v9
	v_pk_fma_f16 v8, v12, v84, v8
	v_pk_fma_f16 v7, v11, v83, v7
	v_pk_fma_f16 v6, v10, v82, v6
	v_pk_add_f16 v10, v54, v74 neg_lo:[0,1] neg_hi:[0,1]
	v_pk_add_f16 v11, v55, v75 neg_lo:[0,1] neg_hi:[0,1]
	v_pk_add_f16 v12, v56, v76 neg_lo:[0,1] neg_hi:[0,1]
	v_pk_add_f16 v13, v57, v77 neg_lo:[0,1] neg_hi:[0,1]
	v_exp_f16_sdwa v34, v10 dst_sel:WORD_0 dst_unused:UNUSED_PAD src0_sel:WORD_0
	v_exp_f16_sdwa v35, v11 dst_sel:WORD_0 dst_unused:UNUSED_PAD src0_sel:WORD_0
	v_exp_f16_sdwa v36, v12 dst_sel:WORD_0 dst_unused:UNUSED_PAD src0_sel:WORD_0
	v_exp_f16_sdwa v37, v13 dst_sel:WORD_0 dst_unused:UNUSED_PAD src0_sel:WORD_0
	v_exp_f16_sdwa v34, v10 dst_sel:WORD_1 dst_unused:UNUSED_PRESERVE src0_sel:WORD_1
	v_exp_f16_sdwa v35, v11 dst_sel:WORD_1 dst_unused:UNUSED_PRESERVE src0_sel:WORD_1
	v_exp_f16_sdwa v36, v12 dst_sel:WORD_1 dst_unused:UNUSED_PRESERVE src0_sel:WORD_1
	v_exp_f16_sdwa v37, v13 dst_sel:WORD_1 dst_unused:UNUSED_PRESERVE src0_sel:WORD_1
	v_pk_add_f16 v10, v18, v34
	v_pk_add_f16 v11, v19, v35
	v_pk_add_f16 v12, v20, v36
	v_pk_add_f16 v13, v21, v37
	v_pk_fma_f16 v6, v14, v34, v6
	v_pk_fma_f16 v7, v15, v35, v7
	v_pk_fma_f16 v8, v16, v36, v8
	v_pk_fma_f16 v9, v17, v37, v9
	v_pk_add_f16 v14, v65, v74 neg_lo:[0,1] neg_hi:[0,1]
	v_pk_add_f16 v15, v64, v75 neg_lo:[0,1] neg_hi:[0,1]
	v_pk_add_f16 v16, v63, v76 neg_lo:[0,1] neg_hi:[0,1]
	v_pk_add_f16 v17, v62, v77 neg_lo:[0,1] neg_hi:[0,1]
	v_exp_f16_sdwa v18, v14 dst_sel:WORD_0 dst_unused:UNUSED_PAD src0_sel:WORD_0
	v_exp_f16_sdwa v19, v15 dst_sel:WORD_0 dst_unused:UNUSED_PAD src0_sel:WORD_0
	v_exp_f16_sdwa v20, v16 dst_sel:WORD_0 dst_unused:UNUSED_PAD src0_sel:WORD_0
	v_exp_f16_sdwa v21, v17 dst_sel:WORD_0 dst_unused:UNUSED_PAD src0_sel:WORD_0
	v_exp_f16_sdwa v18, v14 dst_sel:WORD_1 dst_unused:UNUSED_PRESERVE src0_sel:WORD_1
	v_exp_f16_sdwa v19, v15 dst_sel:WORD_1 dst_unused:UNUSED_PRESERVE src0_sel:WORD_1
	v_exp_f16_sdwa v20, v16 dst_sel:WORD_1 dst_unused:UNUSED_PRESERVE src0_sel:WORD_1
	v_exp_f16_sdwa v21, v17 dst_sel:WORD_1 dst_unused:UNUSED_PRESERVE src0_sel:WORD_1
	v_pk_add_f16 v14, v69, v74 neg_lo:[0,1] neg_hi:[0,1]
	v_pk_add_f16 v13, v13, v21
	v_pk_add_f16 v12, v12, v20
	v_pk_add_f16 v11, v11, v19
	v_pk_add_f16 v10, v10, v18
	v_pk_fma_f16 v9, v29, v21, v9
	v_pk_fma_f16 v8, v28, v20, v8
	v_pk_fma_f16 v7, v27, v19, v7
	v_pk_fma_f16 v6, v26, v18, v6
	v_pk_add_f16 v15, v68, v75 neg_lo:[0,1] neg_hi:[0,1]
	v_pk_add_f16 v16, v67, v76 neg_lo:[0,1] neg_hi:[0,1]
	v_pk_add_f16 v17, v66, v77 neg_lo:[0,1] neg_hi:[0,1]
	v_exp_f16_sdwa v18, v14 dst_sel:WORD_0 dst_unused:UNUSED_PAD src0_sel:WORD_0
	v_exp_f16_sdwa v19, v15 dst_sel:WORD_0 dst_unused:UNUSED_PAD src0_sel:WORD_0
	v_exp_f16_sdwa v20, v16 dst_sel:WORD_0 dst_unused:UNUSED_PAD src0_sel:WORD_0
	v_exp_f16_sdwa v21, v17 dst_sel:WORD_0 dst_unused:UNUSED_PAD src0_sel:WORD_0
	v_exp_f16_sdwa v18, v14 dst_sel:WORD_1 dst_unused:UNUSED_PRESERVE src0_sel:WORD_1
	v_exp_f16_sdwa v19, v15 dst_sel:WORD_1 dst_unused:UNUSED_PRESERVE src0_sel:WORD_1
	v_exp_f16_sdwa v20, v16 dst_sel:WORD_1 dst_unused:UNUSED_PRESERVE src0_sel:WORD_1
	v_exp_f16_sdwa v21, v17 dst_sel:WORD_1 dst_unused:UNUSED_PRESERVE src0_sel:WORD_1
	v_pk_add_f16 v14, v73, v74 neg_lo:[0,1] neg_hi:[0,1]
	v_pk_add_f16 v10, v10, v18
	v_pk_add_f16 v11, v11, v19
	v_pk_add_f16 v12, v12, v20
	v_pk_add_f16 v13, v13, v21
	v_pk_fma_f16 v6, v38, v18, v6
	v_pk_fma_f16 v7, v39, v19, v7
	v_pk_fma_f16 v8, v40, v20, v8
	v_pk_fma_f16 v9, v41, v21, v9
	v_pk_add_f16 v15, v72, v75 neg_lo:[0,1] neg_hi:[0,1]
	v_pk_add_f16 v16, v71, v76 neg_lo:[0,1] neg_hi:[0,1]
	v_pk_add_f16 v17, v70, v77 neg_lo:[0,1] neg_hi:[0,1]
	v_exp_f16_sdwa v18, v14 dst_sel:WORD_0 dst_unused:UNUSED_PAD src0_sel:WORD_0
	v_exp_f16_sdwa v19, v15 dst_sel:WORD_0 dst_unused:UNUSED_PAD src0_sel:WORD_0
	v_exp_f16_sdwa v20, v16 dst_sel:WORD_0 dst_unused:UNUSED_PAD src0_sel:WORD_0
	v_exp_f16_sdwa v21, v17 dst_sel:WORD_0 dst_unused:UNUSED_PAD src0_sel:WORD_0
	v_exp_f16_sdwa v18, v14 dst_sel:WORD_1 dst_unused:UNUSED_PRESERVE src0_sel:WORD_1
	v_exp_f16_sdwa v19, v15 dst_sel:WORD_1 dst_unused:UNUSED_PRESERVE src0_sel:WORD_1
	v_exp_f16_sdwa v20, v16 dst_sel:WORD_1 dst_unused:UNUSED_PRESERVE src0_sel:WORD_1
	v_exp_f16_sdwa v21, v17 dst_sel:WORD_1 dst_unused:UNUSED_PRESERVE src0_sel:WORD_1
	v_pk_add_f16 v14, v30, v74 neg_lo:[0,1] neg_hi:[0,1]
	v_pk_add_f16 v13, v13, v21
	v_pk_add_f16 v12, v12, v20
	v_pk_add_f16 v11, v11, v19
	v_pk_add_f16 v10, v10, v18
	v_pk_fma_f16 v9, v61, v21, v9
	v_pk_fma_f16 v8, v60, v20, v8
	v_pk_fma_f16 v7, v59, v19, v7
	v_pk_fma_f16 v6, v58, v18, v6
	v_pk_add_f16 v15, v31, v75 neg_lo:[0,1] neg_hi:[0,1]
	v_pk_add_f16 v16, v32, v76 neg_lo:[0,1] neg_hi:[0,1]
	v_pk_add_f16 v17, v33, v77 neg_lo:[0,1] neg_hi:[0,1]
	v_exp_f16_sdwa v18, v14 dst_sel:WORD_0 dst_unused:UNUSED_PAD src0_sel:WORD_0
	v_exp_f16_sdwa v19, v15 dst_sel:WORD_0 dst_unused:UNUSED_PAD src0_sel:WORD_0
	v_exp_f16_sdwa v20, v16 dst_sel:WORD_0 dst_unused:UNUSED_PAD src0_sel:WORD_0
	v_exp_f16_sdwa v21, v17 dst_sel:WORD_0 dst_unused:UNUSED_PAD src0_sel:WORD_0
	v_exp_f16_sdwa v18, v14 dst_sel:WORD_1 dst_unused:UNUSED_PRESERVE src0_sel:WORD_1
	v_exp_f16_sdwa v19, v15 dst_sel:WORD_1 dst_unused:UNUSED_PRESERVE src0_sel:WORD_1
	v_exp_f16_sdwa v20, v16 dst_sel:WORD_1 dst_unused:UNUSED_PRESERVE src0_sel:WORD_1
	v_exp_f16_sdwa v21, v17 dst_sel:WORD_1 dst_unused:UNUSED_PRESERVE src0_sel:WORD_1
	v_pk_add_f16 v10, v10, v18
	v_pk_add_f16 v11, v11, v19
	v_pk_add_f16 v12, v12, v20
	v_pk_add_f16 v13, v13, v21
	v_pk_fma_f16 v14, v78, v18, v6
	v_pk_fma_f16 v15, v79, v19, v7
	v_pk_fma_f16 v16, v80, v20, v8
	v_pk_fma_f16 v17, v81, v21, v9
	v_pk_add_f16 v6, v46, v74 neg_lo:[0,1] neg_hi:[0,1]
	v_pk_add_f16 v7, v47, v75 neg_lo:[0,1] neg_hi:[0,1]
	v_pk_add_f16 v8, v48, v76 neg_lo:[0,1] neg_hi:[0,1]
	v_pk_add_f16 v9, v49, v77 neg_lo:[0,1] neg_hi:[0,1]
	v_exp_f16_sdwa v18, v6 dst_sel:WORD_0 dst_unused:UNUSED_PAD src0_sel:WORD_0
	v_exp_f16_sdwa v19, v7 dst_sel:WORD_0 dst_unused:UNUSED_PAD src0_sel:WORD_0
	v_exp_f16_sdwa v20, v8 dst_sel:WORD_0 dst_unused:UNUSED_PAD src0_sel:WORD_0
	v_exp_f16_sdwa v21, v9 dst_sel:WORD_0 dst_unused:UNUSED_PAD src0_sel:WORD_0
	v_exp_f16_sdwa v18, v6 dst_sel:WORD_1 dst_unused:UNUSED_PRESERVE src0_sel:WORD_1
	v_exp_f16_sdwa v19, v7 dst_sel:WORD_1 dst_unused:UNUSED_PRESERVE src0_sel:WORD_1
	v_exp_f16_sdwa v20, v8 dst_sel:WORD_1 dst_unused:UNUSED_PRESERVE src0_sel:WORD_1
	v_exp_f16_sdwa v21, v9 dst_sel:WORD_1 dst_unused:UNUSED_PRESERVE src0_sel:WORD_1
	s_nop 0
	v_pk_add_f16 v9, v13, v21
	v_pk_add_f16 v8, v12, v20
	v_pk_add_f16 v7, v11, v19
	v_pk_add_f16 v6, v10, v18
	v_pk_fma_f16 v13, v93, v21, v17
	v_pk_fma_f16 v12, v92, v20, v16
	v_pk_fma_f16 v11, v91, v19, v15
	v_pk_fma_f16 v10, v90, v18, v14
	v_pk_add_f16 v18, v50, v74 neg_lo:[0,1] neg_hi:[0,1]
	v_pk_add_f16 v19, v51, v75 neg_lo:[0,1] neg_hi:[0,1]
	v_pk_add_f16 v20, v52, v76 neg_lo:[0,1] neg_hi:[0,1]
	v_pk_add_f16 v21, v53, v77 neg_lo:[0,1] neg_hi:[0,1]
	v_exp_f16_sdwa v14, v18 dst_sel:WORD_0 dst_unused:UNUSED_PAD src0_sel:WORD_0
	v_exp_f16_sdwa v17, v19 dst_sel:WORD_0 dst_unused:UNUSED_PAD src0_sel:WORD_0
	v_exp_f16_sdwa v15, v20 dst_sel:WORD_0 dst_unused:UNUSED_PAD src0_sel:WORD_0
	v_exp_f16_sdwa v16, v21 dst_sel:WORD_0 dst_unused:UNUSED_PAD src0_sel:WORD_0
	v_exp_f16_sdwa v14, v18 dst_sel:WORD_1 dst_unused:UNUSED_PRESERVE src0_sel:WORD_1
	v_exp_f16_sdwa v17, v19 dst_sel:WORD_1 dst_unused:UNUSED_PRESERVE src0_sel:WORD_1
	v_exp_f16_sdwa v15, v20 dst_sel:WORD_1 dst_unused:UNUSED_PRESERVE src0_sel:WORD_1
	v_exp_f16_sdwa v16, v21 dst_sel:WORD_1 dst_unused:UNUSED_PRESERVE src0_sel:WORD_1
	s_nop 0
